# code placement: every 16-MFMA group of the GEMM K-loops starts 8-byte aligned (s_nop 0 pads in front of s_setprio 1)
# baseline (speedup 1.0000x reference)
; #define PG8_STAGE(bufoff, gbase, voff) do { _Pragma("unroll") for (int _i = 0; _i < 2; ++_i) \
;         __builtin_amdgcn_global_load_lds((const unsigned*)((const char*)(gbase) + (voff)[_i]), (PG8_LAS unsigned*)(lds + (bufoff) + ldsw + _i * 8192), 16, 0, 0); } while (0)
; #define PG8_STAGE_A(bufoff, gbase, h, nx) do { _Pragma("unroll") for (int _i = 0; _i < 2; ++_i) { \
;         const unsigned vo_ = GA ? ((nx) ? vgn[h][_i] : vgc[h][_i]) : voffA[_i]; \
;         __builtin_amdgcn_global_load_lds((const unsigned*)((const char*)(gbase) + vo_), (PG8_LAS unsigned*)(lds + (bufoff) + ldsw + _i * 8192), 16, 0, 0); } } while (0)
; #define PG8_LDA(dst, b, h) do { _Pragma("unroll") for (int m = 0; m < 4; ++m) _Pragma("unroll") for (int k = 0; k < 2; ++k) dst[m][k] = *(const PG8_LAS bf16x8*)(lds + PG8_SA(b, h) + aoff + m * 2048 + k * 1024); } while (0)
; #define PG8_LDB(dst, b, h) do { _Pragma("unroll") for (int n = 0; n < 2; ++n) _Pragma("unroll") for (int k = 0; k < 2; ++k) dst[n][k] = *(const PG8_LAS bf16x8*)(lds + PG8_SB(b, h) + boff + n * 2048 + k * 1024); } while (0)
; #define PG8_MMA(ai, bj, At, Bt) do { __builtin_amdgcn_s_setprio(1); _Pragma("unroll") for (int m = 0; m < 4; ++m) _Pragma("unroll") for (int n = 0; n < 2; ++n) _Pragma("unroll") for (int k = 0; k < 2; ++k) \
;         acc[ai][bj][m][n] = __builtin_amdgcn_mfma_f32_16x16x32_bf16(Bt[n][k], At[m][k], acc[ai][bj][m][n], 0, 0, 0); __builtin_amdgcn_s_setprio(0); } while (0)
; #define PG8_WAIT_V(n) asm volatile("s_waitcnt vmcnt(" #n ")" ::: "memory")
; #define PG8_WAIT_L(n) asm volatile("s_waitcnt lgkmcnt(" #n ")" ::: "memory")
; #define PG8_BAR __builtin_amdgcn_s_barrier()
; #define PG8_SCHED __builtin_amdgcn_sched_barrier(0)
; template <class Epi, class Sched>
; __device__ __forceinline__ void gemm_phase(const int WID_, PG8_LAS unsigned char* lds, const Sched& S, const Epi& E) {
;     ...
;             PG8_LDB(B0, 0, 0); PG8_LDB(B1, 0, 1); PG8_SCHED; PG8_LDA(At, 0, 0); PG8_STAGE_A(PG8_SA(1, 1), a1 + hstepA, 1, false);
;             PG8_WAIT_V(8); PG8_WAIT_L(0); PG8_BAR; PG8_MMA(0, 0, At, B0); PG8_MMA(0, 1, At, B1); PG8_BAR; PG8_SCHED;
;             PG8_LDA(At, 0, 1); PG8_STAGE(PG8_SB(0, 0), b2, voffB); PG8_STAGE(PG8_SB(0, 1), b2 + hstepB, voffB); PG8_STAGE_A(PG8_SA(0, 0), a2, 0, last);
.LBB0_114:
	ds_read_b128 v[148:151], v156
	ds_read_b128 v[160:163], v156 offset:1024
	ds_read_b128 v[164:167], v156 offset:2048
	ds_read_b128 v[168:171], v156 offset:3072
	ds_read_b128 v[172:175], v157
	ds_read_b128 v[176:179], v157 offset:1024
	ds_read_b128 v[180:183], v157 offset:2048
	ds_read_b128 v[184:187], v157 offset:3072
	s_add_u32 s22, s20, 0xfffc0080
	s_addc_u32 s23, s21, -1
	s_cmp_eq_u32 s48, 12
	s_cselect_b32 s29, s3, s23
	s_cselect_b32 s28, s13, s22
	s_cselect_b32 s23, s11, s47
	s_cselect_b32 s22, s19, s46
	v_lshl_add_u64 v[152:153], s[20:21], 0, v[140:141]
	s_add_i32 m0, s31, 0xc000
	ds_read_b128 v[188:191], v158
	ds_read_b128 v[192:195], v158 offset:1024
	ds_read_b128 v[196:199], v158 offset:2048
	ds_read_b128 v[200:203], v158 offset:3072
	ds_read_b128 v[204:207], v158 offset:4096
	ds_read_b128 v[208:211], v158 offset:5120
	ds_read_b128 v[212:215], v158 offset:6144
	ds_read_b128 v[216:219], v158 offset:7168
	global_load_lds_dwordx4 v[152:153], off
	v_lshl_add_u64 v[152:153], s[20:21], 0, v[142:143]
	s_add_i32 m0, s31, 0xe000
	s_nop 0
	global_load_lds_dwordx4 v[152:153], off
	s_waitcnt vmcnt(8)
	s_waitcnt lgkmcnt(0)
	s_barrier
	s_setprio 1
	s_waitcnt lgkmcnt(0)
	v_mfma_f32_16x16x32_bf16 v[124:127], v[148:151], v[188:191], v[124:127]
	v_mfma_f32_16x16x32_bf16 v[120:123], v[164:167], v[188:191], v[120:123]
	v_mfma_f32_16x16x32_bf16 v[108:111], v[148:151], v[196:199], v[108:111]
	v_mfma_f32_16x16x32_bf16 v[104:107], v[164:167], v[196:199], v[104:107]
	v_mfma_f32_16x16x32_bf16 v[92:95], v[148:151], v[204:207], v[92:95]
	v_mfma_f32_16x16x32_bf16 v[88:91], v[164:167], v[204:207], v[88:91]
	v_mfma_f32_16x16x32_bf16 v[76:79], v[148:151], v[212:215], v[76:79]
	v_mfma_f32_16x16x32_bf16 v[72:75], v[164:167], v[212:215], v[72:75]
	v_mfma_f32_16x16x32_bf16 v[124:127], v[160:163], v[192:195], v[124:127]
	v_mfma_f32_16x16x32_bf16 v[120:123], v[168:171], v[192:195], v[120:123]
	v_mfma_f32_16x16x32_bf16 v[108:111], v[160:163], v[200:203], v[108:111]
	v_mfma_f32_16x16x32_bf16 v[104:107], v[168:171], v[200:203], v[104:107]
	v_mfma_f32_16x16x32_bf16 v[92:95], v[160:163], v[208:211], v[92:95]
	v_mfma_f32_16x16x32_bf16 v[88:91], v[168:171], v[208:211], v[88:91]
	v_mfma_f32_16x16x32_bf16 v[76:79], v[160:163], v[216:219], v[76:79]
	v_mfma_f32_16x16x32_bf16 v[72:75], v[168:171], v[216:219], v[72:75]
	s_setprio 0
	s_setprio 1
	v_mfma_f32_16x16x32_bf16 v[116:119], v[172:175], v[188:191], v[116:119]
	v_mfma_f32_16x16x32_bf16 v[112:115], v[180:183], v[188:191], v[112:115]
	v_mfma_f32_16x16x32_bf16 v[100:103], v[172:175], v[196:199], v[100:103]
	v_mfma_f32_16x16x32_bf16 v[96:99], v[180:183], v[196:199], v[96:99]
	v_mfma_f32_16x16x32_bf16 v[84:87], v[172:175], v[204:207], v[84:87]
	v_mfma_f32_16x16x32_bf16 v[80:83], v[180:183], v[204:207], v[80:83]
	v_mfma_f32_16x16x32_bf16 v[68:71], v[172:175], v[212:215], v[68:71]
	v_mfma_f32_16x16x32_bf16 v[64:67], v[180:183], v[212:215], v[64:67]
	v_mfma_f32_16x16x32_bf16 v[116:119], v[176:179], v[192:195], v[116:119]
	v_mfma_f32_16x16x32_bf16 v[112:115], v[184:187], v[192:195], v[112:115]
	v_mfma_f32_16x16x32_bf16 v[100:103], v[176:179], v[200:203], v[100:103]
	v_mfma_f32_16x16x32_bf16 v[96:99], v[184:187], v[200:203], v[96:99]
	v_mfma_f32_16x16x32_bf16 v[84:87], v[176:179], v[208:211], v[84:87]
	v_mfma_f32_16x16x32_bf16 v[80:83], v[184:187], v[208:211], v[80:83]
	v_mfma_f32_16x16x32_bf16 v[68:71], v[176:179], v[216:219], v[68:71]
	v_mfma_f32_16x16x32_bf16 v[64:67], v[184:187], v[216:219], v[64:67]
	s_setprio 0
	s_barrier
	s_add_i32 s49, s42, s30
	v_lshl_add_u64 v[152:153], s[22:23], 0, v[130:131]
	s_mov_b32 m0, s49
	ds_read_b128 v[188:191], v158 offset:16384
	ds_read_b128 v[192:195], v158 offset:17408
	ds_read_b128 v[196:199], v158 offset:18432
	ds_read_b128 v[200:203], v158 offset:19456
	ds_read_b128 v[204:207], v158 offset:20480
	ds_read_b128 v[208:211], v158 offset:21504
	ds_read_b128 v[212:215], v158 offset:22528
	ds_read_b128 v[216:219], v158 offset:23552
	global_load_lds_dwordx4 v[152:153], off
	s_add_i32 m0, s49, 0x2000
	s_add_u32 s50, s22, 0x40000
	v_lshl_add_u64 v[220:221], s[22:23], 0, v[134:135]
	s_addc_u32 s51, s23, 0
	s_add_i32 s49, s43, s30
	global_load_lds_dwordx4 v[220:221], off
	v_lshl_add_u64 v[222:223], s[50:51], 0, v[130:131]
	s_mov_b32 m0, s49
	v_lshl_add_u64 v[224:225], s[28:29], 0, v[132:133]
	global_load_lds_dwordx4 v[222:223], off
	v_lshl_add_u64 v[222:223], s[50:51], 0, v[134:135]
	s_add_i32 m0, s49, 0x2000
	s_nop 0
	global_load_lds_dwordx4 v[222:223], off
	v_lshl_add_u64 v[222:223], s[28:29], 0, v[128:129]
	s_mov_b32 m0, s31
	s_nop 0
	global_load_lds_dwordx4 v[222:223], off
	s_mov_b32 m0, s33
	s_nop 0
	global_load_lds_dwordx4 v[224:225], off
	s_waitcnt vmcnt(8)
	s_waitcnt lgkmcnt(0)
	s_barrier
; #define PG8_STAGE_A(bufoff, gbase, h, nx) do { _Pragma("unroll") for (int _i = 0; _i < 2; ++_i) { \
;         const unsigned vo_ = GA ? ((nx) ? vgn[h][_i] : vgc[h][_i]) : voffA[_i]; \
;         __builtin_amdgcn_global_load_lds((const unsigned*)((const char*)(gbase) + vo_), (PG8_LAS unsigned*)(lds + (bufoff) + ldsw + _i * 8192), 16, 0, 0); } } while (0)
; #define PG8_LDA(dst, b, h) do { _Pragma("unroll") for (int m = 0; m < 4; ++m) _Pragma("unroll") for (int k = 0; k < 2; ++k) dst[m][k] = *(const PG8_LAS bf16x8*)(lds + PG8_SA(b, h) + aoff + m * 2048 + k * 1024); } while (0)
; #define PG8_LDB(dst, b, h) do { _Pragma("unroll") for (int n = 0; n < 2; ++n) _Pragma("unroll") for (int k = 0; k < 2; ++k) dst[n][k] = *(const PG8_LAS bf16x8*)(lds + PG8_SB(b, h) + boff + n * 2048 + k * 1024); } while (0)
; #define PG8_MMA(ai, bj, At, Bt) do { __builtin_amdgcn_s_setprio(1); _Pragma("unroll") for (int m = 0; m < 4; ++m) _Pragma("unroll") for (int n = 0; n < 2; ++n) _Pragma("unroll") for (int k = 0; k < 2; ++k) \
;         acc[ai][bj][m][n] = __builtin_amdgcn_mfma_f32_16x16x32_bf16(Bt[n][k], At[m][k], acc[ai][bj][m][n], 0, 0, 0); __builtin_amdgcn_s_setprio(0); } while (0)
; #define PG8_WAIT_V(n) asm volatile("s_waitcnt vmcnt(" #n ")" ::: "memory")
; #define PG8_WAIT_L(n) asm volatile("s_waitcnt lgkmcnt(" #n ")" ::: "memory")
; #define PG8_BAR __builtin_amdgcn_s_barrier()
; #define PG8_SCHED __builtin_amdgcn_sched_barrier(0)
; template <class Epi, class Sched>
; __device__ __forceinline__ void gemm_phase(const int WID_, PG8_LAS unsigned char* lds, const Sched& S, const Epi& E) {
;     ...
;             PG8_WAIT_V(8); PG8_WAIT_L(0); PG8_BAR; PG8_MMA(1, 0, At, B0); PG8_MMA(1, 1, At, B1); PG8_BAR; PG8_SCHED;
;             PG8_LDB(B0, 1, 0); PG8_LDB(B1, 1, 1); PG8_SCHED; PG8_LDA(At, 1, 0); PG8_STAGE_A(PG8_SA(0, 1), a2 + hstepA, 1, last);
;             PG8_WAIT_V(8); PG8_WAIT_L(0); PG8_BAR; PG8_MMA(0, 0, At, B0); PG8_MMA(0, 1, At, B1); PG8_BAR; PG8_SCHED;
	s_nop 0
	s_setprio 1
	s_waitcnt lgkmcnt(0)
	v_mfma_f32_16x16x32_bf16 v[60:63], v[148:151], v[188:191], v[60:63]
	v_mfma_f32_16x16x32_bf16 v[56:59], v[164:167], v[188:191], v[56:59]
	v_mfma_f32_16x16x32_bf16 v[44:47], v[148:151], v[196:199], v[44:47]
	v_mfma_f32_16x16x32_bf16 v[40:43], v[164:167], v[196:199], v[40:43]
	v_mfma_f32_16x16x32_bf16 v[28:31], v[148:151], v[204:207], v[28:31]
	v_mfma_f32_16x16x32_bf16 v[24:27], v[164:167], v[204:207], v[24:27]
	v_mfma_f32_16x16x32_bf16 v[12:15], v[148:151], v[212:215], v[12:15]
	v_mfma_f32_16x16x32_bf16 v[8:11], v[164:167], v[212:215], v[8:11]
	v_mfma_f32_16x16x32_bf16 v[60:63], v[160:163], v[192:195], v[60:63]
	v_mfma_f32_16x16x32_bf16 v[56:59], v[168:171], v[192:195], v[56:59]
	v_mfma_f32_16x16x32_bf16 v[44:47], v[160:163], v[200:203], v[44:47]
	v_mfma_f32_16x16x32_bf16 v[40:43], v[168:171], v[200:203], v[40:43]
	v_mfma_f32_16x16x32_bf16 v[28:31], v[160:163], v[208:211], v[28:31]
	v_mfma_f32_16x16x32_bf16 v[24:27], v[168:171], v[208:211], v[24:27]
	v_mfma_f32_16x16x32_bf16 v[12:15], v[160:163], v[216:219], v[12:15]
	v_mfma_f32_16x16x32_bf16 v[8:11], v[168:171], v[216:219], v[8:11]
	s_setprio 0
	s_setprio 1
	v_mfma_f32_16x16x32_bf16 v[52:55], v[172:175], v[188:191], v[52:55]
	v_mfma_f32_16x16x32_bf16 v[48:51], v[180:183], v[188:191], v[48:51]
	v_mfma_f32_16x16x32_bf16 v[36:39], v[172:175], v[196:199], v[36:39]
	v_mfma_f32_16x16x32_bf16 v[32:35], v[180:183], v[196:199], v[32:35]
	v_mfma_f32_16x16x32_bf16 v[20:23], v[172:175], v[204:207], v[20:23]
	v_mfma_f32_16x16x32_bf16 v[16:19], v[180:183], v[204:207], v[16:19]
	v_mfma_f32_16x16x32_bf16 v[4:7], v[172:175], v[212:215], v[4:7]
	v_mfma_f32_16x16x32_bf16 v[0:3], v[180:183], v[212:215], v[0:3]
	v_mfma_f32_16x16x32_bf16 v[52:55], v[176:179], v[192:195], v[52:55]
	v_mfma_f32_16x16x32_bf16 v[48:51], v[184:187], v[192:195], v[48:51]
	v_mfma_f32_16x16x32_bf16 v[36:39], v[176:179], v[200:203], v[36:39]
	v_mfma_f32_16x16x32_bf16 v[32:35], v[184:187], v[200:203], v[32:35]
	v_mfma_f32_16x16x32_bf16 v[20:23], v[176:179], v[208:211], v[20:23]
	v_mfma_f32_16x16x32_bf16 v[16:19], v[184:187], v[208:211], v[16:19]
	v_mfma_f32_16x16x32_bf16 v[4:7], v[176:179], v[216:219], v[4:7]
	v_mfma_f32_16x16x32_bf16 v[0:3], v[184:187], v[216:219], v[0:3]
	s_setprio 0
	s_barrier
	s_add_i32 s49, 0, 0x18000
	v_add_u32_e32 v136, s49, v154
	s_add_i32 s50, 0, 0x1c000
	ds_read_b128 v[148:151], v136
	ds_read_b128 v[160:163], v136 offset:1024
	ds_read_b128 v[164:167], v136 offset:2048
	ds_read_b128 v[168:171], v136 offset:3072
	v_add_u32_e32 v136, s50, v154
	ds_read_b128 v[172:175], v136
	ds_read_b128 v[176:179], v136 offset:1024
	ds_read_b128 v[180:183], v136 offset:2048
	ds_read_b128 v[184:187], v136 offset:3072
	s_add_u32 s28, s28, 0x40000
	s_addc_u32 s29, s29, 0
	s_mov_b32 m0, s34
	v_lshl_add_u64 v[226:227], s[28:29], 0, v[128:129]
	ds_read_b128 v[188:191], v158 offset:32768
	ds_read_b128 v[192:195], v158 offset:33792
	ds_read_b128 v[196:199], v158 offset:34816
	ds_read_b128 v[200:203], v158 offset:35840
	ds_read_b128 v[204:207], v158 offset:36864
	ds_read_b128 v[208:211], v158 offset:37888
	ds_read_b128 v[212:215], v158 offset:38912
	ds_read_b128 v[216:219], v158 offset:39936
	global_load_lds_dwordx4 v[226:227], off
	v_lshl_add_u64 v[226:227], s[28:29], 0, v[132:133]
	s_mov_b32 m0, s35
	s_nop 0
	global_load_lds_dwordx4 v[226:227], off
	s_waitcnt vmcnt(8)
	s_waitcnt lgkmcnt(0)
	s_barrier
	s_nop 0
	s_setprio 1
	s_waitcnt lgkmcnt(0)
	v_mfma_f32_16x16x32_bf16 v[124:127], v[148:151], v[188:191], v[124:127]
	v_mfma_f32_16x16x32_bf16 v[120:123], v[164:167], v[188:191], v[120:123]
	v_mfma_f32_16x16x32_bf16 v[108:111], v[148:151], v[196:199], v[108:111]
	v_mfma_f32_16x16x32_bf16 v[104:107], v[164:167], v[196:199], v[104:107]
	v_mfma_f32_16x16x32_bf16 v[92:95], v[148:151], v[204:207], v[92:95]
	v_mfma_f32_16x16x32_bf16 v[88:91], v[164:167], v[204:207], v[88:91]
	v_mfma_f32_16x16x32_bf16 v[76:79], v[148:151], v[212:215], v[76:79]
	v_mfma_f32_16x16x32_bf16 v[72:75], v[164:167], v[212:215], v[72:75]
	v_mfma_f32_16x16x32_bf16 v[124:127], v[160:163], v[192:195], v[124:127]
	v_mfma_f32_16x16x32_bf16 v[120:123], v[168:171], v[192:195], v[120:123]
	v_mfma_f32_16x16x32_bf16 v[108:111], v[160:163], v[200:203], v[108:111]
	v_mfma_f32_16x16x32_bf16 v[104:107], v[168:171], v[200:203], v[104:107]
	v_mfma_f32_16x16x32_bf16 v[92:95], v[160:163], v[208:211], v[92:95]
	v_mfma_f32_16x16x32_bf16 v[88:91], v[168:171], v[208:211], v[88:91]
	v_mfma_f32_16x16x32_bf16 v[76:79], v[160:163], v[216:219], v[76:79]
	v_mfma_f32_16x16x32_bf16 v[72:75], v[168:171], v[216:219], v[72:75]
	s_setprio 0
	s_setprio 1
	v_mfma_f32_16x16x32_bf16 v[116:119], v[172:175], v[188:191], v[116:119]
	v_mfma_f32_16x16x32_bf16 v[112:115], v[180:183], v[188:191], v[112:115]
	v_mfma_f32_16x16x32_bf16 v[100:103], v[172:175], v[196:199], v[100:103]
	v_mfma_f32_16x16x32_bf16 v[96:99], v[180:183], v[196:199], v[96:99]
	v_mfma_f32_16x16x32_bf16 v[84:87], v[172:175], v[204:207], v[84:87]
	v_mfma_f32_16x16x32_bf16 v[80:83], v[180:183], v[204:207], v[80:83]
	v_mfma_f32_16x16x32_bf16 v[68:71], v[172:175], v[212:215], v[68:71]
	v_mfma_f32_16x16x32_bf16 v[64:67], v[180:183], v[212:215], v[64:67]
	v_mfma_f32_16x16x32_bf16 v[116:119], v[176:179], v[192:195], v[116:119]
	v_mfma_f32_16x16x32_bf16 v[112:115], v[184:187], v[192:195], v[112:115]
	v_mfma_f32_16x16x32_bf16 v[100:103], v[176:179], v[200:203], v[100:103]
	v_mfma_f32_16x16x32_bf16 v[96:99], v[184:187], v[200:203], v[96:99]
	v_mfma_f32_16x16x32_bf16 v[84:87], v[176:179], v[208:211], v[84:87]
	v_mfma_f32_16x16x32_bf16 v[80:83], v[184:187], v[208:211], v[80:83]
	v_mfma_f32_16x16x32_bf16 v[68:71], v[176:179], v[216:219], v[68:71]
	v_mfma_f32_16x16x32_bf16 v[64:67], v[184:187], v[216:219], v[64:67]
	s_setprio 0
	s_barrier
; #define PG8_STAGE(bufoff, gbase, voff) do { _Pragma("unroll") for (int _i = 0; _i < 2; ++_i) \
;         __builtin_amdgcn_global_load_lds((const unsigned*)((const char*)(gbase) + (voff)[_i]), (PG8_LAS unsigned*)(lds + (bufoff) + ldsw + _i * 8192), 16, 0, 0); } while (0)
; #define PG8_STAGE_A(bufoff, gbase, h, nx) do { _Pragma("unroll") for (int _i = 0; _i < 2; ++_i) { \
;         const unsigned vo_ = GA ? ((nx) ? vgn[h][_i] : vgc[h][_i]) : voffA[_i]; \
;         __builtin_amdgcn_global_load_lds((const unsigned*)((const char*)(gbase) + vo_), (PG8_LAS unsigned*)(lds + (bufoff) + ldsw + _i * 8192), 16, 0, 0); } } while (0)
; #define PG8_LDA(dst, b, h) do { _Pragma("unroll") for (int m = 0; m < 4; ++m) _Pragma("unroll") for (int k = 0; k < 2; ++k) dst[m][k] = *(const PG8_LAS bf16x8*)(lds + PG8_SA(b, h) + aoff + m * 2048 + k * 1024); } while (0)
; #define PG8_MMA(ai, bj, At, Bt) do { __builtin_amdgcn_s_setprio(1); _Pragma("unroll") for (int m = 0; m < 4; ++m) _Pragma("unroll") for (int n = 0; n < 2; ++n) _Pragma("unroll") for (int k = 0; k < 2; ++k) \
;         acc[ai][bj][m][n] = __builtin_amdgcn_mfma_f32_16x16x32_bf16(Bt[n][k], At[m][k], acc[ai][bj][m][n], 0, 0, 0); __builtin_amdgcn_s_setprio(0); } while (0)
; #define PG8_WAIT_V(n) asm volatile("s_waitcnt vmcnt(" #n ")" ::: "memory")
; #define PG8_WAIT_L(n) asm volatile("s_waitcnt lgkmcnt(" #n ")" ::: "memory")
; #define PG8_BAR __builtin_amdgcn_s_barrier()
; #define PG8_SCHED __builtin_amdgcn_sched_barrier(0)
; template <class Epi, class Sched>
; __device__ __forceinline__ void gemm_phase(const int WID_, PG8_LAS unsigned char* lds, const Sched& S, const Epi& E) {
;     ...
;             PG8_LDA(At, 1, 1); PG8_STAGE(PG8_SB(1, 0), b3, voffB); PG8_STAGE(PG8_SB(1, 1), b3 + hstepB, voffB); PG8_STAGE_A(PG8_SA(1, 0), a3, 0, last);
;             PG8_WAIT_V(8); PG8_WAIT_L(0); PG8_BAR; PG8_MMA(1, 0, At, B0); PG8_MMA(1, 1, At, B1); PG8_BAR; PG8_SCHED;
;         }
	s_add_i32 s28, s49, s30
	v_lshl_add_u64 v[152:153], v[152:153], 0, s[6:7]
	s_mov_b32 m0, s28
	ds_read_b128 v[188:191], v158 offset:49152
	ds_read_b128 v[192:195], v158 offset:50176
	ds_read_b128 v[196:199], v158 offset:51200
	ds_read_b128 v[200:203], v158 offset:52224
	ds_read_b128 v[204:207], v158 offset:53248
	ds_read_b128 v[208:211], v158 offset:54272
	ds_read_b128 v[212:215], v158 offset:55296
	ds_read_b128 v[216:219], v158 offset:56320
	global_load_lds_dwordx4 v[152:153], off
	s_add_i32 m0, s28, 0x2000
	s_add_u32 s22, s22, 0x40080
	v_lshl_add_u64 v[152:153], v[220:221], 0, s[6:7]
	s_addc_u32 s23, s23, 0
	s_add_i32 s28, s50, s30
	global_load_lds_dwordx4 v[152:153], off
	v_lshl_add_u64 v[152:153], s[22:23], 0, v[130:131]
	s_mov_b32 m0, s28
	s_nop 0
	global_load_lds_dwordx4 v[152:153], off
	v_lshl_add_u64 v[152:153], s[22:23], 0, v[134:135]
	s_add_i32 m0, s28, 0x2000
	s_nop 0
	global_load_lds_dwordx4 v[152:153], off
	v_lshl_add_u64 v[152:153], v[222:223], 0, s[6:7]
	s_mov_b32 m0, s37
	s_nop 0
	global_load_lds_dwordx4 v[152:153], off
	v_lshl_add_u64 v[152:153], v[224:225], 0, s[6:7]
	s_mov_b32 m0, s38
	s_nop 0
	global_load_lds_dwordx4 v[152:153], off
	s_waitcnt vmcnt(8)
	s_waitcnt lgkmcnt(0)
	s_barrier
	s_setprio 1
	s_waitcnt lgkmcnt(0)
	v_mfma_f32_16x16x32_bf16 v[60:63], v[148:151], v[188:191], v[60:63]
	v_mfma_f32_16x16x32_bf16 v[56:59], v[164:167], v[188:191], v[56:59]
	v_mfma_f32_16x16x32_bf16 v[44:47], v[148:151], v[196:199], v[44:47]
	v_mfma_f32_16x16x32_bf16 v[40:43], v[164:167], v[196:199], v[40:43]
	v_mfma_f32_16x16x32_bf16 v[28:31], v[148:151], v[204:207], v[28:31]
	v_mfma_f32_16x16x32_bf16 v[24:27], v[164:167], v[204:207], v[24:27]
	v_mfma_f32_16x16x32_bf16 v[12:15], v[148:151], v[212:215], v[12:15]
	v_mfma_f32_16x16x32_bf16 v[8:11], v[164:167], v[212:215], v[8:11]
	v_mfma_f32_16x16x32_bf16 v[60:63], v[160:163], v[192:195], v[60:63]
	v_mfma_f32_16x16x32_bf16 v[56:59], v[168:171], v[192:195], v[56:59]
	v_mfma_f32_16x16x32_bf16 v[44:47], v[160:163], v[200:203], v[44:47]
	v_mfma_f32_16x16x32_bf16 v[40:43], v[168:171], v[200:203], v[40:43]
	v_mfma_f32_16x16x32_bf16 v[28:31], v[160:163], v[208:211], v[28:31]
	v_mfma_f32_16x16x32_bf16 v[24:27], v[168:171], v[208:211], v[24:27]
	v_mfma_f32_16x16x32_bf16 v[12:15], v[160:163], v[216:219], v[12:15]
	v_mfma_f32_16x16x32_bf16 v[8:11], v[168:171], v[216:219], v[8:11]
	s_setprio 0
	s_setprio 1
	v_mfma_f32_16x16x32_bf16 v[52:55], v[172:175], v[188:191], v[52:55]
	v_mfma_f32_16x16x32_bf16 v[48:51], v[180:183], v[188:191], v[48:51]
	v_mfma_f32_16x16x32_bf16 v[36:39], v[172:175], v[196:199], v[36:39]
	v_mfma_f32_16x16x32_bf16 v[32:35], v[180:183], v[196:199], v[32:35]
	v_mfma_f32_16x16x32_bf16 v[20:23], v[172:175], v[204:207], v[20:23]
	v_mfma_f32_16x16x32_bf16 v[16:19], v[180:183], v[204:207], v[16:19]
	v_mfma_f32_16x16x32_bf16 v[4:7], v[172:175], v[212:215], v[4:7]
	v_mfma_f32_16x16x32_bf16 v[0:3], v[180:183], v[212:215], v[0:3]
	v_mfma_f32_16x16x32_bf16 v[52:55], v[176:179], v[192:195], v[52:55]
	v_mfma_f32_16x16x32_bf16 v[48:51], v[184:187], v[192:195], v[48:51]
	v_mfma_f32_16x16x32_bf16 v[36:39], v[176:179], v[200:203], v[36:39]
	v_mfma_f32_16x16x32_bf16 v[32:35], v[184:187], v[200:203], v[32:35]
	v_mfma_f32_16x16x32_bf16 v[20:23], v[176:179], v[208:211], v[20:23]
	v_mfma_f32_16x16x32_bf16 v[16:19], v[184:187], v[208:211], v[16:19]
	v_mfma_f32_16x16x32_bf16 v[4:7], v[176:179], v[216:219], v[4:7]
	v_mfma_f32_16x16x32_bf16 v[0:3], v[184:187], v[216:219], v[0:3]
	s_setprio 0
	s_barrier
	s_add_i32 s48, s48, 2
	s_add_u32 s20, s20, 0x100
	s_addc_u32 s21, s21, 0
	s_add_u32 s46, s46, 0x100
	s_addc_u32 s47, s47, 0
	s_cmp_gt_u32 s48, 13
	s_cbranch_scc0 .LBB0_114
	s_and_b64 vcc, exec, s[8:9]
	s_cbranch_vccz .LBB0_117
	s_barrier

; #define PG8_STAGE(bufoff, gbase, voff) do { _Pragma("unroll") for (int _i = 0; _i < 2; ++_i) \
;         __builtin_amdgcn_global_load_lds((const unsigned*)((const char*)(gbase) + (voff)[_i]), (PG8_LAS unsigned*)(lds + (bufoff) + ldsw + _i * 8192), 16, 0, 0); } while (0)
; #define PG8_STAGE_A(bufoff, gbase, h, nx) do { _Pragma("unroll") for (int _i = 0; _i < 2; ++_i) { \
;         const unsigned vo_ = GA ? ((nx) ? vgn[h][_i] : vgc[h][_i]) : voffA[_i]; \
;         __builtin_amdgcn_global_load_lds((const unsigned*)((const char*)(gbase) + vo_), (PG8_LAS unsigned*)(lds + (bufoff) + ldsw + _i * 8192), 16, 0, 0); } } while (0)
; #define PG8_LDA(dst, b, h) do { _Pragma("unroll") for (int m = 0; m < 4; ++m) _Pragma("unroll") for (int k = 0; k < 2; ++k) dst[m][k] = *(const PG8_LAS bf16x8*)(lds + PG8_SA(b, h) + aoff + m * 2048 + k * 1024); } while (0)
; #define PG8_LDB(dst, b, h) do { _Pragma("unroll") for (int n = 0; n < 2; ++n) _Pragma("unroll") for (int k = 0; k < 2; ++k) dst[n][k] = *(const PG8_LAS bf16x8*)(lds + PG8_SB(b, h) + boff + n * 2048 + k * 1024); } while (0)
; #define PG8_MMA(ai, bj, At, Bt) do { __builtin_amdgcn_s_setprio(1); _Pragma("unroll") for (int m = 0; m < 4; ++m) _Pragma("unroll") for (int n = 0; n < 2; ++n) _Pragma("unroll") for (int k = 0; k < 2; ++k) \
;         acc[ai][bj][m][n] = __builtin_amdgcn_mfma_f32_16x16x32_bf16(Bt[n][k], At[m][k], acc[ai][bj][m][n], 0, 0, 0); __builtin_amdgcn_s_setprio(0); } while (0)
; #define PG8_WAIT_V(n) asm volatile("s_waitcnt vmcnt(" #n ")" ::: "memory")
; #define PG8_WAIT_L(n) asm volatile("s_waitcnt lgkmcnt(" #n ")" ::: "memory")
; #define PG8_BAR __builtin_amdgcn_s_barrier()
; #define PG8_SCHED __builtin_amdgcn_sched_barrier(0)
; template <class Epi, class Sched>
; __device__ __forceinline__ void gemm_phase(const int WID_, PG8_LAS unsigned char* lds, const Sched& S, const Epi& E) {
;     ...
;             PG8_LDB(B0, 0, 0); PG8_LDB(B1, 0, 1); PG8_SCHED; PG8_LDA(At, 0, 0); PG8_STAGE_A(PG8_SA(1, 1), a1 + hstepA, 1, false);
;             PG8_WAIT_V(8); PG8_WAIT_L(0); PG8_BAR; PG8_MMA(0, 0, At, B0); PG8_MMA(0, 1, At, B1); PG8_BAR; PG8_SCHED;
;             PG8_LDA(At, 0, 1); PG8_STAGE(PG8_SB(0, 0), b2, voffB); PG8_STAGE(PG8_SB(0, 1), b2 + hstepB, voffB); PG8_STAGE_A(PG8_SA(0, 0), a2, 0, last);
.LBB0_263:
	ds_read_b128 v[138:141], v149
	ds_read_b128 v[142:145], v149 offset:1024
	ds_read_b128 v[152:155], v149 offset:2048
	ds_read_b128 v[156:159], v149 offset:3072
	ds_read_b128 v[160:163], v150
	ds_read_b128 v[164:167], v150 offset:1024
	ds_read_b128 v[168:171], v150 offset:2048
	ds_read_b128 v[172:175], v150 offset:3072
	s_add_u32 s8, s6, 0xfffe0080
	s_addc_u32 s9, s7, -1
	s_cmp_eq_u32 s35, 4
	s_cselect_b32 s11, s23, s9
	s_cselect_b32 s10, s22, s8
	s_cselect_b32 s9, s29, s21
	s_cselect_b32 s8, s28, s5
	v_lshl_add_u64 v[208:209], s[6:7], 0, v[134:135]
	s_add_i32 m0, s38, 0xc000
	ds_read_b128 v[176:179], v151
	ds_read_b128 v[180:183], v151 offset:1024
	ds_read_b128 v[184:187], v151 offset:2048
	ds_read_b128 v[188:191], v151 offset:3072
	ds_read_b128 v[192:195], v151 offset:4096
	ds_read_b128 v[196:199], v151 offset:5120
	ds_read_b128 v[200:203], v151 offset:6144
	ds_read_b128 v[204:207], v151 offset:7168
	global_load_lds_dwordx4 v[208:209], off
	v_lshl_add_u64 v[208:209], s[6:7], 0, v[136:137]
	s_add_i32 m0, s38, 0xe000
	s_nop 0
	global_load_lds_dwordx4 v[208:209], off
	s_waitcnt vmcnt(8)
	s_waitcnt lgkmcnt(0)
	s_barrier
	s_nop 0
	s_setprio 1
	s_waitcnt lgkmcnt(0)
	v_mfma_f32_16x16x32_bf16 v[124:127], v[138:141], v[176:179], v[124:127]
	v_mfma_f32_16x16x32_bf16 v[120:123], v[152:155], v[176:179], v[120:123]
	v_mfma_f32_16x16x32_bf16 v[108:111], v[138:141], v[184:187], v[108:111]
	v_mfma_f32_16x16x32_bf16 v[104:107], v[152:155], v[184:187], v[104:107]
	v_mfma_f32_16x16x32_bf16 v[92:95], v[138:141], v[192:195], v[92:95]
	v_mfma_f32_16x16x32_bf16 v[88:91], v[152:155], v[192:195], v[88:91]
	v_mfma_f32_16x16x32_bf16 v[76:79], v[138:141], v[200:203], v[76:79]
	v_mfma_f32_16x16x32_bf16 v[72:75], v[152:155], v[200:203], v[72:75]
	v_mfma_f32_16x16x32_bf16 v[124:127], v[142:145], v[180:183], v[124:127]
	v_mfma_f32_16x16x32_bf16 v[120:123], v[156:159], v[180:183], v[120:123]
	v_mfma_f32_16x16x32_bf16 v[108:111], v[142:145], v[188:191], v[108:111]
	v_mfma_f32_16x16x32_bf16 v[104:107], v[156:159], v[188:191], v[104:107]
	v_mfma_f32_16x16x32_bf16 v[92:95], v[142:145], v[196:199], v[92:95]
	v_mfma_f32_16x16x32_bf16 v[88:91], v[156:159], v[196:199], v[88:91]
	v_mfma_f32_16x16x32_bf16 v[76:79], v[142:145], v[204:207], v[76:79]
	v_mfma_f32_16x16x32_bf16 v[72:75], v[156:159], v[204:207], v[72:75]
	s_setprio 0
	s_setprio 1
	v_mfma_f32_16x16x32_bf16 v[116:119], v[160:163], v[176:179], v[116:119]
	v_mfma_f32_16x16x32_bf16 v[112:115], v[168:171], v[176:179], v[112:115]
	v_mfma_f32_16x16x32_bf16 v[100:103], v[160:163], v[184:187], v[100:103]
	v_mfma_f32_16x16x32_bf16 v[96:99], v[168:171], v[184:187], v[96:99]
	v_mfma_f32_16x16x32_bf16 v[84:87], v[160:163], v[192:195], v[84:87]
	v_mfma_f32_16x16x32_bf16 v[80:83], v[168:171], v[192:195], v[80:83]
	v_mfma_f32_16x16x32_bf16 v[68:71], v[160:163], v[200:203], v[68:71]
	v_mfma_f32_16x16x32_bf16 v[64:67], v[168:171], v[200:203], v[64:67]
	v_mfma_f32_16x16x32_bf16 v[116:119], v[164:167], v[180:183], v[116:119]
	v_mfma_f32_16x16x32_bf16 v[112:115], v[172:175], v[180:183], v[112:115]
	v_mfma_f32_16x16x32_bf16 v[100:103], v[164:167], v[188:191], v[100:103]
	v_mfma_f32_16x16x32_bf16 v[96:99], v[172:175], v[188:191], v[96:99]
	v_mfma_f32_16x16x32_bf16 v[84:87], v[164:167], v[196:199], v[84:87]
	v_mfma_f32_16x16x32_bf16 v[80:83], v[172:175], v[196:199], v[80:83]
	v_mfma_f32_16x16x32_bf16 v[68:71], v[164:167], v[204:207], v[68:71]
	v_mfma_f32_16x16x32_bf16 v[64:67], v[172:175], v[204:207], v[64:67]
	s_setprio 0
	s_barrier
	s_add_i32 s36, s47, s33
	v_lshl_add_u64 v[208:209], s[8:9], 0, v[128:129]
	s_mov_b32 m0, s36
	ds_read_b128 v[176:179], v151 offset:16384
	ds_read_b128 v[180:183], v151 offset:17408
	ds_read_b128 v[184:187], v151 offset:18432
	ds_read_b128 v[188:191], v151 offset:19456
	ds_read_b128 v[192:195], v151 offset:20480
	ds_read_b128 v[196:199], v151 offset:21504
	ds_read_b128 v[200:203], v151 offset:22528
	ds_read_b128 v[204:207], v151 offset:23552
	global_load_lds_dwordx4 v[208:209], off
	s_add_i32 m0, s36, 0x2000
	s_add_u32 s36, s8, 0x20000
	v_lshl_add_u64 v[210:211], s[8:9], 0, v[130:131]
	s_addc_u32 s37, s9, 0
	s_add_i32 s52, s48, s33
	global_load_lds_dwordx4 v[210:211], off
	v_lshl_add_u64 v[212:213], s[36:37], 0, v[128:129]
	s_mov_b32 m0, s52
	v_lshl_add_u64 v[214:215], s[10:11], 0, v[130:131]
	global_load_lds_dwordx4 v[212:213], off
	v_lshl_add_u64 v[212:213], s[36:37], 0, v[130:131]
	s_add_i32 m0, s52, 0x2000
	s_nop 0
	global_load_lds_dwordx4 v[212:213], off
	v_lshl_add_u64 v[212:213], s[10:11], 0, v[128:129]
	s_mov_b32 m0, s38
	s_nop 0
	global_load_lds_dwordx4 v[212:213], off
	s_mov_b32 m0, s39
	s_nop 0
	global_load_lds_dwordx4 v[214:215], off
	s_waitcnt vmcnt(8)
	s_waitcnt lgkmcnt(0)
	s_barrier
; #define PG8_STAGE_A(bufoff, gbase, h, nx) do { _Pragma("unroll") for (int _i = 0; _i < 2; ++_i) { \
;         const unsigned vo_ = GA ? ((nx) ? vgn[h][_i] : vgc[h][_i]) : voffA[_i]; \
;         __builtin_amdgcn_global_load_lds((const unsigned*)((const char*)(gbase) + vo_), (PG8_LAS unsigned*)(lds + (bufoff) + ldsw + _i * 8192), 16, 0, 0); } } while (0)
; #define PG8_LDA(dst, b, h) do { _Pragma("unroll") for (int m = 0; m < 4; ++m) _Pragma("unroll") for (int k = 0; k < 2; ++k) dst[m][k] = *(const PG8_LAS bf16x8*)(lds + PG8_SA(b, h) + aoff + m * 2048 + k * 1024); } while (0)
; #define PG8_LDB(dst, b, h) do { _Pragma("unroll") for (int n = 0; n < 2; ++n) _Pragma("unroll") for (int k = 0; k < 2; ++k) dst[n][k] = *(const PG8_LAS bf16x8*)(lds + PG8_SB(b, h) + boff + n * 2048 + k * 1024); } while (0)
; #define PG8_MMA(ai, bj, At, Bt) do { __builtin_amdgcn_s_setprio(1); _Pragma("unroll") for (int m = 0; m < 4; ++m) _Pragma("unroll") for (int n = 0; n < 2; ++n) _Pragma("unroll") for (int k = 0; k < 2; ++k) \
;         acc[ai][bj][m][n] = __builtin_amdgcn_mfma_f32_16x16x32_bf16(Bt[n][k], At[m][k], acc[ai][bj][m][n], 0, 0, 0); __builtin_amdgcn_s_setprio(0); } while (0)
; #define PG8_WAIT_V(n) asm volatile("s_waitcnt vmcnt(" #n ")" ::: "memory")
; #define PG8_WAIT_L(n) asm volatile("s_waitcnt lgkmcnt(" #n ")" ::: "memory")
; #define PG8_BAR __builtin_amdgcn_s_barrier()
; #define PG8_SCHED __builtin_amdgcn_sched_barrier(0)
; template <class Epi, class Sched>
; __device__ __forceinline__ void gemm_phase(const int WID_, PG8_LAS unsigned char* lds, const Sched& S, const Epi& E) {
;     ...
;             PG8_WAIT_V(8); PG8_WAIT_L(0); PG8_BAR; PG8_MMA(1, 0, At, B0); PG8_MMA(1, 1, At, B1); PG8_BAR; PG8_SCHED;
;             PG8_LDB(B0, 1, 0); PG8_LDB(B1, 1, 1); PG8_SCHED; PG8_LDA(At, 1, 0); PG8_STAGE_A(PG8_SA(0, 1), a2 + hstepA, 1, last);
;             PG8_WAIT_V(8); PG8_WAIT_L(0); PG8_BAR; PG8_MMA(0, 0, At, B0); PG8_MMA(0, 1, At, B1); PG8_BAR; PG8_SCHED;
	s_nop 0
	s_setprio 1
	s_waitcnt lgkmcnt(0)
	v_mfma_f32_16x16x32_bf16 v[60:63], v[138:141], v[176:179], v[60:63]
	v_mfma_f32_16x16x32_bf16 v[56:59], v[152:155], v[176:179], v[56:59]
	v_mfma_f32_16x16x32_bf16 v[44:47], v[138:141], v[184:187], v[44:47]
	v_mfma_f32_16x16x32_bf16 v[40:43], v[152:155], v[184:187], v[40:43]
	v_mfma_f32_16x16x32_bf16 v[28:31], v[138:141], v[192:195], v[28:31]
	v_mfma_f32_16x16x32_bf16 v[24:27], v[152:155], v[192:195], v[24:27]
	v_mfma_f32_16x16x32_bf16 v[12:15], v[138:141], v[200:203], v[12:15]
	v_mfma_f32_16x16x32_bf16 v[8:11], v[152:155], v[200:203], v[8:11]
	v_mfma_f32_16x16x32_bf16 v[60:63], v[142:145], v[180:183], v[60:63]
	v_mfma_f32_16x16x32_bf16 v[56:59], v[156:159], v[180:183], v[56:59]
	v_mfma_f32_16x16x32_bf16 v[44:47], v[142:145], v[188:191], v[44:47]
	v_mfma_f32_16x16x32_bf16 v[40:43], v[156:159], v[188:191], v[40:43]
	v_mfma_f32_16x16x32_bf16 v[28:31], v[142:145], v[196:199], v[28:31]
	v_mfma_f32_16x16x32_bf16 v[24:27], v[156:159], v[196:199], v[24:27]
	v_mfma_f32_16x16x32_bf16 v[12:15], v[142:145], v[204:207], v[12:15]
	v_mfma_f32_16x16x32_bf16 v[8:11], v[156:159], v[204:207], v[8:11]
	s_setprio 0
	s_setprio 1
	v_mfma_f32_16x16x32_bf16 v[52:55], v[160:163], v[176:179], v[52:55]
	v_mfma_f32_16x16x32_bf16 v[48:51], v[168:171], v[176:179], v[48:51]
	v_mfma_f32_16x16x32_bf16 v[36:39], v[160:163], v[184:187], v[36:39]
	v_mfma_f32_16x16x32_bf16 v[32:35], v[168:171], v[184:187], v[32:35]
	v_mfma_f32_16x16x32_bf16 v[20:23], v[160:163], v[192:195], v[20:23]
	v_mfma_f32_16x16x32_bf16 v[16:19], v[168:171], v[192:195], v[16:19]
	v_mfma_f32_16x16x32_bf16 v[4:7], v[160:163], v[200:203], v[4:7]
	v_mfma_f32_16x16x32_bf16 v[0:3], v[168:171], v[200:203], v[0:3]
	v_mfma_f32_16x16x32_bf16 v[52:55], v[164:167], v[180:183], v[52:55]
	v_mfma_f32_16x16x32_bf16 v[48:51], v[172:175], v[180:183], v[48:51]
	v_mfma_f32_16x16x32_bf16 v[36:39], v[164:167], v[188:191], v[36:39]
	v_mfma_f32_16x16x32_bf16 v[32:35], v[172:175], v[188:191], v[32:35]
	v_mfma_f32_16x16x32_bf16 v[20:23], v[164:167], v[196:199], v[20:23]
	v_mfma_f32_16x16x32_bf16 v[16:19], v[172:175], v[196:199], v[16:19]
	v_mfma_f32_16x16x32_bf16 v[4:7], v[164:167], v[204:207], v[4:7]
	v_mfma_f32_16x16x32_bf16 v[0:3], v[172:175], v[204:207], v[0:3]
	s_setprio 0
	s_barrier
	s_add_i32 s36, 0, 0x18000
	v_add_u32_e32 v132, s36, v147
	s_add_i32 s37, 0, 0x1c000
	ds_read_b128 v[138:141], v132
	ds_read_b128 v[142:145], v132 offset:1024
	ds_read_b128 v[152:155], v132 offset:2048
	ds_read_b128 v[156:159], v132 offset:3072
	v_add_u32_e32 v132, s37, v147
	ds_read_b128 v[160:163], v132
	ds_read_b128 v[164:167], v132 offset:1024
	ds_read_b128 v[168:171], v132 offset:2048
	ds_read_b128 v[172:175], v132 offset:3072
	s_add_u32 s10, s10, 0x20000
	s_addc_u32 s11, s11, 0
	s_mov_b32 m0, s40
	v_lshl_add_u64 v[216:217], s[10:11], 0, v[128:129]
	ds_read_b128 v[176:179], v151 offset:32768
	ds_read_b128 v[180:183], v151 offset:33792
	ds_read_b128 v[184:187], v151 offset:34816
	ds_read_b128 v[188:191], v151 offset:35840
	ds_read_b128 v[192:195], v151 offset:36864
	ds_read_b128 v[196:199], v151 offset:37888
	ds_read_b128 v[200:203], v151 offset:38912
	ds_read_b128 v[204:207], v151 offset:39936
	global_load_lds_dwordx4 v[216:217], off
	v_lshl_add_u64 v[216:217], s[10:11], 0, v[130:131]
	s_mov_b32 m0, s41
	s_nop 0
	global_load_lds_dwordx4 v[216:217], off
	s_waitcnt vmcnt(8)
	s_waitcnt lgkmcnt(0)
	s_barrier
	s_nop 0
	s_setprio 1
	s_waitcnt lgkmcnt(0)
	v_mfma_f32_16x16x32_bf16 v[124:127], v[138:141], v[176:179], v[124:127]
	v_mfma_f32_16x16x32_bf16 v[120:123], v[152:155], v[176:179], v[120:123]
	v_mfma_f32_16x16x32_bf16 v[108:111], v[138:141], v[184:187], v[108:111]
	v_mfma_f32_16x16x32_bf16 v[104:107], v[152:155], v[184:187], v[104:107]
	v_mfma_f32_16x16x32_bf16 v[92:95], v[138:141], v[192:195], v[92:95]
	v_mfma_f32_16x16x32_bf16 v[88:91], v[152:155], v[192:195], v[88:91]
	v_mfma_f32_16x16x32_bf16 v[76:79], v[138:141], v[200:203], v[76:79]
	v_mfma_f32_16x16x32_bf16 v[72:75], v[152:155], v[200:203], v[72:75]
	v_mfma_f32_16x16x32_bf16 v[124:127], v[142:145], v[180:183], v[124:127]
	v_mfma_f32_16x16x32_bf16 v[120:123], v[156:159], v[180:183], v[120:123]
	v_mfma_f32_16x16x32_bf16 v[108:111], v[142:145], v[188:191], v[108:111]
	v_mfma_f32_16x16x32_bf16 v[104:107], v[156:159], v[188:191], v[104:107]
	v_mfma_f32_16x16x32_bf16 v[92:95], v[142:145], v[196:199], v[92:95]
	v_mfma_f32_16x16x32_bf16 v[88:91], v[156:159], v[196:199], v[88:91]
	v_mfma_f32_16x16x32_bf16 v[76:79], v[142:145], v[204:207], v[76:79]
	v_mfma_f32_16x16x32_bf16 v[72:75], v[156:159], v[204:207], v[72:75]
	s_setprio 0
	s_setprio 1
	v_mfma_f32_16x16x32_bf16 v[116:119], v[160:163], v[176:179], v[116:119]
	v_mfma_f32_16x16x32_bf16 v[112:115], v[168:171], v[176:179], v[112:115]
	v_mfma_f32_16x16x32_bf16 v[100:103], v[160:163], v[184:187], v[100:103]
	v_mfma_f32_16x16x32_bf16 v[96:99], v[168:171], v[184:187], v[96:99]
	v_mfma_f32_16x16x32_bf16 v[84:87], v[160:163], v[192:195], v[84:87]
	v_mfma_f32_16x16x32_bf16 v[80:83], v[168:171], v[192:195], v[80:83]
	v_mfma_f32_16x16x32_bf16 v[68:71], v[160:163], v[200:203], v[68:71]
	v_mfma_f32_16x16x32_bf16 v[64:67], v[168:171], v[200:203], v[64:67]
	v_mfma_f32_16x16x32_bf16 v[116:119], v[164:167], v[180:183], v[116:119]
	v_mfma_f32_16x16x32_bf16 v[112:115], v[172:175], v[180:183], v[112:115]
	v_mfma_f32_16x16x32_bf16 v[100:103], v[164:167], v[188:191], v[100:103]
	v_mfma_f32_16x16x32_bf16 v[96:99], v[172:175], v[188:191], v[96:99]
	v_mfma_f32_16x16x32_bf16 v[84:87], v[164:167], v[196:199], v[84:87]
	v_mfma_f32_16x16x32_bf16 v[80:83], v[172:175], v[196:199], v[80:83]
	v_mfma_f32_16x16x32_bf16 v[68:71], v[164:167], v[204:207], v[68:71]
	v_mfma_f32_16x16x32_bf16 v[64:67], v[172:175], v[204:207], v[64:67]
	s_setprio 0
	s_barrier
; #define PG8_STAGE(bufoff, gbase, voff) do { _Pragma("unroll") for (int _i = 0; _i < 2; ++_i) \
;         __builtin_amdgcn_global_load_lds((const unsigned*)((const char*)(gbase) + (voff)[_i]), (PG8_LAS unsigned*)(lds + (bufoff) + ldsw + _i * 8192), 16, 0, 0); } while (0)
; #define PG8_STAGE_A(bufoff, gbase, h, nx) do { _Pragma("unroll") for (int _i = 0; _i < 2; ++_i) { \
;         const unsigned vo_ = GA ? ((nx) ? vgn[h][_i] : vgc[h][_i]) : voffA[_i]; \
;         __builtin_amdgcn_global_load_lds((const unsigned*)((const char*)(gbase) + vo_), (PG8_LAS unsigned*)(lds + (bufoff) + ldsw + _i * 8192), 16, 0, 0); } } while (0)
; #define PG8_LDA(dst, b, h) do { _Pragma("unroll") for (int m = 0; m < 4; ++m) _Pragma("unroll") for (int k = 0; k < 2; ++k) dst[m][k] = *(const PG8_LAS bf16x8*)(lds + PG8_SA(b, h) + aoff + m * 2048 + k * 1024); } while (0)
; #define PG8_MMA(ai, bj, At, Bt) do { __builtin_amdgcn_s_setprio(1); _Pragma("unroll") for (int m = 0; m < 4; ++m) _Pragma("unroll") for (int n = 0; n < 2; ++n) _Pragma("unroll") for (int k = 0; k < 2; ++k) \
;         acc[ai][bj][m][n] = __builtin_amdgcn_mfma_f32_16x16x32_bf16(Bt[n][k], At[m][k], acc[ai][bj][m][n], 0, 0, 0); __builtin_amdgcn_s_setprio(0); } while (0)
; #define PG8_WAIT_V(n) asm volatile("s_waitcnt vmcnt(" #n ")" ::: "memory")
; #define PG8_WAIT_L(n) asm volatile("s_waitcnt lgkmcnt(" #n ")" ::: "memory")
; #define PG8_BAR __builtin_amdgcn_s_barrier()
; #define PG8_SCHED __builtin_amdgcn_sched_barrier(0)
; template <class Epi, class Sched>
; __device__ __forceinline__ void gemm_phase(const int WID_, PG8_LAS unsigned char* lds, const Sched& S, const Epi& E) {
;     ...
;             PG8_LDA(At, 1, 1); PG8_STAGE(PG8_SB(1, 0), b3, voffB); PG8_STAGE(PG8_SB(1, 1), b3 + hstepB, voffB); PG8_STAGE_A(PG8_SA(1, 0), a3, 0, last);
;             PG8_WAIT_V(8); PG8_WAIT_L(0); PG8_BAR; PG8_MMA(1, 0, At, B0); PG8_MMA(1, 1, At, B1); PG8_BAR; PG8_SCHED;
;         }
	s_add_i32 s10, s36, s33
	v_lshl_add_u64 v[208:209], v[208:209], 0, s[16:17]
	s_mov_b32 m0, s10
	ds_read_b128 v[176:179], v151 offset:49152
	ds_read_b128 v[180:183], v151 offset:50176
	ds_read_b128 v[184:187], v151 offset:51200
	ds_read_b128 v[188:191], v151 offset:52224
	ds_read_b128 v[192:195], v151 offset:53248
	ds_read_b128 v[196:199], v151 offset:54272
	ds_read_b128 v[200:203], v151 offset:55296
	ds_read_b128 v[204:207], v151 offset:56320
	global_load_lds_dwordx4 v[208:209], off
	s_add_i32 m0, s10, 0x2000
	s_add_u32 s8, s8, 0x20080
	v_lshl_add_u64 v[208:209], v[210:211], 0, s[16:17]
	s_addc_u32 s9, s9, 0
	s_add_i32 s10, s37, s33
	global_load_lds_dwordx4 v[208:209], off
	v_lshl_add_u64 v[208:209], s[8:9], 0, v[128:129]
	s_mov_b32 m0, s10
	s_nop 0
	global_load_lds_dwordx4 v[208:209], off
	v_lshl_add_u64 v[208:209], s[8:9], 0, v[130:131]
	s_add_i32 m0, s10, 0x2000
	s_nop 0
	global_load_lds_dwordx4 v[208:209], off
	v_lshl_add_u64 v[208:209], v[212:213], 0, s[16:17]
	s_mov_b32 m0, s43
	s_nop 0
	global_load_lds_dwordx4 v[208:209], off
	v_lshl_add_u64 v[208:209], v[214:215], 0, s[16:17]
	s_mov_b32 m0, s44
	s_nop 0
	global_load_lds_dwordx4 v[208:209], off
	s_waitcnt vmcnt(8)
	s_waitcnt lgkmcnt(0)
	s_barrier
	s_setprio 1
	s_waitcnt lgkmcnt(0)
	v_mfma_f32_16x16x32_bf16 v[60:63], v[138:141], v[176:179], v[60:63]
	v_mfma_f32_16x16x32_bf16 v[56:59], v[152:155], v[176:179], v[56:59]
	v_mfma_f32_16x16x32_bf16 v[44:47], v[138:141], v[184:187], v[44:47]
	v_mfma_f32_16x16x32_bf16 v[40:43], v[152:155], v[184:187], v[40:43]
	v_mfma_f32_16x16x32_bf16 v[28:31], v[138:141], v[192:195], v[28:31]
	v_mfma_f32_16x16x32_bf16 v[24:27], v[152:155], v[192:195], v[24:27]
	v_mfma_f32_16x16x32_bf16 v[12:15], v[138:141], v[200:203], v[12:15]
	v_mfma_f32_16x16x32_bf16 v[8:11], v[152:155], v[200:203], v[8:11]
	v_mfma_f32_16x16x32_bf16 v[60:63], v[142:145], v[180:183], v[60:63]
	v_mfma_f32_16x16x32_bf16 v[56:59], v[156:159], v[180:183], v[56:59]
	v_mfma_f32_16x16x32_bf16 v[44:47], v[142:145], v[188:191], v[44:47]
	v_mfma_f32_16x16x32_bf16 v[40:43], v[156:159], v[188:191], v[40:43]
	v_mfma_f32_16x16x32_bf16 v[28:31], v[142:145], v[196:199], v[28:31]
	v_mfma_f32_16x16x32_bf16 v[24:27], v[156:159], v[196:199], v[24:27]
	v_mfma_f32_16x16x32_bf16 v[12:15], v[142:145], v[204:207], v[12:15]
	v_mfma_f32_16x16x32_bf16 v[8:11], v[156:159], v[204:207], v[8:11]
	s_setprio 0
	s_setprio 1
	v_mfma_f32_16x16x32_bf16 v[52:55], v[160:163], v[176:179], v[52:55]
	v_mfma_f32_16x16x32_bf16 v[48:51], v[168:171], v[176:179], v[48:51]
	v_mfma_f32_16x16x32_bf16 v[36:39], v[160:163], v[184:187], v[36:39]
	v_mfma_f32_16x16x32_bf16 v[32:35], v[168:171], v[184:187], v[32:35]
	v_mfma_f32_16x16x32_bf16 v[20:23], v[160:163], v[192:195], v[20:23]
	v_mfma_f32_16x16x32_bf16 v[16:19], v[168:171], v[192:195], v[16:19]
	v_mfma_f32_16x16x32_bf16 v[4:7], v[160:163], v[200:203], v[4:7]
	v_mfma_f32_16x16x32_bf16 v[0:3], v[168:171], v[200:203], v[0:3]
	v_mfma_f32_16x16x32_bf16 v[52:55], v[164:167], v[180:183], v[52:55]
	v_mfma_f32_16x16x32_bf16 v[48:51], v[172:175], v[180:183], v[48:51]
	v_mfma_f32_16x16x32_bf16 v[36:39], v[164:167], v[188:191], v[36:39]
	v_mfma_f32_16x16x32_bf16 v[32:35], v[172:175], v[188:191], v[32:35]
	v_mfma_f32_16x16x32_bf16 v[20:23], v[164:167], v[196:199], v[20:23]
	v_mfma_f32_16x16x32_bf16 v[16:19], v[172:175], v[196:199], v[16:19]
	v_mfma_f32_16x16x32_bf16 v[4:7], v[164:167], v[204:207], v[4:7]
	v_mfma_f32_16x16x32_bf16 v[0:3], v[172:175], v[204:207], v[0:3]
	s_setprio 0
	s_barrier
	s_add_i32 s35, s35, 2
	s_add_u32 s6, s6, 0x100
	s_addc_u32 s7, s7, 0
	s_add_u32 s5, s5, 0x100
	s_addc_u32 s21, s21, 0
	s_cmp_gt_u32 s35, 5
	s_cbranch_scc0 .LBB0_263
	s_and_b64 vcc, exec, s[18:19]
	s_cbranch_vccz .LBB0_266
	s_barrier

; #define PG8_STAGE(bufoff, gbase, voff) do { _Pragma("unroll") for (int _i = 0; _i < 2; ++_i) \
;         __builtin_amdgcn_global_load_lds((const unsigned*)((const char*)(gbase) + (voff)[_i]), (PG8_LAS unsigned*)(lds + (bufoff) + ldsw + _i * 8192), 16, 0, 0); } while (0)
; #define PG8_STAGE_A(bufoff, gbase, h, nx) do { _Pragma("unroll") for (int _i = 0; _i < 2; ++_i) { \
;         const unsigned vo_ = GA ? ((nx) ? vgn[h][_i] : vgc[h][_i]) : voffA[_i]; \
;         __builtin_amdgcn_global_load_lds((const unsigned*)((const char*)(gbase) + vo_), (PG8_LAS unsigned*)(lds + (bufoff) + ldsw + _i * 8192), 16, 0, 0); } } while (0)
; #define PG8_LDA(dst, b, h) do { _Pragma("unroll") for (int m = 0; m < 4; ++m) _Pragma("unroll") for (int k = 0; k < 2; ++k) dst[m][k] = *(const PG8_LAS bf16x8*)(lds + PG8_SA(b, h) + aoff + m * 2048 + k * 1024); } while (0)
; #define PG8_LDB(dst, b, h) do { _Pragma("unroll") for (int n = 0; n < 2; ++n) _Pragma("unroll") for (int k = 0; k < 2; ++k) dst[n][k] = *(const PG8_LAS bf16x8*)(lds + PG8_SB(b, h) + boff + n * 2048 + k * 1024); } while (0)
; #define PG8_MMA(ai, bj, At, Bt) do { __builtin_amdgcn_s_setprio(1); _Pragma("unroll") for (int m = 0; m < 4; ++m) _Pragma("unroll") for (int n = 0; n < 2; ++n) _Pragma("unroll") for (int k = 0; k < 2; ++k) \
;         acc[ai][bj][m][n] = __builtin_amdgcn_mfma_f32_16x16x32_bf16(Bt[n][k], At[m][k], acc[ai][bj][m][n], 0, 0, 0); __builtin_amdgcn_s_setprio(0); } while (0)
; #define PG8_WAIT_V(n) asm volatile("s_waitcnt vmcnt(" #n ")" ::: "memory")
; #define PG8_WAIT_L(n) asm volatile("s_waitcnt lgkmcnt(" #n ")" ::: "memory")
; #define PG8_BAR __builtin_amdgcn_s_barrier()
; #define PG8_SCHED __builtin_amdgcn_sched_barrier(0)
; template <class Epi, class Sched>
; __device__ __forceinline__ void gemm_phase(const int WID_, PG8_LAS unsigned char* lds, const Sched& S, const Epi& E) {
;     ...
;             PG8_LDB(B0, 0, 0); PG8_LDB(B1, 0, 1); PG8_SCHED; PG8_LDA(At, 0, 0); PG8_STAGE_A(PG8_SA(1, 1), a1 + hstepA, 1, false);
;             PG8_WAIT_V(8); PG8_WAIT_L(0); PG8_BAR; PG8_MMA(0, 0, At, B0); PG8_MMA(0, 1, At, B1); PG8_BAR; PG8_SCHED;
;             PG8_LDA(At, 0, 1); PG8_STAGE(PG8_SB(0, 0), b2, voffB); PG8_STAGE(PG8_SB(0, 1), b2 + hstepB, voffB); PG8_STAGE_A(PG8_SA(0, 0), a2, 0, last);
.LBB0_568:
	s_add_i32 s62, s2, 2
	s_add_u32 s3, s0, 0xffff0080
	s_addc_u32 s4, s1, -1
	s_add_i32 s63, 0, 0x10000
	s_cmp_eq_u32 s11, s2
	s_cselect_b32 s5, s53, s4
	s_cselect_b32 s4, s52, s3
	v_add_u32_e32 v136, s63, v153
	s_cselect_b32 s3, s61, s51
	s_cselect_b32 s2, s60, s49
	s_add_i32 s69, 0, 0x14000
	ds_read_b128 v[80:83], v136
	ds_read_b128 v[88:91], v136 offset:1024
	ds_read_b128 v[156:159], v136 offset:2048
	ds_read_b128 v[160:163], v136 offset:3072
	v_add_u32_e32 v136, s69, v153
	ds_read_b128 v[164:167], v136
	ds_read_b128 v[168:171], v136 offset:1024
	ds_read_b128 v[172:175], v136 offset:2048
	ds_read_b128 v[176:179], v136 offset:3072
	v_lshl_add_u64 v[212:213], s[0:1], 0, v[146:147]
	s_add_i32 m0, s37, 0xc000
	ds_read_b128 v[180:183], v155
	ds_read_b128 v[184:187], v155 offset:1024
	ds_read_b128 v[188:191], v155 offset:2048
	ds_read_b128 v[192:195], v155 offset:3072
	ds_read_b128 v[196:199], v155 offset:4096
	ds_read_b128 v[200:203], v155 offset:5120
	ds_read_b128 v[204:207], v155 offset:6144
	ds_read_b128 v[208:211], v155 offset:7168
	global_load_lds_dwordx4 v[212:213], off
	v_lshl_add_u64 v[212:213], s[0:1], 0, v[148:149]
	s_add_i32 m0, s37, 0xe000
	s_nop 0
	global_load_lds_dwordx4 v[212:213], off
	s_waitcnt vmcnt(8)
	s_waitcnt lgkmcnt(0)
	s_barrier
	s_nop 0
	s_setprio 1
	s_waitcnt lgkmcnt(0)
	v_mfma_f32_16x16x32_bf16 v[132:135], v[80:83], v[180:183], v[132:135]
	v_mfma_f32_16x16x32_bf16 v[128:131], v[156:159], v[180:183], v[128:131]
	v_mfma_f32_16x16x32_bf16 v[124:127], v[80:83], v[188:191], v[124:127]
	v_mfma_f32_16x16x32_bf16 v[120:123], v[156:159], v[188:191], v[120:123]
	v_mfma_f32_16x16x32_bf16 v[116:119], v[80:83], v[196:199], v[116:119]
	v_mfma_f32_16x16x32_bf16 v[112:115], v[156:159], v[196:199], v[112:115]
	v_mfma_f32_16x16x32_bf16 v[108:111], v[80:83], v[204:207], v[108:111]
	v_mfma_f32_16x16x32_bf16 v[104:107], v[156:159], v[204:207], v[104:107]
	v_mfma_f32_16x16x32_bf16 v[132:135], v[88:91], v[184:187], v[132:135]
	v_mfma_f32_16x16x32_bf16 v[128:131], v[160:163], v[184:187], v[128:131]
	v_mfma_f32_16x16x32_bf16 v[124:127], v[88:91], v[192:195], v[124:127]
	v_mfma_f32_16x16x32_bf16 v[120:123], v[160:163], v[192:195], v[120:123]
	v_mfma_f32_16x16x32_bf16 v[116:119], v[88:91], v[200:203], v[116:119]
	v_mfma_f32_16x16x32_bf16 v[112:115], v[160:163], v[200:203], v[112:115]
	v_mfma_f32_16x16x32_bf16 v[108:111], v[88:91], v[208:211], v[108:111]
	v_mfma_f32_16x16x32_bf16 v[104:107], v[160:163], v[208:211], v[104:107]
	s_setprio 0
	s_setprio 1
	v_mfma_f32_16x16x32_bf16 v[60:63], v[164:167], v[180:183], v[60:63]
	v_mfma_f32_16x16x32_bf16 v[56:59], v[172:175], v[180:183], v[56:59]
	v_mfma_f32_16x16x32_bf16 v[52:55], v[164:167], v[188:191], v[52:55]
	v_mfma_f32_16x16x32_bf16 v[48:51], v[172:175], v[188:191], v[48:51]
	v_mfma_f32_16x16x32_bf16 v[44:47], v[164:167], v[196:199], v[44:47]
	v_mfma_f32_16x16x32_bf16 v[40:43], v[172:175], v[196:199], v[40:43]
	v_mfma_f32_16x16x32_bf16 v[36:39], v[164:167], v[204:207], v[36:39]
	v_mfma_f32_16x16x32_bf16 v[32:35], v[172:175], v[204:207], v[32:35]
	v_mfma_f32_16x16x32_bf16 v[60:63], v[168:171], v[184:187], v[60:63]
	v_mfma_f32_16x16x32_bf16 v[56:59], v[176:179], v[184:187], v[56:59]
	v_mfma_f32_16x16x32_bf16 v[52:55], v[168:171], v[192:195], v[52:55]
	v_mfma_f32_16x16x32_bf16 v[48:51], v[176:179], v[192:195], v[48:51]
	v_mfma_f32_16x16x32_bf16 v[44:47], v[168:171], v[200:203], v[44:47]
	v_mfma_f32_16x16x32_bf16 v[40:43], v[176:179], v[200:203], v[40:43]
	v_mfma_f32_16x16x32_bf16 v[36:39], v[168:171], v[208:211], v[36:39]
	v_mfma_f32_16x16x32_bf16 v[32:35], v[176:179], v[208:211], v[32:35]
	s_setprio 0
	s_barrier
	s_add_i32 s63, s63, s35
	v_lshl_add_u64 v[212:213], s[2:3], 0, v[140:141]
	s_mov_b32 m0, s63
	ds_read_b128 v[180:183], v155 offset:16384
	ds_read_b128 v[184:187], v155 offset:17408
	ds_read_b128 v[188:191], v155 offset:18432
	ds_read_b128 v[192:195], v155 offset:19456
	ds_read_b128 v[196:199], v155 offset:20480
	ds_read_b128 v[200:203], v155 offset:21504
	ds_read_b128 v[204:207], v155 offset:22528
	ds_read_b128 v[208:211], v155 offset:23552
	global_load_lds_dwordx4 v[212:213], off
	s_add_i32 m0, s63, 0x2000
	s_add_u32 s76, s2, 0x10000
	v_lshl_add_u64 v[214:215], s[2:3], 0, v[144:145]
	s_addc_u32 s77, s3, 0
	s_add_i32 s63, s69, s35
	global_load_lds_dwordx4 v[214:215], off
	v_lshl_add_u64 v[216:217], s[76:77], 0, v[140:141]
	s_mov_b32 m0, s63
	v_lshl_add_u64 v[218:219], s[4:5], 0, v[142:143]
	global_load_lds_dwordx4 v[216:217], off
	v_lshl_add_u64 v[216:217], s[76:77], 0, v[144:145]
	s_add_i32 m0, s63, 0x2000
	s_nop 0
	global_load_lds_dwordx4 v[216:217], off
	v_lshl_add_u64 v[216:217], s[4:5], 0, v[138:139]
	s_mov_b32 m0, s37
	s_nop 0
	global_load_lds_dwordx4 v[216:217], off
	s_mov_b32 m0, s39
	s_nop 0
	global_load_lds_dwordx4 v[218:219], off
	s_waitcnt vmcnt(8)
	s_waitcnt lgkmcnt(0)
	s_barrier
; #define PG8_STAGE_A(bufoff, gbase, h, nx) do { _Pragma("unroll") for (int _i = 0; _i < 2; ++_i) { \
;         const unsigned vo_ = GA ? ((nx) ? vgn[h][_i] : vgc[h][_i]) : voffA[_i]; \
;         __builtin_amdgcn_global_load_lds((const unsigned*)((const char*)(gbase) + vo_), (PG8_LAS unsigned*)(lds + (bufoff) + ldsw + _i * 8192), 16, 0, 0); } } while (0)
; #define PG8_LDA(dst, b, h) do { _Pragma("unroll") for (int m = 0; m < 4; ++m) _Pragma("unroll") for (int k = 0; k < 2; ++k) dst[m][k] = *(const PG8_LAS bf16x8*)(lds + PG8_SA(b, h) + aoff + m * 2048 + k * 1024); } while (0)
; #define PG8_LDB(dst, b, h) do { _Pragma("unroll") for (int n = 0; n < 2; ++n) _Pragma("unroll") for (int k = 0; k < 2; ++k) dst[n][k] = *(const PG8_LAS bf16x8*)(lds + PG8_SB(b, h) + boff + n * 2048 + k * 1024); } while (0)
; #define PG8_MMA(ai, bj, At, Bt) do { __builtin_amdgcn_s_setprio(1); _Pragma("unroll") for (int m = 0; m < 4; ++m) _Pragma("unroll") for (int n = 0; n < 2; ++n) _Pragma("unroll") for (int k = 0; k < 2; ++k) \
;         acc[ai][bj][m][n] = __builtin_amdgcn_mfma_f32_16x16x32_bf16(Bt[n][k], At[m][k], acc[ai][bj][m][n], 0, 0, 0); __builtin_amdgcn_s_setprio(0); } while (0)
; #define PG8_WAIT_V(n) asm volatile("s_waitcnt vmcnt(" #n ")" ::: "memory")
; #define PG8_WAIT_L(n) asm volatile("s_waitcnt lgkmcnt(" #n ")" ::: "memory")
; #define PG8_BAR __builtin_amdgcn_s_barrier()
; #define PG8_SCHED __builtin_amdgcn_sched_barrier(0)
; template <class Epi, class Sched>
; __device__ __forceinline__ void gemm_phase(const int WID_, PG8_LAS unsigned char* lds, const Sched& S, const Epi& E) {
;     ...
;             PG8_WAIT_V(8); PG8_WAIT_L(0); PG8_BAR; PG8_MMA(1, 0, At, B0); PG8_MMA(1, 1, At, B1); PG8_BAR; PG8_SCHED;
;             PG8_LDB(B0, 1, 0); PG8_LDB(B1, 1, 1); PG8_SCHED; PG8_LDA(At, 1, 0); PG8_STAGE_A(PG8_SA(0, 1), a2 + hstepA, 1, last);
;             PG8_WAIT_V(8); PG8_WAIT_L(0); PG8_BAR; PG8_MMA(0, 0, At, B0); PG8_MMA(0, 1, At, B1); PG8_BAR; PG8_SCHED;
	s_nop 0
	s_setprio 1
	s_waitcnt lgkmcnt(0)
	v_mfma_f32_16x16x32_bf16 v[100:103], v[80:83], v[180:183], v[100:103]
	v_mfma_f32_16x16x32_bf16 v[96:99], v[156:159], v[180:183], v[96:99]
	v_mfma_f32_16x16x32_bf16 v[92:95], v[80:83], v[188:191], v[92:95]
	v_mfma_f32_16x16x32_bf16 v[84:87], v[156:159], v[188:191], v[84:87]
	v_mfma_f32_16x16x32_bf16 v[76:79], v[80:83], v[196:199], v[76:79]
	v_mfma_f32_16x16x32_bf16 v[72:75], v[156:159], v[196:199], v[72:75]
	v_mfma_f32_16x16x32_bf16 v[68:71], v[80:83], v[204:207], v[68:71]
	v_mfma_f32_16x16x32_bf16 v[64:67], v[156:159], v[204:207], v[64:67]
	v_mfma_f32_16x16x32_bf16 v[100:103], v[88:91], v[184:187], v[100:103]
	v_mfma_f32_16x16x32_bf16 v[96:99], v[160:163], v[184:187], v[96:99]
	v_mfma_f32_16x16x32_bf16 v[92:95], v[88:91], v[192:195], v[92:95]
	v_mfma_f32_16x16x32_bf16 v[84:87], v[160:163], v[192:195], v[84:87]
	v_mfma_f32_16x16x32_bf16 v[76:79], v[88:91], v[200:203], v[76:79]
	v_mfma_f32_16x16x32_bf16 v[72:75], v[160:163], v[200:203], v[72:75]
	v_mfma_f32_16x16x32_bf16 v[68:71], v[88:91], v[208:211], v[68:71]
	v_mfma_f32_16x16x32_bf16 v[64:67], v[160:163], v[208:211], v[64:67]
	s_setprio 0
	s_setprio 1
	v_mfma_f32_16x16x32_bf16 v[28:31], v[164:167], v[180:183], v[28:31]
	v_mfma_f32_16x16x32_bf16 v[24:27], v[172:175], v[180:183], v[24:27]
	v_mfma_f32_16x16x32_bf16 v[20:23], v[164:167], v[188:191], v[20:23]
	v_mfma_f32_16x16x32_bf16 v[16:19], v[172:175], v[188:191], v[16:19]
	v_mfma_f32_16x16x32_bf16 v[12:15], v[164:167], v[196:199], v[12:15]
	v_mfma_f32_16x16x32_bf16 v[8:11], v[172:175], v[196:199], v[8:11]
	v_mfma_f32_16x16x32_bf16 v[4:7], v[164:167], v[204:207], v[4:7]
	v_mfma_f32_16x16x32_bf16 v[0:3], v[172:175], v[204:207], v[0:3]
	v_mfma_f32_16x16x32_bf16 v[28:31], v[168:171], v[184:187], v[28:31]
	v_mfma_f32_16x16x32_bf16 v[24:27], v[176:179], v[184:187], v[24:27]
	v_mfma_f32_16x16x32_bf16 v[20:23], v[168:171], v[192:195], v[20:23]
	v_mfma_f32_16x16x32_bf16 v[16:19], v[176:179], v[192:195], v[16:19]
	v_mfma_f32_16x16x32_bf16 v[12:15], v[168:171], v[200:203], v[12:15]
	v_mfma_f32_16x16x32_bf16 v[8:11], v[176:179], v[200:203], v[8:11]
	v_mfma_f32_16x16x32_bf16 v[4:7], v[168:171], v[208:211], v[4:7]
	v_mfma_f32_16x16x32_bf16 v[0:3], v[176:179], v[208:211], v[0:3]
	s_setprio 0
	s_barrier
	s_add_i32 s63, 0, 0x18000
	v_add_u32_e32 v136, s63, v153
	s_add_i32 s69, 0, 0x1c000
	ds_read_b128 v[80:83], v136
	ds_read_b128 v[88:91], v136 offset:1024
	ds_read_b128 v[156:159], v136 offset:2048
	ds_read_b128 v[160:163], v136 offset:3072
	v_add_u32_e32 v136, s69, v153
	ds_read_b128 v[164:167], v136
	ds_read_b128 v[168:171], v136 offset:1024
	ds_read_b128 v[172:175], v136 offset:2048
	ds_read_b128 v[176:179], v136 offset:3072
	s_add_u32 s4, s4, 0x10000
	s_addc_u32 s5, s5, 0
	s_mov_b32 m0, s41
	v_lshl_add_u64 v[220:221], s[4:5], 0, v[138:139]
	ds_read_b128 v[180:183], v155 offset:32768
	ds_read_b128 v[184:187], v155 offset:33792
	ds_read_b128 v[188:191], v155 offset:34816
	ds_read_b128 v[192:195], v155 offset:35840
	ds_read_b128 v[196:199], v155 offset:36864
	ds_read_b128 v[200:203], v155 offset:37888
	ds_read_b128 v[204:207], v155 offset:38912
	ds_read_b128 v[208:211], v155 offset:39936
	global_load_lds_dwordx4 v[220:221], off
	v_lshl_add_u64 v[220:221], s[4:5], 0, v[142:143]
	s_mov_b32 m0, s84
	s_nop 0
	global_load_lds_dwordx4 v[220:221], off
	s_waitcnt vmcnt(8)
	s_waitcnt lgkmcnt(0)
	s_barrier
	s_nop 0
	s_setprio 1
	s_waitcnt lgkmcnt(0)
	v_mfma_f32_16x16x32_bf16 v[132:135], v[80:83], v[180:183], v[132:135]
	v_mfma_f32_16x16x32_bf16 v[128:131], v[156:159], v[180:183], v[128:131]
	v_mfma_f32_16x16x32_bf16 v[124:127], v[80:83], v[188:191], v[124:127]
	v_mfma_f32_16x16x32_bf16 v[120:123], v[156:159], v[188:191], v[120:123]
	v_mfma_f32_16x16x32_bf16 v[116:119], v[80:83], v[196:199], v[116:119]
	v_mfma_f32_16x16x32_bf16 v[112:115], v[156:159], v[196:199], v[112:115]
	v_mfma_f32_16x16x32_bf16 v[108:111], v[80:83], v[204:207], v[108:111]
	v_mfma_f32_16x16x32_bf16 v[104:107], v[156:159], v[204:207], v[104:107]
	v_mfma_f32_16x16x32_bf16 v[132:135], v[88:91], v[184:187], v[132:135]
	v_mfma_f32_16x16x32_bf16 v[128:131], v[160:163], v[184:187], v[128:131]
	v_mfma_f32_16x16x32_bf16 v[124:127], v[88:91], v[192:195], v[124:127]
	v_mfma_f32_16x16x32_bf16 v[120:123], v[160:163], v[192:195], v[120:123]
	v_mfma_f32_16x16x32_bf16 v[116:119], v[88:91], v[200:203], v[116:119]
	v_mfma_f32_16x16x32_bf16 v[112:115], v[160:163], v[200:203], v[112:115]
	v_mfma_f32_16x16x32_bf16 v[108:111], v[88:91], v[208:211], v[108:111]
	v_mfma_f32_16x16x32_bf16 v[104:107], v[160:163], v[208:211], v[104:107]
	s_setprio 0
	s_setprio 1
	v_mfma_f32_16x16x32_bf16 v[60:63], v[164:167], v[180:183], v[60:63]
	v_mfma_f32_16x16x32_bf16 v[56:59], v[172:175], v[180:183], v[56:59]
	v_mfma_f32_16x16x32_bf16 v[52:55], v[164:167], v[188:191], v[52:55]
	v_mfma_f32_16x16x32_bf16 v[48:51], v[172:175], v[188:191], v[48:51]
	v_mfma_f32_16x16x32_bf16 v[44:47], v[164:167], v[196:199], v[44:47]
	v_mfma_f32_16x16x32_bf16 v[40:43], v[172:175], v[196:199], v[40:43]
	v_mfma_f32_16x16x32_bf16 v[36:39], v[164:167], v[204:207], v[36:39]
	v_mfma_f32_16x16x32_bf16 v[32:35], v[172:175], v[204:207], v[32:35]
	v_mfma_f32_16x16x32_bf16 v[60:63], v[168:171], v[184:187], v[60:63]
	v_mfma_f32_16x16x32_bf16 v[56:59], v[176:179], v[184:187], v[56:59]
	v_mfma_f32_16x16x32_bf16 v[52:55], v[168:171], v[192:195], v[52:55]
	v_mfma_f32_16x16x32_bf16 v[48:51], v[176:179], v[192:195], v[48:51]
	v_mfma_f32_16x16x32_bf16 v[44:47], v[168:171], v[200:203], v[44:47]
	v_mfma_f32_16x16x32_bf16 v[40:43], v[176:179], v[200:203], v[40:43]
	v_mfma_f32_16x16x32_bf16 v[36:39], v[168:171], v[208:211], v[36:39]
	v_mfma_f32_16x16x32_bf16 v[32:35], v[176:179], v[208:211], v[32:35]
	s_setprio 0
	s_barrier
; #define PG8_STAGE(bufoff, gbase, voff) do { _Pragma("unroll") for (int _i = 0; _i < 2; ++_i) \
;         __builtin_amdgcn_global_load_lds((const unsigned*)((const char*)(gbase) + (voff)[_i]), (PG8_LAS unsigned*)(lds + (bufoff) + ldsw + _i * 8192), 16, 0, 0); } while (0)
; #define PG8_STAGE_A(bufoff, gbase, h, nx) do { _Pragma("unroll") for (int _i = 0; _i < 2; ++_i) { \
;         const unsigned vo_ = GA ? ((nx) ? vgn[h][_i] : vgc[h][_i]) : voffA[_i]; \
;         __builtin_amdgcn_global_load_lds((const unsigned*)((const char*)(gbase) + vo_), (PG8_LAS unsigned*)(lds + (bufoff) + ldsw + _i * 8192), 16, 0, 0); } } while (0)
; #define PG8_LDA(dst, b, h) do { _Pragma("unroll") for (int m = 0; m < 4; ++m) _Pragma("unroll") for (int k = 0; k < 2; ++k) dst[m][k] = *(const PG8_LAS bf16x8*)(lds + PG8_SA(b, h) + aoff + m * 2048 + k * 1024); } while (0)
; #define PG8_MMA(ai, bj, At, Bt) do { __builtin_amdgcn_s_setprio(1); _Pragma("unroll") for (int m = 0; m < 4; ++m) _Pragma("unroll") for (int n = 0; n < 2; ++n) _Pragma("unroll") for (int k = 0; k < 2; ++k) \
;         acc[ai][bj][m][n] = __builtin_amdgcn_mfma_f32_16x16x32_bf16(Bt[n][k], At[m][k], acc[ai][bj][m][n], 0, 0, 0); __builtin_amdgcn_s_setprio(0); } while (0)
; #define PG8_WAIT_V(n) asm volatile("s_waitcnt vmcnt(" #n ")" ::: "memory")
; #define PG8_WAIT_L(n) asm volatile("s_waitcnt lgkmcnt(" #n ")" ::: "memory")
; #define PG8_BAR __builtin_amdgcn_s_barrier()
; #define PG8_SCHED __builtin_amdgcn_sched_barrier(0)
; template <class Epi, class Sched>
; __device__ __forceinline__ void gemm_phase(const int WID_, PG8_LAS unsigned char* lds, const Sched& S, const Epi& E) {
;     ...
;             PG8_LDA(At, 1, 1); PG8_STAGE(PG8_SB(1, 0), b3, voffB); PG8_STAGE(PG8_SB(1, 1), b3 + hstepB, voffB); PG8_STAGE_A(PG8_SA(1, 0), a3, 0, last);
;             PG8_WAIT_V(8); PG8_WAIT_L(0); PG8_BAR; PG8_MMA(1, 0, At, B0); PG8_MMA(1, 1, At, B1); PG8_BAR; PG8_SCHED;
;         }
	s_add_i32 s4, s63, s35
	v_lshl_add_u64 v[212:213], v[212:213], 0, s[42:43]
	s_mov_b32 m0, s4
	ds_read_b128 v[180:183], v155 offset:49152
	ds_read_b128 v[184:187], v155 offset:50176
	ds_read_b128 v[188:191], v155 offset:51200
	ds_read_b128 v[192:195], v155 offset:52224
	ds_read_b128 v[196:199], v155 offset:53248
	ds_read_b128 v[200:203], v155 offset:54272
	ds_read_b128 v[204:207], v155 offset:55296
	ds_read_b128 v[208:211], v155 offset:56320
	global_load_lds_dwordx4 v[212:213], off
	s_add_i32 m0, s4, 0x2000
	s_add_u32 s2, s2, 0x10080
	v_lshl_add_u64 v[212:213], v[214:215], 0, s[42:43]
	s_addc_u32 s3, s3, 0
	s_add_i32 s4, s69, s35
	global_load_lds_dwordx4 v[212:213], off
	v_lshl_add_u64 v[212:213], s[2:3], 0, v[140:141]
	s_mov_b32 m0, s4
	s_nop 0
	global_load_lds_dwordx4 v[212:213], off
	v_lshl_add_u64 v[212:213], s[2:3], 0, v[144:145]
	s_add_i32 m0, s4, 0x2000
	s_nop 0
	global_load_lds_dwordx4 v[212:213], off
	v_lshl_add_u64 v[212:213], v[216:217], 0, s[42:43]
	s_mov_b32 m0, s6
	s_nop 0
	global_load_lds_dwordx4 v[212:213], off
	v_lshl_add_u64 v[212:213], v[218:219], 0, s[42:43]
	s_mov_b32 m0, s10
	s_nop 0
	global_load_lds_dwordx4 v[212:213], off
	s_waitcnt vmcnt(8)
	s_waitcnt lgkmcnt(0)
	s_barrier
	s_setprio 1
	s_waitcnt lgkmcnt(0)
	v_mfma_f32_16x16x32_bf16 v[100:103], v[80:83], v[180:183], v[100:103]
	v_mfma_f32_16x16x32_bf16 v[96:99], v[156:159], v[180:183], v[96:99]
	v_mfma_f32_16x16x32_bf16 v[92:95], v[80:83], v[188:191], v[92:95]
	v_mfma_f32_16x16x32_bf16 v[84:87], v[156:159], v[188:191], v[84:87]
	v_mfma_f32_16x16x32_bf16 v[76:79], v[80:83], v[196:199], v[76:79]
	v_mfma_f32_16x16x32_bf16 v[72:75], v[156:159], v[196:199], v[72:75]
	v_mfma_f32_16x16x32_bf16 v[68:71], v[80:83], v[204:207], v[68:71]
	v_mfma_f32_16x16x32_bf16 v[64:67], v[156:159], v[204:207], v[64:67]
	v_mfma_f32_16x16x32_bf16 v[100:103], v[88:91], v[184:187], v[100:103]
	v_mfma_f32_16x16x32_bf16 v[96:99], v[160:163], v[184:187], v[96:99]
	v_mfma_f32_16x16x32_bf16 v[92:95], v[88:91], v[192:195], v[92:95]
	v_mfma_f32_16x16x32_bf16 v[84:87], v[160:163], v[192:195], v[84:87]
	v_mfma_f32_16x16x32_bf16 v[76:79], v[88:91], v[200:203], v[76:79]
	v_mfma_f32_16x16x32_bf16 v[72:75], v[160:163], v[200:203], v[72:75]
	v_mfma_f32_16x16x32_bf16 v[68:71], v[88:91], v[208:211], v[68:71]
	v_mfma_f32_16x16x32_bf16 v[64:67], v[160:163], v[208:211], v[64:67]
	s_setprio 0
	s_setprio 1
	v_mfma_f32_16x16x32_bf16 v[28:31], v[164:167], v[180:183], v[28:31]
	v_mfma_f32_16x16x32_bf16 v[24:27], v[172:175], v[180:183], v[24:27]
	v_mfma_f32_16x16x32_bf16 v[20:23], v[164:167], v[188:191], v[20:23]
	v_mfma_f32_16x16x32_bf16 v[16:19], v[172:175], v[188:191], v[16:19]
	v_mfma_f32_16x16x32_bf16 v[12:15], v[164:167], v[196:199], v[12:15]
	v_mfma_f32_16x16x32_bf16 v[8:11], v[172:175], v[196:199], v[8:11]
	v_mfma_f32_16x16x32_bf16 v[4:7], v[164:167], v[204:207], v[4:7]
	v_mfma_f32_16x16x32_bf16 v[0:3], v[172:175], v[204:207], v[0:3]
	v_mfma_f32_16x16x32_bf16 v[28:31], v[168:171], v[184:187], v[28:31]
	v_mfma_f32_16x16x32_bf16 v[24:27], v[176:179], v[184:187], v[24:27]
	v_mfma_f32_16x16x32_bf16 v[20:23], v[168:171], v[192:195], v[20:23]
	v_mfma_f32_16x16x32_bf16 v[16:19], v[176:179], v[192:195], v[16:19]
	v_mfma_f32_16x16x32_bf16 v[12:15], v[168:171], v[200:203], v[12:15]
	v_mfma_f32_16x16x32_bf16 v[8:11], v[176:179], v[200:203], v[8:11]
	v_mfma_f32_16x16x32_bf16 v[4:7], v[168:171], v[208:211], v[4:7]
	v_mfma_f32_16x16x32_bf16 v[0:3], v[176:179], v[208:211], v[0:3]
	s_setprio 0
	s_barrier
	s_add_u32 s0, s0, 0x100
	s_addc_u32 s1, s1, 0
	s_add_u32 s49, s49, 0x100
	s_addc_u32 s51, s51, 0
	s_cmp_ge_i32 s62, s58
	s_mov_b32 s2, s62
	s_cbranch_scc0 .LBB0_568

; #define PG8_STAGE(bufoff, gbase, voff) do { _Pragma("unroll") for (int _i = 0; _i < 2; ++_i) \
;         __builtin_amdgcn_global_load_lds((const unsigned*)((const char*)(gbase) + (voff)[_i]), (PG8_LAS unsigned*)(lds + (bufoff) + ldsw + _i * 8192), 16, 0, 0); } while (0)
; #define PG8_STAGE_A(bufoff, gbase, h, nx) do { _Pragma("unroll") for (int _i = 0; _i < 2; ++_i) { \
;         const unsigned vo_ = GA ? ((nx) ? vgn[h][_i] : vgc[h][_i]) : voffA[_i]; \
;         __builtin_amdgcn_global_load_lds((const unsigned*)((const char*)(gbase) + vo_), (PG8_LAS unsigned*)(lds + (bufoff) + ldsw + _i * 8192), 16, 0, 0); } } while (0)
; #define PG8_LDA(dst, b, h) do { _Pragma("unroll") for (int m = 0; m < 4; ++m) _Pragma("unroll") for (int k = 0; k < 2; ++k) dst[m][k] = *(const PG8_LAS bf16x8*)(lds + PG8_SA(b, h) + aoff + m * 2048 + k * 1024); } while (0)
; #define PG8_LDB(dst, b, h) do { _Pragma("unroll") for (int n = 0; n < 2; ++n) _Pragma("unroll") for (int k = 0; k < 2; ++k) dst[n][k] = *(const PG8_LAS bf16x8*)(lds + PG8_SB(b, h) + boff + n * 2048 + k * 1024); } while (0)
; #define PG8_MMA(ai, bj, At, Bt) do { __builtin_amdgcn_s_setprio(1); _Pragma("unroll") for (int m = 0; m < 4; ++m) _Pragma("unroll") for (int n = 0; n < 2; ++n) _Pragma("unroll") for (int k = 0; k < 2; ++k) \
;         acc[ai][bj][m][n] = __builtin_amdgcn_mfma_f32_16x16x32_bf16(Bt[n][k], At[m][k], acc[ai][bj][m][n], 0, 0, 0); __builtin_amdgcn_s_setprio(0); } while (0)
; #define PG8_WAIT_V(n) asm volatile("s_waitcnt vmcnt(" #n ")" ::: "memory")
; #define PG8_WAIT_L(n) asm volatile("s_waitcnt lgkmcnt(" #n ")" ::: "memory")
; #define PG8_BAR __builtin_amdgcn_s_barrier()
; #define PG8_SCHED __builtin_amdgcn_sched_barrier(0)
; template <class Epi, class Sched>
; __device__ __forceinline__ void gemm_phase(const int WID_, PG8_LAS unsigned char* lds, const Sched& S, const Epi& E) {
;     ...
;             PG8_LDB(B0, 0, 0); PG8_LDB(B1, 0, 1); PG8_SCHED; PG8_LDA(At, 0, 0); PG8_STAGE_A(PG8_SA(1, 1), a1 + hstepA, 1, false);
;             PG8_WAIT_V(8); PG8_WAIT_L(0); PG8_BAR; PG8_MMA(0, 0, At, B0); PG8_MMA(0, 1, At, B1); PG8_BAR; PG8_SCHED;
;             PG8_LDA(At, 0, 1); PG8_STAGE(PG8_SB(0, 0), b2, voffB); PG8_STAGE(PG8_SB(0, 1), b2 + hstepB, voffB); PG8_STAGE_A(PG8_SA(0, 0), a2, 0, last);
.LBB0_1563:
	ds_read_b128 v[146:149], v143
	ds_read_b128 v[150:153], v143 offset:1024
	ds_read_b128 v[154:157], v143 offset:2048
	ds_read_b128 v[158:161], v143 offset:3072
	ds_read_b128 v[162:165], v144
	ds_read_b128 v[166:169], v144 offset:1024
	ds_read_b128 v[170:173], v144 offset:2048
	ds_read_b128 v[174:177], v144 offset:3072
	s_add_u32 s48, s46, 0xfffc0080
	s_addc_u32 s49, s47, -1
	s_cmp_eq_u32 s71, 12
	s_cselect_b32 s51, s37, s49
	s_cselect_b32 s50, s67, s48
	s_cselect_b32 s49, s39, s70
	s_cselect_b32 s48, s68, s69
	v_lshl_add_u64 v[210:211], s[46:47], 0, v[136:137]
	s_add_i32 m0, s52, 0xc000
	ds_read_b128 v[178:181], v145
	ds_read_b128 v[182:185], v145 offset:1024
	ds_read_b128 v[186:189], v145 offset:2048
	ds_read_b128 v[190:193], v145 offset:3072
	ds_read_b128 v[194:197], v145 offset:4096
	ds_read_b128 v[198:201], v145 offset:5120
	ds_read_b128 v[202:205], v145 offset:6144
	ds_read_b128 v[206:209], v145 offset:7168
	global_load_lds_dwordx4 v[210:211], off
	v_lshl_add_u64 v[210:211], s[46:47], 0, v[138:139]
	s_add_i32 m0, s52, 0xe000
	s_nop 0
	global_load_lds_dwordx4 v[210:211], off
	s_waitcnt vmcnt(8)
	s_waitcnt lgkmcnt(0)
	s_barrier
	s_nop 0
	s_setprio 1
	s_waitcnt lgkmcnt(0)
	v_mfma_f32_16x16x32_bf16 v[124:127], v[146:149], v[178:181], v[124:127]
	v_mfma_f32_16x16x32_bf16 v[120:123], v[154:157], v[178:181], v[120:123]
	v_mfma_f32_16x16x32_bf16 v[116:119], v[146:149], v[186:189], v[116:119]
	v_mfma_f32_16x16x32_bf16 v[112:115], v[154:157], v[186:189], v[112:115]
	v_mfma_f32_16x16x32_bf16 v[100:103], v[146:149], v[194:197], v[100:103]
	v_mfma_f32_16x16x32_bf16 v[96:99], v[154:157], v[194:197], v[96:99]
	v_mfma_f32_16x16x32_bf16 v[84:87], v[146:149], v[202:205], v[84:87]
	v_mfma_f32_16x16x32_bf16 v[80:83], v[154:157], v[202:205], v[80:83]
	v_mfma_f32_16x16x32_bf16 v[124:127], v[150:153], v[182:185], v[124:127]
	v_mfma_f32_16x16x32_bf16 v[120:123], v[158:161], v[182:185], v[120:123]
	v_mfma_f32_16x16x32_bf16 v[116:119], v[150:153], v[190:193], v[116:119]
	v_mfma_f32_16x16x32_bf16 v[112:115], v[158:161], v[190:193], v[112:115]
	v_mfma_f32_16x16x32_bf16 v[100:103], v[150:153], v[198:201], v[100:103]
	v_mfma_f32_16x16x32_bf16 v[96:99], v[158:161], v[198:201], v[96:99]
	v_mfma_f32_16x16x32_bf16 v[84:87], v[150:153], v[206:209], v[84:87]
	v_mfma_f32_16x16x32_bf16 v[80:83], v[158:161], v[206:209], v[80:83]
	s_setprio 0
	s_setprio 1
	v_mfma_f32_16x16x32_bf16 v[108:111], v[162:165], v[178:181], v[108:111]
	v_mfma_f32_16x16x32_bf16 v[104:107], v[170:173], v[178:181], v[104:107]
	v_mfma_f32_16x16x32_bf16 v[92:95], v[162:165], v[186:189], v[92:95]
	v_mfma_f32_16x16x32_bf16 v[88:91], v[170:173], v[186:189], v[88:91]
	v_mfma_f32_16x16x32_bf16 v[76:79], v[162:165], v[194:197], v[76:79]
	v_mfma_f32_16x16x32_bf16 v[72:75], v[170:173], v[194:197], v[72:75]
	v_mfma_f32_16x16x32_bf16 v[68:71], v[162:165], v[202:205], v[68:71]
	v_mfma_f32_16x16x32_bf16 v[64:67], v[170:173], v[202:205], v[64:67]
	v_mfma_f32_16x16x32_bf16 v[108:111], v[166:169], v[182:185], v[108:111]
	v_mfma_f32_16x16x32_bf16 v[104:107], v[174:177], v[182:185], v[104:107]
	v_mfma_f32_16x16x32_bf16 v[92:95], v[166:169], v[190:193], v[92:95]
	v_mfma_f32_16x16x32_bf16 v[88:91], v[174:177], v[190:193], v[88:91]
	v_mfma_f32_16x16x32_bf16 v[76:79], v[166:169], v[198:201], v[76:79]
	v_mfma_f32_16x16x32_bf16 v[72:75], v[174:177], v[198:201], v[72:75]
	v_mfma_f32_16x16x32_bf16 v[68:71], v[166:169], v[206:209], v[68:71]
	v_mfma_f32_16x16x32_bf16 v[64:67], v[174:177], v[206:209], v[64:67]
	s_setprio 0
	s_barrier
	s_add_i32 s76, s63, s33
	v_lshl_add_u64 v[210:211], s[48:49], 0, v[130:131]
	s_mov_b32 m0, s76
	ds_read_b128 v[178:181], v145 offset:16384
	ds_read_b128 v[182:185], v145 offset:17408
	ds_read_b128 v[186:189], v145 offset:18432
	ds_read_b128 v[190:193], v145 offset:19456
	ds_read_b128 v[194:197], v145 offset:20480
	ds_read_b128 v[198:201], v145 offset:21504
	ds_read_b128 v[202:205], v145 offset:22528
	ds_read_b128 v[206:209], v145 offset:23552
	global_load_lds_dwordx4 v[210:211], off
	s_add_i32 m0, s76, 0x2000
	s_add_u32 s76, s48, 0x40000
	v_lshl_add_u64 v[212:213], s[48:49], 0, v[134:135]
	s_addc_u32 s77, s49, 0
	s_add_i32 s78, s66, s33
	global_load_lds_dwordx4 v[212:213], off
	v_lshl_add_u64 v[214:215], s[76:77], 0, v[130:131]
	s_mov_b32 m0, s78
	v_lshl_add_u64 v[216:217], s[50:51], 0, v[132:133]
	global_load_lds_dwordx4 v[214:215], off
	v_lshl_add_u64 v[214:215], s[76:77], 0, v[134:135]
	s_add_i32 m0, s78, 0x2000
	s_nop 0
	global_load_lds_dwordx4 v[214:215], off
	v_lshl_add_u64 v[214:215], s[50:51], 0, v[128:129]
	s_mov_b32 m0, s52
	s_nop 0
	global_load_lds_dwordx4 v[214:215], off
	s_mov_b32 m0, s53
	s_nop 0
	global_load_lds_dwordx4 v[216:217], off
	s_waitcnt vmcnt(8)
	s_waitcnt lgkmcnt(0)
	s_barrier
; #define PG8_STAGE_A(bufoff, gbase, h, nx) do { _Pragma("unroll") for (int _i = 0; _i < 2; ++_i) { \
;         const unsigned vo_ = GA ? ((nx) ? vgn[h][_i] : vgc[h][_i]) : voffA[_i]; \
;         __builtin_amdgcn_global_load_lds((const unsigned*)((const char*)(gbase) + vo_), (PG8_LAS unsigned*)(lds + (bufoff) + ldsw + _i * 8192), 16, 0, 0); } } while (0)
; #define PG8_LDA(dst, b, h) do { _Pragma("unroll") for (int m = 0; m < 4; ++m) _Pragma("unroll") for (int k = 0; k < 2; ++k) dst[m][k] = *(const PG8_LAS bf16x8*)(lds + PG8_SA(b, h) + aoff + m * 2048 + k * 1024); } while (0)
; #define PG8_LDB(dst, b, h) do { _Pragma("unroll") for (int n = 0; n < 2; ++n) _Pragma("unroll") for (int k = 0; k < 2; ++k) dst[n][k] = *(const PG8_LAS bf16x8*)(lds + PG8_SB(b, h) + boff + n * 2048 + k * 1024); } while (0)
; #define PG8_MMA(ai, bj, At, Bt) do { __builtin_amdgcn_s_setprio(1); _Pragma("unroll") for (int m = 0; m < 4; ++m) _Pragma("unroll") for (int n = 0; n < 2; ++n) _Pragma("unroll") for (int k = 0; k < 2; ++k) \
;         acc[ai][bj][m][n] = __builtin_amdgcn_mfma_f32_16x16x32_bf16(Bt[n][k], At[m][k], acc[ai][bj][m][n], 0, 0, 0); __builtin_amdgcn_s_setprio(0); } while (0)
; #define PG8_WAIT_V(n) asm volatile("s_waitcnt vmcnt(" #n ")" ::: "memory")
; #define PG8_WAIT_L(n) asm volatile("s_waitcnt lgkmcnt(" #n ")" ::: "memory")
; #define PG8_BAR __builtin_amdgcn_s_barrier()
; #define PG8_SCHED __builtin_amdgcn_sched_barrier(0)
; template <class Epi, class Sched>
; __device__ __forceinline__ void gemm_phase(const int WID_, PG8_LAS unsigned char* lds, const Sched& S, const Epi& E) {
;     ...
;             PG8_WAIT_V(8); PG8_WAIT_L(0); PG8_BAR; PG8_MMA(1, 0, At, B0); PG8_MMA(1, 1, At, B1); PG8_BAR; PG8_SCHED;
;             PG8_LDB(B0, 1, 0); PG8_LDB(B1, 1, 1); PG8_SCHED; PG8_LDA(At, 1, 0); PG8_STAGE_A(PG8_SA(0, 1), a2 + hstepA, 1, last);
;             PG8_WAIT_V(8); PG8_WAIT_L(0); PG8_BAR; PG8_MMA(0, 0, At, B0); PG8_MMA(0, 1, At, B1); PG8_BAR; PG8_SCHED;
	s_nop 0
	s_setprio 1
	s_waitcnt lgkmcnt(0)
	v_mfma_f32_16x16x32_bf16 v[60:63], v[146:149], v[178:181], v[60:63]
	v_mfma_f32_16x16x32_bf16 v[56:59], v[154:157], v[178:181], v[56:59]
	v_mfma_f32_16x16x32_bf16 v[52:55], v[146:149], v[186:189], v[52:55]
	v_mfma_f32_16x16x32_bf16 v[48:51], v[154:157], v[186:189], v[48:51]
	v_mfma_f32_16x16x32_bf16 v[36:39], v[146:149], v[194:197], v[36:39]
	v_mfma_f32_16x16x32_bf16 v[32:35], v[154:157], v[194:197], v[32:35]
	v_mfma_f32_16x16x32_bf16 v[20:23], v[146:149], v[202:205], v[20:23]
	v_mfma_f32_16x16x32_bf16 v[16:19], v[154:157], v[202:205], v[16:19]
	v_mfma_f32_16x16x32_bf16 v[60:63], v[150:153], v[182:185], v[60:63]
	v_mfma_f32_16x16x32_bf16 v[56:59], v[158:161], v[182:185], v[56:59]
	v_mfma_f32_16x16x32_bf16 v[52:55], v[150:153], v[190:193], v[52:55]
	v_mfma_f32_16x16x32_bf16 v[48:51], v[158:161], v[190:193], v[48:51]
	v_mfma_f32_16x16x32_bf16 v[36:39], v[150:153], v[198:201], v[36:39]
	v_mfma_f32_16x16x32_bf16 v[32:35], v[158:161], v[198:201], v[32:35]
	v_mfma_f32_16x16x32_bf16 v[20:23], v[150:153], v[206:209], v[20:23]
	v_mfma_f32_16x16x32_bf16 v[16:19], v[158:161], v[206:209], v[16:19]
	s_setprio 0
	s_setprio 1
	v_mfma_f32_16x16x32_bf16 v[44:47], v[162:165], v[178:181], v[44:47]
	v_mfma_f32_16x16x32_bf16 v[40:43], v[170:173], v[178:181], v[40:43]
	v_mfma_f32_16x16x32_bf16 v[28:31], v[162:165], v[186:189], v[28:31]
	v_mfma_f32_16x16x32_bf16 v[24:27], v[170:173], v[186:189], v[24:27]
	v_mfma_f32_16x16x32_bf16 v[12:15], v[162:165], v[194:197], v[12:15]
	v_mfma_f32_16x16x32_bf16 v[8:11], v[170:173], v[194:197], v[8:11]
	v_mfma_f32_16x16x32_bf16 v[4:7], v[162:165], v[202:205], v[4:7]
	v_mfma_f32_16x16x32_bf16 v[0:3], v[170:173], v[202:205], v[0:3]
	v_mfma_f32_16x16x32_bf16 v[44:47], v[166:169], v[182:185], v[44:47]
	v_mfma_f32_16x16x32_bf16 v[40:43], v[174:177], v[182:185], v[40:43]
	v_mfma_f32_16x16x32_bf16 v[28:31], v[166:169], v[190:193], v[28:31]
	v_mfma_f32_16x16x32_bf16 v[24:27], v[174:177], v[190:193], v[24:27]
	v_mfma_f32_16x16x32_bf16 v[12:15], v[166:169], v[198:201], v[12:15]
	v_mfma_f32_16x16x32_bf16 v[8:11], v[174:177], v[198:201], v[8:11]
	v_mfma_f32_16x16x32_bf16 v[4:7], v[166:169], v[206:209], v[4:7]
	v_mfma_f32_16x16x32_bf16 v[0:3], v[174:177], v[206:209], v[0:3]
	s_setprio 0
	s_barrier
	s_add_i32 s76, 0, 0x18000
	s_add_i32 s77, 0, 0x1c000
	v_add_u32_e32 v158, s76, v141
	v_add_u32_e32 v174, s77, v141
	ds_read_b128 v[146:149], v158
	ds_read_b128 v[150:153], v158 offset:1024
	ds_read_b128 v[154:157], v158 offset:2048
	ds_read_b128 v[158:161], v158 offset:3072
	ds_read_b128 v[162:165], v174
	ds_read_b128 v[166:169], v174 offset:1024
	ds_read_b128 v[170:173], v174 offset:2048
	ds_read_b128 v[174:177], v174 offset:3072
	s_add_u32 s50, s50, 0x40000
	s_addc_u32 s51, s51, 0
	s_mov_b32 m0, s58
	v_lshl_add_u64 v[218:219], s[50:51], 0, v[128:129]
	ds_read_b128 v[178:181], v145 offset:32768
	ds_read_b128 v[182:185], v145 offset:33792
	ds_read_b128 v[186:189], v145 offset:34816
	ds_read_b128 v[190:193], v145 offset:35840
	ds_read_b128 v[194:197], v145 offset:36864
	ds_read_b128 v[198:201], v145 offset:37888
	ds_read_b128 v[202:205], v145 offset:38912
	ds_read_b128 v[206:209], v145 offset:39936
	global_load_lds_dwordx4 v[218:219], off
	v_lshl_add_u64 v[218:219], s[50:51], 0, v[132:133]
	s_mov_b32 m0, s59
	s_nop 0
	global_load_lds_dwordx4 v[218:219], off
	s_waitcnt vmcnt(8)
	s_waitcnt lgkmcnt(0)
	s_barrier
	s_nop 0
	s_setprio 1
	s_waitcnt lgkmcnt(0)
	v_mfma_f32_16x16x32_bf16 v[124:127], v[146:149], v[178:181], v[124:127]
	v_mfma_f32_16x16x32_bf16 v[120:123], v[154:157], v[178:181], v[120:123]
	v_mfma_f32_16x16x32_bf16 v[116:119], v[146:149], v[186:189], v[116:119]
	v_mfma_f32_16x16x32_bf16 v[112:115], v[154:157], v[186:189], v[112:115]
	v_mfma_f32_16x16x32_bf16 v[100:103], v[146:149], v[194:197], v[100:103]
	v_mfma_f32_16x16x32_bf16 v[96:99], v[154:157], v[194:197], v[96:99]
	v_mfma_f32_16x16x32_bf16 v[84:87], v[146:149], v[202:205], v[84:87]
	v_mfma_f32_16x16x32_bf16 v[80:83], v[154:157], v[202:205], v[80:83]
	v_mfma_f32_16x16x32_bf16 v[124:127], v[150:153], v[182:185], v[124:127]
	v_mfma_f32_16x16x32_bf16 v[120:123], v[158:161], v[182:185], v[120:123]
	v_mfma_f32_16x16x32_bf16 v[116:119], v[150:153], v[190:193], v[116:119]
	v_mfma_f32_16x16x32_bf16 v[112:115], v[158:161], v[190:193], v[112:115]
	v_mfma_f32_16x16x32_bf16 v[100:103], v[150:153], v[198:201], v[100:103]
	v_mfma_f32_16x16x32_bf16 v[96:99], v[158:161], v[198:201], v[96:99]
	v_mfma_f32_16x16x32_bf16 v[84:87], v[150:153], v[206:209], v[84:87]
	v_mfma_f32_16x16x32_bf16 v[80:83], v[158:161], v[206:209], v[80:83]
	s_setprio 0
	s_setprio 1
	v_mfma_f32_16x16x32_bf16 v[108:111], v[162:165], v[178:181], v[108:111]
	v_mfma_f32_16x16x32_bf16 v[104:107], v[170:173], v[178:181], v[104:107]
	v_mfma_f32_16x16x32_bf16 v[92:95], v[162:165], v[186:189], v[92:95]
	v_mfma_f32_16x16x32_bf16 v[88:91], v[170:173], v[186:189], v[88:91]
	v_mfma_f32_16x16x32_bf16 v[76:79], v[162:165], v[194:197], v[76:79]
	v_mfma_f32_16x16x32_bf16 v[72:75], v[170:173], v[194:197], v[72:75]
	v_mfma_f32_16x16x32_bf16 v[68:71], v[162:165], v[202:205], v[68:71]
	v_mfma_f32_16x16x32_bf16 v[64:67], v[170:173], v[202:205], v[64:67]
	v_mfma_f32_16x16x32_bf16 v[108:111], v[166:169], v[182:185], v[108:111]
	v_mfma_f32_16x16x32_bf16 v[104:107], v[174:177], v[182:185], v[104:107]
	v_mfma_f32_16x16x32_bf16 v[92:95], v[166:169], v[190:193], v[92:95]
	v_mfma_f32_16x16x32_bf16 v[88:91], v[174:177], v[190:193], v[88:91]
	v_mfma_f32_16x16x32_bf16 v[76:79], v[166:169], v[198:201], v[76:79]
	v_mfma_f32_16x16x32_bf16 v[72:75], v[174:177], v[198:201], v[72:75]
	v_mfma_f32_16x16x32_bf16 v[68:71], v[166:169], v[206:209], v[68:71]
	v_mfma_f32_16x16x32_bf16 v[64:67], v[174:177], v[206:209], v[64:67]
	s_setprio 0
	s_barrier
; #define PG8_STAGE(bufoff, gbase, voff) do { _Pragma("unroll") for (int _i = 0; _i < 2; ++_i) \
;         __builtin_amdgcn_global_load_lds((const unsigned*)((const char*)(gbase) + (voff)[_i]), (PG8_LAS unsigned*)(lds + (bufoff) + ldsw + _i * 8192), 16, 0, 0); } while (0)
; #define PG8_STAGE_A(bufoff, gbase, h, nx) do { _Pragma("unroll") for (int _i = 0; _i < 2; ++_i) { \
;         const unsigned vo_ = GA ? ((nx) ? vgn[h][_i] : vgc[h][_i]) : voffA[_i]; \
;         __builtin_amdgcn_global_load_lds((const unsigned*)((const char*)(gbase) + vo_), (PG8_LAS unsigned*)(lds + (bufoff) + ldsw + _i * 8192), 16, 0, 0); } } while (0)
; #define PG8_LDA(dst, b, h) do { _Pragma("unroll") for (int m = 0; m < 4; ++m) _Pragma("unroll") for (int k = 0; k < 2; ++k) dst[m][k] = *(const PG8_LAS bf16x8*)(lds + PG8_SA(b, h) + aoff + m * 2048 + k * 1024); } while (0)
; #define PG8_MMA(ai, bj, At, Bt) do { __builtin_amdgcn_s_setprio(1); _Pragma("unroll") for (int m = 0; m < 4; ++m) _Pragma("unroll") for (int n = 0; n < 2; ++n) _Pragma("unroll") for (int k = 0; k < 2; ++k) \
;         acc[ai][bj][m][n] = __builtin_amdgcn_mfma_f32_16x16x32_bf16(Bt[n][k], At[m][k], acc[ai][bj][m][n], 0, 0, 0); __builtin_amdgcn_s_setprio(0); } while (0)
; #define PG8_WAIT_V(n) asm volatile("s_waitcnt vmcnt(" #n ")" ::: "memory")
; #define PG8_WAIT_L(n) asm volatile("s_waitcnt lgkmcnt(" #n ")" ::: "memory")
; #define PG8_BAR __builtin_amdgcn_s_barrier()
; #define PG8_SCHED __builtin_amdgcn_sched_barrier(0)
; template <class Epi, class Sched>
; __device__ __forceinline__ void gemm_phase(const int WID_, PG8_LAS unsigned char* lds, const Sched& S, const Epi& E) {
;     ...
;             PG8_LDA(At, 1, 1); PG8_STAGE(PG8_SB(1, 0), b3, voffB); PG8_STAGE(PG8_SB(1, 1), b3 + hstepB, voffB); PG8_STAGE_A(PG8_SA(1, 0), a3, 0, last);
;             PG8_WAIT_V(8); PG8_WAIT_L(0); PG8_BAR; PG8_MMA(1, 0, At, B0); PG8_MMA(1, 1, At, B1); PG8_BAR; PG8_SCHED;
;         }
	s_add_i32 s50, s76, s33
	v_lshl_add_u64 v[210:211], v[210:211], 0, s[4:5]
	s_mov_b32 m0, s50
	ds_read_b128 v[178:181], v145 offset:49152
	ds_read_b128 v[182:185], v145 offset:50176
	ds_read_b128 v[186:189], v145 offset:51200
	ds_read_b128 v[190:193], v145 offset:52224
	ds_read_b128 v[194:197], v145 offset:53248
	ds_read_b128 v[198:201], v145 offset:54272
	ds_read_b128 v[202:205], v145 offset:55296
	ds_read_b128 v[206:209], v145 offset:56320
	global_load_lds_dwordx4 v[210:211], off
	s_add_i32 m0, s50, 0x2000
	s_add_u32 s48, s48, 0x40080
	v_lshl_add_u64 v[210:211], v[212:213], 0, s[4:5]
	s_addc_u32 s49, s49, 0
	s_add_i32 s50, s77, s33
	global_load_lds_dwordx4 v[210:211], off
	v_lshl_add_u64 v[210:211], s[48:49], 0, v[130:131]
	s_mov_b32 m0, s50
	s_nop 0
	global_load_lds_dwordx4 v[210:211], off
	v_lshl_add_u64 v[210:211], s[48:49], 0, v[134:135]
	s_add_i32 m0, s50, 0x2000
	s_nop 0
	global_load_lds_dwordx4 v[210:211], off
	v_lshl_add_u64 v[210:211], v[214:215], 0, s[4:5]
	s_mov_b32 m0, s60
	s_nop 0
	global_load_lds_dwordx4 v[210:211], off
	v_lshl_add_u64 v[210:211], v[216:217], 0, s[4:5]
	s_mov_b32 m0, s61
	s_nop 0
	global_load_lds_dwordx4 v[210:211], off
	s_waitcnt vmcnt(8)
	s_waitcnt lgkmcnt(0)
	s_barrier
	s_setprio 1
	s_waitcnt lgkmcnt(0)
	v_mfma_f32_16x16x32_bf16 v[60:63], v[146:149], v[178:181], v[60:63]
	v_mfma_f32_16x16x32_bf16 v[56:59], v[154:157], v[178:181], v[56:59]
	v_mfma_f32_16x16x32_bf16 v[52:55], v[146:149], v[186:189], v[52:55]
	v_mfma_f32_16x16x32_bf16 v[48:51], v[154:157], v[186:189], v[48:51]
	v_mfma_f32_16x16x32_bf16 v[36:39], v[146:149], v[194:197], v[36:39]
	v_mfma_f32_16x16x32_bf16 v[32:35], v[154:157], v[194:197], v[32:35]
	v_mfma_f32_16x16x32_bf16 v[20:23], v[146:149], v[202:205], v[20:23]
	v_mfma_f32_16x16x32_bf16 v[16:19], v[154:157], v[202:205], v[16:19]
	v_mfma_f32_16x16x32_bf16 v[60:63], v[150:153], v[182:185], v[60:63]
	v_mfma_f32_16x16x32_bf16 v[56:59], v[158:161], v[182:185], v[56:59]
	v_mfma_f32_16x16x32_bf16 v[52:55], v[150:153], v[190:193], v[52:55]
	v_mfma_f32_16x16x32_bf16 v[48:51], v[158:161], v[190:193], v[48:51]
	v_mfma_f32_16x16x32_bf16 v[36:39], v[150:153], v[198:201], v[36:39]
	v_mfma_f32_16x16x32_bf16 v[32:35], v[158:161], v[198:201], v[32:35]
	v_mfma_f32_16x16x32_bf16 v[20:23], v[150:153], v[206:209], v[20:23]
	v_mfma_f32_16x16x32_bf16 v[16:19], v[158:161], v[206:209], v[16:19]
	s_setprio 0
	s_setprio 1
	v_mfma_f32_16x16x32_bf16 v[44:47], v[162:165], v[178:181], v[44:47]
	v_mfma_f32_16x16x32_bf16 v[40:43], v[170:173], v[178:181], v[40:43]
	v_mfma_f32_16x16x32_bf16 v[28:31], v[162:165], v[186:189], v[28:31]
	v_mfma_f32_16x16x32_bf16 v[24:27], v[170:173], v[186:189], v[24:27]
	v_mfma_f32_16x16x32_bf16 v[12:15], v[162:165], v[194:197], v[12:15]
	v_mfma_f32_16x16x32_bf16 v[8:11], v[170:173], v[194:197], v[8:11]
	v_mfma_f32_16x16x32_bf16 v[4:7], v[162:165], v[202:205], v[4:7]
	v_mfma_f32_16x16x32_bf16 v[0:3], v[170:173], v[202:205], v[0:3]
	v_mfma_f32_16x16x32_bf16 v[44:47], v[166:169], v[182:185], v[44:47]
	v_mfma_f32_16x16x32_bf16 v[40:43], v[174:177], v[182:185], v[40:43]
	v_mfma_f32_16x16x32_bf16 v[28:31], v[166:169], v[190:193], v[28:31]
	v_mfma_f32_16x16x32_bf16 v[24:27], v[174:177], v[190:193], v[24:27]
	v_mfma_f32_16x16x32_bf16 v[12:15], v[166:169], v[198:201], v[12:15]
	v_mfma_f32_16x16x32_bf16 v[8:11], v[174:177], v[198:201], v[8:11]
	v_mfma_f32_16x16x32_bf16 v[4:7], v[166:169], v[206:209], v[4:7]
	v_mfma_f32_16x16x32_bf16 v[0:3], v[174:177], v[206:209], v[0:3]
	s_setprio 0
	s_barrier
	s_add_i32 s71, s71, 2
	s_add_u32 s46, s46, 0x100
	s_addc_u32 s47, s47, 0
	s_add_u32 s69, s69, 0x100
	s_addc_u32 s70, s70, 0
	s_cmp_gt_u32 s71, 13
	s_cbranch_scc0 .LBB0_1563
	s_and_b64 vcc, exec, s[18:19]
	s_cbranch_vccz .LBB0_1566
	s_barrier

; #define PG8_STAGE(bufoff, gbase, voff) do { _Pragma("unroll") for (int _i = 0; _i < 2; ++_i) \
;         __builtin_amdgcn_global_load_lds((const unsigned*)((const char*)(gbase) + (voff)[_i]), (PG8_LAS unsigned*)(lds + (bufoff) + ldsw + _i * 8192), 16, 0, 0); } while (0)
; #define PG8_STAGE_A(bufoff, gbase, h, nx) do { _Pragma("unroll") for (int _i = 0; _i < 2; ++_i) { \
;         const unsigned vo_ = GA ? ((nx) ? vgn[h][_i] : vgc[h][_i]) : voffA[_i]; \
;         __builtin_amdgcn_global_load_lds((const unsigned*)((const char*)(gbase) + vo_), (PG8_LAS unsigned*)(lds + (bufoff) + ldsw + _i * 8192), 16, 0, 0); } } while (0)
; #define PG8_LDA(dst, b, h) do { _Pragma("unroll") for (int m = 0; m < 4; ++m) _Pragma("unroll") for (int k = 0; k < 2; ++k) dst[m][k] = *(const PG8_LAS bf16x8*)(lds + PG8_SA(b, h) + aoff + m * 2048 + k * 1024); } while (0)
; #define PG8_LDB(dst, b, h) do { _Pragma("unroll") for (int n = 0; n < 2; ++n) _Pragma("unroll") for (int k = 0; k < 2; ++k) dst[n][k] = *(const PG8_LAS bf16x8*)(lds + PG8_SB(b, h) + boff + n * 2048 + k * 1024); } while (0)
; #define PG8_MMA(ai, bj, At, Bt) do { __builtin_amdgcn_s_setprio(1); _Pragma("unroll") for (int m = 0; m < 4; ++m) _Pragma("unroll") for (int n = 0; n < 2; ++n) _Pragma("unroll") for (int k = 0; k < 2; ++k) \
;         acc[ai][bj][m][n] = __builtin_amdgcn_mfma_f32_16x16x32_bf16(Bt[n][k], At[m][k], acc[ai][bj][m][n], 0, 0, 0); __builtin_amdgcn_s_setprio(0); } while (0)
; #define PG8_WAIT_V(n) asm volatile("s_waitcnt vmcnt(" #n ")" ::: "memory")
; #define PG8_WAIT_L(n) asm volatile("s_waitcnt lgkmcnt(" #n ")" ::: "memory")
; #define PG8_BAR __builtin_amdgcn_s_barrier()
; #define PG8_SCHED __builtin_amdgcn_sched_barrier(0)
; template <class Epi, class Sched>
; __device__ __forceinline__ void gemm_phase(const int WID_, PG8_LAS unsigned char* lds, const Sched& S, const Epi& E) {
;     ...
;             PG8_LDB(B0, 0, 0); PG8_LDB(B1, 0, 1); PG8_SCHED; PG8_LDA(At, 0, 0); PG8_STAGE_A(PG8_SA(1, 1), a1 + hstepA, 1, false);
;             PG8_WAIT_V(8); PG8_WAIT_L(0); PG8_BAR; PG8_MMA(0, 0, At, B0); PG8_MMA(0, 1, At, B1); PG8_BAR; PG8_SCHED;
;             PG8_LDA(At, 0, 1); PG8_STAGE(PG8_SB(0, 0), b2, voffB); PG8_STAGE(PG8_SB(0, 1), b2 + hstepB, voffB); PG8_STAGE_A(PG8_SA(0, 0), a2, 0, last);
.LBB0_1786:
	ds_read_b128 v[146:149], v143
	ds_read_b128 v[150:153], v143 offset:1024
	ds_read_b128 v[154:157], v143 offset:2048
	ds_read_b128 v[158:161], v143 offset:3072
	ds_read_b128 v[162:165], v144
	ds_read_b128 v[166:169], v144 offset:1024
	ds_read_b128 v[170:173], v144 offset:2048
	ds_read_b128 v[174:177], v144 offset:3072
	s_add_u32 s44, s42, 0xfffc0080
	s_addc_u32 s45, s43, -1
	s_cmp_eq_u32 s67, 12
	s_cselect_b32 s47, s37, s45
	s_cselect_b32 s46, s61, s44
	s_cselect_b32 s45, s23, s66
	s_cselect_b32 s44, s62, s63
	v_lshl_add_u64 v[210:211], s[42:43], 0, v[136:137]
	s_add_i32 m0, s33, 0xc000
	ds_read_b128 v[178:181], v145
	ds_read_b128 v[182:185], v145 offset:1024
	ds_read_b128 v[186:189], v145 offset:2048
	ds_read_b128 v[190:193], v145 offset:3072
	ds_read_b128 v[194:197], v145 offset:4096
	ds_read_b128 v[198:201], v145 offset:5120
	ds_read_b128 v[202:205], v145 offset:6144
	ds_read_b128 v[206:209], v145 offset:7168
	global_load_lds_dwordx4 v[210:211], off
	v_lshl_add_u64 v[210:211], s[42:43], 0, v[138:139]
	s_add_i32 m0, s33, 0xe000
	s_nop 0
	global_load_lds_dwordx4 v[210:211], off
	s_waitcnt vmcnt(8)
	s_waitcnt lgkmcnt(0)
	s_barrier
	s_setprio 1
	s_waitcnt lgkmcnt(0)
	v_mfma_f32_16x16x32_bf16 v[124:127], v[146:149], v[178:181], v[124:127]
	v_mfma_f32_16x16x32_bf16 v[120:123], v[154:157], v[178:181], v[120:123]
	v_mfma_f32_16x16x32_bf16 v[116:119], v[146:149], v[186:189], v[116:119]
	v_mfma_f32_16x16x32_bf16 v[112:115], v[154:157], v[186:189], v[112:115]
	v_mfma_f32_16x16x32_bf16 v[100:103], v[146:149], v[194:197], v[100:103]
	v_mfma_f32_16x16x32_bf16 v[96:99], v[154:157], v[194:197], v[96:99]
	v_mfma_f32_16x16x32_bf16 v[84:87], v[146:149], v[202:205], v[84:87]
	v_mfma_f32_16x16x32_bf16 v[80:83], v[154:157], v[202:205], v[80:83]
	v_mfma_f32_16x16x32_bf16 v[124:127], v[150:153], v[182:185], v[124:127]
	v_mfma_f32_16x16x32_bf16 v[120:123], v[158:161], v[182:185], v[120:123]
	v_mfma_f32_16x16x32_bf16 v[116:119], v[150:153], v[190:193], v[116:119]
	v_mfma_f32_16x16x32_bf16 v[112:115], v[158:161], v[190:193], v[112:115]
	v_mfma_f32_16x16x32_bf16 v[100:103], v[150:153], v[198:201], v[100:103]
	v_mfma_f32_16x16x32_bf16 v[96:99], v[158:161], v[198:201], v[96:99]
	v_mfma_f32_16x16x32_bf16 v[84:87], v[150:153], v[206:209], v[84:87]
	v_mfma_f32_16x16x32_bf16 v[80:83], v[158:161], v[206:209], v[80:83]
	s_setprio 0
	s_setprio 1
	v_mfma_f32_16x16x32_bf16 v[108:111], v[162:165], v[178:181], v[108:111]
	v_mfma_f32_16x16x32_bf16 v[104:107], v[170:173], v[178:181], v[104:107]
	v_mfma_f32_16x16x32_bf16 v[92:95], v[162:165], v[186:189], v[92:95]
	v_mfma_f32_16x16x32_bf16 v[88:91], v[170:173], v[186:189], v[88:91]
	v_mfma_f32_16x16x32_bf16 v[76:79], v[162:165], v[194:197], v[76:79]
	v_mfma_f32_16x16x32_bf16 v[72:75], v[170:173], v[194:197], v[72:75]
	v_mfma_f32_16x16x32_bf16 v[68:71], v[162:165], v[202:205], v[68:71]
	v_mfma_f32_16x16x32_bf16 v[64:67], v[170:173], v[202:205], v[64:67]
	v_mfma_f32_16x16x32_bf16 v[108:111], v[166:169], v[182:185], v[108:111]
	v_mfma_f32_16x16x32_bf16 v[104:107], v[174:177], v[182:185], v[104:107]
	v_mfma_f32_16x16x32_bf16 v[92:95], v[166:169], v[190:193], v[92:95]
	v_mfma_f32_16x16x32_bf16 v[88:91], v[174:177], v[190:193], v[88:91]
	v_mfma_f32_16x16x32_bf16 v[76:79], v[166:169], v[198:201], v[76:79]
	v_mfma_f32_16x16x32_bf16 v[72:75], v[174:177], v[198:201], v[72:75]
	v_mfma_f32_16x16x32_bf16 v[68:71], v[166:169], v[206:209], v[68:71]
	v_mfma_f32_16x16x32_bf16 v[64:67], v[174:177], v[206:209], v[64:67]
	s_setprio 0
	s_barrier
	s_add_i32 s68, s59, s9
	v_lshl_add_u64 v[210:211], s[44:45], 0, v[130:131]
	s_mov_b32 m0, s68
	ds_read_b128 v[178:181], v145 offset:16384
	ds_read_b128 v[182:185], v145 offset:17408
	ds_read_b128 v[186:189], v145 offset:18432
	ds_read_b128 v[190:193], v145 offset:19456
	ds_read_b128 v[194:197], v145 offset:20480
	ds_read_b128 v[198:201], v145 offset:21504
	ds_read_b128 v[202:205], v145 offset:22528
	ds_read_b128 v[206:209], v145 offset:23552
	global_load_lds_dwordx4 v[210:211], off
	s_add_i32 m0, s68, 0x2000
	s_add_u32 s68, s44, 0x40000
	v_lshl_add_u64 v[212:213], s[44:45], 0, v[134:135]
	s_addc_u32 s69, s45, 0
	s_add_i32 s70, s60, s9
	global_load_lds_dwordx4 v[212:213], off
	v_lshl_add_u64 v[214:215], s[68:69], 0, v[130:131]
	s_mov_b32 m0, s70
	v_lshl_add_u64 v[216:217], s[46:47], 0, v[132:133]
	global_load_lds_dwordx4 v[214:215], off
	v_lshl_add_u64 v[214:215], s[68:69], 0, v[134:135]
	s_add_i32 m0, s70, 0x2000
	s_nop 0
	global_load_lds_dwordx4 v[214:215], off
	v_lshl_add_u64 v[214:215], s[46:47], 0, v[128:129]
	s_mov_b32 m0, s33
	s_nop 0
	global_load_lds_dwordx4 v[214:215], off
	s_mov_b32 m0, s48
	s_nop 0
	global_load_lds_dwordx4 v[216:217], off
	s_waitcnt vmcnt(8)
	s_waitcnt lgkmcnt(0)
	s_barrier
; #define PG8_STAGE_A(bufoff, gbase, h, nx) do { _Pragma("unroll") for (int _i = 0; _i < 2; ++_i) { \
;         const unsigned vo_ = GA ? ((nx) ? vgn[h][_i] : vgc[h][_i]) : voffA[_i]; \
;         __builtin_amdgcn_global_load_lds((const unsigned*)((const char*)(gbase) + vo_), (PG8_LAS unsigned*)(lds + (bufoff) + ldsw + _i * 8192), 16, 0, 0); } } while (0)
; #define PG8_LDA(dst, b, h) do { _Pragma("unroll") for (int m = 0; m < 4; ++m) _Pragma("unroll") for (int k = 0; k < 2; ++k) dst[m][k] = *(const PG8_LAS bf16x8*)(lds + PG8_SA(b, h) + aoff + m * 2048 + k * 1024); } while (0)
; #define PG8_LDB(dst, b, h) do { _Pragma("unroll") for (int n = 0; n < 2; ++n) _Pragma("unroll") for (int k = 0; k < 2; ++k) dst[n][k] = *(const PG8_LAS bf16x8*)(lds + PG8_SB(b, h) + boff + n * 2048 + k * 1024); } while (0)
; #define PG8_MMA(ai, bj, At, Bt) do { __builtin_amdgcn_s_setprio(1); _Pragma("unroll") for (int m = 0; m < 4; ++m) _Pragma("unroll") for (int n = 0; n < 2; ++n) _Pragma("unroll") for (int k = 0; k < 2; ++k) \
;         acc[ai][bj][m][n] = __builtin_amdgcn_mfma_f32_16x16x32_bf16(Bt[n][k], At[m][k], acc[ai][bj][m][n], 0, 0, 0); __builtin_amdgcn_s_setprio(0); } while (0)
; #define PG8_WAIT_V(n) asm volatile("s_waitcnt vmcnt(" #n ")" ::: "memory")
; #define PG8_WAIT_L(n) asm volatile("s_waitcnt lgkmcnt(" #n ")" ::: "memory")
; #define PG8_BAR __builtin_amdgcn_s_barrier()
; #define PG8_SCHED __builtin_amdgcn_sched_barrier(0)
; template <class Epi, class Sched>
; __device__ __forceinline__ void gemm_phase(const int WID_, PG8_LAS unsigned char* lds, const Sched& S, const Epi& E) {
;     ...
;             PG8_WAIT_V(8); PG8_WAIT_L(0); PG8_BAR; PG8_MMA(1, 0, At, B0); PG8_MMA(1, 1, At, B1); PG8_BAR; PG8_SCHED;
;             PG8_LDB(B0, 1, 0); PG8_LDB(B1, 1, 1); PG8_SCHED; PG8_LDA(At, 1, 0); PG8_STAGE_A(PG8_SA(0, 1), a2 + hstepA, 1, last);
;             PG8_WAIT_V(8); PG8_WAIT_L(0); PG8_BAR; PG8_MMA(0, 0, At, B0); PG8_MMA(0, 1, At, B1); PG8_BAR; PG8_SCHED;
	s_nop 0
	s_setprio 1
	s_waitcnt lgkmcnt(0)
	v_mfma_f32_16x16x32_bf16 v[60:63], v[146:149], v[178:181], v[60:63]
	v_mfma_f32_16x16x32_bf16 v[56:59], v[154:157], v[178:181], v[56:59]
	v_mfma_f32_16x16x32_bf16 v[52:55], v[146:149], v[186:189], v[52:55]
	v_mfma_f32_16x16x32_bf16 v[48:51], v[154:157], v[186:189], v[48:51]
	v_mfma_f32_16x16x32_bf16 v[36:39], v[146:149], v[194:197], v[36:39]
	v_mfma_f32_16x16x32_bf16 v[32:35], v[154:157], v[194:197], v[32:35]
	v_mfma_f32_16x16x32_bf16 v[20:23], v[146:149], v[202:205], v[20:23]
	v_mfma_f32_16x16x32_bf16 v[16:19], v[154:157], v[202:205], v[16:19]
	v_mfma_f32_16x16x32_bf16 v[60:63], v[150:153], v[182:185], v[60:63]
	v_mfma_f32_16x16x32_bf16 v[56:59], v[158:161], v[182:185], v[56:59]
	v_mfma_f32_16x16x32_bf16 v[52:55], v[150:153], v[190:193], v[52:55]
	v_mfma_f32_16x16x32_bf16 v[48:51], v[158:161], v[190:193], v[48:51]
	v_mfma_f32_16x16x32_bf16 v[36:39], v[150:153], v[198:201], v[36:39]
	v_mfma_f32_16x16x32_bf16 v[32:35], v[158:161], v[198:201], v[32:35]
	v_mfma_f32_16x16x32_bf16 v[20:23], v[150:153], v[206:209], v[20:23]
	v_mfma_f32_16x16x32_bf16 v[16:19], v[158:161], v[206:209], v[16:19]
	s_setprio 0
	s_setprio 1
	v_mfma_f32_16x16x32_bf16 v[44:47], v[162:165], v[178:181], v[44:47]
	v_mfma_f32_16x16x32_bf16 v[40:43], v[170:173], v[178:181], v[40:43]
	v_mfma_f32_16x16x32_bf16 v[28:31], v[162:165], v[186:189], v[28:31]
	v_mfma_f32_16x16x32_bf16 v[24:27], v[170:173], v[186:189], v[24:27]
	v_mfma_f32_16x16x32_bf16 v[12:15], v[162:165], v[194:197], v[12:15]
	v_mfma_f32_16x16x32_bf16 v[8:11], v[170:173], v[194:197], v[8:11]
	v_mfma_f32_16x16x32_bf16 v[4:7], v[162:165], v[202:205], v[4:7]
	v_mfma_f32_16x16x32_bf16 v[0:3], v[170:173], v[202:205], v[0:3]
	v_mfma_f32_16x16x32_bf16 v[44:47], v[166:169], v[182:185], v[44:47]
	v_mfma_f32_16x16x32_bf16 v[40:43], v[174:177], v[182:185], v[40:43]
	v_mfma_f32_16x16x32_bf16 v[28:31], v[166:169], v[190:193], v[28:31]
	v_mfma_f32_16x16x32_bf16 v[24:27], v[174:177], v[190:193], v[24:27]
	v_mfma_f32_16x16x32_bf16 v[12:15], v[166:169], v[198:201], v[12:15]
	v_mfma_f32_16x16x32_bf16 v[8:11], v[174:177], v[198:201], v[8:11]
	v_mfma_f32_16x16x32_bf16 v[4:7], v[166:169], v[206:209], v[4:7]
	v_mfma_f32_16x16x32_bf16 v[0:3], v[174:177], v[206:209], v[0:3]
	s_setprio 0
	s_barrier
	s_add_i32 s68, 0, 0x18000
	s_add_i32 s69, 0, 0x1c000
	v_add_u32_e32 v158, s68, v141
	v_add_u32_e32 v174, s69, v141
	ds_read_b128 v[146:149], v158
	ds_read_b128 v[150:153], v158 offset:1024
	ds_read_b128 v[154:157], v158 offset:2048
	ds_read_b128 v[158:161], v158 offset:3072
	ds_read_b128 v[162:165], v174
	ds_read_b128 v[166:169], v174 offset:1024
	ds_read_b128 v[170:173], v174 offset:2048
	ds_read_b128 v[174:177], v174 offset:3072
	s_add_u32 s46, s46, 0x40000
	s_addc_u32 s47, s47, 0
	s_mov_b32 m0, s49
	v_lshl_add_u64 v[218:219], s[46:47], 0, v[128:129]
	ds_read_b128 v[178:181], v145 offset:32768
	ds_read_b128 v[182:185], v145 offset:33792
	ds_read_b128 v[186:189], v145 offset:34816
	ds_read_b128 v[190:193], v145 offset:35840
	ds_read_b128 v[194:197], v145 offset:36864
	ds_read_b128 v[198:201], v145 offset:37888
	ds_read_b128 v[202:205], v145 offset:38912
	ds_read_b128 v[206:209], v145 offset:39936
	global_load_lds_dwordx4 v[218:219], off
	v_lshl_add_u64 v[218:219], s[46:47], 0, v[132:133]
	s_mov_b32 m0, s50
	s_nop 0
	global_load_lds_dwordx4 v[218:219], off
	s_waitcnt vmcnt(8)
	s_waitcnt lgkmcnt(0)
	s_barrier
	s_nop 0
	s_setprio 1
	s_waitcnt lgkmcnt(0)
	v_mfma_f32_16x16x32_bf16 v[124:127], v[146:149], v[178:181], v[124:127]
	v_mfma_f32_16x16x32_bf16 v[120:123], v[154:157], v[178:181], v[120:123]
	v_mfma_f32_16x16x32_bf16 v[116:119], v[146:149], v[186:189], v[116:119]
	v_mfma_f32_16x16x32_bf16 v[112:115], v[154:157], v[186:189], v[112:115]
	v_mfma_f32_16x16x32_bf16 v[100:103], v[146:149], v[194:197], v[100:103]
	v_mfma_f32_16x16x32_bf16 v[96:99], v[154:157], v[194:197], v[96:99]
	v_mfma_f32_16x16x32_bf16 v[84:87], v[146:149], v[202:205], v[84:87]
	v_mfma_f32_16x16x32_bf16 v[80:83], v[154:157], v[202:205], v[80:83]
	v_mfma_f32_16x16x32_bf16 v[124:127], v[150:153], v[182:185], v[124:127]
	v_mfma_f32_16x16x32_bf16 v[120:123], v[158:161], v[182:185], v[120:123]
	v_mfma_f32_16x16x32_bf16 v[116:119], v[150:153], v[190:193], v[116:119]
	v_mfma_f32_16x16x32_bf16 v[112:115], v[158:161], v[190:193], v[112:115]
	v_mfma_f32_16x16x32_bf16 v[100:103], v[150:153], v[198:201], v[100:103]
	v_mfma_f32_16x16x32_bf16 v[96:99], v[158:161], v[198:201], v[96:99]
	v_mfma_f32_16x16x32_bf16 v[84:87], v[150:153], v[206:209], v[84:87]
	v_mfma_f32_16x16x32_bf16 v[80:83], v[158:161], v[206:209], v[80:83]
	s_setprio 0
	s_setprio 1
	v_mfma_f32_16x16x32_bf16 v[108:111], v[162:165], v[178:181], v[108:111]
	v_mfma_f32_16x16x32_bf16 v[104:107], v[170:173], v[178:181], v[104:107]
	v_mfma_f32_16x16x32_bf16 v[92:95], v[162:165], v[186:189], v[92:95]
	v_mfma_f32_16x16x32_bf16 v[88:91], v[170:173], v[186:189], v[88:91]
	v_mfma_f32_16x16x32_bf16 v[76:79], v[162:165], v[194:197], v[76:79]
	v_mfma_f32_16x16x32_bf16 v[72:75], v[170:173], v[194:197], v[72:75]
	v_mfma_f32_16x16x32_bf16 v[68:71], v[162:165], v[202:205], v[68:71]
	v_mfma_f32_16x16x32_bf16 v[64:67], v[170:173], v[202:205], v[64:67]
	v_mfma_f32_16x16x32_bf16 v[108:111], v[166:169], v[182:185], v[108:111]
	v_mfma_f32_16x16x32_bf16 v[104:107], v[174:177], v[182:185], v[104:107]
	v_mfma_f32_16x16x32_bf16 v[92:95], v[166:169], v[190:193], v[92:95]
	v_mfma_f32_16x16x32_bf16 v[88:91], v[174:177], v[190:193], v[88:91]
	v_mfma_f32_16x16x32_bf16 v[76:79], v[166:169], v[198:201], v[76:79]
	v_mfma_f32_16x16x32_bf16 v[72:75], v[174:177], v[198:201], v[72:75]
	v_mfma_f32_16x16x32_bf16 v[68:71], v[166:169], v[206:209], v[68:71]
	v_mfma_f32_16x16x32_bf16 v[64:67], v[174:177], v[206:209], v[64:67]
	s_setprio 0
	s_barrier
; #define PG8_STAGE(bufoff, gbase, voff) do { _Pragma("unroll") for (int _i = 0; _i < 2; ++_i) \
;         __builtin_amdgcn_global_load_lds((const unsigned*)((const char*)(gbase) + (voff)[_i]), (PG8_LAS unsigned*)(lds + (bufoff) + ldsw + _i * 8192), 16, 0, 0); } while (0)
; #define PG8_STAGE_A(bufoff, gbase, h, nx) do { _Pragma("unroll") for (int _i = 0; _i < 2; ++_i) { \
;         const unsigned vo_ = GA ? ((nx) ? vgn[h][_i] : vgc[h][_i]) : voffA[_i]; \
;         __builtin_amdgcn_global_load_lds((const unsigned*)((const char*)(gbase) + vo_), (PG8_LAS unsigned*)(lds + (bufoff) + ldsw + _i * 8192), 16, 0, 0); } } while (0)
; #define PG8_LDA(dst, b, h) do { _Pragma("unroll") for (int m = 0; m < 4; ++m) _Pragma("unroll") for (int k = 0; k < 2; ++k) dst[m][k] = *(const PG8_LAS bf16x8*)(lds + PG8_SA(b, h) + aoff + m * 2048 + k * 1024); } while (0)
; #define PG8_MMA(ai, bj, At, Bt) do { __builtin_amdgcn_s_setprio(1); _Pragma("unroll") for (int m = 0; m < 4; ++m) _Pragma("unroll") for (int n = 0; n < 2; ++n) _Pragma("unroll") for (int k = 0; k < 2; ++k) \
;         acc[ai][bj][m][n] = __builtin_amdgcn_mfma_f32_16x16x32_bf16(Bt[n][k], At[m][k], acc[ai][bj][m][n], 0, 0, 0); __builtin_amdgcn_s_setprio(0); } while (0)
; #define PG8_WAIT_V(n) asm volatile("s_waitcnt vmcnt(" #n ")" ::: "memory")
; #define PG8_WAIT_L(n) asm volatile("s_waitcnt lgkmcnt(" #n ")" ::: "memory")
; #define PG8_BAR __builtin_amdgcn_s_barrier()
; #define PG8_SCHED __builtin_amdgcn_sched_barrier(0)
; template <class Epi, class Sched>
; __device__ __forceinline__ void gemm_phase(const int WID_, PG8_LAS unsigned char* lds, const Sched& S, const Epi& E) {
;     ...
;             PG8_LDA(At, 1, 1); PG8_STAGE(PG8_SB(1, 0), b3, voffB); PG8_STAGE(PG8_SB(1, 1), b3 + hstepB, voffB); PG8_STAGE_A(PG8_SA(1, 0), a3, 0, last);
;             PG8_WAIT_V(8); PG8_WAIT_L(0); PG8_BAR; PG8_MMA(1, 0, At, B0); PG8_MMA(1, 1, At, B1); PG8_BAR; PG8_SCHED;
;         }
	s_add_i32 s46, s68, s9
	v_lshl_add_u64 v[210:211], v[210:211], 0, s[2:3]
	s_mov_b32 m0, s46
	ds_read_b128 v[178:181], v145 offset:49152
	ds_read_b128 v[182:185], v145 offset:50176
	ds_read_b128 v[186:189], v145 offset:51200
	ds_read_b128 v[190:193], v145 offset:52224
	ds_read_b128 v[194:197], v145 offset:53248
	ds_read_b128 v[198:201], v145 offset:54272
	ds_read_b128 v[202:205], v145 offset:55296
	ds_read_b128 v[206:209], v145 offset:56320
	global_load_lds_dwordx4 v[210:211], off
	s_add_i32 m0, s46, 0x2000
	s_add_u32 s44, s44, 0x40080
	v_lshl_add_u64 v[210:211], v[212:213], 0, s[2:3]
	s_addc_u32 s45, s45, 0
	s_add_i32 s46, s69, s9
	global_load_lds_dwordx4 v[210:211], off
	v_lshl_add_u64 v[210:211], s[44:45], 0, v[130:131]
	s_mov_b32 m0, s46
	s_nop 0
	global_load_lds_dwordx4 v[210:211], off
	v_lshl_add_u64 v[210:211], s[44:45], 0, v[134:135]
	s_add_i32 m0, s46, 0x2000
	s_nop 0
	global_load_lds_dwordx4 v[210:211], off
	v_lshl_add_u64 v[210:211], v[214:215], 0, s[2:3]
	s_mov_b32 m0, s52
	s_nop 0
	global_load_lds_dwordx4 v[210:211], off
	v_lshl_add_u64 v[210:211], v[216:217], 0, s[2:3]
	s_mov_b32 m0, s53
	s_nop 0
	global_load_lds_dwordx4 v[210:211], off
	s_waitcnt vmcnt(8)
	s_waitcnt lgkmcnt(0)
	s_barrier
	s_setprio 1
	s_waitcnt lgkmcnt(0)
	v_mfma_f32_16x16x32_bf16 v[60:63], v[146:149], v[178:181], v[60:63]
	v_mfma_f32_16x16x32_bf16 v[56:59], v[154:157], v[178:181], v[56:59]
	v_mfma_f32_16x16x32_bf16 v[52:55], v[146:149], v[186:189], v[52:55]
	v_mfma_f32_16x16x32_bf16 v[48:51], v[154:157], v[186:189], v[48:51]
	v_mfma_f32_16x16x32_bf16 v[36:39], v[146:149], v[194:197], v[36:39]
	v_mfma_f32_16x16x32_bf16 v[32:35], v[154:157], v[194:197], v[32:35]
	v_mfma_f32_16x16x32_bf16 v[20:23], v[146:149], v[202:205], v[20:23]
	v_mfma_f32_16x16x32_bf16 v[16:19], v[154:157], v[202:205], v[16:19]
	v_mfma_f32_16x16x32_bf16 v[60:63], v[150:153], v[182:185], v[60:63]
	v_mfma_f32_16x16x32_bf16 v[56:59], v[158:161], v[182:185], v[56:59]
	v_mfma_f32_16x16x32_bf16 v[52:55], v[150:153], v[190:193], v[52:55]
	v_mfma_f32_16x16x32_bf16 v[48:51], v[158:161], v[190:193], v[48:51]
	v_mfma_f32_16x16x32_bf16 v[36:39], v[150:153], v[198:201], v[36:39]
	v_mfma_f32_16x16x32_bf16 v[32:35], v[158:161], v[198:201], v[32:35]
	v_mfma_f32_16x16x32_bf16 v[20:23], v[150:153], v[206:209], v[20:23]
	v_mfma_f32_16x16x32_bf16 v[16:19], v[158:161], v[206:209], v[16:19]
	s_setprio 0
	s_setprio 1
	v_mfma_f32_16x16x32_bf16 v[44:47], v[162:165], v[178:181], v[44:47]
	v_mfma_f32_16x16x32_bf16 v[40:43], v[170:173], v[178:181], v[40:43]
	v_mfma_f32_16x16x32_bf16 v[28:31], v[162:165], v[186:189], v[28:31]
	v_mfma_f32_16x16x32_bf16 v[24:27], v[170:173], v[186:189], v[24:27]
	v_mfma_f32_16x16x32_bf16 v[12:15], v[162:165], v[194:197], v[12:15]
	v_mfma_f32_16x16x32_bf16 v[8:11], v[170:173], v[194:197], v[8:11]
	v_mfma_f32_16x16x32_bf16 v[4:7], v[162:165], v[202:205], v[4:7]
	v_mfma_f32_16x16x32_bf16 v[0:3], v[170:173], v[202:205], v[0:3]
	v_mfma_f32_16x16x32_bf16 v[44:47], v[166:169], v[182:185], v[44:47]
	v_mfma_f32_16x16x32_bf16 v[40:43], v[174:177], v[182:185], v[40:43]
	v_mfma_f32_16x16x32_bf16 v[28:31], v[166:169], v[190:193], v[28:31]
	v_mfma_f32_16x16x32_bf16 v[24:27], v[174:177], v[190:193], v[24:27]
	v_mfma_f32_16x16x32_bf16 v[12:15], v[166:169], v[198:201], v[12:15]
	v_mfma_f32_16x16x32_bf16 v[8:11], v[174:177], v[198:201], v[8:11]
	v_mfma_f32_16x16x32_bf16 v[4:7], v[166:169], v[206:209], v[4:7]
	v_mfma_f32_16x16x32_bf16 v[0:3], v[174:177], v[206:209], v[0:3]
	s_setprio 0
	s_barrier
	s_add_i32 s67, s67, 2
	s_add_u32 s42, s42, 0x100
	s_addc_u32 s43, s43, 0
	s_add_u32 s63, s63, 0x100
	s_addc_u32 s66, s66, 0
	s_cmp_gt_u32 s67, 13
	s_cbranch_scc0 .LBB0_1786
	s_and_b64 vcc, exec, s[4:5]
	s_cbranch_vccz .LBB0_1789
	s_barrier

; #define PG8_STAGE(bufoff, gbase, voff) do { _Pragma("unroll") for (int _i = 0; _i < 2; ++_i) \
;         __builtin_amdgcn_global_load_lds((const unsigned*)((const char*)(gbase) + (voff)[_i]), (PG8_LAS unsigned*)(lds + (bufoff) + ldsw + _i * 8192), 16, 0, 0); } while (0)
; #define PG8_STAGE_A(bufoff, gbase, h, nx) do { _Pragma("unroll") for (int _i = 0; _i < 2; ++_i) { \
;         const unsigned vo_ = GA ? ((nx) ? vgn[h][_i] : vgc[h][_i]) : voffA[_i]; \
;         __builtin_amdgcn_global_load_lds((const unsigned*)((const char*)(gbase) + vo_), (PG8_LAS unsigned*)(lds + (bufoff) + ldsw + _i * 8192), 16, 0, 0); } } while (0)
; #define PG8_LDA(dst, b, h) do { _Pragma("unroll") for (int m = 0; m < 4; ++m) _Pragma("unroll") for (int k = 0; k < 2; ++k) dst[m][k] = *(const PG8_LAS bf16x8*)(lds + PG8_SA(b, h) + aoff + m * 2048 + k * 1024); } while (0)
; #define PG8_LDB(dst, b, h) do { _Pragma("unroll") for (int n = 0; n < 2; ++n) _Pragma("unroll") for (int k = 0; k < 2; ++k) dst[n][k] = *(const PG8_LAS bf16x8*)(lds + PG8_SB(b, h) + boff + n * 2048 + k * 1024); } while (0)
; #define PG8_MMA(ai, bj, At, Bt) do { __builtin_amdgcn_s_setprio(1); _Pragma("unroll") for (int m = 0; m < 4; ++m) _Pragma("unroll") for (int n = 0; n < 2; ++n) _Pragma("unroll") for (int k = 0; k < 2; ++k) \
;         acc[ai][bj][m][n] = __builtin_amdgcn_mfma_f32_16x16x32_bf16(Bt[n][k], At[m][k], acc[ai][bj][m][n], 0, 0, 0); __builtin_amdgcn_s_setprio(0); } while (0)
; #define PG8_WAIT_V(n) asm volatile("s_waitcnt vmcnt(" #n ")" ::: "memory")
; #define PG8_WAIT_L(n) asm volatile("s_waitcnt lgkmcnt(" #n ")" ::: "memory")
; #define PG8_BAR __builtin_amdgcn_s_barrier()
; #define PG8_SCHED __builtin_amdgcn_sched_barrier(0)
; template <class Epi, class Sched>
; __device__ __forceinline__ void gemm_phase(const int WID_, PG8_LAS unsigned char* lds, const Sched& S, const Epi& E) {
;     ...
;             PG8_LDB(B0, 0, 0); PG8_LDB(B1, 0, 1); PG8_SCHED; PG8_LDA(At, 0, 0); PG8_STAGE_A(PG8_SA(1, 1), a1 + hstepA, 1, false);
;             PG8_WAIT_V(8); PG8_WAIT_L(0); PG8_BAR; PG8_MMA(0, 0, At, B0); PG8_MMA(0, 1, At, B1); PG8_BAR; PG8_SCHED;
;             PG8_LDA(At, 0, 1); PG8_STAGE(PG8_SB(0, 0), b2, voffB); PG8_STAGE(PG8_SB(0, 1), b2 + hstepB, voffB); PG8_STAGE_A(PG8_SA(0, 0), a2, 0, last);
.LBB0_1810:
	ds_read_b128 v[146:149], v143
	ds_read_b128 v[150:153], v143 offset:1024
	ds_read_b128 v[154:157], v143 offset:2048
	ds_read_b128 v[158:161], v143 offset:3072
	ds_read_b128 v[162:165], v144
	ds_read_b128 v[166:169], v144 offset:1024
	ds_read_b128 v[170:173], v144 offset:2048
	ds_read_b128 v[174:177], v144 offset:3072
	s_add_u32 s44, s42, 0xfffc0080
	s_addc_u32 s45, s43, -1
	s_cmp_eq_u32 s68, 12
	s_cselect_b32 s47, s37, s45
	s_cselect_b32 s46, s62, s44
	s_cselect_b32 s45, s23, s67
	s_cselect_b32 s44, s63, s66
	v_lshl_add_u64 v[210:211], s[42:43], 0, v[136:137]
	s_add_i32 m0, s48, 0xc000
	ds_read_b128 v[178:181], v145
	ds_read_b128 v[182:185], v145 offset:1024
	ds_read_b128 v[186:189], v145 offset:2048
	ds_read_b128 v[190:193], v145 offset:3072
	ds_read_b128 v[194:197], v145 offset:4096
	ds_read_b128 v[198:201], v145 offset:5120
	ds_read_b128 v[202:205], v145 offset:6144
	ds_read_b128 v[206:209], v145 offset:7168
	global_load_lds_dwordx4 v[210:211], off
	v_lshl_add_u64 v[210:211], s[42:43], 0, v[138:139]
	s_add_i32 m0, s48, 0xe000
	s_nop 0
	global_load_lds_dwordx4 v[210:211], off
	s_waitcnt vmcnt(8)
	s_waitcnt lgkmcnt(0)
	s_barrier
	s_setprio 1
	s_waitcnt lgkmcnt(0)
	v_mfma_f32_16x16x32_bf16 v[124:127], v[146:149], v[178:181], v[124:127]
	v_mfma_f32_16x16x32_bf16 v[120:123], v[154:157], v[178:181], v[120:123]
	v_mfma_f32_16x16x32_bf16 v[116:119], v[146:149], v[186:189], v[116:119]
	v_mfma_f32_16x16x32_bf16 v[112:115], v[154:157], v[186:189], v[112:115]
	v_mfma_f32_16x16x32_bf16 v[100:103], v[146:149], v[194:197], v[100:103]
	v_mfma_f32_16x16x32_bf16 v[96:99], v[154:157], v[194:197], v[96:99]
	v_mfma_f32_16x16x32_bf16 v[84:87], v[146:149], v[202:205], v[84:87]
	v_mfma_f32_16x16x32_bf16 v[80:83], v[154:157], v[202:205], v[80:83]
	v_mfma_f32_16x16x32_bf16 v[124:127], v[150:153], v[182:185], v[124:127]
	v_mfma_f32_16x16x32_bf16 v[120:123], v[158:161], v[182:185], v[120:123]
	v_mfma_f32_16x16x32_bf16 v[116:119], v[150:153], v[190:193], v[116:119]
	v_mfma_f32_16x16x32_bf16 v[112:115], v[158:161], v[190:193], v[112:115]
	v_mfma_f32_16x16x32_bf16 v[100:103], v[150:153], v[198:201], v[100:103]
	v_mfma_f32_16x16x32_bf16 v[96:99], v[158:161], v[198:201], v[96:99]
	v_mfma_f32_16x16x32_bf16 v[84:87], v[150:153], v[206:209], v[84:87]
	v_mfma_f32_16x16x32_bf16 v[80:83], v[158:161], v[206:209], v[80:83]
	s_setprio 0
	s_setprio 1
	v_mfma_f32_16x16x32_bf16 v[108:111], v[162:165], v[178:181], v[108:111]
	v_mfma_f32_16x16x32_bf16 v[104:107], v[170:173], v[178:181], v[104:107]
	v_mfma_f32_16x16x32_bf16 v[92:95], v[162:165], v[186:189], v[92:95]
	v_mfma_f32_16x16x32_bf16 v[88:91], v[170:173], v[186:189], v[88:91]
	v_mfma_f32_16x16x32_bf16 v[76:79], v[162:165], v[194:197], v[76:79]
	v_mfma_f32_16x16x32_bf16 v[72:75], v[170:173], v[194:197], v[72:75]
	v_mfma_f32_16x16x32_bf16 v[68:71], v[162:165], v[202:205], v[68:71]
	v_mfma_f32_16x16x32_bf16 v[64:67], v[170:173], v[202:205], v[64:67]
	v_mfma_f32_16x16x32_bf16 v[108:111], v[166:169], v[182:185], v[108:111]
	v_mfma_f32_16x16x32_bf16 v[104:107], v[174:177], v[182:185], v[104:107]
	v_mfma_f32_16x16x32_bf16 v[92:95], v[166:169], v[190:193], v[92:95]
	v_mfma_f32_16x16x32_bf16 v[88:91], v[174:177], v[190:193], v[88:91]
	v_mfma_f32_16x16x32_bf16 v[76:79], v[166:169], v[198:201], v[76:79]
	v_mfma_f32_16x16x32_bf16 v[72:75], v[174:177], v[198:201], v[72:75]
	v_mfma_f32_16x16x32_bf16 v[68:71], v[166:169], v[206:209], v[68:71]
	v_mfma_f32_16x16x32_bf16 v[64:67], v[174:177], v[206:209], v[64:67]
	s_setprio 0
	s_barrier
	s_add_i32 s69, s60, s33
	v_lshl_add_u64 v[210:211], s[44:45], 0, v[130:131]
	s_mov_b32 m0, s69
	ds_read_b128 v[178:181], v145 offset:16384
	ds_read_b128 v[182:185], v145 offset:17408
	ds_read_b128 v[186:189], v145 offset:18432
	ds_read_b128 v[190:193], v145 offset:19456
	ds_read_b128 v[194:197], v145 offset:20480
	ds_read_b128 v[198:201], v145 offset:21504
	ds_read_b128 v[202:205], v145 offset:22528
	ds_read_b128 v[206:209], v145 offset:23552
	global_load_lds_dwordx4 v[210:211], off
	s_add_i32 m0, s69, 0x2000
	s_add_u32 s70, s44, 0x40000
	v_lshl_add_u64 v[212:213], s[44:45], 0, v[134:135]
	s_addc_u32 s71, s45, 0
	s_add_i32 s69, s61, s33
	global_load_lds_dwordx4 v[212:213], off
	v_lshl_add_u64 v[214:215], s[70:71], 0, v[130:131]
	s_mov_b32 m0, s69
	v_lshl_add_u64 v[216:217], s[46:47], 0, v[132:133]
	global_load_lds_dwordx4 v[214:215], off
	v_lshl_add_u64 v[214:215], s[70:71], 0, v[134:135]
	s_add_i32 m0, s69, 0x2000
	s_nop 0
	global_load_lds_dwordx4 v[214:215], off
	v_lshl_add_u64 v[214:215], s[46:47], 0, v[128:129]
	s_mov_b32 m0, s48
	s_nop 0
	global_load_lds_dwordx4 v[214:215], off
	s_mov_b32 m0, s49
	s_nop 0
	global_load_lds_dwordx4 v[216:217], off
	s_waitcnt vmcnt(8)
	s_waitcnt lgkmcnt(0)
	s_barrier
; #define PG8_STAGE_A(bufoff, gbase, h, nx) do { _Pragma("unroll") for (int _i = 0; _i < 2; ++_i) { \
;         const unsigned vo_ = GA ? ((nx) ? vgn[h][_i] : vgc[h][_i]) : voffA[_i]; \
;         __builtin_amdgcn_global_load_lds((const unsigned*)((const char*)(gbase) + vo_), (PG8_LAS unsigned*)(lds + (bufoff) + ldsw + _i * 8192), 16, 0, 0); } } while (0)
; #define PG8_LDA(dst, b, h) do { _Pragma("unroll") for (int m = 0; m < 4; ++m) _Pragma("unroll") for (int k = 0; k < 2; ++k) dst[m][k] = *(const PG8_LAS bf16x8*)(lds + PG8_SA(b, h) + aoff + m * 2048 + k * 1024); } while (0)
; #define PG8_LDB(dst, b, h) do { _Pragma("unroll") for (int n = 0; n < 2; ++n) _Pragma("unroll") for (int k = 0; k < 2; ++k) dst[n][k] = *(const PG8_LAS bf16x8*)(lds + PG8_SB(b, h) + boff + n * 2048 + k * 1024); } while (0)
; #define PG8_MMA(ai, bj, At, Bt) do { __builtin_amdgcn_s_setprio(1); _Pragma("unroll") for (int m = 0; m < 4; ++m) _Pragma("unroll") for (int n = 0; n < 2; ++n) _Pragma("unroll") for (int k = 0; k < 2; ++k) \
;         acc[ai][bj][m][n] = __builtin_amdgcn_mfma_f32_16x16x32_bf16(Bt[n][k], At[m][k], acc[ai][bj][m][n], 0, 0, 0); __builtin_amdgcn_s_setprio(0); } while (0)
; #define PG8_WAIT_V(n) asm volatile("s_waitcnt vmcnt(" #n ")" ::: "memory")
; #define PG8_WAIT_L(n) asm volatile("s_waitcnt lgkmcnt(" #n ")" ::: "memory")
; #define PG8_BAR __builtin_amdgcn_s_barrier()
; #define PG8_SCHED __builtin_amdgcn_sched_barrier(0)
; template <class Epi, class Sched>
; __device__ __forceinline__ void gemm_phase(const int WID_, PG8_LAS unsigned char* lds, const Sched& S, const Epi& E) {
;     ...
;             PG8_WAIT_V(8); PG8_WAIT_L(0); PG8_BAR; PG8_MMA(1, 0, At, B0); PG8_MMA(1, 1, At, B1); PG8_BAR; PG8_SCHED;
;             PG8_LDB(B0, 1, 0); PG8_LDB(B1, 1, 1); PG8_SCHED; PG8_LDA(At, 1, 0); PG8_STAGE_A(PG8_SA(0, 1), a2 + hstepA, 1, last);
;             PG8_WAIT_V(8); PG8_WAIT_L(0); PG8_BAR; PG8_MMA(0, 0, At, B0); PG8_MMA(0, 1, At, B1); PG8_BAR; PG8_SCHED;
	s_nop 0
	s_setprio 1
	s_waitcnt lgkmcnt(0)
	v_mfma_f32_16x16x32_bf16 v[60:63], v[146:149], v[178:181], v[60:63]
	v_mfma_f32_16x16x32_bf16 v[56:59], v[154:157], v[178:181], v[56:59]
	v_mfma_f32_16x16x32_bf16 v[52:55], v[146:149], v[186:189], v[52:55]
	v_mfma_f32_16x16x32_bf16 v[48:51], v[154:157], v[186:189], v[48:51]
	v_mfma_f32_16x16x32_bf16 v[36:39], v[146:149], v[194:197], v[36:39]
	v_mfma_f32_16x16x32_bf16 v[32:35], v[154:157], v[194:197], v[32:35]
	v_mfma_f32_16x16x32_bf16 v[20:23], v[146:149], v[202:205], v[20:23]
	v_mfma_f32_16x16x32_bf16 v[16:19], v[154:157], v[202:205], v[16:19]
	v_mfma_f32_16x16x32_bf16 v[60:63], v[150:153], v[182:185], v[60:63]
	v_mfma_f32_16x16x32_bf16 v[56:59], v[158:161], v[182:185], v[56:59]
	v_mfma_f32_16x16x32_bf16 v[52:55], v[150:153], v[190:193], v[52:55]
	v_mfma_f32_16x16x32_bf16 v[48:51], v[158:161], v[190:193], v[48:51]
	v_mfma_f32_16x16x32_bf16 v[36:39], v[150:153], v[198:201], v[36:39]
	v_mfma_f32_16x16x32_bf16 v[32:35], v[158:161], v[198:201], v[32:35]
	v_mfma_f32_16x16x32_bf16 v[20:23], v[150:153], v[206:209], v[20:23]
	v_mfma_f32_16x16x32_bf16 v[16:19], v[158:161], v[206:209], v[16:19]
	s_setprio 0
	s_setprio 1
	v_mfma_f32_16x16x32_bf16 v[44:47], v[162:165], v[178:181], v[44:47]
	v_mfma_f32_16x16x32_bf16 v[40:43], v[170:173], v[178:181], v[40:43]
	v_mfma_f32_16x16x32_bf16 v[28:31], v[162:165], v[186:189], v[28:31]
	v_mfma_f32_16x16x32_bf16 v[24:27], v[170:173], v[186:189], v[24:27]
	v_mfma_f32_16x16x32_bf16 v[12:15], v[162:165], v[194:197], v[12:15]
	v_mfma_f32_16x16x32_bf16 v[8:11], v[170:173], v[194:197], v[8:11]
	v_mfma_f32_16x16x32_bf16 v[4:7], v[162:165], v[202:205], v[4:7]
	v_mfma_f32_16x16x32_bf16 v[0:3], v[170:173], v[202:205], v[0:3]
	v_mfma_f32_16x16x32_bf16 v[44:47], v[166:169], v[182:185], v[44:47]
	v_mfma_f32_16x16x32_bf16 v[40:43], v[174:177], v[182:185], v[40:43]
	v_mfma_f32_16x16x32_bf16 v[28:31], v[166:169], v[190:193], v[28:31]
	v_mfma_f32_16x16x32_bf16 v[24:27], v[174:177], v[190:193], v[24:27]
	v_mfma_f32_16x16x32_bf16 v[12:15], v[166:169], v[198:201], v[12:15]
	v_mfma_f32_16x16x32_bf16 v[8:11], v[174:177], v[198:201], v[8:11]
	v_mfma_f32_16x16x32_bf16 v[4:7], v[166:169], v[206:209], v[4:7]
	v_mfma_f32_16x16x32_bf16 v[0:3], v[174:177], v[206:209], v[0:3]
	s_setprio 0
	s_barrier
	s_add_i32 s69, 0, 0x18000
	s_add_i32 s70, 0, 0x1c000
	v_add_u32_e32 v158, s69, v141
	v_add_u32_e32 v174, s70, v141
	ds_read_b128 v[146:149], v158
	ds_read_b128 v[150:153], v158 offset:1024
	ds_read_b128 v[154:157], v158 offset:2048
	ds_read_b128 v[158:161], v158 offset:3072
	ds_read_b128 v[162:165], v174
	ds_read_b128 v[166:169], v174 offset:1024
	ds_read_b128 v[170:173], v174 offset:2048
	ds_read_b128 v[174:177], v174 offset:3072
	s_add_u32 s46, s46, 0x40000
	s_addc_u32 s47, s47, 0
	s_mov_b32 m0, s50
	v_lshl_add_u64 v[218:219], s[46:47], 0, v[128:129]
	ds_read_b128 v[178:181], v145 offset:32768
	ds_read_b128 v[182:185], v145 offset:33792
	ds_read_b128 v[186:189], v145 offset:34816
	ds_read_b128 v[190:193], v145 offset:35840
	ds_read_b128 v[194:197], v145 offset:36864
	ds_read_b128 v[198:201], v145 offset:37888
	ds_read_b128 v[202:205], v145 offset:38912
	ds_read_b128 v[206:209], v145 offset:39936
	global_load_lds_dwordx4 v[218:219], off
	v_lshl_add_u64 v[218:219], s[46:47], 0, v[132:133]
	s_mov_b32 m0, s51
	s_nop 0
	global_load_lds_dwordx4 v[218:219], off
	s_waitcnt vmcnt(8)
	s_waitcnt lgkmcnt(0)
	s_barrier
	s_nop 0
	s_setprio 1
	s_waitcnt lgkmcnt(0)
	v_mfma_f32_16x16x32_bf16 v[124:127], v[146:149], v[178:181], v[124:127]
	v_mfma_f32_16x16x32_bf16 v[120:123], v[154:157], v[178:181], v[120:123]
	v_mfma_f32_16x16x32_bf16 v[116:119], v[146:149], v[186:189], v[116:119]
	v_mfma_f32_16x16x32_bf16 v[112:115], v[154:157], v[186:189], v[112:115]
	v_mfma_f32_16x16x32_bf16 v[100:103], v[146:149], v[194:197], v[100:103]
	v_mfma_f32_16x16x32_bf16 v[96:99], v[154:157], v[194:197], v[96:99]
	v_mfma_f32_16x16x32_bf16 v[84:87], v[146:149], v[202:205], v[84:87]
	v_mfma_f32_16x16x32_bf16 v[80:83], v[154:157], v[202:205], v[80:83]
	v_mfma_f32_16x16x32_bf16 v[124:127], v[150:153], v[182:185], v[124:127]
	v_mfma_f32_16x16x32_bf16 v[120:123], v[158:161], v[182:185], v[120:123]
	v_mfma_f32_16x16x32_bf16 v[116:119], v[150:153], v[190:193], v[116:119]
	v_mfma_f32_16x16x32_bf16 v[112:115], v[158:161], v[190:193], v[112:115]
	v_mfma_f32_16x16x32_bf16 v[100:103], v[150:153], v[198:201], v[100:103]
	v_mfma_f32_16x16x32_bf16 v[96:99], v[158:161], v[198:201], v[96:99]
	v_mfma_f32_16x16x32_bf16 v[84:87], v[150:153], v[206:209], v[84:87]
	v_mfma_f32_16x16x32_bf16 v[80:83], v[158:161], v[206:209], v[80:83]
	s_setprio 0
	s_setprio 1
	v_mfma_f32_16x16x32_bf16 v[108:111], v[162:165], v[178:181], v[108:111]
	v_mfma_f32_16x16x32_bf16 v[104:107], v[170:173], v[178:181], v[104:107]
	v_mfma_f32_16x16x32_bf16 v[92:95], v[162:165], v[186:189], v[92:95]
	v_mfma_f32_16x16x32_bf16 v[88:91], v[170:173], v[186:189], v[88:91]
	v_mfma_f32_16x16x32_bf16 v[76:79], v[162:165], v[194:197], v[76:79]
	v_mfma_f32_16x16x32_bf16 v[72:75], v[170:173], v[194:197], v[72:75]
	v_mfma_f32_16x16x32_bf16 v[68:71], v[162:165], v[202:205], v[68:71]
	v_mfma_f32_16x16x32_bf16 v[64:67], v[170:173], v[202:205], v[64:67]
	v_mfma_f32_16x16x32_bf16 v[108:111], v[166:169], v[182:185], v[108:111]
	v_mfma_f32_16x16x32_bf16 v[104:107], v[174:177], v[182:185], v[104:107]
	v_mfma_f32_16x16x32_bf16 v[92:95], v[166:169], v[190:193], v[92:95]
	v_mfma_f32_16x16x32_bf16 v[88:91], v[174:177], v[190:193], v[88:91]
	v_mfma_f32_16x16x32_bf16 v[76:79], v[166:169], v[198:201], v[76:79]
	v_mfma_f32_16x16x32_bf16 v[72:75], v[174:177], v[198:201], v[72:75]
	v_mfma_f32_16x16x32_bf16 v[68:71], v[166:169], v[206:209], v[68:71]
	v_mfma_f32_16x16x32_bf16 v[64:67], v[174:177], v[206:209], v[64:67]
	s_setprio 0
	s_barrier
; #define PG8_STAGE(bufoff, gbase, voff) do { _Pragma("unroll") for (int _i = 0; _i < 2; ++_i) \
;         __builtin_amdgcn_global_load_lds((const unsigned*)((const char*)(gbase) + (voff)[_i]), (PG8_LAS unsigned*)(lds + (bufoff) + ldsw + _i * 8192), 16, 0, 0); } while (0)
; #define PG8_STAGE_A(bufoff, gbase, h, nx) do { _Pragma("unroll") for (int _i = 0; _i < 2; ++_i) { \
;         const unsigned vo_ = GA ? ((nx) ? vgn[h][_i] : vgc[h][_i]) : voffA[_i]; \
;         __builtin_amdgcn_global_load_lds((const unsigned*)((const char*)(gbase) + vo_), (PG8_LAS unsigned*)(lds + (bufoff) + ldsw + _i * 8192), 16, 0, 0); } } while (0)
; #define PG8_LDA(dst, b, h) do { _Pragma("unroll") for (int m = 0; m < 4; ++m) _Pragma("unroll") for (int k = 0; k < 2; ++k) dst[m][k] = *(const PG8_LAS bf16x8*)(lds + PG8_SA(b, h) + aoff + m * 2048 + k * 1024); } while (0)
; #define PG8_MMA(ai, bj, At, Bt) do { __builtin_amdgcn_s_setprio(1); _Pragma("unroll") for (int m = 0; m < 4; ++m) _Pragma("unroll") for (int n = 0; n < 2; ++n) _Pragma("unroll") for (int k = 0; k < 2; ++k) \
;         acc[ai][bj][m][n] = __builtin_amdgcn_mfma_f32_16x16x32_bf16(Bt[n][k], At[m][k], acc[ai][bj][m][n], 0, 0, 0); __builtin_amdgcn_s_setprio(0); } while (0)
; #define PG8_WAIT_V(n) asm volatile("s_waitcnt vmcnt(" #n ")" ::: "memory")
; #define PG8_WAIT_L(n) asm volatile("s_waitcnt lgkmcnt(" #n ")" ::: "memory")
; #define PG8_BAR __builtin_amdgcn_s_barrier()
; #define PG8_SCHED __builtin_amdgcn_sched_barrier(0)
; template <class Epi, class Sched>
; __device__ __forceinline__ void gemm_phase(const int WID_, PG8_LAS unsigned char* lds, const Sched& S, const Epi& E) {
;     ...
;             PG8_LDA(At, 1, 1); PG8_STAGE(PG8_SB(1, 0), b3, voffB); PG8_STAGE(PG8_SB(1, 1), b3 + hstepB, voffB); PG8_STAGE_A(PG8_SA(1, 0), a3, 0, last);
;             PG8_WAIT_V(8); PG8_WAIT_L(0); PG8_BAR; PG8_MMA(1, 0, At, B0); PG8_MMA(1, 1, At, B1); PG8_BAR; PG8_SCHED;
;         }
;         if (wr == 0) PG8_BAR;
	s_add_i32 s46, s69, s33
	v_lshl_add_u64 v[210:211], v[210:211], 0, s[2:3]
	s_mov_b32 m0, s46
	ds_read_b128 v[178:181], v145 offset:49152
	ds_read_b128 v[182:185], v145 offset:50176
	ds_read_b128 v[186:189], v145 offset:51200
	ds_read_b128 v[190:193], v145 offset:52224
	ds_read_b128 v[194:197], v145 offset:53248
	ds_read_b128 v[198:201], v145 offset:54272
	ds_read_b128 v[202:205], v145 offset:55296
	ds_read_b128 v[206:209], v145 offset:56320
	global_load_lds_dwordx4 v[210:211], off
	s_add_i32 m0, s46, 0x2000
	s_add_u32 s44, s44, 0x40080
	v_lshl_add_u64 v[210:211], v[212:213], 0, s[2:3]
	s_addc_u32 s45, s45, 0
	s_add_i32 s46, s70, s33
	global_load_lds_dwordx4 v[210:211], off
	v_lshl_add_u64 v[210:211], s[44:45], 0, v[130:131]
	s_mov_b32 m0, s46
	s_nop 0
	global_load_lds_dwordx4 v[210:211], off
	v_lshl_add_u64 v[210:211], s[44:45], 0, v[134:135]
	s_add_i32 m0, s46, 0x2000
	s_nop 0
	global_load_lds_dwordx4 v[210:211], off
	v_lshl_add_u64 v[210:211], v[214:215], 0, s[2:3]
	s_mov_b32 m0, s53
	s_nop 0
	global_load_lds_dwordx4 v[210:211], off
	v_lshl_add_u64 v[210:211], v[216:217], 0, s[2:3]
	s_mov_b32 m0, s58
	s_nop 0
	global_load_lds_dwordx4 v[210:211], off
	s_waitcnt vmcnt(8)
	s_waitcnt lgkmcnt(0)
	s_barrier
	s_setprio 1
	s_waitcnt lgkmcnt(0)
	v_mfma_f32_16x16x32_bf16 v[60:63], v[146:149], v[178:181], v[60:63]
	v_mfma_f32_16x16x32_bf16 v[56:59], v[154:157], v[178:181], v[56:59]
	v_mfma_f32_16x16x32_bf16 v[52:55], v[146:149], v[186:189], v[52:55]
	v_mfma_f32_16x16x32_bf16 v[48:51], v[154:157], v[186:189], v[48:51]
	v_mfma_f32_16x16x32_bf16 v[36:39], v[146:149], v[194:197], v[36:39]
	v_mfma_f32_16x16x32_bf16 v[32:35], v[154:157], v[194:197], v[32:35]
	v_mfma_f32_16x16x32_bf16 v[20:23], v[146:149], v[202:205], v[20:23]
	v_mfma_f32_16x16x32_bf16 v[16:19], v[154:157], v[202:205], v[16:19]
	v_mfma_f32_16x16x32_bf16 v[60:63], v[150:153], v[182:185], v[60:63]
	v_mfma_f32_16x16x32_bf16 v[56:59], v[158:161], v[182:185], v[56:59]
	v_mfma_f32_16x16x32_bf16 v[52:55], v[150:153], v[190:193], v[52:55]
	v_mfma_f32_16x16x32_bf16 v[48:51], v[158:161], v[190:193], v[48:51]
	v_mfma_f32_16x16x32_bf16 v[36:39], v[150:153], v[198:201], v[36:39]
	v_mfma_f32_16x16x32_bf16 v[32:35], v[158:161], v[198:201], v[32:35]
	v_mfma_f32_16x16x32_bf16 v[20:23], v[150:153], v[206:209], v[20:23]
	v_mfma_f32_16x16x32_bf16 v[16:19], v[158:161], v[206:209], v[16:19]
	s_setprio 0
	s_setprio 1
	v_mfma_f32_16x16x32_bf16 v[44:47], v[162:165], v[178:181], v[44:47]
	v_mfma_f32_16x16x32_bf16 v[40:43], v[170:173], v[178:181], v[40:43]
	v_mfma_f32_16x16x32_bf16 v[28:31], v[162:165], v[186:189], v[28:31]
	v_mfma_f32_16x16x32_bf16 v[24:27], v[170:173], v[186:189], v[24:27]
	v_mfma_f32_16x16x32_bf16 v[12:15], v[162:165], v[194:197], v[12:15]
	v_mfma_f32_16x16x32_bf16 v[8:11], v[170:173], v[194:197], v[8:11]
	v_mfma_f32_16x16x32_bf16 v[4:7], v[162:165], v[202:205], v[4:7]
	v_mfma_f32_16x16x32_bf16 v[0:3], v[170:173], v[202:205], v[0:3]
	v_mfma_f32_16x16x32_bf16 v[44:47], v[166:169], v[182:185], v[44:47]
	v_mfma_f32_16x16x32_bf16 v[40:43], v[174:177], v[182:185], v[40:43]
	v_mfma_f32_16x16x32_bf16 v[28:31], v[166:169], v[190:193], v[28:31]
	v_mfma_f32_16x16x32_bf16 v[24:27], v[174:177], v[190:193], v[24:27]
	v_mfma_f32_16x16x32_bf16 v[12:15], v[166:169], v[198:201], v[12:15]
	v_mfma_f32_16x16x32_bf16 v[8:11], v[174:177], v[198:201], v[8:11]
	v_mfma_f32_16x16x32_bf16 v[4:7], v[166:169], v[206:209], v[4:7]
	v_mfma_f32_16x16x32_bf16 v[0:3], v[174:177], v[206:209], v[0:3]
	s_setprio 0
	s_barrier
	s_add_i32 s68, s68, 2
	s_add_u32 s42, s42, 0x100
	s_addc_u32 s43, s43, 0
	s_add_u32 s66, s66, 0x100
	s_addc_u32 s67, s67, 0
	s_cmp_gt_u32 s68, 13
	s_cbranch_scc0 .LBB0_1810
	s_and_b64 vcc, exec, s[4:5]
	s_cbranch_vccz .LBB0_1813
	s_barrier

; #define PG8_STAGE(bufoff, gbase, voff) do { _Pragma("unroll") for (int _i = 0; _i < 2; ++_i) \
;         __builtin_amdgcn_global_load_lds((const unsigned*)((const char*)(gbase) + (voff)[_i]), (PG8_LAS unsigned*)(lds + (bufoff) + ldsw + _i * 8192), 16, 0, 0); } while (0)
; #define PG8_STAGE_A(bufoff, gbase, h, nx) do { _Pragma("unroll") for (int _i = 0; _i < 2; ++_i) { \
;         const unsigned vo_ = GA ? ((nx) ? vgn[h][_i] : vgc[h][_i]) : voffA[_i]; \
;         __builtin_amdgcn_global_load_lds((const unsigned*)((const char*)(gbase) + vo_), (PG8_LAS unsigned*)(lds + (bufoff) + ldsw + _i * 8192), 16, 0, 0); } } while (0)
; #define PG8_LDA(dst, b, h) do { _Pragma("unroll") for (int m = 0; m < 4; ++m) _Pragma("unroll") for (int k = 0; k < 2; ++k) dst[m][k] = *(const PG8_LAS bf16x8*)(lds + PG8_SA(b, h) + aoff + m * 2048 + k * 1024); } while (0)
; #define PG8_LDB(dst, b, h) do { _Pragma("unroll") for (int n = 0; n < 2; ++n) _Pragma("unroll") for (int k = 0; k < 2; ++k) dst[n][k] = *(const PG8_LAS bf16x8*)(lds + PG8_SB(b, h) + boff + n * 2048 + k * 1024); } while (0)
; #define PG8_WAIT_V(n) asm volatile("s_waitcnt vmcnt(" #n ")" ::: "memory")
; #define PG8_WAIT_L(n) asm volatile("s_waitcnt lgkmcnt(" #n ")" ::: "memory")
; #define PG8_BAR __builtin_amdgcn_s_barrier()
; #define PG8_SCHED __builtin_amdgcn_sched_barrier(0)
; template <class Epi, class Sched>
; __device__ __forceinline__ void gemm_phase(const int WID_, PG8_LAS unsigned char* lds, const Sched& S, const Epi& E) {
;     ...
;         for (int t = 0; t < nt; t += 2) {
;             const bool last = (t == nt - 2);
;             const char* a1 = cA + (size_t)(t + 1) * kstep;
;             const char* a2 = last ? nA : cA + (size_t)(t + 2) * kstep; const char* b2 = last ? nB : cB + (size_t)(t + 2) * kstep;
;             const char* a3 = a2 + kstep; const char* b3 = b2 + kstep;
;             PG8_LDB(B0, 0, 0); PG8_LDB(B1, 0, 1); PG8_SCHED; PG8_LDA(At, 0, 0); PG8_STAGE_A(PG8_SA(1, 1), a1 + hstepA, 1, false);
;             PG8_WAIT_V(8); PG8_WAIT_L(0); PG8_BAR; PG8_MMA(0, 0, At, B0); PG8_MMA(0, 1, At, B1); PG8_BAR; PG8_SCHED;
;             PG8_LDA(At, 0, 1); PG8_STAGE(PG8_SB(0, 0), b2, voffB); PG8_STAGE(PG8_SB(0, 1), b2 + hstepB, voffB); PG8_STAGE_A(PG8_SA(0, 0), a2, 0, last);
;             PG8_WAIT_V(8); PG8_WAIT_L(0); PG8_BAR; PG8_MMA(1, 0, At, B0); PG8_MMA(1, 1, At, B1); PG8_BAR; PG8_SCHED;
.LBB0_1892:
	s_add_u32 s47, s50, s41
	s_addc_u32 s70, s51, 0
	s_add_u32 s66, s47, 0x100
	s_addc_u32 s67, s70, 0
	s_and_b64 s[62:63], s[60:61], exec
	s_cselect_b32 s67, s43, s67
	s_cselect_b32 s66, s42, s66
	s_add_u32 s41, s48, s41
	s_addc_u32 s62, s49, 0
	s_add_u32 s41, s41, 0x100
	s_addc_u32 s62, s62, 0
	s_and_b64 s[60:61], s[60:61], exec
	ds_read_b128 v[128:131], v157
	ds_read_b128 v[142:145], v157 offset:1024
	ds_read_b128 v[146:149], v157 offset:2048
	ds_read_b128 v[150:153], v157 offset:3072
	ds_read_b128 v[160:163], v158
	ds_read_b128 v[164:167], v158 offset:1024
	ds_read_b128 v[168:171], v158 offset:2048
	ds_read_b128 v[172:175], v158 offset:3072
	s_cselect_b32 s69, s45, s62
	s_cselect_b32 s68, s44, s41
	s_add_u32 s72, s47, 0x10080
	s_addc_u32 s73, s70, 0
	s_add_u32 s70, s68, 0x10000
	s_addc_u32 s71, s69, 0
	s_add_i32 s86, s80, 0x2000
	s_add_i32 s85, 0, 0x18000
	s_add_i32 s84, 0, 0x1c000
	s_add_u32 s62, s66, 0x10000
	s_addc_u32 s63, s67, 0
	s_add_i32 s83, s85, s8
	s_add_i32 s47, s83, 0x2000
	s_add_u32 s60, s68, 0x10080
	s_addc_u32 s61, s69, 0
	s_add_i32 s82, s84, s8
	s_add_i32 s41, s82, 0x2000
	s_mov_b32 m0, s76
	v_lshl_add_u64 v[208:209], s[72:73], 0, v[138:139]
	ds_read_b128 v[176:179], v159
	ds_read_b128 v[180:183], v159 offset:1024
	ds_read_b128 v[184:187], v159 offset:2048
	ds_read_b128 v[188:191], v159 offset:3072
	ds_read_b128 v[192:195], v159 offset:4096
	ds_read_b128 v[196:199], v159 offset:5120
	ds_read_b128 v[200:203], v159 offset:6144
	ds_read_b128 v[204:207], v159 offset:7168
	global_load_lds_dwordx4 v[208:209], off
	v_lshl_add_u64 v[208:209], s[72:73], 0, v[134:135]
	s_mov_b32 m0, s77
	s_nop 0
	global_load_lds_dwordx4 v[208:209], off
	s_waitcnt vmcnt(8)
	s_waitcnt lgkmcnt(0)
	s_barrier
	s_nop 0
	s_setprio 1
	s_waitcnt lgkmcnt(0)
	v_mfma_f32_16x16x32_bf16 v[124:127], v[128:131], v[176:179], v[124:127]
	v_mfma_f32_16x16x32_bf16 v[120:123], v[146:149], v[176:179], v[120:123]
	v_mfma_f32_16x16x32_bf16 v[108:111], v[128:131], v[184:187], v[108:111]
	v_mfma_f32_16x16x32_bf16 v[104:107], v[146:149], v[184:187], v[104:107]
	v_mfma_f32_16x16x32_bf16 v[92:95], v[128:131], v[192:195], v[92:95]
	v_mfma_f32_16x16x32_bf16 v[88:91], v[146:149], v[192:195], v[88:91]
	v_mfma_f32_16x16x32_bf16 v[76:79], v[128:131], v[200:203], v[76:79]
	v_mfma_f32_16x16x32_bf16 v[72:75], v[146:149], v[200:203], v[72:75]
	v_mfma_f32_16x16x32_bf16 v[124:127], v[142:145], v[180:183], v[124:127]
	v_mfma_f32_16x16x32_bf16 v[120:123], v[150:153], v[180:183], v[120:123]
	v_mfma_f32_16x16x32_bf16 v[108:111], v[142:145], v[188:191], v[108:111]
	v_mfma_f32_16x16x32_bf16 v[104:107], v[150:153], v[188:191], v[104:107]
	v_mfma_f32_16x16x32_bf16 v[92:95], v[142:145], v[196:199], v[92:95]
	v_mfma_f32_16x16x32_bf16 v[88:91], v[150:153], v[196:199], v[88:91]
	v_mfma_f32_16x16x32_bf16 v[76:79], v[142:145], v[204:207], v[76:79]
	v_mfma_f32_16x16x32_bf16 v[72:75], v[150:153], v[204:207], v[72:75]
	s_setprio 0
	s_setprio 1
	v_mfma_f32_16x16x32_bf16 v[116:119], v[160:163], v[176:179], v[116:119]
	v_mfma_f32_16x16x32_bf16 v[112:115], v[168:171], v[176:179], v[112:115]
	v_mfma_f32_16x16x32_bf16 v[100:103], v[160:163], v[184:187], v[100:103]
	v_mfma_f32_16x16x32_bf16 v[96:99], v[168:171], v[184:187], v[96:99]
	v_mfma_f32_16x16x32_bf16 v[84:87], v[160:163], v[192:195], v[84:87]
	v_mfma_f32_16x16x32_bf16 v[80:83], v[168:171], v[192:195], v[80:83]
	v_mfma_f32_16x16x32_bf16 v[68:71], v[160:163], v[200:203], v[68:71]
	v_mfma_f32_16x16x32_bf16 v[64:67], v[168:171], v[200:203], v[64:67]
	v_mfma_f32_16x16x32_bf16 v[116:119], v[164:167], v[180:183], v[116:119]
	v_mfma_f32_16x16x32_bf16 v[112:115], v[172:175], v[180:183], v[112:115]
	v_mfma_f32_16x16x32_bf16 v[100:103], v[164:167], v[188:191], v[100:103]
	v_mfma_f32_16x16x32_bf16 v[96:99], v[172:175], v[188:191], v[96:99]
	v_mfma_f32_16x16x32_bf16 v[84:87], v[164:167], v[196:199], v[84:87]
	v_mfma_f32_16x16x32_bf16 v[80:83], v[172:175], v[196:199], v[80:83]
	v_mfma_f32_16x16x32_bf16 v[68:71], v[164:167], v[204:207], v[68:71]
	v_mfma_f32_16x16x32_bf16 v[64:67], v[172:175], v[204:207], v[64:67]
	s_setprio 0
	s_barrier
	s_mov_b32 m0, s78
	v_lshl_add_u64 v[208:209], s[68:69], 0, v[136:137]
	ds_read_b128 v[176:179], v159 offset:16384
	ds_read_b128 v[180:183], v159 offset:17408
	ds_read_b128 v[184:187], v159 offset:18432
	ds_read_b128 v[188:191], v159 offset:19456
	ds_read_b128 v[192:195], v159 offset:20480
	ds_read_b128 v[196:199], v159 offset:21504
	ds_read_b128 v[200:203], v159 offset:22528
	ds_read_b128 v[204:207], v159 offset:23552
	global_load_lds_dwordx4 v[208:209], off
	v_lshl_add_u64 v[210:211], s[68:69], 0, v[132:133]
	s_mov_b32 m0, s79
	v_lshl_add_u64 v[212:213], s[70:71], 0, v[136:137]
	global_load_lds_dwordx4 v[210:211], off
	s_mov_b32 m0, s80
	v_lshl_add_u64 v[214:215], s[66:67], 0, v[134:135]
	global_load_lds_dwordx4 v[212:213], off
	v_lshl_add_u64 v[212:213], s[70:71], 0, v[132:133]
	s_mov_b32 m0, s86
	s_nop 0
	global_load_lds_dwordx4 v[212:213], off
	v_lshl_add_u64 v[212:213], s[66:67], 0, v[138:139]
	s_mov_b32 m0, s9
	s_nop 0
	global_load_lds_dwordx4 v[212:213], off
	s_mov_b32 m0, s34
	s_nop 0
	global_load_lds_dwordx4 v[214:215], off
	s_waitcnt vmcnt(8)
	s_waitcnt lgkmcnt(0)
	s_barrier
; #define PG8_STAGE_A(bufoff, gbase, h, nx) do { _Pragma("unroll") for (int _i = 0; _i < 2; ++_i) { \
;         const unsigned vo_ = GA ? ((nx) ? vgn[h][_i] : vgc[h][_i]) : voffA[_i]; \
;         __builtin_amdgcn_global_load_lds((const unsigned*)((const char*)(gbase) + vo_), (PG8_LAS unsigned*)(lds + (bufoff) + ldsw + _i * 8192), 16, 0, 0); } } while (0)
; #define PG8_LDA(dst, b, h) do { _Pragma("unroll") for (int m = 0; m < 4; ++m) _Pragma("unroll") for (int k = 0; k < 2; ++k) dst[m][k] = *(const PG8_LAS bf16x8*)(lds + PG8_SA(b, h) + aoff + m * 2048 + k * 1024); } while (0)
; #define PG8_LDB(dst, b, h) do { _Pragma("unroll") for (int n = 0; n < 2; ++n) _Pragma("unroll") for (int k = 0; k < 2; ++k) dst[n][k] = *(const PG8_LAS bf16x8*)(lds + PG8_SB(b, h) + boff + n * 2048 + k * 1024); } while (0)
; #define PG8_MMA(ai, bj, At, Bt) do { __builtin_amdgcn_s_setprio(1); _Pragma("unroll") for (int m = 0; m < 4; ++m) _Pragma("unroll") for (int n = 0; n < 2; ++n) _Pragma("unroll") for (int k = 0; k < 2; ++k) \
;         acc[ai][bj][m][n] = __builtin_amdgcn_mfma_f32_16x16x32_bf16(Bt[n][k], At[m][k], acc[ai][bj][m][n], 0, 0, 0); __builtin_amdgcn_s_setprio(0); } while (0)
; #define PG8_WAIT_V(n) asm volatile("s_waitcnt vmcnt(" #n ")" ::: "memory")
; #define PG8_WAIT_L(n) asm volatile("s_waitcnt lgkmcnt(" #n ")" ::: "memory")
; #define PG8_BAR __builtin_amdgcn_s_barrier()
; #define PG8_SCHED __builtin_amdgcn_sched_barrier(0)
; template <class Epi, class Sched>
; __device__ __forceinline__ void gemm_phase(const int WID_, PG8_LAS unsigned char* lds, const Sched& S, const Epi& E) {
;     ...
;             PG8_WAIT_V(8); PG8_WAIT_L(0); PG8_BAR; PG8_MMA(1, 0, At, B0); PG8_MMA(1, 1, At, B1); PG8_BAR; PG8_SCHED;
;             PG8_LDB(B0, 1, 0); PG8_LDB(B1, 1, 1); PG8_SCHED; PG8_LDA(At, 1, 0); PG8_STAGE_A(PG8_SA(0, 1), a2 + hstepA, 1, last);
;             PG8_WAIT_V(8); PG8_WAIT_L(0); PG8_BAR; PG8_MMA(0, 0, At, B0); PG8_MMA(0, 1, At, B1); PG8_BAR; PG8_SCHED;
	s_setprio 1
	s_waitcnt lgkmcnt(0)
	v_mfma_f32_16x16x32_bf16 v[60:63], v[128:131], v[176:179], v[60:63]
	v_mfma_f32_16x16x32_bf16 v[56:59], v[146:149], v[176:179], v[56:59]
	v_mfma_f32_16x16x32_bf16 v[44:47], v[128:131], v[184:187], v[44:47]
	v_mfma_f32_16x16x32_bf16 v[40:43], v[146:149], v[184:187], v[40:43]
	v_mfma_f32_16x16x32_bf16 v[28:31], v[128:131], v[192:195], v[28:31]
	v_mfma_f32_16x16x32_bf16 v[24:27], v[146:149], v[192:195], v[24:27]
	v_mfma_f32_16x16x32_bf16 v[12:15], v[128:131], v[200:203], v[12:15]
	v_mfma_f32_16x16x32_bf16 v[8:11], v[146:149], v[200:203], v[8:11]
	v_mfma_f32_16x16x32_bf16 v[60:63], v[142:145], v[180:183], v[60:63]
	v_mfma_f32_16x16x32_bf16 v[56:59], v[150:153], v[180:183], v[56:59]
	v_mfma_f32_16x16x32_bf16 v[44:47], v[142:145], v[188:191], v[44:47]
	v_mfma_f32_16x16x32_bf16 v[40:43], v[150:153], v[188:191], v[40:43]
	v_mfma_f32_16x16x32_bf16 v[28:31], v[142:145], v[196:199], v[28:31]
	v_mfma_f32_16x16x32_bf16 v[24:27], v[150:153], v[196:199], v[24:27]
	v_mfma_f32_16x16x32_bf16 v[12:15], v[142:145], v[204:207], v[12:15]
	v_mfma_f32_16x16x32_bf16 v[8:11], v[150:153], v[204:207], v[8:11]
	s_setprio 0
	s_setprio 1
	v_mfma_f32_16x16x32_bf16 v[52:55], v[160:163], v[176:179], v[52:55]
	v_mfma_f32_16x16x32_bf16 v[48:51], v[168:171], v[176:179], v[48:51]
	v_mfma_f32_16x16x32_bf16 v[36:39], v[160:163], v[184:187], v[36:39]
	v_mfma_f32_16x16x32_bf16 v[32:35], v[168:171], v[184:187], v[32:35]
	v_mfma_f32_16x16x32_bf16 v[20:23], v[160:163], v[192:195], v[20:23]
	v_mfma_f32_16x16x32_bf16 v[16:19], v[168:171], v[192:195], v[16:19]
	v_mfma_f32_16x16x32_bf16 v[4:7], v[160:163], v[200:203], v[4:7]
	v_mfma_f32_16x16x32_bf16 v[0:3], v[168:171], v[200:203], v[0:3]
	v_mfma_f32_16x16x32_bf16 v[52:55], v[164:167], v[180:183], v[52:55]
	v_mfma_f32_16x16x32_bf16 v[48:51], v[172:175], v[180:183], v[48:51]
	v_mfma_f32_16x16x32_bf16 v[36:39], v[164:167], v[188:191], v[36:39]
	v_mfma_f32_16x16x32_bf16 v[32:35], v[172:175], v[188:191], v[32:35]
	v_mfma_f32_16x16x32_bf16 v[20:23], v[164:167], v[196:199], v[20:23]
	v_mfma_f32_16x16x32_bf16 v[16:19], v[172:175], v[196:199], v[16:19]
	v_mfma_f32_16x16x32_bf16 v[4:7], v[164:167], v[204:207], v[4:7]
	v_mfma_f32_16x16x32_bf16 v[0:3], v[172:175], v[204:207], v[0:3]
	s_setprio 0
	s_barrier
	v_add_u32_e32 v150, s85, v155
	v_add_u32_e32 v172, s84, v155
	ds_read_b128 v[128:131], v150
	ds_read_b128 v[142:145], v150 offset:1024
	ds_read_b128 v[146:149], v150 offset:2048
	ds_read_b128 v[150:153], v150 offset:3072
	ds_read_b128 v[160:163], v172
	ds_read_b128 v[164:167], v172 offset:1024
	ds_read_b128 v[168:171], v172 offset:2048
	ds_read_b128 v[172:175], v172 offset:3072
	s_mov_b32 m0, s35
	v_lshl_add_u64 v[216:217], s[62:63], 0, v[138:139]
	ds_read_b128 v[176:179], v159 offset:32768
	ds_read_b128 v[180:183], v159 offset:33792
	ds_read_b128 v[184:187], v159 offset:34816
	ds_read_b128 v[188:191], v159 offset:35840
	ds_read_b128 v[192:195], v159 offset:36864
	ds_read_b128 v[196:199], v159 offset:37888
	ds_read_b128 v[200:203], v159 offset:38912
	ds_read_b128 v[204:207], v159 offset:39936
	global_load_lds_dwordx4 v[216:217], off
	v_lshl_add_u64 v[216:217], s[62:63], 0, v[134:135]
	s_mov_b32 m0, s58
	s_nop 0
	global_load_lds_dwordx4 v[216:217], off
	s_waitcnt vmcnt(8)
	s_waitcnt lgkmcnt(0)
	s_barrier
	s_setprio 1
	s_waitcnt lgkmcnt(0)
	v_mfma_f32_16x16x32_bf16 v[124:127], v[128:131], v[176:179], v[124:127]
	v_mfma_f32_16x16x32_bf16 v[120:123], v[146:149], v[176:179], v[120:123]
	v_mfma_f32_16x16x32_bf16 v[108:111], v[128:131], v[184:187], v[108:111]
	v_mfma_f32_16x16x32_bf16 v[104:107], v[146:149], v[184:187], v[104:107]
	v_mfma_f32_16x16x32_bf16 v[92:95], v[128:131], v[192:195], v[92:95]
	v_mfma_f32_16x16x32_bf16 v[88:91], v[146:149], v[192:195], v[88:91]
	v_mfma_f32_16x16x32_bf16 v[76:79], v[128:131], v[200:203], v[76:79]
	v_mfma_f32_16x16x32_bf16 v[72:75], v[146:149], v[200:203], v[72:75]
	v_mfma_f32_16x16x32_bf16 v[124:127], v[142:145], v[180:183], v[124:127]
	v_mfma_f32_16x16x32_bf16 v[120:123], v[150:153], v[180:183], v[120:123]
	v_mfma_f32_16x16x32_bf16 v[108:111], v[142:145], v[188:191], v[108:111]
	v_mfma_f32_16x16x32_bf16 v[104:107], v[150:153], v[188:191], v[104:107]
	v_mfma_f32_16x16x32_bf16 v[92:95], v[142:145], v[196:199], v[92:95]
	v_mfma_f32_16x16x32_bf16 v[88:91], v[150:153], v[196:199], v[88:91]
	v_mfma_f32_16x16x32_bf16 v[76:79], v[142:145], v[204:207], v[76:79]
	v_mfma_f32_16x16x32_bf16 v[72:75], v[150:153], v[204:207], v[72:75]
	s_setprio 0
	s_setprio 1
	v_mfma_f32_16x16x32_bf16 v[116:119], v[160:163], v[176:179], v[116:119]
	v_mfma_f32_16x16x32_bf16 v[112:115], v[168:171], v[176:179], v[112:115]
	v_mfma_f32_16x16x32_bf16 v[100:103], v[160:163], v[184:187], v[100:103]
	v_mfma_f32_16x16x32_bf16 v[96:99], v[168:171], v[184:187], v[96:99]
	v_mfma_f32_16x16x32_bf16 v[84:87], v[160:163], v[192:195], v[84:87]
	v_mfma_f32_16x16x32_bf16 v[80:83], v[168:171], v[192:195], v[80:83]
	v_mfma_f32_16x16x32_bf16 v[68:71], v[160:163], v[200:203], v[68:71]
	v_mfma_f32_16x16x32_bf16 v[64:67], v[168:171], v[200:203], v[64:67]
	v_mfma_f32_16x16x32_bf16 v[116:119], v[164:167], v[180:183], v[116:119]
	v_mfma_f32_16x16x32_bf16 v[112:115], v[172:175], v[180:183], v[112:115]
	v_mfma_f32_16x16x32_bf16 v[100:103], v[164:167], v[188:191], v[100:103]
	v_mfma_f32_16x16x32_bf16 v[96:99], v[172:175], v[188:191], v[96:99]
	v_mfma_f32_16x16x32_bf16 v[84:87], v[164:167], v[196:199], v[84:87]
	v_mfma_f32_16x16x32_bf16 v[80:83], v[172:175], v[196:199], v[80:83]
	v_mfma_f32_16x16x32_bf16 v[68:71], v[164:167], v[204:207], v[68:71]
	v_mfma_f32_16x16x32_bf16 v[64:67], v[172:175], v[204:207], v[64:67]
	s_setprio 0
	s_barrier
; #define PG8_STAGE(bufoff, gbase, voff) do { _Pragma("unroll") for (int _i = 0; _i < 2; ++_i) \
;         __builtin_amdgcn_global_load_lds((const unsigned*)((const char*)(gbase) + (voff)[_i]), (PG8_LAS unsigned*)(lds + (bufoff) + ldsw + _i * 8192), 16, 0, 0); } while (0)
; #define PG8_STAGE_A(bufoff, gbase, h, nx) do { _Pragma("unroll") for (int _i = 0; _i < 2; ++_i) { \
;         const unsigned vo_ = GA ? ((nx) ? vgn[h][_i] : vgc[h][_i]) : voffA[_i]; \
;         __builtin_amdgcn_global_load_lds((const unsigned*)((const char*)(gbase) + vo_), (PG8_LAS unsigned*)(lds + (bufoff) + ldsw + _i * 8192), 16, 0, 0); } } while (0)
; #define PG8_LDA(dst, b, h) do { _Pragma("unroll") for (int m = 0; m < 4; ++m) _Pragma("unroll") for (int k = 0; k < 2; ++k) dst[m][k] = *(const PG8_LAS bf16x8*)(lds + PG8_SA(b, h) + aoff + m * 2048 + k * 1024); } while (0)
; #define PG8_MMA(ai, bj, At, Bt) do { __builtin_amdgcn_s_setprio(1); _Pragma("unroll") for (int m = 0; m < 4; ++m) _Pragma("unroll") for (int n = 0; n < 2; ++n) _Pragma("unroll") for (int k = 0; k < 2; ++k) \
;         acc[ai][bj][m][n] = __builtin_amdgcn_mfma_f32_16x16x32_bf16(Bt[n][k], At[m][k], acc[ai][bj][m][n], 0, 0, 0); __builtin_amdgcn_s_setprio(0); } while (0)
; #define PG8_WAIT_V(n) asm volatile("s_waitcnt vmcnt(" #n ")" ::: "memory")
; #define PG8_WAIT_L(n) asm volatile("s_waitcnt lgkmcnt(" #n ")" ::: "memory")
; #define PG8_BAR __builtin_amdgcn_s_barrier()
; #define PG8_SCHED __builtin_amdgcn_sched_barrier(0)
; template <class Epi, class Sched>
; __device__ __forceinline__ void gemm_phase(const int WID_, PG8_LAS unsigned char* lds, const Sched& S, const Epi& E) {
;     ...
;             PG8_LDA(At, 1, 1); PG8_STAGE(PG8_SB(1, 0), b3, voffB); PG8_STAGE(PG8_SB(1, 1), b3 + hstepB, voffB); PG8_STAGE_A(PG8_SA(1, 0), a3, 0, last);
;             PG8_WAIT_V(8); PG8_WAIT_L(0); PG8_BAR; PG8_MMA(1, 0, At, B0); PG8_MMA(1, 1, At, B1); PG8_BAR; PG8_SCHED;
;         }
;         if (wr == 0) PG8_BAR;
;         E(acc, cur, wr, wc, fr, fq);
;         if (!has_next) break;
	s_mov_b32 m0, s83
	v_lshl_add_u64 v[208:209], v[208:209], 0, s[22:23]
	ds_read_b128 v[176:179], v159 offset:49152
	ds_read_b128 v[180:183], v159 offset:50176
	ds_read_b128 v[184:187], v159 offset:51200
	ds_read_b128 v[188:191], v159 offset:52224
	ds_read_b128 v[192:195], v159 offset:53248
	ds_read_b128 v[196:199], v159 offset:54272
	ds_read_b128 v[200:203], v159 offset:55296
	ds_read_b128 v[204:207], v159 offset:56320
	global_load_lds_dwordx4 v[208:209], off
	v_lshl_add_u64 v[208:209], v[210:211], 0, s[22:23]
	s_mov_b32 m0, s47
	s_nop 0
	global_load_lds_dwordx4 v[208:209], off
	v_lshl_add_u64 v[208:209], s[60:61], 0, v[136:137]
	s_mov_b32 m0, s82
	s_nop 0
	global_load_lds_dwordx4 v[208:209], off
	v_lshl_add_u64 v[208:209], s[60:61], 0, v[132:133]
	s_mov_b32 m0, s41
	s_nop 0
	global_load_lds_dwordx4 v[208:209], off
	v_lshl_add_u64 v[208:209], v[212:213], 0, s[22:23]
	s_mov_b32 m0, s74
	s_nop 0
	global_load_lds_dwordx4 v[208:209], off
	v_lshl_add_u64 v[208:209], v[214:215], 0, s[22:23]
	s_mov_b32 m0, s75
	s_nop 0
	global_load_lds_dwordx4 v[208:209], off
	s_waitcnt vmcnt(8)
	s_waitcnt lgkmcnt(0)
	s_barrier
	s_setprio 1
	s_waitcnt lgkmcnt(0)
	v_mfma_f32_16x16x32_bf16 v[60:63], v[128:131], v[176:179], v[60:63]
	v_mfma_f32_16x16x32_bf16 v[56:59], v[146:149], v[176:179], v[56:59]
	v_mfma_f32_16x16x32_bf16 v[44:47], v[128:131], v[184:187], v[44:47]
	v_mfma_f32_16x16x32_bf16 v[40:43], v[146:149], v[184:187], v[40:43]
	v_mfma_f32_16x16x32_bf16 v[28:31], v[128:131], v[192:195], v[28:31]
	v_mfma_f32_16x16x32_bf16 v[24:27], v[146:149], v[192:195], v[24:27]
	v_mfma_f32_16x16x32_bf16 v[12:15], v[128:131], v[200:203], v[12:15]
	v_mfma_f32_16x16x32_bf16 v[8:11], v[146:149], v[200:203], v[8:11]
	v_mfma_f32_16x16x32_bf16 v[60:63], v[142:145], v[180:183], v[60:63]
	v_mfma_f32_16x16x32_bf16 v[56:59], v[150:153], v[180:183], v[56:59]
	v_mfma_f32_16x16x32_bf16 v[44:47], v[142:145], v[188:191], v[44:47]
	v_mfma_f32_16x16x32_bf16 v[40:43], v[150:153], v[188:191], v[40:43]
	v_mfma_f32_16x16x32_bf16 v[28:31], v[142:145], v[196:199], v[28:31]
	v_mfma_f32_16x16x32_bf16 v[24:27], v[150:153], v[196:199], v[24:27]
	v_mfma_f32_16x16x32_bf16 v[12:15], v[142:145], v[204:207], v[12:15]
	v_mfma_f32_16x16x32_bf16 v[8:11], v[150:153], v[204:207], v[8:11]
	s_setprio 0
	s_setprio 1
	v_mfma_f32_16x16x32_bf16 v[52:55], v[160:163], v[176:179], v[52:55]
	v_mfma_f32_16x16x32_bf16 v[48:51], v[168:171], v[176:179], v[48:51]
	v_mfma_f32_16x16x32_bf16 v[36:39], v[160:163], v[184:187], v[36:39]
	v_mfma_f32_16x16x32_bf16 v[32:35], v[168:171], v[184:187], v[32:35]
	v_mfma_f32_16x16x32_bf16 v[20:23], v[160:163], v[192:195], v[20:23]
	v_mfma_f32_16x16x32_bf16 v[16:19], v[168:171], v[192:195], v[16:19]
	v_mfma_f32_16x16x32_bf16 v[4:7], v[160:163], v[200:203], v[4:7]
	v_mfma_f32_16x16x32_bf16 v[0:3], v[168:171], v[200:203], v[0:3]
	v_mfma_f32_16x16x32_bf16 v[52:55], v[164:167], v[180:183], v[52:55]
	v_mfma_f32_16x16x32_bf16 v[48:51], v[172:175], v[180:183], v[48:51]
	v_mfma_f32_16x16x32_bf16 v[36:39], v[164:167], v[188:191], v[36:39]
	v_mfma_f32_16x16x32_bf16 v[32:35], v[172:175], v[188:191], v[32:35]
	v_mfma_f32_16x16x32_bf16 v[20:23], v[164:167], v[196:199], v[20:23]
	v_mfma_f32_16x16x32_bf16 v[16:19], v[172:175], v[196:199], v[16:19]
	v_mfma_f32_16x16x32_bf16 v[4:7], v[164:167], v[204:207], v[4:7]
	v_mfma_f32_16x16x32_bf16 v[0:3], v[172:175], v[204:207], v[0:3]
	s_setprio 0
	s_barrier
	s_movk_i32 s41, 0x100
	s_andn2_b64 vcc, exec, s[52:53]
	s_mov_b64 s[60:61], -1
	s_mov_b64 s[52:53], 0
	s_cbranch_vccz .LBB0_1892
	s_and_b64 vcc, exec, s[38:39]
	s_cbranch_vccz .LBB0_1895
	s_barrier

; #define PG8_STAGE(bufoff, gbase, voff) do { _Pragma("unroll") for (int _i = 0; _i < 2; ++_i) \
;         __builtin_amdgcn_global_load_lds((const unsigned*)((const char*)(gbase) + (voff)[_i]), (PG8_LAS unsigned*)(lds + (bufoff) + ldsw + _i * 8192), 16, 0, 0); } while (0)
; #define PG8_STAGE_A(bufoff, gbase, h, nx) do { _Pragma("unroll") for (int _i = 0; _i < 2; ++_i) { \
;         const unsigned vo_ = GA ? ((nx) ? vgn[h][_i] : vgc[h][_i]) : voffA[_i]; \
;         __builtin_amdgcn_global_load_lds((const unsigned*)((const char*)(gbase) + vo_), (PG8_LAS unsigned*)(lds + (bufoff) + ldsw + _i * 8192), 16, 0, 0); } } while (0)
; #define PG8_LDA(dst, b, h) do { _Pragma("unroll") for (int m = 0; m < 4; ++m) _Pragma("unroll") for (int k = 0; k < 2; ++k) dst[m][k] = *(const PG8_LAS bf16x8*)(lds + PG8_SA(b, h) + aoff + m * 2048 + k * 1024); } while (0)
; #define PG8_LDB(dst, b, h) do { _Pragma("unroll") for (int n = 0; n < 2; ++n) _Pragma("unroll") for (int k = 0; k < 2; ++k) dst[n][k] = *(const PG8_LAS bf16x8*)(lds + PG8_SB(b, h) + boff + n * 2048 + k * 1024); } while (0)
; #define PG8_WAIT_V(n) asm volatile("s_waitcnt vmcnt(" #n ")" ::: "memory")
; #define PG8_WAIT_L(n) asm volatile("s_waitcnt lgkmcnt(" #n ")" ::: "memory")
; #define PG8_BAR __builtin_amdgcn_s_barrier()
; #define PG8_SCHED __builtin_amdgcn_sched_barrier(0)
; template <class Epi, class Sched>
; __device__ __forceinline__ void gemm_phase(const int WID_, PG8_LAS unsigned char* lds, const Sched& S, const Epi& E) {
;     ...
;         for (int t = 0; t < nt; t += 2) {
;             const bool last = (t == nt - 2);
;             const char* a1 = cA + (size_t)(t + 1) * kstep;
;             const char* a2 = last ? nA : cA + (size_t)(t + 2) * kstep; const char* b2 = last ? nB : cB + (size_t)(t + 2) * kstep;
;             const char* a3 = a2 + kstep; const char* b3 = b2 + kstep;
;             PG8_LDB(B0, 0, 0); PG8_LDB(B1, 0, 1); PG8_SCHED; PG8_LDA(At, 0, 0); PG8_STAGE_A(PG8_SA(1, 1), a1 + hstepA, 1, false);
;             PG8_WAIT_V(8); PG8_WAIT_L(0); PG8_BAR; PG8_MMA(0, 0, At, B0); PG8_MMA(0, 1, At, B1); PG8_BAR; PG8_SCHED;
;             PG8_LDA(At, 0, 1); PG8_STAGE(PG8_SB(0, 0), b2, voffB); PG8_STAGE(PG8_SB(0, 1), b2 + hstepB, voffB); PG8_STAGE_A(PG8_SA(0, 0), a2, 0, last);
;             PG8_WAIT_V(8); PG8_WAIT_L(0); PG8_BAR; PG8_MMA(1, 0, At, B0); PG8_MMA(1, 1, At, B1); PG8_BAR; PG8_SCHED;
.LBB0_2018:
	s_add_u32 s18, s16, 0xfffe0080
	s_addc_u32 s19, s17, -1
	s_add_i32 s43, 0, 0x10000
	s_cmp_eq_u32 s60, 4
	s_cselect_b32 s21, s9, s19
	s_cselect_b32 s20, s33, s18
	v_add_u32_e32 v148, s43, v151
	s_cselect_b32 s19, s44, s51
	s_cselect_b32 s18, s49, s50
	s_add_i32 s67, 0, 0x14000
	ds_read_b128 v[140:143], v148
	ds_read_b128 v[144:147], v148 offset:1024
	ds_read_b128 v[154:157], v148 offset:2048
	ds_read_b128 v[158:161], v148 offset:3072
	v_add_u32_e32 v148, s67, v151
	ds_read_b128 v[162:165], v148
	ds_read_b128 v[166:169], v148 offset:1024
	ds_read_b128 v[170:173], v148 offset:2048
	ds_read_b128 v[174:177], v148 offset:3072
	v_lshl_add_u64 v[148:149], s[16:17], 0, v[136:137]
	s_add_i32 m0, s23, 0xc000
	ds_read_b128 v[178:181], v153
	ds_read_b128 v[182:185], v153 offset:1024
	ds_read_b128 v[186:189], v153 offset:2048
	ds_read_b128 v[190:193], v153 offset:3072
	ds_read_b128 v[198:201], v153 offset:4096
	ds_read_b128 v[202:205], v153 offset:5120
	ds_read_b128 v[206:209], v153 offset:6144
	ds_read_b128 v[210:213], v153 offset:7168
	global_load_lds_dwordx4 v[148:149], off
	v_lshl_add_u64 v[148:149], s[16:17], 0, v[138:139]
	s_add_i32 m0, s23, 0xe000
	s_nop 0
	global_load_lds_dwordx4 v[148:149], off
	s_waitcnt vmcnt(8)
	s_waitcnt lgkmcnt(0)
	s_barrier
	s_setprio 1
	s_waitcnt lgkmcnt(0)
	v_mfma_f32_16x16x32_bf16 v[124:127], v[140:143], v[178:181], v[124:127]
	v_mfma_f32_16x16x32_bf16 v[120:123], v[154:157], v[178:181], v[120:123]
	v_mfma_f32_16x16x32_bf16 v[108:111], v[140:143], v[186:189], v[108:111]
	v_mfma_f32_16x16x32_bf16 v[104:107], v[154:157], v[186:189], v[104:107]
	v_mfma_f32_16x16x32_bf16 v[92:95], v[140:143], v[198:201], v[92:95]
	v_mfma_f32_16x16x32_bf16 v[88:91], v[154:157], v[198:201], v[88:91]
	v_mfma_f32_16x16x32_bf16 v[76:79], v[140:143], v[206:209], v[76:79]
	v_mfma_f32_16x16x32_bf16 v[72:75], v[154:157], v[206:209], v[72:75]
	v_mfma_f32_16x16x32_bf16 v[124:127], v[144:147], v[182:185], v[124:127]
	v_mfma_f32_16x16x32_bf16 v[120:123], v[158:161], v[182:185], v[120:123]
	v_mfma_f32_16x16x32_bf16 v[108:111], v[144:147], v[190:193], v[108:111]
	v_mfma_f32_16x16x32_bf16 v[104:107], v[158:161], v[190:193], v[104:107]
	v_mfma_f32_16x16x32_bf16 v[92:95], v[144:147], v[202:205], v[92:95]
	v_mfma_f32_16x16x32_bf16 v[88:91], v[158:161], v[202:205], v[88:91]
	v_mfma_f32_16x16x32_bf16 v[76:79], v[144:147], v[210:213], v[76:79]
	v_mfma_f32_16x16x32_bf16 v[72:75], v[158:161], v[210:213], v[72:75]
	s_setprio 0
	s_setprio 1
	v_mfma_f32_16x16x32_bf16 v[116:119], v[162:165], v[178:181], v[116:119]
	v_mfma_f32_16x16x32_bf16 v[112:115], v[170:173], v[178:181], v[112:115]
	v_mfma_f32_16x16x32_bf16 v[100:103], v[162:165], v[186:189], v[100:103]
	v_mfma_f32_16x16x32_bf16 v[96:99], v[170:173], v[186:189], v[96:99]
	v_mfma_f32_16x16x32_bf16 v[84:87], v[162:165], v[198:201], v[84:87]
	v_mfma_f32_16x16x32_bf16 v[80:83], v[170:173], v[198:201], v[80:83]
	v_mfma_f32_16x16x32_bf16 v[68:71], v[162:165], v[206:209], v[68:71]
	v_mfma_f32_16x16x32_bf16 v[64:67], v[170:173], v[206:209], v[64:67]
	v_mfma_f32_16x16x32_bf16 v[116:119], v[166:169], v[182:185], v[116:119]
	v_mfma_f32_16x16x32_bf16 v[112:115], v[174:177], v[182:185], v[112:115]
	v_mfma_f32_16x16x32_bf16 v[100:103], v[166:169], v[190:193], v[100:103]
	v_mfma_f32_16x16x32_bf16 v[96:99], v[174:177], v[190:193], v[96:99]
	v_mfma_f32_16x16x32_bf16 v[84:87], v[166:169], v[202:205], v[84:87]
	v_mfma_f32_16x16x32_bf16 v[80:83], v[174:177], v[202:205], v[80:83]
	v_mfma_f32_16x16x32_bf16 v[68:71], v[166:169], v[210:213], v[68:71]
	v_mfma_f32_16x16x32_bf16 v[64:67], v[174:177], v[210:213], v[64:67]
	s_setprio 0
	s_barrier
	s_add_i32 s46, s43, s22
	v_lshl_add_u64 v[148:149], s[18:19], 0, v[128:129]
	s_mov_b32 m0, s46
	ds_read_b128 v[178:181], v153 offset:16384
	ds_read_b128 v[182:185], v153 offset:17408
	ds_read_b128 v[186:189], v153 offset:18432
	ds_read_b128 v[190:193], v153 offset:19456
	ds_read_b128 v[198:201], v153 offset:20480
	ds_read_b128 v[202:205], v153 offset:21504
	ds_read_b128 v[206:209], v153 offset:22528
	ds_read_b128 v[210:213], v153 offset:23552
	global_load_lds_dwordx4 v[148:149], off
	s_add_i32 m0, s46, 0x2000
	s_add_u32 s62, s18, 0x20000
	v_lshl_add_u64 v[214:215], s[18:19], 0, v[130:131]
	s_addc_u32 s63, s19, 0
	s_add_i32 s46, s67, s22
	global_load_lds_dwordx4 v[214:215], off
	v_lshl_add_u64 v[216:217], s[62:63], 0, v[128:129]
	s_mov_b32 m0, s46
	v_lshl_add_u64 v[218:219], s[20:21], 0, v[132:133]
	global_load_lds_dwordx4 v[216:217], off
	v_lshl_add_u64 v[216:217], s[62:63], 0, v[130:131]
	s_add_i32 m0, s46, 0x2000
	s_nop 0
	global_load_lds_dwordx4 v[216:217], off
	v_lshl_add_u64 v[216:217], s[20:21], 0, v[134:135]
	s_mov_b32 m0, s23
	s_nop 0
	global_load_lds_dwordx4 v[216:217], off
	s_mov_b32 m0, s78
	s_nop 0
	global_load_lds_dwordx4 v[218:219], off
	s_waitcnt vmcnt(8)
	s_waitcnt lgkmcnt(0)
	s_barrier
; #define PG8_STAGE_A(bufoff, gbase, h, nx) do { _Pragma("unroll") for (int _i = 0; _i < 2; ++_i) { \
;         const unsigned vo_ = GA ? ((nx) ? vgn[h][_i] : vgc[h][_i]) : voffA[_i]; \
;         __builtin_amdgcn_global_load_lds((const unsigned*)((const char*)(gbase) + vo_), (PG8_LAS unsigned*)(lds + (bufoff) + ldsw + _i * 8192), 16, 0, 0); } } while (0)
; #define PG8_LDA(dst, b, h) do { _Pragma("unroll") for (int m = 0; m < 4; ++m) _Pragma("unroll") for (int k = 0; k < 2; ++k) dst[m][k] = *(const PG8_LAS bf16x8*)(lds + PG8_SA(b, h) + aoff + m * 2048 + k * 1024); } while (0)
; #define PG8_LDB(dst, b, h) do { _Pragma("unroll") for (int n = 0; n < 2; ++n) _Pragma("unroll") for (int k = 0; k < 2; ++k) dst[n][k] = *(const PG8_LAS bf16x8*)(lds + PG8_SB(b, h) + boff + n * 2048 + k * 1024); } while (0)
; #define PG8_MMA(ai, bj, At, Bt) do { __builtin_amdgcn_s_setprio(1); _Pragma("unroll") for (int m = 0; m < 4; ++m) _Pragma("unroll") for (int n = 0; n < 2; ++n) _Pragma("unroll") for (int k = 0; k < 2; ++k) \
;         acc[ai][bj][m][n] = __builtin_amdgcn_mfma_f32_16x16x32_bf16(Bt[n][k], At[m][k], acc[ai][bj][m][n], 0, 0, 0); __builtin_amdgcn_s_setprio(0); } while (0)
; #define PG8_WAIT_V(n) asm volatile("s_waitcnt vmcnt(" #n ")" ::: "memory")
; #define PG8_WAIT_L(n) asm volatile("s_waitcnt lgkmcnt(" #n ")" ::: "memory")
; #define PG8_BAR __builtin_amdgcn_s_barrier()
; #define PG8_SCHED __builtin_amdgcn_sched_barrier(0)
; template <class Epi, class Sched>
; __device__ __forceinline__ void gemm_phase(const int WID_, PG8_LAS unsigned char* lds, const Sched& S, const Epi& E) {
;     ...
;             PG8_WAIT_V(8); PG8_WAIT_L(0); PG8_BAR; PG8_MMA(1, 0, At, B0); PG8_MMA(1, 1, At, B1); PG8_BAR; PG8_SCHED;
;             PG8_LDB(B0, 1, 0); PG8_LDB(B1, 1, 1); PG8_SCHED; PG8_LDA(At, 1, 0); PG8_STAGE_A(PG8_SA(0, 1), a2 + hstepA, 1, last);
;             PG8_WAIT_V(8); PG8_WAIT_L(0); PG8_BAR; PG8_MMA(0, 0, At, B0); PG8_MMA(0, 1, At, B1); PG8_BAR; PG8_SCHED;
	s_nop 0
	s_setprio 1
	s_waitcnt lgkmcnt(0)
	v_mfma_f32_16x16x32_bf16 v[60:63], v[140:143], v[178:181], v[60:63]
	v_mfma_f32_16x16x32_bf16 v[56:59], v[154:157], v[178:181], v[56:59]
	v_mfma_f32_16x16x32_bf16 v[44:47], v[140:143], v[186:189], v[44:47]
	v_mfma_f32_16x16x32_bf16 v[40:43], v[154:157], v[186:189], v[40:43]
	v_mfma_f32_16x16x32_bf16 v[28:31], v[140:143], v[198:201], v[28:31]
	v_mfma_f32_16x16x32_bf16 v[24:27], v[154:157], v[198:201], v[24:27]
	v_mfma_f32_16x16x32_bf16 v[12:15], v[140:143], v[206:209], v[12:15]
	v_mfma_f32_16x16x32_bf16 v[8:11], v[154:157], v[206:209], v[8:11]
	v_mfma_f32_16x16x32_bf16 v[60:63], v[144:147], v[182:185], v[60:63]
	v_mfma_f32_16x16x32_bf16 v[56:59], v[158:161], v[182:185], v[56:59]
	v_mfma_f32_16x16x32_bf16 v[44:47], v[144:147], v[190:193], v[44:47]
	v_mfma_f32_16x16x32_bf16 v[40:43], v[158:161], v[190:193], v[40:43]
	v_mfma_f32_16x16x32_bf16 v[28:31], v[144:147], v[202:205], v[28:31]
	v_mfma_f32_16x16x32_bf16 v[24:27], v[158:161], v[202:205], v[24:27]
	v_mfma_f32_16x16x32_bf16 v[12:15], v[144:147], v[210:213], v[12:15]
	v_mfma_f32_16x16x32_bf16 v[8:11], v[158:161], v[210:213], v[8:11]
	s_setprio 0
	s_setprio 1
	v_mfma_f32_16x16x32_bf16 v[52:55], v[162:165], v[178:181], v[52:55]
	v_mfma_f32_16x16x32_bf16 v[48:51], v[170:173], v[178:181], v[48:51]
	v_mfma_f32_16x16x32_bf16 v[36:39], v[162:165], v[186:189], v[36:39]
	v_mfma_f32_16x16x32_bf16 v[32:35], v[170:173], v[186:189], v[32:35]
	v_mfma_f32_16x16x32_bf16 v[20:23], v[162:165], v[198:201], v[20:23]
	v_mfma_f32_16x16x32_bf16 v[16:19], v[170:173], v[198:201], v[16:19]
	v_mfma_f32_16x16x32_bf16 v[0:3], v[162:165], v[206:209], v[0:3]
	v_mfma_f32_16x16x32_bf16 v[4:7], v[170:173], v[206:209], v[4:7]
	v_mfma_f32_16x16x32_bf16 v[52:55], v[166:169], v[182:185], v[52:55]
	v_mfma_f32_16x16x32_bf16 v[48:51], v[174:177], v[182:185], v[48:51]
	v_mfma_f32_16x16x32_bf16 v[36:39], v[166:169], v[190:193], v[36:39]
	v_mfma_f32_16x16x32_bf16 v[32:35], v[174:177], v[190:193], v[32:35]
	v_mfma_f32_16x16x32_bf16 v[20:23], v[166:169], v[202:205], v[20:23]
	v_mfma_f32_16x16x32_bf16 v[16:19], v[174:177], v[202:205], v[16:19]
	v_mfma_f32_16x16x32_bf16 v[0:3], v[166:169], v[210:213], v[0:3]
	v_mfma_f32_16x16x32_bf16 v[4:7], v[174:177], v[210:213], v[4:7]
	s_setprio 0
	s_barrier
	s_add_i32 s82, 0, 0x18000
	s_add_i32 s83, 0, 0x1c000
	v_add_u32_e32 v158, s82, v151
	v_add_u32_e32 v174, s83, v151
	ds_read_b128 v[140:143], v158
	ds_read_b128 v[144:147], v158 offset:1024
	ds_read_b128 v[154:157], v158 offset:2048
	ds_read_b128 v[158:161], v158 offset:3072
	ds_read_b128 v[162:165], v174
	ds_read_b128 v[166:169], v174 offset:1024
	ds_read_b128 v[170:173], v174 offset:2048
	ds_read_b128 v[174:177], v174 offset:3072
	s_add_u32 s20, s20, 0x20000
	s_addc_u32 s21, s21, 0
	s_mov_b32 m0, s79
	v_lshl_add_u64 v[220:221], s[20:21], 0, v[134:135]
	ds_read_b128 v[178:181], v153 offset:32768
	ds_read_b128 v[182:185], v153 offset:33792
	ds_read_b128 v[186:189], v153 offset:34816
	ds_read_b128 v[190:193], v153 offset:35840
	ds_read_b128 v[198:201], v153 offset:36864
	ds_read_b128 v[202:205], v153 offset:37888
	ds_read_b128 v[206:209], v153 offset:38912
	ds_read_b128 v[210:213], v153 offset:39936
	global_load_lds_dwordx4 v[220:221], off
	v_lshl_add_u64 v[220:221], s[20:21], 0, v[132:133]
	s_mov_b32 m0, s80
	s_nop 0
	global_load_lds_dwordx4 v[220:221], off
	s_waitcnt vmcnt(8)
	s_waitcnt lgkmcnt(0)
	s_barrier
	s_nop 0
	s_setprio 1
	s_waitcnt lgkmcnt(0)
	v_mfma_f32_16x16x32_bf16 v[124:127], v[140:143], v[178:181], v[124:127]
	v_mfma_f32_16x16x32_bf16 v[120:123], v[154:157], v[178:181], v[120:123]
	v_mfma_f32_16x16x32_bf16 v[108:111], v[140:143], v[186:189], v[108:111]
	v_mfma_f32_16x16x32_bf16 v[104:107], v[154:157], v[186:189], v[104:107]
	v_mfma_f32_16x16x32_bf16 v[92:95], v[140:143], v[198:201], v[92:95]
	v_mfma_f32_16x16x32_bf16 v[88:91], v[154:157], v[198:201], v[88:91]
	v_mfma_f32_16x16x32_bf16 v[76:79], v[140:143], v[206:209], v[76:79]
	v_mfma_f32_16x16x32_bf16 v[72:75], v[154:157], v[206:209], v[72:75]
	v_mfma_f32_16x16x32_bf16 v[124:127], v[144:147], v[182:185], v[124:127]
	v_mfma_f32_16x16x32_bf16 v[120:123], v[158:161], v[182:185], v[120:123]
	v_mfma_f32_16x16x32_bf16 v[108:111], v[144:147], v[190:193], v[108:111]
	v_mfma_f32_16x16x32_bf16 v[104:107], v[158:161], v[190:193], v[104:107]
	v_mfma_f32_16x16x32_bf16 v[92:95], v[144:147], v[202:205], v[92:95]
	v_mfma_f32_16x16x32_bf16 v[88:91], v[158:161], v[202:205], v[88:91]
	v_mfma_f32_16x16x32_bf16 v[76:79], v[144:147], v[210:213], v[76:79]
	v_mfma_f32_16x16x32_bf16 v[72:75], v[158:161], v[210:213], v[72:75]
	s_setprio 0
	s_setprio 1
	v_mfma_f32_16x16x32_bf16 v[116:119], v[162:165], v[178:181], v[116:119]
	v_mfma_f32_16x16x32_bf16 v[112:115], v[170:173], v[178:181], v[112:115]
	v_mfma_f32_16x16x32_bf16 v[100:103], v[162:165], v[186:189], v[100:103]
	v_mfma_f32_16x16x32_bf16 v[96:99], v[170:173], v[186:189], v[96:99]
	v_mfma_f32_16x16x32_bf16 v[84:87], v[162:165], v[198:201], v[84:87]
	v_mfma_f32_16x16x32_bf16 v[80:83], v[170:173], v[198:201], v[80:83]
	v_mfma_f32_16x16x32_bf16 v[68:71], v[162:165], v[206:209], v[68:71]
	v_mfma_f32_16x16x32_bf16 v[64:67], v[170:173], v[206:209], v[64:67]
	v_mfma_f32_16x16x32_bf16 v[116:119], v[166:169], v[182:185], v[116:119]
	v_mfma_f32_16x16x32_bf16 v[112:115], v[174:177], v[182:185], v[112:115]
	v_mfma_f32_16x16x32_bf16 v[100:103], v[166:169], v[190:193], v[100:103]
	v_mfma_f32_16x16x32_bf16 v[96:99], v[174:177], v[190:193], v[96:99]
	v_mfma_f32_16x16x32_bf16 v[84:87], v[166:169], v[202:205], v[84:87]
	v_mfma_f32_16x16x32_bf16 v[80:83], v[174:177], v[202:205], v[80:83]
	v_mfma_f32_16x16x32_bf16 v[68:71], v[166:169], v[210:213], v[68:71]
	v_mfma_f32_16x16x32_bf16 v[64:67], v[174:177], v[210:213], v[64:67]
	s_setprio 0
	s_barrier
; #define PG8_STAGE(bufoff, gbase, voff) do { _Pragma("unroll") for (int _i = 0; _i < 2; ++_i) \
;         __builtin_amdgcn_global_load_lds((const unsigned*)((const char*)(gbase) + (voff)[_i]), (PG8_LAS unsigned*)(lds + (bufoff) + ldsw + _i * 8192), 16, 0, 0); } while (0)
; #define PG8_STAGE_A(bufoff, gbase, h, nx) do { _Pragma("unroll") for (int _i = 0; _i < 2; ++_i) { \
;         const unsigned vo_ = GA ? ((nx) ? vgn[h][_i] : vgc[h][_i]) : voffA[_i]; \
;         __builtin_amdgcn_global_load_lds((const unsigned*)((const char*)(gbase) + vo_), (PG8_LAS unsigned*)(lds + (bufoff) + ldsw + _i * 8192), 16, 0, 0); } } while (0)
; #define PG8_LDA(dst, b, h) do { _Pragma("unroll") for (int m = 0; m < 4; ++m) _Pragma("unroll") for (int k = 0; k < 2; ++k) dst[m][k] = *(const PG8_LAS bf16x8*)(lds + PG8_SA(b, h) + aoff + m * 2048 + k * 1024); } while (0)
; #define PG8_MMA(ai, bj, At, Bt) do { __builtin_amdgcn_s_setprio(1); _Pragma("unroll") for (int m = 0; m < 4; ++m) _Pragma("unroll") for (int n = 0; n < 2; ++n) _Pragma("unroll") for (int k = 0; k < 2; ++k) \
;         acc[ai][bj][m][n] = __builtin_amdgcn_mfma_f32_16x16x32_bf16(Bt[n][k], At[m][k], acc[ai][bj][m][n], 0, 0, 0); __builtin_amdgcn_s_setprio(0); } while (0)
; #define PG8_WAIT_V(n) asm volatile("s_waitcnt vmcnt(" #n ")" ::: "memory")
; #define PG8_WAIT_L(n) asm volatile("s_waitcnt lgkmcnt(" #n ")" ::: "memory")
; #define PG8_BAR __builtin_amdgcn_s_barrier()
; #define PG8_SCHED __builtin_amdgcn_sched_barrier(0)
; template <class Epi, class Sched>
; __device__ __forceinline__ void gemm_phase(const int WID_, PG8_LAS unsigned char* lds, const Sched& S, const Epi& E) {
;     ...
;             PG8_LDA(At, 1, 1); PG8_STAGE(PG8_SB(1, 0), b3, voffB); PG8_STAGE(PG8_SB(1, 1), b3 + hstepB, voffB); PG8_STAGE_A(PG8_SA(1, 0), a3, 0, last);
;             PG8_WAIT_V(8); PG8_WAIT_L(0); PG8_BAR; PG8_MMA(1, 0, At, B0); PG8_MMA(1, 1, At, B1); PG8_BAR; PG8_SCHED;
;         }
;         if (wr == 0) PG8_BAR;
	s_add_i32 s20, s82, s22
	v_lshl_add_u64 v[148:149], v[148:149], 0, s[68:69]
	s_mov_b32 m0, s20
	ds_read_b128 v[178:181], v153 offset:49152
	ds_read_b128 v[182:185], v153 offset:50176
	ds_read_b128 v[186:189], v153 offset:51200
	ds_read_b128 v[190:193], v153 offset:52224
	ds_read_b128 v[198:201], v153 offset:53248
	ds_read_b128 v[202:205], v153 offset:54272
	ds_read_b128 v[206:209], v153 offset:55296
	ds_read_b128 v[210:213], v153 offset:56320
	global_load_lds_dwordx4 v[148:149], off
	s_add_i32 m0, s20, 0x2000
	s_add_u32 s18, s18, 0x20080
	v_lshl_add_u64 v[148:149], v[214:215], 0, s[68:69]
	s_addc_u32 s19, s19, 0
	s_add_i32 s20, s83, s22
	global_load_lds_dwordx4 v[148:149], off
	v_lshl_add_u64 v[148:149], s[18:19], 0, v[128:129]
	s_mov_b32 m0, s20
	s_nop 0
	global_load_lds_dwordx4 v[148:149], off
	v_lshl_add_u64 v[148:149], s[18:19], 0, v[130:131]
	s_add_i32 m0, s20, 0x2000
	s_nop 0
	global_load_lds_dwordx4 v[148:149], off
	v_lshl_add_u64 v[148:149], v[216:217], 0, s[68:69]
	s_mov_b32 m0, s81
	s_nop 0
	global_load_lds_dwordx4 v[148:149], off
	v_lshl_add_u64 v[148:149], v[218:219], 0, s[68:69]
	s_mov_b32 m0, s48
	s_nop 0
	global_load_lds_dwordx4 v[148:149], off
	s_waitcnt vmcnt(8)
	s_waitcnt lgkmcnt(0)
	s_barrier
	s_setprio 1
	s_waitcnt lgkmcnt(0)
	v_mfma_f32_16x16x32_bf16 v[60:63], v[140:143], v[178:181], v[60:63]
	v_mfma_f32_16x16x32_bf16 v[56:59], v[154:157], v[178:181], v[56:59]
	v_mfma_f32_16x16x32_bf16 v[44:47], v[140:143], v[186:189], v[44:47]
	v_mfma_f32_16x16x32_bf16 v[40:43], v[154:157], v[186:189], v[40:43]
	v_mfma_f32_16x16x32_bf16 v[28:31], v[140:143], v[198:201], v[28:31]
	v_mfma_f32_16x16x32_bf16 v[24:27], v[154:157], v[198:201], v[24:27]
	v_mfma_f32_16x16x32_bf16 v[12:15], v[140:143], v[206:209], v[12:15]
	v_mfma_f32_16x16x32_bf16 v[8:11], v[154:157], v[206:209], v[8:11]
	v_mfma_f32_16x16x32_bf16 v[60:63], v[144:147], v[182:185], v[60:63]
	v_mfma_f32_16x16x32_bf16 v[56:59], v[158:161], v[182:185], v[56:59]
	v_mfma_f32_16x16x32_bf16 v[44:47], v[144:147], v[190:193], v[44:47]
	v_mfma_f32_16x16x32_bf16 v[40:43], v[158:161], v[190:193], v[40:43]
	v_mfma_f32_16x16x32_bf16 v[28:31], v[144:147], v[202:205], v[28:31]
	v_mfma_f32_16x16x32_bf16 v[24:27], v[158:161], v[202:205], v[24:27]
	v_mfma_f32_16x16x32_bf16 v[12:15], v[144:147], v[210:213], v[12:15]
	v_mfma_f32_16x16x32_bf16 v[8:11], v[158:161], v[210:213], v[8:11]
	s_setprio 0
	s_setprio 1
	v_mfma_f32_16x16x32_bf16 v[52:55], v[162:165], v[178:181], v[52:55]
	v_mfma_f32_16x16x32_bf16 v[48:51], v[170:173], v[178:181], v[48:51]
	v_mfma_f32_16x16x32_bf16 v[36:39], v[162:165], v[186:189], v[36:39]
	v_mfma_f32_16x16x32_bf16 v[32:35], v[170:173], v[186:189], v[32:35]
	v_mfma_f32_16x16x32_bf16 v[20:23], v[162:165], v[198:201], v[20:23]
	v_mfma_f32_16x16x32_bf16 v[16:19], v[170:173], v[198:201], v[16:19]
	v_mfma_f32_16x16x32_bf16 v[0:3], v[162:165], v[206:209], v[0:3]
	v_mfma_f32_16x16x32_bf16 v[4:7], v[170:173], v[206:209], v[4:7]
	v_mfma_f32_16x16x32_bf16 v[52:55], v[166:169], v[182:185], v[52:55]
	v_mfma_f32_16x16x32_bf16 v[48:51], v[174:177], v[182:185], v[48:51]
	v_mfma_f32_16x16x32_bf16 v[36:39], v[166:169], v[190:193], v[36:39]
	v_mfma_f32_16x16x32_bf16 v[32:35], v[174:177], v[190:193], v[32:35]
	v_mfma_f32_16x16x32_bf16 v[20:23], v[166:169], v[202:205], v[20:23]
	v_mfma_f32_16x16x32_bf16 v[16:19], v[174:177], v[202:205], v[16:19]
	v_mfma_f32_16x16x32_bf16 v[0:3], v[166:169], v[210:213], v[0:3]
	v_mfma_f32_16x16x32_bf16 v[4:7], v[174:177], v[210:213], v[4:7]
	s_setprio 0
	s_barrier
	s_add_i32 s60, s60, 2
	s_add_u32 s16, s16, 0x100
	s_addc_u32 s17, s17, 0
	s_add_u32 s50, s50, 0x100
	s_addc_u32 s51, s51, 0
	s_cmp_gt_u32 s60, 5
	s_cbranch_scc0 .LBB0_2018
	s_and_b64 vcc, exec, s[28:29]
	s_cbranch_vccz .LBB0_2021
	s_barrier

; #define PG8_STAGE(bufoff, gbase, voff) do { _Pragma("unroll") for (int _i = 0; _i < 2; ++_i) \
;         __builtin_amdgcn_global_load_lds((const unsigned*)((const char*)(gbase) + (voff)[_i]), (PG8_LAS unsigned*)(lds + (bufoff) + ldsw + _i * 8192), 16, 0, 0); } while (0)
; #define PG8_STAGE_A(bufoff, gbase, h, nx) do { _Pragma("unroll") for (int _i = 0; _i < 2; ++_i) { \
;         const unsigned vo_ = GA ? ((nx) ? vgn[h][_i] : vgc[h][_i]) : voffA[_i]; \
;         __builtin_amdgcn_global_load_lds((const unsigned*)((const char*)(gbase) + vo_), (PG8_LAS unsigned*)(lds + (bufoff) + ldsw + _i * 8192), 16, 0, 0); } } while (0)
; #define PG8_LDA(dst, b, h) do { _Pragma("unroll") for (int m = 0; m < 4; ++m) _Pragma("unroll") for (int k = 0; k < 2; ++k) dst[m][k] = *(const PG8_LAS bf16x8*)(lds + PG8_SA(b, h) + aoff + m * 2048 + k * 1024); } while (0)
; #define PG8_LDB(dst, b, h) do { _Pragma("unroll") for (int n = 0; n < 2; ++n) _Pragma("unroll") for (int k = 0; k < 2; ++k) dst[n][k] = *(const PG8_LAS bf16x8*)(lds + PG8_SB(b, h) + boff + n * 2048 + k * 1024); } while (0)
; #define PG8_WAIT_V(n) asm volatile("s_waitcnt vmcnt(" #n ")" ::: "memory")
; #define PG8_WAIT_L(n) asm volatile("s_waitcnt lgkmcnt(" #n ")" ::: "memory")
; #define PG8_BAR __builtin_amdgcn_s_barrier()
; #define PG8_SCHED __builtin_amdgcn_sched_barrier(0)
; template <class Epi, class Sched>
; __device__ __forceinline__ void gemm_phase(const int WID_, PG8_LAS unsigned char* lds, const Sched& S, const Epi& E) {
;     ...
;         for (int t = 0; t < nt; t += 2) {
;             const bool last = (t == nt - 2);
;             const char* a1 = cA + (size_t)(t + 1) * kstep;
;             const char* a2 = last ? nA : cA + (size_t)(t + 2) * kstep; const char* b2 = last ? nB : cB + (size_t)(t + 2) * kstep;
;             const char* a3 = a2 + kstep; const char* b3 = b2 + kstep;
;             PG8_LDB(B0, 0, 0); PG8_LDB(B1, 0, 1); PG8_SCHED; PG8_LDA(At, 0, 0); PG8_STAGE_A(PG8_SA(1, 1), a1 + hstepA, 1, false);
;             PG8_WAIT_V(8); PG8_WAIT_L(0); PG8_BAR; PG8_MMA(0, 0, At, B0); PG8_MMA(0, 1, At, B1); PG8_BAR; PG8_SCHED;
;             PG8_LDA(At, 0, 1); PG8_STAGE(PG8_SB(0, 0), b2, voffB); PG8_STAGE(PG8_SB(0, 1), b2 + hstepB, voffB); PG8_STAGE_A(PG8_SA(0, 0), a2, 0, last);
;             PG8_WAIT_V(8); PG8_WAIT_L(0); PG8_BAR; PG8_MMA(1, 0, At, B0); PG8_MMA(1, 1, At, B1); PG8_BAR; PG8_SCHED;
.LBB0_2036:
	v_add_u32_e32 v149, s43, v145
	ds_read_b128 v[140:143], v149
	ds_read_b128 v[150:153], v149 offset:1024
	ds_read_b128 v[154:157], v149 offset:2048
	ds_read_b128 v[158:161], v149 offset:3072
	v_add_u32_e32 v149, s67, v145
	ds_read_b128 v[162:165], v149
	ds_read_b128 v[166:169], v149 offset:1024
	ds_read_b128 v[170:173], v149 offset:2048
	ds_read_b128 v[174:177], v149 offset:3072
	s_add_u32 s20, s18, 0xfffc0080
	s_addc_u32 s21, s19, -1
	s_cmp_eq_u32 s63, 12
	s_cselect_b32 s23, s13, s21
	s_cselect_b32 s22, s12, s20
	s_cselect_b32 s21, s15, s11
	s_cselect_b32 s20, s14, s9
	v_lshl_add_u64 v[214:215], s[18:19], 0, v[136:137]
	s_add_i32 m0, s44, 0xc000
	ds_read_b128 v[178:181], v148
	ds_read_b128 v[182:185], v148 offset:1024
	ds_read_b128 v[186:189], v148 offset:2048
	ds_read_b128 v[190:193], v148 offset:3072
	ds_read_b128 v[198:201], v148 offset:4096
	ds_read_b128 v[202:205], v148 offset:5120
	ds_read_b128 v[206:209], v148 offset:6144
	ds_read_b128 v[210:213], v148 offset:7168
	global_load_lds_dwordx4 v[214:215], off
	v_lshl_add_u64 v[214:215], s[18:19], 0, v[138:139]
	s_add_i32 m0, s44, 0xe000
	s_nop 0
	global_load_lds_dwordx4 v[214:215], off
	s_waitcnt vmcnt(8)
	s_waitcnt lgkmcnt(0)
	s_barrier
	s_nop 0
	s_setprio 1
	s_waitcnt lgkmcnt(0)
	v_mfma_f32_16x16x32_bf16 v[124:127], v[140:143], v[178:181], v[124:127]
	v_mfma_f32_16x16x32_bf16 v[120:123], v[154:157], v[178:181], v[120:123]
	v_mfma_f32_16x16x32_bf16 v[108:111], v[140:143], v[186:189], v[108:111]
	v_mfma_f32_16x16x32_bf16 v[104:107], v[154:157], v[186:189], v[104:107]
	v_mfma_f32_16x16x32_bf16 v[92:95], v[140:143], v[198:201], v[92:95]
	v_mfma_f32_16x16x32_bf16 v[88:91], v[154:157], v[198:201], v[88:91]
	v_mfma_f32_16x16x32_bf16 v[76:79], v[140:143], v[206:209], v[76:79]
	v_mfma_f32_16x16x32_bf16 v[72:75], v[154:157], v[206:209], v[72:75]
	v_mfma_f32_16x16x32_bf16 v[124:127], v[150:153], v[182:185], v[124:127]
	v_mfma_f32_16x16x32_bf16 v[120:123], v[158:161], v[182:185], v[120:123]
	v_mfma_f32_16x16x32_bf16 v[108:111], v[150:153], v[190:193], v[108:111]
	v_mfma_f32_16x16x32_bf16 v[104:107], v[158:161], v[190:193], v[104:107]
	v_mfma_f32_16x16x32_bf16 v[92:95], v[150:153], v[202:205], v[92:95]
	v_mfma_f32_16x16x32_bf16 v[88:91], v[158:161], v[202:205], v[88:91]
	v_mfma_f32_16x16x32_bf16 v[76:79], v[150:153], v[210:213], v[76:79]
	v_mfma_f32_16x16x32_bf16 v[72:75], v[158:161], v[210:213], v[72:75]
	s_setprio 0
	s_setprio 1
	v_mfma_f32_16x16x32_bf16 v[116:119], v[162:165], v[178:181], v[116:119]
	v_mfma_f32_16x16x32_bf16 v[112:115], v[170:173], v[178:181], v[112:115]
	v_mfma_f32_16x16x32_bf16 v[100:103], v[162:165], v[186:189], v[100:103]
	v_mfma_f32_16x16x32_bf16 v[96:99], v[170:173], v[186:189], v[96:99]
	v_mfma_f32_16x16x32_bf16 v[84:87], v[162:165], v[198:201], v[84:87]
	v_mfma_f32_16x16x32_bf16 v[80:83], v[170:173], v[198:201], v[80:83]
	v_mfma_f32_16x16x32_bf16 v[68:71], v[162:165], v[206:209], v[68:71]
	v_mfma_f32_16x16x32_bf16 v[64:67], v[170:173], v[206:209], v[64:67]
	v_mfma_f32_16x16x32_bf16 v[116:119], v[166:169], v[182:185], v[116:119]
	v_mfma_f32_16x16x32_bf16 v[112:115], v[174:177], v[182:185], v[112:115]
	v_mfma_f32_16x16x32_bf16 v[100:103], v[166:169], v[190:193], v[100:103]
	v_mfma_f32_16x16x32_bf16 v[96:99], v[174:177], v[190:193], v[96:99]
	v_mfma_f32_16x16x32_bf16 v[84:87], v[166:169], v[202:205], v[84:87]
	v_mfma_f32_16x16x32_bf16 v[80:83], v[174:177], v[202:205], v[80:83]
	v_mfma_f32_16x16x32_bf16 v[68:71], v[166:169], v[210:213], v[68:71]
	v_mfma_f32_16x16x32_bf16 v[64:67], v[174:177], v[210:213], v[64:67]
	s_setprio 0
	s_barrier
	s_add_i32 s46, s43, s33
	v_lshl_add_u64 v[214:215], s[20:21], 0, v[128:129]
	s_mov_b32 m0, s46
	ds_read_b128 v[178:181], v148 offset:16384
	ds_read_b128 v[182:185], v148 offset:17408
	ds_read_b128 v[186:189], v148 offset:18432
	ds_read_b128 v[190:193], v148 offset:19456
	ds_read_b128 v[198:201], v148 offset:20480
	ds_read_b128 v[202:205], v148 offset:21504
	ds_read_b128 v[206:209], v148 offset:22528
	ds_read_b128 v[210:213], v148 offset:23552
	global_load_lds_dwordx4 v[214:215], off
	s_add_i32 m0, s46, 0x2000
	s_add_u32 s78, s20, 0x40000
	v_lshl_add_u64 v[216:217], s[20:21], 0, v[134:135]
	s_addc_u32 s79, s21, 0
	s_add_i32 s46, s67, s33
	global_load_lds_dwordx4 v[216:217], off
	v_lshl_add_u64 v[218:219], s[78:79], 0, v[128:129]
	s_mov_b32 m0, s46
	v_lshl_add_u64 v[220:221], s[22:23], 0, v[132:133]
	global_load_lds_dwordx4 v[218:219], off
	v_lshl_add_u64 v[218:219], s[78:79], 0, v[134:135]
	s_add_i32 m0, s46, 0x2000
	s_nop 0
	global_load_lds_dwordx4 v[218:219], off
	v_lshl_add_u64 v[218:219], s[22:23], 0, v[130:131]
	s_mov_b32 m0, s44
	s_nop 0
	global_load_lds_dwordx4 v[218:219], off
	s_mov_b32 m0, s48
	s_nop 0
	global_load_lds_dwordx4 v[220:221], off
	s_waitcnt vmcnt(8)
	s_waitcnt lgkmcnt(0)
	s_barrier
; #define PG8_STAGE_A(bufoff, gbase, h, nx) do { _Pragma("unroll") for (int _i = 0; _i < 2; ++_i) { \
;         const unsigned vo_ = GA ? ((nx) ? vgn[h][_i] : vgc[h][_i]) : voffA[_i]; \
;         __builtin_amdgcn_global_load_lds((const unsigned*)((const char*)(gbase) + vo_), (PG8_LAS unsigned*)(lds + (bufoff) + ldsw + _i * 8192), 16, 0, 0); } } while (0)
; #define PG8_LDA(dst, b, h) do { _Pragma("unroll") for (int m = 0; m < 4; ++m) _Pragma("unroll") for (int k = 0; k < 2; ++k) dst[m][k] = *(const PG8_LAS bf16x8*)(lds + PG8_SA(b, h) + aoff + m * 2048 + k * 1024); } while (0)
; #define PG8_LDB(dst, b, h) do { _Pragma("unroll") for (int n = 0; n < 2; ++n) _Pragma("unroll") for (int k = 0; k < 2; ++k) dst[n][k] = *(const PG8_LAS bf16x8*)(lds + PG8_SB(b, h) + boff + n * 2048 + k * 1024); } while (0)
; #define PG8_MMA(ai, bj, At, Bt) do { __builtin_amdgcn_s_setprio(1); _Pragma("unroll") for (int m = 0; m < 4; ++m) _Pragma("unroll") for (int n = 0; n < 2; ++n) _Pragma("unroll") for (int k = 0; k < 2; ++k) \
;         acc[ai][bj][m][n] = __builtin_amdgcn_mfma_f32_16x16x32_bf16(Bt[n][k], At[m][k], acc[ai][bj][m][n], 0, 0, 0); __builtin_amdgcn_s_setprio(0); } while (0)
; #define PG8_WAIT_V(n) asm volatile("s_waitcnt vmcnt(" #n ")" ::: "memory")
; #define PG8_WAIT_L(n) asm volatile("s_waitcnt lgkmcnt(" #n ")" ::: "memory")
; #define PG8_BAR __builtin_amdgcn_s_barrier()
; #define PG8_SCHED __builtin_amdgcn_sched_barrier(0)
; template <class Epi, class Sched>
; __device__ __forceinline__ void gemm_phase(const int WID_, PG8_LAS unsigned char* lds, const Sched& S, const Epi& E) {
;     ...
;             PG8_WAIT_V(8); PG8_WAIT_L(0); PG8_BAR; PG8_MMA(1, 0, At, B0); PG8_MMA(1, 1, At, B1); PG8_BAR; PG8_SCHED;
;             PG8_LDB(B0, 1, 0); PG8_LDB(B1, 1, 1); PG8_SCHED; PG8_LDA(At, 1, 0); PG8_STAGE_A(PG8_SA(0, 1), a2 + hstepA, 1, last);
;             PG8_WAIT_V(8); PG8_WAIT_L(0); PG8_BAR; PG8_MMA(0, 0, At, B0); PG8_MMA(0, 1, At, B1); PG8_BAR; PG8_SCHED;
	s_nop 0
	s_setprio 1
	s_waitcnt lgkmcnt(0)
	v_mfma_f32_16x16x32_bf16 v[60:63], v[140:143], v[178:181], v[60:63]
	v_mfma_f32_16x16x32_bf16 v[56:59], v[154:157], v[178:181], v[56:59]
	v_mfma_f32_16x16x32_bf16 v[44:47], v[140:143], v[186:189], v[44:47]
	v_mfma_f32_16x16x32_bf16 v[40:43], v[154:157], v[186:189], v[40:43]
	v_mfma_f32_16x16x32_bf16 v[28:31], v[140:143], v[198:201], v[28:31]
	v_mfma_f32_16x16x32_bf16 v[24:27], v[154:157], v[198:201], v[24:27]
	v_mfma_f32_16x16x32_bf16 v[12:15], v[140:143], v[206:209], v[12:15]
	v_mfma_f32_16x16x32_bf16 v[8:11], v[154:157], v[206:209], v[8:11]
	v_mfma_f32_16x16x32_bf16 v[60:63], v[150:153], v[182:185], v[60:63]
	v_mfma_f32_16x16x32_bf16 v[56:59], v[158:161], v[182:185], v[56:59]
	v_mfma_f32_16x16x32_bf16 v[44:47], v[150:153], v[190:193], v[44:47]
	v_mfma_f32_16x16x32_bf16 v[40:43], v[158:161], v[190:193], v[40:43]
	v_mfma_f32_16x16x32_bf16 v[28:31], v[150:153], v[202:205], v[28:31]
	v_mfma_f32_16x16x32_bf16 v[24:27], v[158:161], v[202:205], v[24:27]
	v_mfma_f32_16x16x32_bf16 v[12:15], v[150:153], v[210:213], v[12:15]
	v_mfma_f32_16x16x32_bf16 v[8:11], v[158:161], v[210:213], v[8:11]
	s_setprio 0
	s_setprio 1
	v_mfma_f32_16x16x32_bf16 v[52:55], v[162:165], v[178:181], v[52:55]
	v_mfma_f32_16x16x32_bf16 v[48:51], v[170:173], v[178:181], v[48:51]
	v_mfma_f32_16x16x32_bf16 v[36:39], v[162:165], v[186:189], v[36:39]
	v_mfma_f32_16x16x32_bf16 v[32:35], v[170:173], v[186:189], v[32:35]
	v_mfma_f32_16x16x32_bf16 v[20:23], v[162:165], v[198:201], v[20:23]
	v_mfma_f32_16x16x32_bf16 v[16:19], v[170:173], v[198:201], v[16:19]
	v_mfma_f32_16x16x32_bf16 v[4:7], v[162:165], v[206:209], v[4:7]
	v_mfma_f32_16x16x32_bf16 v[0:3], v[170:173], v[206:209], v[0:3]
	v_mfma_f32_16x16x32_bf16 v[52:55], v[166:169], v[182:185], v[52:55]
	v_mfma_f32_16x16x32_bf16 v[48:51], v[174:177], v[182:185], v[48:51]
	v_mfma_f32_16x16x32_bf16 v[36:39], v[166:169], v[190:193], v[36:39]
	v_mfma_f32_16x16x32_bf16 v[32:35], v[174:177], v[190:193], v[32:35]
	v_mfma_f32_16x16x32_bf16 v[20:23], v[166:169], v[202:205], v[20:23]
	v_mfma_f32_16x16x32_bf16 v[16:19], v[174:177], v[202:205], v[16:19]
	v_mfma_f32_16x16x32_bf16 v[4:7], v[166:169], v[210:213], v[4:7]
	v_mfma_f32_16x16x32_bf16 v[0:3], v[174:177], v[210:213], v[0:3]
	s_setprio 0
	s_barrier
	v_add_u32_e32 v149, s82, v145
	ds_read_b128 v[140:143], v149
	ds_read_b128 v[150:153], v149 offset:1024
	ds_read_b128 v[154:157], v149 offset:2048
	ds_read_b128 v[158:161], v149 offset:3072
	v_add_u32_e32 v149, s83, v145
	ds_read_b128 v[162:165], v149
	ds_read_b128 v[166:169], v149 offset:1024
	ds_read_b128 v[170:173], v149 offset:2048
	ds_read_b128 v[174:177], v149 offset:3072
	s_add_u32 s22, s22, 0x40000
	s_addc_u32 s23, s23, 0
	s_mov_b32 m0, s49
	v_lshl_add_u64 v[222:223], s[22:23], 0, v[130:131]
	ds_read_b128 v[178:181], v148 offset:32768
	ds_read_b128 v[182:185], v148 offset:33792
	ds_read_b128 v[186:189], v148 offset:34816
	ds_read_b128 v[190:193], v148 offset:35840
	ds_read_b128 v[198:201], v148 offset:36864
	ds_read_b128 v[202:205], v148 offset:37888
	ds_read_b128 v[206:209], v148 offset:38912
	ds_read_b128 v[210:213], v148 offset:39936
	global_load_lds_dwordx4 v[222:223], off
	v_lshl_add_u64 v[222:223], s[22:23], 0, v[132:133]
	s_mov_b32 m0, s50
	s_nop 0
	global_load_lds_dwordx4 v[222:223], off
	s_waitcnt vmcnt(8)
	s_waitcnt lgkmcnt(0)
	s_barrier
	s_nop 0
	s_setprio 1
	s_waitcnt lgkmcnt(0)
	v_mfma_f32_16x16x32_bf16 v[124:127], v[140:143], v[178:181], v[124:127]
	v_mfma_f32_16x16x32_bf16 v[120:123], v[154:157], v[178:181], v[120:123]
	v_mfma_f32_16x16x32_bf16 v[108:111], v[140:143], v[186:189], v[108:111]
	v_mfma_f32_16x16x32_bf16 v[104:107], v[154:157], v[186:189], v[104:107]
	v_mfma_f32_16x16x32_bf16 v[92:95], v[140:143], v[198:201], v[92:95]
	v_mfma_f32_16x16x32_bf16 v[88:91], v[154:157], v[198:201], v[88:91]
	v_mfma_f32_16x16x32_bf16 v[76:79], v[140:143], v[206:209], v[76:79]
	v_mfma_f32_16x16x32_bf16 v[72:75], v[154:157], v[206:209], v[72:75]
	v_mfma_f32_16x16x32_bf16 v[124:127], v[150:153], v[182:185], v[124:127]
	v_mfma_f32_16x16x32_bf16 v[120:123], v[158:161], v[182:185], v[120:123]
	v_mfma_f32_16x16x32_bf16 v[108:111], v[150:153], v[190:193], v[108:111]
	v_mfma_f32_16x16x32_bf16 v[104:107], v[158:161], v[190:193], v[104:107]
	v_mfma_f32_16x16x32_bf16 v[92:95], v[150:153], v[202:205], v[92:95]
	v_mfma_f32_16x16x32_bf16 v[88:91], v[158:161], v[202:205], v[88:91]
	v_mfma_f32_16x16x32_bf16 v[76:79], v[150:153], v[210:213], v[76:79]
	v_mfma_f32_16x16x32_bf16 v[72:75], v[158:161], v[210:213], v[72:75]
	s_setprio 0
	s_setprio 1
	v_mfma_f32_16x16x32_bf16 v[116:119], v[162:165], v[178:181], v[116:119]
	v_mfma_f32_16x16x32_bf16 v[112:115], v[170:173], v[178:181], v[112:115]
	v_mfma_f32_16x16x32_bf16 v[100:103], v[162:165], v[186:189], v[100:103]
	v_mfma_f32_16x16x32_bf16 v[96:99], v[170:173], v[186:189], v[96:99]
	v_mfma_f32_16x16x32_bf16 v[84:87], v[162:165], v[198:201], v[84:87]
	v_mfma_f32_16x16x32_bf16 v[80:83], v[170:173], v[198:201], v[80:83]
	v_mfma_f32_16x16x32_bf16 v[68:71], v[162:165], v[206:209], v[68:71]
	v_mfma_f32_16x16x32_bf16 v[64:67], v[170:173], v[206:209], v[64:67]
	v_mfma_f32_16x16x32_bf16 v[116:119], v[166:169], v[182:185], v[116:119]
	v_mfma_f32_16x16x32_bf16 v[112:115], v[174:177], v[182:185], v[112:115]
	v_mfma_f32_16x16x32_bf16 v[100:103], v[166:169], v[190:193], v[100:103]
	v_mfma_f32_16x16x32_bf16 v[96:99], v[174:177], v[190:193], v[96:99]
	v_mfma_f32_16x16x32_bf16 v[84:87], v[166:169], v[202:205], v[84:87]
	v_mfma_f32_16x16x32_bf16 v[80:83], v[174:177], v[202:205], v[80:83]
	v_mfma_f32_16x16x32_bf16 v[68:71], v[166:169], v[210:213], v[68:71]
	v_mfma_f32_16x16x32_bf16 v[64:67], v[174:177], v[210:213], v[64:67]
	s_setprio 0
	s_barrier
; #define PG8_STAGE(bufoff, gbase, voff) do { _Pragma("unroll") for (int _i = 0; _i < 2; ++_i) \
;         __builtin_amdgcn_global_load_lds((const unsigned*)((const char*)(gbase) + (voff)[_i]), (PG8_LAS unsigned*)(lds + (bufoff) + ldsw + _i * 8192), 16, 0, 0); } while (0)
; #define PG8_STAGE_A(bufoff, gbase, h, nx) do { _Pragma("unroll") for (int _i = 0; _i < 2; ++_i) { \
;         const unsigned vo_ = GA ? ((nx) ? vgn[h][_i] : vgc[h][_i]) : voffA[_i]; \
;         __builtin_amdgcn_global_load_lds((const unsigned*)((const char*)(gbase) + vo_), (PG8_LAS unsigned*)(lds + (bufoff) + ldsw + _i * 8192), 16, 0, 0); } } while (0)
; #define PG8_LDA(dst, b, h) do { _Pragma("unroll") for (int m = 0; m < 4; ++m) _Pragma("unroll") for (int k = 0; k < 2; ++k) dst[m][k] = *(const PG8_LAS bf16x8*)(lds + PG8_SA(b, h) + aoff + m * 2048 + k * 1024); } while (0)
; #define PG8_MMA(ai, bj, At, Bt) do { __builtin_amdgcn_s_setprio(1); _Pragma("unroll") for (int m = 0; m < 4; ++m) _Pragma("unroll") for (int n = 0; n < 2; ++n) _Pragma("unroll") for (int k = 0; k < 2; ++k) \
;         acc[ai][bj][m][n] = __builtin_amdgcn_mfma_f32_16x16x32_bf16(Bt[n][k], At[m][k], acc[ai][bj][m][n], 0, 0, 0); __builtin_amdgcn_s_setprio(0); } while (0)
; #define PG8_WAIT_V(n) asm volatile("s_waitcnt vmcnt(" #n ")" ::: "memory")
; #define PG8_WAIT_L(n) asm volatile("s_waitcnt lgkmcnt(" #n ")" ::: "memory")
; #define PG8_BAR __builtin_amdgcn_s_barrier()
; #define PG8_SCHED __builtin_amdgcn_sched_barrier(0)
; template <class Epi, class Sched>
; __device__ __forceinline__ void gemm_phase(const int WID_, PG8_LAS unsigned char* lds, const Sched& S, const Epi& E) {
;     ...
;             PG8_LDA(At, 1, 1); PG8_STAGE(PG8_SB(1, 0), b3, voffB); PG8_STAGE(PG8_SB(1, 1), b3 + hstepB, voffB); PG8_STAGE_A(PG8_SA(1, 0), a3, 0, last);
;             PG8_WAIT_V(8); PG8_WAIT_L(0); PG8_BAR; PG8_MMA(1, 0, At, B0); PG8_MMA(1, 1, At, B1); PG8_BAR; PG8_SCHED;
;         }
;         if (wr == 0) PG8_BAR;
	s_add_i32 s22, s82, s33
	v_lshl_add_u64 v[214:215], v[214:215], 0, s[68:69]
	s_mov_b32 m0, s22
	ds_read_b128 v[178:181], v148 offset:49152
	ds_read_b128 v[182:185], v148 offset:50176
	ds_read_b128 v[186:189], v148 offset:51200
	ds_read_b128 v[190:193], v148 offset:52224
	ds_read_b128 v[198:201], v148 offset:53248
	ds_read_b128 v[202:205], v148 offset:54272
	ds_read_b128 v[206:209], v148 offset:55296
	ds_read_b128 v[210:213], v148 offset:56320
	global_load_lds_dwordx4 v[214:215], off
	s_add_i32 m0, s22, 0x2000
	s_add_u32 s20, s20, 0x40080
	v_lshl_add_u64 v[214:215], v[216:217], 0, s[68:69]
	s_addc_u32 s21, s21, 0
	s_add_i32 s22, s83, s33
	global_load_lds_dwordx4 v[214:215], off
	v_lshl_add_u64 v[214:215], s[20:21], 0, v[128:129]
	s_mov_b32 m0, s22
	s_nop 0
	global_load_lds_dwordx4 v[214:215], off
	v_lshl_add_u64 v[214:215], s[20:21], 0, v[134:135]
	s_add_i32 m0, s22, 0x2000
	s_nop 0
	global_load_lds_dwordx4 v[214:215], off
	v_lshl_add_u64 v[214:215], v[218:219], 0, s[68:69]
	s_mov_b32 m0, s51
	s_nop 0
	global_load_lds_dwordx4 v[214:215], off
	v_lshl_add_u64 v[214:215], v[220:221], 0, s[68:69]
	s_mov_b32 m0, s60
	s_nop 0
	global_load_lds_dwordx4 v[214:215], off
	s_waitcnt vmcnt(8)
	s_waitcnt lgkmcnt(0)
	s_barrier
	s_setprio 1
	s_waitcnt lgkmcnt(0)
	v_mfma_f32_16x16x32_bf16 v[60:63], v[140:143], v[178:181], v[60:63]
	v_mfma_f32_16x16x32_bf16 v[56:59], v[154:157], v[178:181], v[56:59]
	v_mfma_f32_16x16x32_bf16 v[44:47], v[140:143], v[186:189], v[44:47]
	v_mfma_f32_16x16x32_bf16 v[40:43], v[154:157], v[186:189], v[40:43]
	v_mfma_f32_16x16x32_bf16 v[28:31], v[140:143], v[198:201], v[28:31]
	v_mfma_f32_16x16x32_bf16 v[24:27], v[154:157], v[198:201], v[24:27]
	v_mfma_f32_16x16x32_bf16 v[12:15], v[140:143], v[206:209], v[12:15]
	v_mfma_f32_16x16x32_bf16 v[8:11], v[154:157], v[206:209], v[8:11]
	v_mfma_f32_16x16x32_bf16 v[60:63], v[150:153], v[182:185], v[60:63]
	v_mfma_f32_16x16x32_bf16 v[56:59], v[158:161], v[182:185], v[56:59]
	v_mfma_f32_16x16x32_bf16 v[44:47], v[150:153], v[190:193], v[44:47]
	v_mfma_f32_16x16x32_bf16 v[40:43], v[158:161], v[190:193], v[40:43]
	v_mfma_f32_16x16x32_bf16 v[28:31], v[150:153], v[202:205], v[28:31]
	v_mfma_f32_16x16x32_bf16 v[24:27], v[158:161], v[202:205], v[24:27]
	v_mfma_f32_16x16x32_bf16 v[12:15], v[150:153], v[210:213], v[12:15]
	v_mfma_f32_16x16x32_bf16 v[8:11], v[158:161], v[210:213], v[8:11]
	s_setprio 0
	s_setprio 1
	v_mfma_f32_16x16x32_bf16 v[52:55], v[162:165], v[178:181], v[52:55]
	v_mfma_f32_16x16x32_bf16 v[48:51], v[170:173], v[178:181], v[48:51]
	v_mfma_f32_16x16x32_bf16 v[36:39], v[162:165], v[186:189], v[36:39]
	v_mfma_f32_16x16x32_bf16 v[32:35], v[170:173], v[186:189], v[32:35]
	v_mfma_f32_16x16x32_bf16 v[20:23], v[162:165], v[198:201], v[20:23]
	v_mfma_f32_16x16x32_bf16 v[16:19], v[170:173], v[198:201], v[16:19]
	v_mfma_f32_16x16x32_bf16 v[4:7], v[162:165], v[206:209], v[4:7]
	v_mfma_f32_16x16x32_bf16 v[0:3], v[170:173], v[206:209], v[0:3]
	v_mfma_f32_16x16x32_bf16 v[52:55], v[166:169], v[182:185], v[52:55]
	v_mfma_f32_16x16x32_bf16 v[48:51], v[174:177], v[182:185], v[48:51]
	v_mfma_f32_16x16x32_bf16 v[36:39], v[166:169], v[190:193], v[36:39]
	v_mfma_f32_16x16x32_bf16 v[32:35], v[174:177], v[190:193], v[32:35]
	v_mfma_f32_16x16x32_bf16 v[20:23], v[166:169], v[202:205], v[20:23]
	v_mfma_f32_16x16x32_bf16 v[16:19], v[174:177], v[202:205], v[16:19]
	v_mfma_f32_16x16x32_bf16 v[4:7], v[166:169], v[210:213], v[4:7]
	v_mfma_f32_16x16x32_bf16 v[0:3], v[174:177], v[210:213], v[0:3]
	s_setprio 0
	s_barrier
	s_add_i32 s63, s63, 2
	s_add_u32 s18, s18, 0x100
	s_addc_u32 s19, s19, 0
	s_add_u32 s9, s9, 0x100
	s_addc_u32 s11, s11, 0
	s_cmp_gt_u32 s63, 13
	s_cbranch_scc0 .LBB0_2036
	s_and_b64 vcc, exec, s[6:7]
	s_cbranch_vccz .LBB0_2039
	s_barrier

; #define PG8_STAGE(bufoff, gbase, voff) do { _Pragma("unroll") for (int _i = 0; _i < 2; ++_i) \
;         __builtin_amdgcn_global_load_lds((const unsigned*)((const char*)(gbase) + (voff)[_i]), (PG8_LAS unsigned*)(lds + (bufoff) + ldsw + _i * 8192), 16, 0, 0); } while (0)
; #define PG8_STAGE_A(bufoff, gbase, h, nx) do { _Pragma("unroll") for (int _i = 0; _i < 2; ++_i) { \
;         const unsigned vo_ = GA ? ((nx) ? vgn[h][_i] : vgc[h][_i]) : voffA[_i]; \
;         __builtin_amdgcn_global_load_lds((const unsigned*)((const char*)(gbase) + vo_), (PG8_LAS unsigned*)(lds + (bufoff) + ldsw + _i * 8192), 16, 0, 0); } } while (0)
; #define PG8_LDA(dst, b, h) do { _Pragma("unroll") for (int m = 0; m < 4; ++m) _Pragma("unroll") for (int k = 0; k < 2; ++k) dst[m][k] = *(const PG8_LAS bf16x8*)(lds + PG8_SA(b, h) + aoff + m * 2048 + k * 1024); } while (0)
; #define PG8_LDB(dst, b, h) do { _Pragma("unroll") for (int n = 0; n < 2; ++n) _Pragma("unroll") for (int k = 0; k < 2; ++k) dst[n][k] = *(const PG8_LAS bf16x8*)(lds + PG8_SB(b, h) + boff + n * 2048 + k * 1024); } while (0)
; #define PG8_WAIT_V(n) asm volatile("s_waitcnt vmcnt(" #n ")" ::: "memory")
; #define PG8_WAIT_L(n) asm volatile("s_waitcnt lgkmcnt(" #n ")" ::: "memory")
; #define PG8_BAR __builtin_amdgcn_s_barrier()
; #define PG8_SCHED __builtin_amdgcn_sched_barrier(0)
; template <class Epi, class Sched>
; __device__ __forceinline__ void gemm_phase(const int WID_, PG8_LAS unsigned char* lds, const Sched& S, const Epi& E) {
;     ...
;         for (int t = 0; t < nt; t += 2) {
;             const bool last = (t == nt - 2);
;             const char* a1 = cA + (size_t)(t + 1) * kstep;
;             const char* a2 = last ? nA : cA + (size_t)(t + 2) * kstep; const char* b2 = last ? nB : cB + (size_t)(t + 2) * kstep;
;             const char* a3 = a2 + kstep; const char* b3 = b2 + kstep;
;             PG8_LDB(B0, 0, 0); PG8_LDB(B1, 0, 1); PG8_SCHED; PG8_LDA(At, 0, 0); PG8_STAGE_A(PG8_SA(1, 1), a1 + hstepA, 1, false);
;             PG8_WAIT_V(8); PG8_WAIT_L(0); PG8_BAR; PG8_MMA(0, 0, At, B0); PG8_MMA(0, 1, At, B1); PG8_BAR; PG8_SCHED;
;             PG8_LDA(At, 0, 1); PG8_STAGE(PG8_SB(0, 0), b2, voffB); PG8_STAGE(PG8_SB(0, 1), b2 + hstepB, voffB); PG8_STAGE_A(PG8_SA(0, 0), a2, 0, last);
;             PG8_WAIT_V(8); PG8_WAIT_L(0); PG8_BAR; PG8_MMA(1, 0, At, B0); PG8_MMA(1, 1, At, B1); PG8_BAR; PG8_SCHED;
.LBB0_2070:
	v_add_u32_e32 v152, s43, v199
	v_add_u32_e32 v168, s67, v199
	ds_read_b128 v[140:143], v152
	ds_read_b128 v[144:147], v152 offset:1024
	ds_read_b128 v[148:151], v152 offset:2048
	ds_read_b128 v[152:155], v152 offset:3072
	ds_read_b128 v[156:159], v168
	ds_read_b128 v[160:163], v168 offset:1024
	ds_read_b128 v[164:167], v168 offset:2048
	ds_read_b128 v[168:171], v168 offset:3072
	s_add_u32 s46, s22, 0xfffc0080
	s_addc_u32 s47, s23, -1
	s_cmp_eq_u32 vcc_lo, 12
	s_cselect_b32 s81, s17, s47
	s_cselect_b32 s80, s16, s46
	s_cselect_b32 s79, s19, s15
	s_cselect_b32 s78, s18, s13
	v_lshl_add_u64 v[192:193], s[22:23], 0, v[136:137]
	s_add_i32 m0, s51, 0xc000
	ds_read_b128 v[172:175], v219
	ds_read_b128 v[176:179], v219 offset:1024
	ds_read_b128 v[180:183], v219 offset:2048
	ds_read_b128 v[184:187], v219 offset:3072
	ds_read_b128 v[188:191], v219 offset:4096
	ds_read_b128 v[222:225], v219 offset:5120
	ds_read_b128 v[226:229], v219 offset:6144
	ds_read_b128 v[230:233], v219 offset:7168
	global_load_lds_dwordx4 v[192:193], off
	v_lshl_add_u64 v[192:193], s[22:23], 0, v[138:139]
	s_add_i32 m0, s51, 0xe000
	s_nop 0
	global_load_lds_dwordx4 v[192:193], off
	s_waitcnt vmcnt(8)
	s_waitcnt lgkmcnt(0)
	s_barrier
	s_nop 0
	s_setprio 1
	s_waitcnt lgkmcnt(0)
	v_mfma_f32_16x16x32_bf16 v[124:127], v[140:143], v[172:175], v[124:127]
	v_mfma_f32_16x16x32_bf16 v[120:123], v[148:151], v[172:175], v[120:123]
	v_mfma_f32_16x16x32_bf16 v[108:111], v[140:143], v[180:183], v[108:111]
	v_mfma_f32_16x16x32_bf16 v[104:107], v[148:151], v[180:183], v[104:107]
	v_mfma_f32_16x16x32_bf16 v[92:95], v[140:143], v[188:191], v[92:95]
	v_mfma_f32_16x16x32_bf16 v[88:91], v[148:151], v[188:191], v[88:91]
	v_mfma_f32_16x16x32_bf16 v[76:79], v[140:143], v[226:229], v[76:79]
	v_mfma_f32_16x16x32_bf16 v[72:75], v[148:151], v[226:229], v[72:75]
	v_mfma_f32_16x16x32_bf16 v[124:127], v[144:147], v[176:179], v[124:127]
	v_mfma_f32_16x16x32_bf16 v[120:123], v[152:155], v[176:179], v[120:123]
	v_mfma_f32_16x16x32_bf16 v[108:111], v[144:147], v[184:187], v[108:111]
	v_mfma_f32_16x16x32_bf16 v[104:107], v[152:155], v[184:187], v[104:107]
	v_mfma_f32_16x16x32_bf16 v[92:95], v[144:147], v[222:225], v[92:95]
	v_mfma_f32_16x16x32_bf16 v[88:91], v[152:155], v[222:225], v[88:91]
	v_mfma_f32_16x16x32_bf16 v[76:79], v[144:147], v[230:233], v[76:79]
	v_mfma_f32_16x16x32_bf16 v[72:75], v[152:155], v[230:233], v[72:75]
	s_setprio 0
	s_setprio 1
	v_mfma_f32_16x16x32_bf16 v[116:119], v[156:159], v[172:175], v[116:119]
	v_mfma_f32_16x16x32_bf16 v[112:115], v[164:167], v[172:175], v[112:115]
	v_mfma_f32_16x16x32_bf16 v[100:103], v[156:159], v[180:183], v[100:103]
	v_mfma_f32_16x16x32_bf16 v[96:99], v[164:167], v[180:183], v[96:99]
	v_mfma_f32_16x16x32_bf16 v[84:87], v[156:159], v[188:191], v[84:87]
	v_mfma_f32_16x16x32_bf16 v[80:83], v[164:167], v[188:191], v[80:83]
	v_mfma_f32_16x16x32_bf16 v[68:71], v[156:159], v[226:229], v[68:71]
	v_mfma_f32_16x16x32_bf16 v[64:67], v[164:167], v[226:229], v[64:67]
	v_mfma_f32_16x16x32_bf16 v[116:119], v[160:163], v[176:179], v[116:119]
	v_mfma_f32_16x16x32_bf16 v[112:115], v[168:171], v[176:179], v[112:115]
	v_mfma_f32_16x16x32_bf16 v[100:103], v[160:163], v[184:187], v[100:103]
	v_mfma_f32_16x16x32_bf16 v[96:99], v[168:171], v[184:187], v[96:99]
	v_mfma_f32_16x16x32_bf16 v[84:87], v[160:163], v[222:225], v[84:87]
	v_mfma_f32_16x16x32_bf16 v[80:83], v[168:171], v[222:225], v[80:83]
	v_mfma_f32_16x16x32_bf16 v[68:71], v[160:163], v[230:233], v[68:71]
	v_mfma_f32_16x16x32_bf16 v[64:67], v[168:171], v[230:233], v[64:67]
	s_setprio 0
	s_barrier
	s_add_i32 s46, s43, s50
	v_lshl_add_u64 v[192:193], s[78:79], 0, v[128:129]
	s_mov_b32 m0, s46
	ds_read_b128 v[172:175], v219 offset:16384
	ds_read_b128 v[176:179], v219 offset:17408
	ds_read_b128 v[180:183], v219 offset:18432
	ds_read_b128 v[184:187], v219 offset:19456
	ds_read_b128 v[188:191], v219 offset:20480
	ds_read_b128 v[222:225], v219 offset:21504
	ds_read_b128 v[226:229], v219 offset:22528
	ds_read_b128 v[230:233], v219 offset:23552
	global_load_lds_dwordx4 v[192:193], off
	s_add_i32 m0, s46, 0x2000
	s_add_u32 s46, s78, 0x40000
	v_lshl_add_u64 v[234:235], s[78:79], 0, v[134:135]
	s_addc_u32 s47, s79, 0
	s_add_i32 vcc_hi, s67, s50
	global_load_lds_dwordx4 v[234:235], off
	v_lshl_add_u64 v[236:237], s[46:47], 0, v[128:129]
	s_mov_b32 m0, vcc_hi
	v_lshl_add_u64 v[238:239], s[80:81], 0, v[132:133]
	global_load_lds_dwordx4 v[236:237], off
	v_lshl_add_u64 v[236:237], s[46:47], 0, v[134:135]
	s_add_i32 m0, vcc_hi, 0x2000
	s_nop 0
	global_load_lds_dwordx4 v[236:237], off
	v_lshl_add_u64 v[236:237], s[80:81], 0, v[130:131]
	s_mov_b32 m0, s51
	s_nop 0
	global_load_lds_dwordx4 v[236:237], off
	s_mov_b32 m0, s60
	s_nop 0
	global_load_lds_dwordx4 v[238:239], off
	s_waitcnt vmcnt(8)
	s_waitcnt lgkmcnt(0)
	s_barrier
; #define PG8_STAGE_A(bufoff, gbase, h, nx) do { _Pragma("unroll") for (int _i = 0; _i < 2; ++_i) { \
;         const unsigned vo_ = GA ? ((nx) ? vgn[h][_i] : vgc[h][_i]) : voffA[_i]; \
;         __builtin_amdgcn_global_load_lds((const unsigned*)((const char*)(gbase) + vo_), (PG8_LAS unsigned*)(lds + (bufoff) + ldsw + _i * 8192), 16, 0, 0); } } while (0)
; #define PG8_LDA(dst, b, h) do { _Pragma("unroll") for (int m = 0; m < 4; ++m) _Pragma("unroll") for (int k = 0; k < 2; ++k) dst[m][k] = *(const PG8_LAS bf16x8*)(lds + PG8_SA(b, h) + aoff + m * 2048 + k * 1024); } while (0)
; #define PG8_LDB(dst, b, h) do { _Pragma("unroll") for (int n = 0; n < 2; ++n) _Pragma("unroll") for (int k = 0; k < 2; ++k) dst[n][k] = *(const PG8_LAS bf16x8*)(lds + PG8_SB(b, h) + boff + n * 2048 + k * 1024); } while (0)
; #define PG8_MMA(ai, bj, At, Bt) do { __builtin_amdgcn_s_setprio(1); _Pragma("unroll") for (int m = 0; m < 4; ++m) _Pragma("unroll") for (int n = 0; n < 2; ++n) _Pragma("unroll") for (int k = 0; k < 2; ++k) \
;         acc[ai][bj][m][n] = __builtin_amdgcn_mfma_f32_16x16x32_bf16(Bt[n][k], At[m][k], acc[ai][bj][m][n], 0, 0, 0); __builtin_amdgcn_s_setprio(0); } while (0)
; #define PG8_WAIT_V(n) asm volatile("s_waitcnt vmcnt(" #n ")" ::: "memory")
; #define PG8_WAIT_L(n) asm volatile("s_waitcnt lgkmcnt(" #n ")" ::: "memory")
; #define PG8_BAR __builtin_amdgcn_s_barrier()
; #define PG8_SCHED __builtin_amdgcn_sched_barrier(0)
; template <class Epi, class Sched>
; __device__ __forceinline__ void gemm_phase(const int WID_, PG8_LAS unsigned char* lds, const Sched& S, const Epi& E) {
;     ...
;             PG8_WAIT_V(8); PG8_WAIT_L(0); PG8_BAR; PG8_MMA(1, 0, At, B0); PG8_MMA(1, 1, At, B1); PG8_BAR; PG8_SCHED;
;             PG8_LDB(B0, 1, 0); PG8_LDB(B1, 1, 1); PG8_SCHED; PG8_LDA(At, 1, 0); PG8_STAGE_A(PG8_SA(0, 1), a2 + hstepA, 1, last);
;             PG8_WAIT_V(8); PG8_WAIT_L(0); PG8_BAR; PG8_MMA(0, 0, At, B0); PG8_MMA(0, 1, At, B1); PG8_BAR; PG8_SCHED;
	s_nop 0
	s_setprio 1
	s_waitcnt lgkmcnt(0)
	v_mfma_f32_16x16x32_bf16 v[60:63], v[140:143], v[172:175], v[60:63]
	v_mfma_f32_16x16x32_bf16 v[56:59], v[148:151], v[172:175], v[56:59]
	v_mfma_f32_16x16x32_bf16 v[44:47], v[140:143], v[180:183], v[44:47]
	v_mfma_f32_16x16x32_bf16 v[40:43], v[148:151], v[180:183], v[40:43]
	v_mfma_f32_16x16x32_bf16 v[28:31], v[140:143], v[188:191], v[28:31]
	v_mfma_f32_16x16x32_bf16 v[24:27], v[148:151], v[188:191], v[24:27]
	v_mfma_f32_16x16x32_bf16 v[12:15], v[140:143], v[226:229], v[12:15]
	v_mfma_f32_16x16x32_bf16 v[8:11], v[148:151], v[226:229], v[8:11]
	v_mfma_f32_16x16x32_bf16 v[60:63], v[144:147], v[176:179], v[60:63]
	v_mfma_f32_16x16x32_bf16 v[56:59], v[152:155], v[176:179], v[56:59]
	v_mfma_f32_16x16x32_bf16 v[44:47], v[144:147], v[184:187], v[44:47]
	v_mfma_f32_16x16x32_bf16 v[40:43], v[152:155], v[184:187], v[40:43]
	v_mfma_f32_16x16x32_bf16 v[28:31], v[144:147], v[222:225], v[28:31]
	v_mfma_f32_16x16x32_bf16 v[24:27], v[152:155], v[222:225], v[24:27]
	v_mfma_f32_16x16x32_bf16 v[12:15], v[144:147], v[230:233], v[12:15]
	v_mfma_f32_16x16x32_bf16 v[8:11], v[152:155], v[230:233], v[8:11]
	s_setprio 0
	s_setprio 1
	v_mfma_f32_16x16x32_bf16 v[52:55], v[156:159], v[172:175], v[52:55]
	v_mfma_f32_16x16x32_bf16 v[48:51], v[164:167], v[172:175], v[48:51]
	v_mfma_f32_16x16x32_bf16 v[36:39], v[156:159], v[180:183], v[36:39]
	v_mfma_f32_16x16x32_bf16 v[32:35], v[164:167], v[180:183], v[32:35]
	v_mfma_f32_16x16x32_bf16 v[20:23], v[156:159], v[188:191], v[20:23]
	v_mfma_f32_16x16x32_bf16 v[16:19], v[164:167], v[188:191], v[16:19]
	v_mfma_f32_16x16x32_bf16 v[4:7], v[156:159], v[226:229], v[4:7]
	v_mfma_f32_16x16x32_bf16 v[0:3], v[164:167], v[226:229], v[0:3]
	v_mfma_f32_16x16x32_bf16 v[52:55], v[160:163], v[176:179], v[52:55]
	v_mfma_f32_16x16x32_bf16 v[48:51], v[168:171], v[176:179], v[48:51]
	v_mfma_f32_16x16x32_bf16 v[36:39], v[160:163], v[184:187], v[36:39]
	v_mfma_f32_16x16x32_bf16 v[32:35], v[168:171], v[184:187], v[32:35]
	v_mfma_f32_16x16x32_bf16 v[20:23], v[160:163], v[222:225], v[20:23]
	v_mfma_f32_16x16x32_bf16 v[16:19], v[168:171], v[222:225], v[16:19]
	v_mfma_f32_16x16x32_bf16 v[4:7], v[160:163], v[230:233], v[4:7]
	v_mfma_f32_16x16x32_bf16 v[0:3], v[168:171], v[230:233], v[0:3]
	s_setprio 0
	s_barrier
	v_add_u32_e32 v152, s82, v199
	v_add_u32_e32 v168, s83, v199
	ds_read_b128 v[140:143], v152
	ds_read_b128 v[144:147], v152 offset:1024
	ds_read_b128 v[148:151], v152 offset:2048
	ds_read_b128 v[152:155], v152 offset:3072
	ds_read_b128 v[156:159], v168
	ds_read_b128 v[160:163], v168 offset:1024
	ds_read_b128 v[164:167], v168 offset:2048
	ds_read_b128 v[168:171], v168 offset:3072
	s_add_u32 s46, s80, 0x40000
	s_addc_u32 s47, s81, 0
	s_mov_b32 m0, s61
	v_lshl_add_u64 v[240:241], s[46:47], 0, v[130:131]
	ds_read_b128 v[172:175], v219 offset:32768
	ds_read_b128 v[176:179], v219 offset:33792
	ds_read_b128 v[180:183], v219 offset:34816
	ds_read_b128 v[184:187], v219 offset:35840
	ds_read_b128 v[188:191], v219 offset:36864
	ds_read_b128 v[222:225], v219 offset:37888
	ds_read_b128 v[226:229], v219 offset:38912
	ds_read_b128 v[230:233], v219 offset:39936
	global_load_lds_dwordx4 v[240:241], off
	v_lshl_add_u64 v[240:241], s[46:47], 0, v[132:133]
	s_mov_b32 m0, s62
	s_nop 0
	global_load_lds_dwordx4 v[240:241], off
	s_waitcnt vmcnt(8)
	s_waitcnt lgkmcnt(0)
	s_barrier
	s_nop 0
	s_setprio 1
	s_waitcnt lgkmcnt(0)
	v_mfma_f32_16x16x32_bf16 v[124:127], v[140:143], v[172:175], v[124:127]
	v_mfma_f32_16x16x32_bf16 v[120:123], v[148:151], v[172:175], v[120:123]
	v_mfma_f32_16x16x32_bf16 v[108:111], v[140:143], v[180:183], v[108:111]
	v_mfma_f32_16x16x32_bf16 v[104:107], v[148:151], v[180:183], v[104:107]
	v_mfma_f32_16x16x32_bf16 v[92:95], v[140:143], v[188:191], v[92:95]
	v_mfma_f32_16x16x32_bf16 v[88:91], v[148:151], v[188:191], v[88:91]
	v_mfma_f32_16x16x32_bf16 v[76:79], v[140:143], v[226:229], v[76:79]
	v_mfma_f32_16x16x32_bf16 v[72:75], v[148:151], v[226:229], v[72:75]
	v_mfma_f32_16x16x32_bf16 v[124:127], v[144:147], v[176:179], v[124:127]
	v_mfma_f32_16x16x32_bf16 v[120:123], v[152:155], v[176:179], v[120:123]
	v_mfma_f32_16x16x32_bf16 v[108:111], v[144:147], v[184:187], v[108:111]
	v_mfma_f32_16x16x32_bf16 v[104:107], v[152:155], v[184:187], v[104:107]
	v_mfma_f32_16x16x32_bf16 v[92:95], v[144:147], v[222:225], v[92:95]
	v_mfma_f32_16x16x32_bf16 v[88:91], v[152:155], v[222:225], v[88:91]
	v_mfma_f32_16x16x32_bf16 v[76:79], v[144:147], v[230:233], v[76:79]
	v_mfma_f32_16x16x32_bf16 v[72:75], v[152:155], v[230:233], v[72:75]
	s_setprio 0
	s_setprio 1
	v_mfma_f32_16x16x32_bf16 v[116:119], v[156:159], v[172:175], v[116:119]
	v_mfma_f32_16x16x32_bf16 v[112:115], v[164:167], v[172:175], v[112:115]
	v_mfma_f32_16x16x32_bf16 v[100:103], v[156:159], v[180:183], v[100:103]
	v_mfma_f32_16x16x32_bf16 v[96:99], v[164:167], v[180:183], v[96:99]
	v_mfma_f32_16x16x32_bf16 v[84:87], v[156:159], v[188:191], v[84:87]
	v_mfma_f32_16x16x32_bf16 v[80:83], v[164:167], v[188:191], v[80:83]
	v_mfma_f32_16x16x32_bf16 v[68:71], v[156:159], v[226:229], v[68:71]
	v_mfma_f32_16x16x32_bf16 v[64:67], v[164:167], v[226:229], v[64:67]
	v_mfma_f32_16x16x32_bf16 v[116:119], v[160:163], v[176:179], v[116:119]
	v_mfma_f32_16x16x32_bf16 v[112:115], v[168:171], v[176:179], v[112:115]
	v_mfma_f32_16x16x32_bf16 v[100:103], v[160:163], v[184:187], v[100:103]
	v_mfma_f32_16x16x32_bf16 v[96:99], v[168:171], v[184:187], v[96:99]
	v_mfma_f32_16x16x32_bf16 v[84:87], v[160:163], v[222:225], v[84:87]
	v_mfma_f32_16x16x32_bf16 v[80:83], v[168:171], v[222:225], v[80:83]
	v_mfma_f32_16x16x32_bf16 v[68:71], v[160:163], v[230:233], v[68:71]
	v_mfma_f32_16x16x32_bf16 v[64:67], v[168:171], v[230:233], v[64:67]
	s_setprio 0
	s_barrier
; #define PG8_STAGE(bufoff, gbase, voff) do { _Pragma("unroll") for (int _i = 0; _i < 2; ++_i) \
;         __builtin_amdgcn_global_load_lds((const unsigned*)((const char*)(gbase) + (voff)[_i]), (PG8_LAS unsigned*)(lds + (bufoff) + ldsw + _i * 8192), 16, 0, 0); } while (0)
; #define PG8_STAGE_A(bufoff, gbase, h, nx) do { _Pragma("unroll") for (int _i = 0; _i < 2; ++_i) { \
;         const unsigned vo_ = GA ? ((nx) ? vgn[h][_i] : vgc[h][_i]) : voffA[_i]; \
;         __builtin_amdgcn_global_load_lds((const unsigned*)((const char*)(gbase) + vo_), (PG8_LAS unsigned*)(lds + (bufoff) + ldsw + _i * 8192), 16, 0, 0); } } while (0)
; #define PG8_LDA(dst, b, h) do { _Pragma("unroll") for (int m = 0; m < 4; ++m) _Pragma("unroll") for (int k = 0; k < 2; ++k) dst[m][k] = *(const PG8_LAS bf16x8*)(lds + PG8_SA(b, h) + aoff + m * 2048 + k * 1024); } while (0)
; #define PG8_MMA(ai, bj, At, Bt) do { __builtin_amdgcn_s_setprio(1); _Pragma("unroll") for (int m = 0; m < 4; ++m) _Pragma("unroll") for (int n = 0; n < 2; ++n) _Pragma("unroll") for (int k = 0; k < 2; ++k) \
;         acc[ai][bj][m][n] = __builtin_amdgcn_mfma_f32_16x16x32_bf16(Bt[n][k], At[m][k], acc[ai][bj][m][n], 0, 0, 0); __builtin_amdgcn_s_setprio(0); } while (0)
; #define PG8_WAIT_V(n) asm volatile("s_waitcnt vmcnt(" #n ")" ::: "memory")
; #define PG8_WAIT_L(n) asm volatile("s_waitcnt lgkmcnt(" #n ")" ::: "memory")
; #define PG8_BAR __builtin_amdgcn_s_barrier()
; #define PG8_SCHED __builtin_amdgcn_sched_barrier(0)
; template <class Epi, class Sched>
; __device__ __forceinline__ void gemm_phase(const int WID_, PG8_LAS unsigned char* lds, const Sched& S, const Epi& E) {
;     ...
;             PG8_LDA(At, 1, 1); PG8_STAGE(PG8_SB(1, 0), b3, voffB); PG8_STAGE(PG8_SB(1, 1), b3 + hstepB, voffB); PG8_STAGE_A(PG8_SA(1, 0), a3, 0, last);
;             PG8_WAIT_V(8); PG8_WAIT_L(0); PG8_BAR; PG8_MMA(1, 0, At, B0); PG8_MMA(1, 1, At, B1); PG8_BAR; PG8_SCHED;
;         }
;         if (wr == 0) PG8_BAR;
	s_add_i32 s46, s82, s50
	v_lshl_add_u64 v[192:193], v[192:193], 0, s[68:69]
	s_mov_b32 m0, s46
	ds_read_b128 v[172:175], v219 offset:49152
	ds_read_b128 v[176:179], v219 offset:50176
	ds_read_b128 v[180:183], v219 offset:51200
	ds_read_b128 v[184:187], v219 offset:52224
	ds_read_b128 v[188:191], v219 offset:53248
	ds_read_b128 v[222:225], v219 offset:54272
	ds_read_b128 v[226:229], v219 offset:55296
	ds_read_b128 v[230:233], v219 offset:56320
	global_load_lds_dwordx4 v[192:193], off
	s_add_i32 m0, s46, 0x2000
	s_add_u32 s46, s78, 0x40080
	v_lshl_add_u64 v[192:193], v[234:235], 0, s[68:69]
	s_addc_u32 s47, s79, 0
	s_add_i32 s78, s83, s50
	global_load_lds_dwordx4 v[192:193], off
	v_lshl_add_u64 v[192:193], s[46:47], 0, v[128:129]
	s_mov_b32 m0, s78
	s_nop 0
	global_load_lds_dwordx4 v[192:193], off
	v_lshl_add_u64 v[192:193], s[46:47], 0, v[134:135]
	s_add_i32 m0, s78, 0x2000
	s_nop 0
	global_load_lds_dwordx4 v[192:193], off
	v_lshl_add_u64 v[192:193], v[236:237], 0, s[68:69]
	s_mov_b32 m0, s63
	s_nop 0
	global_load_lds_dwordx4 v[192:193], off
	v_lshl_add_u64 v[192:193], v[238:239], 0, s[68:69]
	s_mov_b32 m0, s86
	s_nop 0
	global_load_lds_dwordx4 v[192:193], off
	s_waitcnt vmcnt(8)
	s_waitcnt lgkmcnt(0)
	s_barrier
	s_setprio 1
	s_waitcnt lgkmcnt(0)
	v_mfma_f32_16x16x32_bf16 v[60:63], v[140:143], v[172:175], v[60:63]
	v_mfma_f32_16x16x32_bf16 v[56:59], v[148:151], v[172:175], v[56:59]
	v_mfma_f32_16x16x32_bf16 v[44:47], v[140:143], v[180:183], v[44:47]
	v_mfma_f32_16x16x32_bf16 v[40:43], v[148:151], v[180:183], v[40:43]
	v_mfma_f32_16x16x32_bf16 v[28:31], v[140:143], v[188:191], v[28:31]
	v_mfma_f32_16x16x32_bf16 v[24:27], v[148:151], v[188:191], v[24:27]
	v_mfma_f32_16x16x32_bf16 v[12:15], v[140:143], v[226:229], v[12:15]
	v_mfma_f32_16x16x32_bf16 v[8:11], v[148:151], v[226:229], v[8:11]
	v_mfma_f32_16x16x32_bf16 v[60:63], v[144:147], v[176:179], v[60:63]
	v_mfma_f32_16x16x32_bf16 v[56:59], v[152:155], v[176:179], v[56:59]
	v_mfma_f32_16x16x32_bf16 v[44:47], v[144:147], v[184:187], v[44:47]
	v_mfma_f32_16x16x32_bf16 v[40:43], v[152:155], v[184:187], v[40:43]
	v_mfma_f32_16x16x32_bf16 v[28:31], v[144:147], v[222:225], v[28:31]
	v_mfma_f32_16x16x32_bf16 v[24:27], v[152:155], v[222:225], v[24:27]
	v_mfma_f32_16x16x32_bf16 v[12:15], v[144:147], v[230:233], v[12:15]
	v_mfma_f32_16x16x32_bf16 v[8:11], v[152:155], v[230:233], v[8:11]
	s_setprio 0
	s_setprio 1
	v_mfma_f32_16x16x32_bf16 v[52:55], v[156:159], v[172:175], v[52:55]
	v_mfma_f32_16x16x32_bf16 v[48:51], v[164:167], v[172:175], v[48:51]
	v_mfma_f32_16x16x32_bf16 v[36:39], v[156:159], v[180:183], v[36:39]
	v_mfma_f32_16x16x32_bf16 v[32:35], v[164:167], v[180:183], v[32:35]
	v_mfma_f32_16x16x32_bf16 v[20:23], v[156:159], v[188:191], v[20:23]
	v_mfma_f32_16x16x32_bf16 v[16:19], v[164:167], v[188:191], v[16:19]
	v_mfma_f32_16x16x32_bf16 v[4:7], v[156:159], v[226:229], v[4:7]
	v_mfma_f32_16x16x32_bf16 v[0:3], v[164:167], v[226:229], v[0:3]
	v_mfma_f32_16x16x32_bf16 v[52:55], v[160:163], v[176:179], v[52:55]
	v_mfma_f32_16x16x32_bf16 v[48:51], v[168:171], v[176:179], v[48:51]
	v_mfma_f32_16x16x32_bf16 v[36:39], v[160:163], v[184:187], v[36:39]
	v_mfma_f32_16x16x32_bf16 v[32:35], v[168:171], v[184:187], v[32:35]
	v_mfma_f32_16x16x32_bf16 v[20:23], v[160:163], v[222:225], v[20:23]
	v_mfma_f32_16x16x32_bf16 v[16:19], v[168:171], v[222:225], v[16:19]
	v_mfma_f32_16x16x32_bf16 v[4:7], v[160:163], v[230:233], v[4:7]
	v_mfma_f32_16x16x32_bf16 v[0:3], v[168:171], v[230:233], v[0:3]
	s_setprio 0
	s_barrier
	s_add_i32 vcc_lo, vcc_lo, 2
	s_add_u32 s22, s22, 0x100
	s_addc_u32 s23, s23, 0
	s_add_u32 s13, s13, 0x100
	s_addc_u32 s15, s15, 0
	s_cmp_gt_u32 vcc_lo, 13
	s_cbranch_scc0 .LBB0_2070
	s_and_b64 vcc, exec, s[10:11]
	s_cbranch_vccz .LBB0_2073
	s_barrier

; #define PG8_STAGE(bufoff, gbase, voff) do { _Pragma("unroll") for (int _i = 0; _i < 2; ++_i) \
;         __builtin_amdgcn_global_load_lds((const unsigned*)((const char*)(gbase) + (voff)[_i]), (PG8_LAS unsigned*)(lds + (bufoff) + ldsw + _i * 8192), 16, 0, 0); } while (0)
; #define PG8_STAGE_A(bufoff, gbase, h, nx) do { _Pragma("unroll") for (int _i = 0; _i < 2; ++_i) { \
;         const unsigned vo_ = GA ? ((nx) ? vgn[h][_i] : vgc[h][_i]) : voffA[_i]; \
;         __builtin_amdgcn_global_load_lds((const unsigned*)((const char*)(gbase) + vo_), (PG8_LAS unsigned*)(lds + (bufoff) + ldsw + _i * 8192), 16, 0, 0); } } while (0)
; #define PG8_LDA(dst, b, h) do { _Pragma("unroll") for (int m = 0; m < 4; ++m) _Pragma("unroll") for (int k = 0; k < 2; ++k) dst[m][k] = *(const PG8_LAS bf16x8*)(lds + PG8_SA(b, h) + aoff + m * 2048 + k * 1024); } while (0)
; #define PG8_LDB(dst, b, h) do { _Pragma("unroll") for (int n = 0; n < 2; ++n) _Pragma("unroll") for (int k = 0; k < 2; ++k) dst[n][k] = *(const PG8_LAS bf16x8*)(lds + PG8_SB(b, h) + boff + n * 2048 + k * 1024); } while (0)
; #define PG8_WAIT_V(n) asm volatile("s_waitcnt vmcnt(" #n ")" ::: "memory")
; #define PG8_WAIT_L(n) asm volatile("s_waitcnt lgkmcnt(" #n ")" ::: "memory")
; #define PG8_BAR __builtin_amdgcn_s_barrier()
; #define PG8_SCHED __builtin_amdgcn_sched_barrier(0)
; template <class Epi, class Sched>
; __device__ __forceinline__ void gemm_phase(const int WID_, PG8_LAS unsigned char* lds, const Sched& S, const Epi& E) {
;     ...
;         for (int t = 0; t < nt; t += 2) {
;             const bool last = (t == nt - 2);
;             const char* a1 = cA + (size_t)(t + 1) * kstep;
;             const char* a2 = last ? nA : cA + (size_t)(t + 2) * kstep; const char* b2 = last ? nB : cB + (size_t)(t + 2) * kstep;
;             const char* a3 = a2 + kstep; const char* b3 = b2 + kstep;
;             PG8_LDB(B0, 0, 0); PG8_LDB(B1, 0, 1); PG8_SCHED; PG8_LDA(At, 0, 0); PG8_STAGE_A(PG8_SA(1, 1), a1 + hstepA, 1, false);
;             PG8_WAIT_V(8); PG8_WAIT_L(0); PG8_BAR; PG8_MMA(0, 0, At, B0); PG8_MMA(0, 1, At, B1); PG8_BAR; PG8_SCHED;
;             PG8_LDA(At, 0, 1); PG8_STAGE(PG8_SB(0, 0), b2, voffB); PG8_STAGE(PG8_SB(0, 1), b2 + hstepB, voffB); PG8_STAGE_A(PG8_SA(0, 0), a2, 0, last);
;             PG8_WAIT_V(8); PG8_WAIT_L(0); PG8_BAR; PG8_MMA(1, 0, At, B0); PG8_MMA(1, 1, At, B1); PG8_BAR; PG8_SCHED;
.LBB0_2120:
	v_add_u32_e32 v144, s43, v147
	ds_read_b128 v[140:143], v144
	ds_read_b128 v[150:153], v144 offset:1024
	ds_read_b128 v[154:157], v144 offset:2048
	ds_read_b128 v[158:161], v144 offset:3072
	v_add_u32_e32 v144, s67, v147
	ds_read_b128 v[162:165], v144
	ds_read_b128 v[166:169], v144 offset:1024
	ds_read_b128 v[170:173], v144 offset:2048
	ds_read_b128 v[174:177], v144 offset:3072
	s_add_u32 s20, s18, 0xfffc0080
	s_addc_u32 s21, s19, -1
	s_cmp_eq_u32 s79, 12
	s_cselect_b32 s23, s13, s21
	s_cselect_b32 s22, s12, s20
	s_cselect_b32 s21, s15, s11
	s_cselect_b32 s20, s14, s9
	v_lshl_add_u64 v[144:145], s[18:19], 0, v[136:137]
	s_add_i32 m0, s49, 0xc000
	ds_read_b128 v[178:181], v149
	ds_read_b128 v[182:185], v149 offset:1024
	ds_read_b128 v[186:189], v149 offset:2048
	ds_read_b128 v[190:193], v149 offset:3072
	ds_read_b128 v[198:201], v149 offset:4096
	ds_read_b128 v[202:205], v149 offset:5120
	ds_read_b128 v[206:209], v149 offset:6144
	ds_read_b128 v[210:213], v149 offset:7168
	global_load_lds_dwordx4 v[144:145], off
	v_lshl_add_u64 v[144:145], s[18:19], 0, v[138:139]
	s_add_i32 m0, s49, 0xe000
	s_nop 0
	global_load_lds_dwordx4 v[144:145], off
	s_waitcnt vmcnt(8)
	s_waitcnt lgkmcnt(0)
	s_barrier
	s_nop 0
	s_setprio 1
	s_waitcnt lgkmcnt(0)
	v_mfma_f32_16x16x32_bf16 v[124:127], v[140:143], v[178:181], v[124:127]
	v_mfma_f32_16x16x32_bf16 v[120:123], v[154:157], v[178:181], v[120:123]
	v_mfma_f32_16x16x32_bf16 v[108:111], v[140:143], v[186:189], v[108:111]
	v_mfma_f32_16x16x32_bf16 v[104:107], v[154:157], v[186:189], v[104:107]
	v_mfma_f32_16x16x32_bf16 v[92:95], v[140:143], v[198:201], v[92:95]
	v_mfma_f32_16x16x32_bf16 v[88:91], v[154:157], v[198:201], v[88:91]
	v_mfma_f32_16x16x32_bf16 v[76:79], v[140:143], v[206:209], v[76:79]
	v_mfma_f32_16x16x32_bf16 v[72:75], v[154:157], v[206:209], v[72:75]
	v_mfma_f32_16x16x32_bf16 v[124:127], v[150:153], v[182:185], v[124:127]
	v_mfma_f32_16x16x32_bf16 v[120:123], v[158:161], v[182:185], v[120:123]
	v_mfma_f32_16x16x32_bf16 v[108:111], v[150:153], v[190:193], v[108:111]
	v_mfma_f32_16x16x32_bf16 v[104:107], v[158:161], v[190:193], v[104:107]
	v_mfma_f32_16x16x32_bf16 v[92:95], v[150:153], v[202:205], v[92:95]
	v_mfma_f32_16x16x32_bf16 v[88:91], v[158:161], v[202:205], v[88:91]
	v_mfma_f32_16x16x32_bf16 v[76:79], v[150:153], v[210:213], v[76:79]
	v_mfma_f32_16x16x32_bf16 v[72:75], v[158:161], v[210:213], v[72:75]
	s_setprio 0
	s_setprio 1
	v_mfma_f32_16x16x32_bf16 v[116:119], v[162:165], v[178:181], v[116:119]
	v_mfma_f32_16x16x32_bf16 v[112:115], v[170:173], v[178:181], v[112:115]
	v_mfma_f32_16x16x32_bf16 v[100:103], v[162:165], v[186:189], v[100:103]
	v_mfma_f32_16x16x32_bf16 v[96:99], v[170:173], v[186:189], v[96:99]
	v_mfma_f32_16x16x32_bf16 v[84:87], v[162:165], v[198:201], v[84:87]
	v_mfma_f32_16x16x32_bf16 v[80:83], v[170:173], v[198:201], v[80:83]
	v_mfma_f32_16x16x32_bf16 v[68:71], v[162:165], v[206:209], v[68:71]
	v_mfma_f32_16x16x32_bf16 v[64:67], v[170:173], v[206:209], v[64:67]
	v_mfma_f32_16x16x32_bf16 v[116:119], v[166:169], v[182:185], v[116:119]
	v_mfma_f32_16x16x32_bf16 v[112:115], v[174:177], v[182:185], v[112:115]
	v_mfma_f32_16x16x32_bf16 v[100:103], v[166:169], v[190:193], v[100:103]
	v_mfma_f32_16x16x32_bf16 v[96:99], v[174:177], v[190:193], v[96:99]
	v_mfma_f32_16x16x32_bf16 v[84:87], v[166:169], v[202:205], v[84:87]
	v_mfma_f32_16x16x32_bf16 v[80:83], v[174:177], v[202:205], v[80:83]
	v_mfma_f32_16x16x32_bf16 v[68:71], v[166:169], v[210:213], v[68:71]
	v_mfma_f32_16x16x32_bf16 v[64:67], v[174:177], v[210:213], v[64:67]
	s_setprio 0
	s_barrier
	s_add_i32 s46, s43, s48
	v_lshl_add_u64 v[144:145], s[20:21], 0, v[128:129]
	s_mov_b32 m0, s46
	ds_read_b128 v[178:181], v149 offset:16384
	ds_read_b128 v[182:185], v149 offset:17408
	ds_read_b128 v[186:189], v149 offset:18432
	ds_read_b128 v[190:193], v149 offset:19456
	ds_read_b128 v[198:201], v149 offset:20480
	ds_read_b128 v[202:205], v149 offset:21504
	ds_read_b128 v[206:209], v149 offset:22528
	ds_read_b128 v[210:213], v149 offset:23552
	global_load_lds_dwordx4 v[144:145], off
	s_add_i32 m0, s46, 0x2000
	s_add_u32 s46, s20, 0x40000
	v_lshl_add_u64 v[214:215], s[20:21], 0, v[130:131]
	s_addc_u32 s47, s21, 0
	s_add_i32 s80, s67, s48
	global_load_lds_dwordx4 v[214:215], off
	v_lshl_add_u64 v[216:217], s[46:47], 0, v[128:129]
	s_mov_b32 m0, s80
	v_lshl_add_u64 v[218:219], s[22:23], 0, v[132:133]
	global_load_lds_dwordx4 v[216:217], off
	v_lshl_add_u64 v[216:217], s[46:47], 0, v[130:131]
	s_add_i32 m0, s80, 0x2000
	s_nop 0
	global_load_lds_dwordx4 v[216:217], off
	v_lshl_add_u64 v[216:217], s[22:23], 0, v[134:135]
	s_mov_b32 m0, s49
	s_nop 0
	global_load_lds_dwordx4 v[216:217], off
	s_mov_b32 m0, s50
	s_nop 0
	global_load_lds_dwordx4 v[218:219], off
	s_waitcnt vmcnt(8)
	s_waitcnt lgkmcnt(0)
	s_barrier
; #define PG8_STAGE_A(bufoff, gbase, h, nx) do { _Pragma("unroll") for (int _i = 0; _i < 2; ++_i) { \
;         const unsigned vo_ = GA ? ((nx) ? vgn[h][_i] : vgc[h][_i]) : voffA[_i]; \
;         __builtin_amdgcn_global_load_lds((const unsigned*)((const char*)(gbase) + vo_), (PG8_LAS unsigned*)(lds + (bufoff) + ldsw + _i * 8192), 16, 0, 0); } } while (0)
; #define PG8_LDA(dst, b, h) do { _Pragma("unroll") for (int m = 0; m < 4; ++m) _Pragma("unroll") for (int k = 0; k < 2; ++k) dst[m][k] = *(const PG8_LAS bf16x8*)(lds + PG8_SA(b, h) + aoff + m * 2048 + k * 1024); } while (0)
; #define PG8_LDB(dst, b, h) do { _Pragma("unroll") for (int n = 0; n < 2; ++n) _Pragma("unroll") for (int k = 0; k < 2; ++k) dst[n][k] = *(const PG8_LAS bf16x8*)(lds + PG8_SB(b, h) + boff + n * 2048 + k * 1024); } while (0)
; #define PG8_MMA(ai, bj, At, Bt) do { __builtin_amdgcn_s_setprio(1); _Pragma("unroll") for (int m = 0; m < 4; ++m) _Pragma("unroll") for (int n = 0; n < 2; ++n) _Pragma("unroll") for (int k = 0; k < 2; ++k) \
;         acc[ai][bj][m][n] = __builtin_amdgcn_mfma_f32_16x16x32_bf16(Bt[n][k], At[m][k], acc[ai][bj][m][n], 0, 0, 0); __builtin_amdgcn_s_setprio(0); } while (0)
; #define PG8_WAIT_V(n) asm volatile("s_waitcnt vmcnt(" #n ")" ::: "memory")
; #define PG8_WAIT_L(n) asm volatile("s_waitcnt lgkmcnt(" #n ")" ::: "memory")
; #define PG8_BAR __builtin_amdgcn_s_barrier()
; #define PG8_SCHED __builtin_amdgcn_sched_barrier(0)
; template <class Epi, class Sched>
; __device__ __forceinline__ void gemm_phase(const int WID_, PG8_LAS unsigned char* lds, const Sched& S, const Epi& E) {
;     ...
;             PG8_WAIT_V(8); PG8_WAIT_L(0); PG8_BAR; PG8_MMA(1, 0, At, B0); PG8_MMA(1, 1, At, B1); PG8_BAR; PG8_SCHED;
;             PG8_LDB(B0, 1, 0); PG8_LDB(B1, 1, 1); PG8_SCHED; PG8_LDA(At, 1, 0); PG8_STAGE_A(PG8_SA(0, 1), a2 + hstepA, 1, last);
;             PG8_WAIT_V(8); PG8_WAIT_L(0); PG8_BAR; PG8_MMA(0, 0, At, B0); PG8_MMA(0, 1, At, B1); PG8_BAR; PG8_SCHED;
	s_nop 0
	s_setprio 1
	s_waitcnt lgkmcnt(0)
	v_mfma_f32_16x16x32_bf16 v[60:63], v[140:143], v[178:181], v[60:63]
	v_mfma_f32_16x16x32_bf16 v[56:59], v[154:157], v[178:181], v[56:59]
	v_mfma_f32_16x16x32_bf16 v[44:47], v[140:143], v[186:189], v[44:47]
	v_mfma_f32_16x16x32_bf16 v[40:43], v[154:157], v[186:189], v[40:43]
	v_mfma_f32_16x16x32_bf16 v[28:31], v[140:143], v[198:201], v[28:31]
	v_mfma_f32_16x16x32_bf16 v[24:27], v[154:157], v[198:201], v[24:27]
	v_mfma_f32_16x16x32_bf16 v[12:15], v[140:143], v[206:209], v[12:15]
	v_mfma_f32_16x16x32_bf16 v[8:11], v[154:157], v[206:209], v[8:11]
	v_mfma_f32_16x16x32_bf16 v[60:63], v[150:153], v[182:185], v[60:63]
	v_mfma_f32_16x16x32_bf16 v[56:59], v[158:161], v[182:185], v[56:59]
	v_mfma_f32_16x16x32_bf16 v[44:47], v[150:153], v[190:193], v[44:47]
	v_mfma_f32_16x16x32_bf16 v[40:43], v[158:161], v[190:193], v[40:43]
	v_mfma_f32_16x16x32_bf16 v[28:31], v[150:153], v[202:205], v[28:31]
	v_mfma_f32_16x16x32_bf16 v[24:27], v[158:161], v[202:205], v[24:27]
	v_mfma_f32_16x16x32_bf16 v[12:15], v[150:153], v[210:213], v[12:15]
	v_mfma_f32_16x16x32_bf16 v[8:11], v[158:161], v[210:213], v[8:11]
	s_setprio 0
	s_setprio 1
	v_mfma_f32_16x16x32_bf16 v[52:55], v[162:165], v[178:181], v[52:55]
	v_mfma_f32_16x16x32_bf16 v[48:51], v[170:173], v[178:181], v[48:51]
	v_mfma_f32_16x16x32_bf16 v[36:39], v[162:165], v[186:189], v[36:39]
	v_mfma_f32_16x16x32_bf16 v[32:35], v[170:173], v[186:189], v[32:35]
	v_mfma_f32_16x16x32_bf16 v[20:23], v[162:165], v[198:201], v[20:23]
	v_mfma_f32_16x16x32_bf16 v[16:19], v[170:173], v[198:201], v[16:19]
	v_mfma_f32_16x16x32_bf16 v[4:7], v[162:165], v[206:209], v[4:7]
	v_mfma_f32_16x16x32_bf16 v[0:3], v[170:173], v[206:209], v[0:3]
	v_mfma_f32_16x16x32_bf16 v[52:55], v[166:169], v[182:185], v[52:55]
	v_mfma_f32_16x16x32_bf16 v[48:51], v[174:177], v[182:185], v[48:51]
	v_mfma_f32_16x16x32_bf16 v[36:39], v[166:169], v[190:193], v[36:39]
	v_mfma_f32_16x16x32_bf16 v[32:35], v[174:177], v[190:193], v[32:35]
	v_mfma_f32_16x16x32_bf16 v[20:23], v[166:169], v[202:205], v[20:23]
	v_mfma_f32_16x16x32_bf16 v[16:19], v[174:177], v[202:205], v[16:19]
	v_mfma_f32_16x16x32_bf16 v[4:7], v[166:169], v[210:213], v[4:7]
	v_mfma_f32_16x16x32_bf16 v[0:3], v[174:177], v[210:213], v[0:3]
	s_setprio 0
	s_barrier
	v_add_u32_e32 v158, s82, v147
	v_add_u32_e32 v174, s83, v147
	ds_read_b128 v[140:143], v158
	ds_read_b128 v[150:153], v158 offset:1024
	ds_read_b128 v[154:157], v158 offset:2048
	ds_read_b128 v[158:161], v158 offset:3072
	ds_read_b128 v[162:165], v174
	ds_read_b128 v[166:169], v174 offset:1024
	ds_read_b128 v[170:173], v174 offset:2048
	ds_read_b128 v[174:177], v174 offset:3072
	s_add_u32 s22, s22, 0x40000
	s_addc_u32 s23, s23, 0
	s_mov_b32 m0, s51
	v_lshl_add_u64 v[220:221], s[22:23], 0, v[134:135]
	ds_read_b128 v[178:181], v149 offset:32768
	ds_read_b128 v[182:185], v149 offset:33792
	ds_read_b128 v[186:189], v149 offset:34816
	ds_read_b128 v[190:193], v149 offset:35840
	ds_read_b128 v[198:201], v149 offset:36864
	ds_read_b128 v[202:205], v149 offset:37888
	ds_read_b128 v[206:209], v149 offset:38912
	ds_read_b128 v[210:213], v149 offset:39936
	global_load_lds_dwordx4 v[220:221], off
	v_lshl_add_u64 v[220:221], s[22:23], 0, v[132:133]
	s_mov_b32 m0, s60
	s_nop 0
	global_load_lds_dwordx4 v[220:221], off
	s_waitcnt vmcnt(8)
	s_waitcnt lgkmcnt(0)
	s_barrier
	s_nop 0
	s_setprio 1
	s_waitcnt lgkmcnt(0)
	v_mfma_f32_16x16x32_bf16 v[124:127], v[140:143], v[178:181], v[124:127]
	v_mfma_f32_16x16x32_bf16 v[120:123], v[154:157], v[178:181], v[120:123]
	v_mfma_f32_16x16x32_bf16 v[108:111], v[140:143], v[186:189], v[108:111]
	v_mfma_f32_16x16x32_bf16 v[104:107], v[154:157], v[186:189], v[104:107]
	v_mfma_f32_16x16x32_bf16 v[92:95], v[140:143], v[198:201], v[92:95]
	v_mfma_f32_16x16x32_bf16 v[88:91], v[154:157], v[198:201], v[88:91]
	v_mfma_f32_16x16x32_bf16 v[76:79], v[140:143], v[206:209], v[76:79]
	v_mfma_f32_16x16x32_bf16 v[72:75], v[154:157], v[206:209], v[72:75]
	v_mfma_f32_16x16x32_bf16 v[124:127], v[150:153], v[182:185], v[124:127]
	v_mfma_f32_16x16x32_bf16 v[120:123], v[158:161], v[182:185], v[120:123]
	v_mfma_f32_16x16x32_bf16 v[108:111], v[150:153], v[190:193], v[108:111]
	v_mfma_f32_16x16x32_bf16 v[104:107], v[158:161], v[190:193], v[104:107]
	v_mfma_f32_16x16x32_bf16 v[92:95], v[150:153], v[202:205], v[92:95]
	v_mfma_f32_16x16x32_bf16 v[88:91], v[158:161], v[202:205], v[88:91]
	v_mfma_f32_16x16x32_bf16 v[76:79], v[150:153], v[210:213], v[76:79]
	v_mfma_f32_16x16x32_bf16 v[72:75], v[158:161], v[210:213], v[72:75]
	s_setprio 0
	s_setprio 1
	v_mfma_f32_16x16x32_bf16 v[116:119], v[162:165], v[178:181], v[116:119]
	v_mfma_f32_16x16x32_bf16 v[112:115], v[170:173], v[178:181], v[112:115]
	v_mfma_f32_16x16x32_bf16 v[100:103], v[162:165], v[186:189], v[100:103]
	v_mfma_f32_16x16x32_bf16 v[96:99], v[170:173], v[186:189], v[96:99]
	v_mfma_f32_16x16x32_bf16 v[84:87], v[162:165], v[198:201], v[84:87]
	v_mfma_f32_16x16x32_bf16 v[80:83], v[170:173], v[198:201], v[80:83]
	v_mfma_f32_16x16x32_bf16 v[68:71], v[162:165], v[206:209], v[68:71]
	v_mfma_f32_16x16x32_bf16 v[64:67], v[170:173], v[206:209], v[64:67]
	v_mfma_f32_16x16x32_bf16 v[116:119], v[166:169], v[182:185], v[116:119]
	v_mfma_f32_16x16x32_bf16 v[112:115], v[174:177], v[182:185], v[112:115]
	v_mfma_f32_16x16x32_bf16 v[100:103], v[166:169], v[190:193], v[100:103]
	v_mfma_f32_16x16x32_bf16 v[96:99], v[174:177], v[190:193], v[96:99]
	v_mfma_f32_16x16x32_bf16 v[84:87], v[166:169], v[202:205], v[84:87]
	v_mfma_f32_16x16x32_bf16 v[80:83], v[174:177], v[202:205], v[80:83]
	v_mfma_f32_16x16x32_bf16 v[68:71], v[166:169], v[210:213], v[68:71]
	v_mfma_f32_16x16x32_bf16 v[64:67], v[174:177], v[210:213], v[64:67]
	s_setprio 0
	s_barrier
; #define PG8_STAGE(bufoff, gbase, voff) do { _Pragma("unroll") for (int _i = 0; _i < 2; ++_i) \
;         __builtin_amdgcn_global_load_lds((const unsigned*)((const char*)(gbase) + (voff)[_i]), (PG8_LAS unsigned*)(lds + (bufoff) + ldsw + _i * 8192), 16, 0, 0); } while (0)
; #define PG8_STAGE_A(bufoff, gbase, h, nx) do { _Pragma("unroll") for (int _i = 0; _i < 2; ++_i) { \
;         const unsigned vo_ = GA ? ((nx) ? vgn[h][_i] : vgc[h][_i]) : voffA[_i]; \
;         __builtin_amdgcn_global_load_lds((const unsigned*)((const char*)(gbase) + vo_), (PG8_LAS unsigned*)(lds + (bufoff) + ldsw + _i * 8192), 16, 0, 0); } } while (0)
; #define PG8_LDA(dst, b, h) do { _Pragma("unroll") for (int m = 0; m < 4; ++m) _Pragma("unroll") for (int k = 0; k < 2; ++k) dst[m][k] = *(const PG8_LAS bf16x8*)(lds + PG8_SA(b, h) + aoff + m * 2048 + k * 1024); } while (0)
; #define PG8_MMA(ai, bj, At, Bt) do { __builtin_amdgcn_s_setprio(1); _Pragma("unroll") for (int m = 0; m < 4; ++m) _Pragma("unroll") for (int n = 0; n < 2; ++n) _Pragma("unroll") for (int k = 0; k < 2; ++k) \
;         acc[ai][bj][m][n] = __builtin_amdgcn_mfma_f32_16x16x32_bf16(Bt[n][k], At[m][k], acc[ai][bj][m][n], 0, 0, 0); __builtin_amdgcn_s_setprio(0); } while (0)
; #define PG8_WAIT_V(n) asm volatile("s_waitcnt vmcnt(" #n ")" ::: "memory")
; #define PG8_WAIT_L(n) asm volatile("s_waitcnt lgkmcnt(" #n ")" ::: "memory")
; #define PG8_BAR __builtin_amdgcn_s_barrier()
; #define PG8_SCHED __builtin_amdgcn_sched_barrier(0)
; template <class Epi, class Sched>
; __device__ __forceinline__ void gemm_phase(const int WID_, PG8_LAS unsigned char* lds, const Sched& S, const Epi& E) {
;     ...
;             PG8_LDA(At, 1, 1); PG8_STAGE(PG8_SB(1, 0), b3, voffB); PG8_STAGE(PG8_SB(1, 1), b3 + hstepB, voffB); PG8_STAGE_A(PG8_SA(1, 0), a3, 0, last);
;             PG8_WAIT_V(8); PG8_WAIT_L(0); PG8_BAR; PG8_MMA(1, 0, At, B0); PG8_MMA(1, 1, At, B1); PG8_BAR; PG8_SCHED;
;         }
;         if (wr == 0) PG8_BAR;
	s_add_i32 s22, s82, s48
	v_lshl_add_u64 v[144:145], v[144:145], 0, s[68:69]
	s_mov_b32 m0, s22
	ds_read_b128 v[178:181], v149 offset:49152
	ds_read_b128 v[182:185], v149 offset:50176
	ds_read_b128 v[186:189], v149 offset:51200
	ds_read_b128 v[190:193], v149 offset:52224
	ds_read_b128 v[198:201], v149 offset:53248
	ds_read_b128 v[202:205], v149 offset:54272
	ds_read_b128 v[206:209], v149 offset:55296
	ds_read_b128 v[210:213], v149 offset:56320
	global_load_lds_dwordx4 v[144:145], off
	s_add_i32 m0, s22, 0x2000
	s_add_u32 s20, s20, 0x40080
	v_lshl_add_u64 v[144:145], v[214:215], 0, s[68:69]
	s_addc_u32 s21, s21, 0
	s_add_i32 s22, s83, s48
	global_load_lds_dwordx4 v[144:145], off
	v_lshl_add_u64 v[144:145], s[20:21], 0, v[128:129]
	s_mov_b32 m0, s22
	s_nop 0
	global_load_lds_dwordx4 v[144:145], off
	v_lshl_add_u64 v[144:145], s[20:21], 0, v[130:131]
	s_add_i32 m0, s22, 0x2000
	s_nop 0
	global_load_lds_dwordx4 v[144:145], off
	v_lshl_add_u64 v[144:145], v[216:217], 0, s[68:69]
	s_mov_b32 m0, s61
	s_nop 0
	global_load_lds_dwordx4 v[144:145], off
	v_lshl_add_u64 v[144:145], v[218:219], 0, s[68:69]
	s_mov_b32 m0, s62
	s_nop 0
	global_load_lds_dwordx4 v[144:145], off
	s_waitcnt vmcnt(8)
	s_waitcnt lgkmcnt(0)
	s_barrier
	s_setprio 1
	s_waitcnt lgkmcnt(0)
	v_mfma_f32_16x16x32_bf16 v[60:63], v[140:143], v[178:181], v[60:63]
	v_mfma_f32_16x16x32_bf16 v[56:59], v[154:157], v[178:181], v[56:59]
	v_mfma_f32_16x16x32_bf16 v[44:47], v[140:143], v[186:189], v[44:47]
	v_mfma_f32_16x16x32_bf16 v[40:43], v[154:157], v[186:189], v[40:43]
	v_mfma_f32_16x16x32_bf16 v[28:31], v[140:143], v[198:201], v[28:31]
	v_mfma_f32_16x16x32_bf16 v[24:27], v[154:157], v[198:201], v[24:27]
	v_mfma_f32_16x16x32_bf16 v[12:15], v[140:143], v[206:209], v[12:15]
	v_mfma_f32_16x16x32_bf16 v[8:11], v[154:157], v[206:209], v[8:11]
	v_mfma_f32_16x16x32_bf16 v[60:63], v[150:153], v[182:185], v[60:63]
	v_mfma_f32_16x16x32_bf16 v[56:59], v[158:161], v[182:185], v[56:59]
	v_mfma_f32_16x16x32_bf16 v[44:47], v[150:153], v[190:193], v[44:47]
	v_mfma_f32_16x16x32_bf16 v[40:43], v[158:161], v[190:193], v[40:43]
	v_mfma_f32_16x16x32_bf16 v[28:31], v[150:153], v[202:205], v[28:31]
	v_mfma_f32_16x16x32_bf16 v[24:27], v[158:161], v[202:205], v[24:27]
	v_mfma_f32_16x16x32_bf16 v[12:15], v[150:153], v[210:213], v[12:15]
	v_mfma_f32_16x16x32_bf16 v[8:11], v[158:161], v[210:213], v[8:11]
	s_setprio 0
	s_setprio 1
	v_mfma_f32_16x16x32_bf16 v[52:55], v[162:165], v[178:181], v[52:55]
	v_mfma_f32_16x16x32_bf16 v[48:51], v[170:173], v[178:181], v[48:51]
	v_mfma_f32_16x16x32_bf16 v[36:39], v[162:165], v[186:189], v[36:39]
	v_mfma_f32_16x16x32_bf16 v[32:35], v[170:173], v[186:189], v[32:35]
	v_mfma_f32_16x16x32_bf16 v[20:23], v[162:165], v[198:201], v[20:23]
	v_mfma_f32_16x16x32_bf16 v[16:19], v[170:173], v[198:201], v[16:19]
	v_mfma_f32_16x16x32_bf16 v[4:7], v[162:165], v[206:209], v[4:7]
	v_mfma_f32_16x16x32_bf16 v[0:3], v[170:173], v[206:209], v[0:3]
	v_mfma_f32_16x16x32_bf16 v[52:55], v[166:169], v[182:185], v[52:55]
	v_mfma_f32_16x16x32_bf16 v[48:51], v[174:177], v[182:185], v[48:51]
	v_mfma_f32_16x16x32_bf16 v[36:39], v[166:169], v[190:193], v[36:39]
	v_mfma_f32_16x16x32_bf16 v[32:35], v[174:177], v[190:193], v[32:35]
	v_mfma_f32_16x16x32_bf16 v[20:23], v[166:169], v[202:205], v[20:23]
	v_mfma_f32_16x16x32_bf16 v[16:19], v[174:177], v[202:205], v[16:19]
	v_mfma_f32_16x16x32_bf16 v[4:7], v[166:169], v[210:213], v[4:7]
	v_mfma_f32_16x16x32_bf16 v[0:3], v[174:177], v[210:213], v[0:3]
	s_setprio 0
	s_barrier
	s_add_i32 s79, s79, 2
	s_add_u32 s18, s18, 0x100
	s_addc_u32 s19, s19, 0
	s_add_u32 s9, s9, 0x100
	s_addc_u32 s11, s11, 0
	s_cmp_gt_u32 s79, 13
	s_cbranch_scc0 .LBB0_2120
	s_and_b64 vcc, exec, s[6:7]
	s_cbranch_vccz .LBB0_2123
	s_barrier

; #define PG8_STAGE(bufoff, gbase, voff) do { _Pragma("unroll") for (int _i = 0; _i < 2; ++_i) \
;         __builtin_amdgcn_global_load_lds((const unsigned*)((const char*)(gbase) + (voff)[_i]), (PG8_LAS unsigned*)(lds + (bufoff) + ldsw + _i * 8192), 16, 0, 0); } while (0)
; #define PG8_STAGE_A(bufoff, gbase, h, nx) do { _Pragma("unroll") for (int _i = 0; _i < 2; ++_i) { \
;         const unsigned vo_ = GA ? ((nx) ? vgn[h][_i] : vgc[h][_i]) : voffA[_i]; \
;         __builtin_amdgcn_global_load_lds((const unsigned*)((const char*)(gbase) + vo_), (PG8_LAS unsigned*)(lds + (bufoff) + ldsw + _i * 8192), 16, 0, 0); } } while (0)
; #define PG8_LDA(dst, b, h) do { _Pragma("unroll") for (int m = 0; m < 4; ++m) _Pragma("unroll") for (int k = 0; k < 2; ++k) dst[m][k] = *(const PG8_LAS bf16x8*)(lds + PG8_SA(b, h) + aoff + m * 2048 + k * 1024); } while (0)
; #define PG8_LDB(dst, b, h) do { _Pragma("unroll") for (int n = 0; n < 2; ++n) _Pragma("unroll") for (int k = 0; k < 2; ++k) dst[n][k] = *(const PG8_LAS bf16x8*)(lds + PG8_SB(b, h) + boff + n * 2048 + k * 1024); } while (0)
; #define PG8_WAIT_V(n) asm volatile("s_waitcnt vmcnt(" #n ")" ::: "memory")
; #define PG8_WAIT_L(n) asm volatile("s_waitcnt lgkmcnt(" #n ")" ::: "memory")
; #define PG8_BAR __builtin_amdgcn_s_barrier()
; #define PG8_SCHED __builtin_amdgcn_sched_barrier(0)
; template <class Epi, class Sched>
; __device__ __forceinline__ void gemm_phase(const int WID_, PG8_LAS unsigned char* lds, const Sched& S, const Epi& E) {
;     ...
;         for (int t = 0; t < nt; t += 2) {
;             const bool last = (t == nt - 2);
;             const char* a1 = cA + (size_t)(t + 1) * kstep;
;             const char* a2 = last ? nA : cA + (size_t)(t + 2) * kstep; const char* b2 = last ? nB : cB + (size_t)(t + 2) * kstep;
;             const char* a3 = a2 + kstep; const char* b3 = b2 + kstep;
;             PG8_LDB(B0, 0, 0); PG8_LDB(B1, 0, 1); PG8_SCHED; PG8_LDA(At, 0, 0); PG8_STAGE_A(PG8_SA(1, 1), a1 + hstepA, 1, false);
;             PG8_WAIT_V(8); PG8_WAIT_L(0); PG8_BAR; PG8_MMA(0, 0, At, B0); PG8_MMA(0, 1, At, B1); PG8_BAR; PG8_SCHED;
;             PG8_LDA(At, 0, 1); PG8_STAGE(PG8_SB(0, 0), b2, voffB); PG8_STAGE(PG8_SB(0, 1), b2 + hstepB, voffB); PG8_STAGE_A(PG8_SA(0, 0), a2, 0, last);
;             PG8_WAIT_V(8); PG8_WAIT_L(0); PG8_BAR; PG8_MMA(1, 0, At, B0); PG8_MMA(1, 1, At, B1); PG8_BAR; PG8_SCHED;
.Lg1_nofix:
	ds_read_b128 v[162:165], v151
	ds_read_b128 v[166:169], v151 offset:1024
	ds_read_b128 v[170:173], v151 offset:2048
	ds_read_b128 v[174:177], v151 offset:3072
	ds_read_b128 v[178:181], v152
	ds_read_b128 v[182:185], v152 offset:1024
	ds_read_b128 v[186:189], v152 offset:2048
	ds_read_b128 v[190:193], v152 offset:3072
	s_add_u32 s8, s2, s4
	s_addc_u32 s9, s3, s5
	s_cmpk_eq_i32 s4, 0x800
	s_cselect_b64 vcc, -1, 0
	s_and_b64 s[6:7], vcc, exec
	s_cselect_b32 s66, 0, s4
	s_cselect_b32 s45, 0, s5
	s_cselect_b32 s6, s42, s8
	s_cselect_b32 s7, s43, s9
	s_add_u32 s8, s92, s66
	s_addc_u32 s9, s93, s45
	v_lshl_add_u64 v[226:227], v[142:143], 0, s[4:5]
	s_mov_b32 m0, s51
	v_lshl_add_u64 v[226:227], v[226:227], 0, s[40:41]
	ds_read_b128 v[194:197], v153
	ds_read_b128 v[198:201], v153 offset:1024
	ds_read_b128 v[202:205], v153 offset:2048
	ds_read_b128 v[206:209], v153 offset:3072
	ds_read_b128 v[210:213], v153 offset:4096
	ds_read_b128 v[214:217], v153 offset:5120
	ds_read_b128 v[218:221], v153 offset:6144
	ds_read_b128 v[222:225], v153 offset:7168
	global_load_lds_dwordx4 v[226:227], off
	v_lshl_add_u64 v[226:227], v[144:145], 0, s[4:5]
	v_lshl_add_u64 v[226:227], v[226:227], 0, s[40:41]
	s_mov_b32 m0, s52
	s_nop 0
	global_load_lds_dwordx4 v[226:227], off
	s_waitcnt vmcnt(8)
	s_waitcnt lgkmcnt(0)
	s_barrier
	s_nop 0
	s_setprio 1
	s_waitcnt lgkmcnt(0)
	v_mfma_f32_16x16x32_bf16 v[124:127], v[162:165], v[194:197], v[124:127]
	v_mfma_f32_16x16x32_bf16 v[116:119], v[170:173], v[194:197], v[116:119]
	v_mfma_f32_16x16x32_bf16 v[108:111], v[162:165], v[202:205], v[108:111]
	v_mfma_f32_16x16x32_bf16 v[100:103], v[170:173], v[202:205], v[100:103]
	v_mfma_f32_16x16x32_bf16 v[92:95], v[162:165], v[210:213], v[92:95]
	v_mfma_f32_16x16x32_bf16 v[84:87], v[170:173], v[210:213], v[84:87]
	v_mfma_f32_16x16x32_bf16 v[76:79], v[162:165], v[218:221], v[76:79]
	v_mfma_f32_16x16x32_bf16 v[68:71], v[170:173], v[218:221], v[68:71]
	v_mfma_f32_16x16x32_bf16 v[124:127], v[166:169], v[198:201], v[124:127]
	v_mfma_f32_16x16x32_bf16 v[116:119], v[174:177], v[198:201], v[116:119]
	v_mfma_f32_16x16x32_bf16 v[108:111], v[166:169], v[206:209], v[108:111]
	v_mfma_f32_16x16x32_bf16 v[100:103], v[174:177], v[206:209], v[100:103]
	v_mfma_f32_16x16x32_bf16 v[92:95], v[166:169], v[214:217], v[92:95]
	v_mfma_f32_16x16x32_bf16 v[84:87], v[174:177], v[214:217], v[84:87]
	v_mfma_f32_16x16x32_bf16 v[76:79], v[166:169], v[222:225], v[76:79]
	v_mfma_f32_16x16x32_bf16 v[68:71], v[174:177], v[222:225], v[68:71]
	s_setprio 0
	s_setprio 1
	v_mfma_f32_16x16x32_bf16 v[120:123], v[178:181], v[194:197], v[120:123]
	v_mfma_f32_16x16x32_bf16 v[112:115], v[186:189], v[194:197], v[112:115]
	v_mfma_f32_16x16x32_bf16 v[104:107], v[178:181], v[202:205], v[104:107]
	v_mfma_f32_16x16x32_bf16 v[96:99], v[186:189], v[202:205], v[96:99]
	v_mfma_f32_16x16x32_bf16 v[88:91], v[178:181], v[210:213], v[88:91]
	v_mfma_f32_16x16x32_bf16 v[80:83], v[186:189], v[210:213], v[80:83]
	v_mfma_f32_16x16x32_bf16 v[72:75], v[178:181], v[218:221], v[72:75]
	v_mfma_f32_16x16x32_bf16 v[64:67], v[186:189], v[218:221], v[64:67]
	v_mfma_f32_16x16x32_bf16 v[120:123], v[182:185], v[198:201], v[120:123]
	v_mfma_f32_16x16x32_bf16 v[112:115], v[190:193], v[198:201], v[112:115]
	v_mfma_f32_16x16x32_bf16 v[104:107], v[182:185], v[206:209], v[104:107]
	v_mfma_f32_16x16x32_bf16 v[96:99], v[190:193], v[206:209], v[96:99]
	v_mfma_f32_16x16x32_bf16 v[88:91], v[182:185], v[214:217], v[88:91]
	v_mfma_f32_16x16x32_bf16 v[80:83], v[190:193], v[214:217], v[80:83]
	v_mfma_f32_16x16x32_bf16 v[72:75], v[182:185], v[222:225], v[72:75]
	v_mfma_f32_16x16x32_bf16 v[64:67], v[190:193], v[222:225], v[64:67]
	s_setprio 0
	s_barrier
	s_mov_b32 m0, s53
	v_lshl_add_u64 v[226:227], s[6:7], 0, v[128:129]
	s_add_u32 s66, s6, 0x40000
	ds_read_b128 v[194:197], v153 offset:16384
	ds_read_b128 v[198:201], v153 offset:17408
	ds_read_b128 v[202:205], v153 offset:18432
	ds_read_b128 v[206:209], v153 offset:19456
	ds_read_b128 v[210:213], v153 offset:20480
	ds_read_b128 v[214:217], v153 offset:21504
	ds_read_b128 v[218:221], v153 offset:22528
	ds_read_b128 v[222:225], v153 offset:23552
	global_load_lds_dwordx4 v[226:227], off
	v_lshl_add_u64 v[228:229], s[6:7], 0, v[130:131]
	s_mov_b32 m0, s54
	s_addc_u32 s67, s7, 0
	global_load_lds_dwordx4 v[228:229], off
	v_lshl_add_u64 v[230:231], s[66:67], 0, v[128:129]
	s_mov_b32 m0, s55
	v_cndmask_b32_e32 v132, v134, v157, vcc
	global_load_lds_dwordx4 v[230:231], off
	v_lshl_add_u64 v[230:231], s[66:67], 0, v[130:131]
	s_mov_b32 m0, s56
	s_nop 0
	global_load_lds_dwordx4 v[230:231], off
	s_mov_b32 m0, s21
	v_lshl_add_u64 v[230:231], s[8:9], 0, v[132:133]
	global_load_lds_dwordx4 v132, s[8:9]
	v_cndmask_b32_e32 v132, v136, v158, vcc
	s_mov_b32 m0, s33
	v_lshl_add_u64 v[232:233], s[8:9], 0, v[132:133]
	global_load_lds_dwordx4 v132, s[8:9]
	s_waitcnt vmcnt(8)
	s_waitcnt lgkmcnt(0)
	s_barrier
; #define PG8_STAGE_A(bufoff, gbase, h, nx) do { _Pragma("unroll") for (int _i = 0; _i < 2; ++_i) { \
;         const unsigned vo_ = GA ? ((nx) ? vgn[h][_i] : vgc[h][_i]) : voffA[_i]; \
;         __builtin_amdgcn_global_load_lds((const unsigned*)((const char*)(gbase) + vo_), (PG8_LAS unsigned*)(lds + (bufoff) + ldsw + _i * 8192), 16, 0, 0); } } while (0)
; #define PG8_LDA(dst, b, h) do { _Pragma("unroll") for (int m = 0; m < 4; ++m) _Pragma("unroll") for (int k = 0; k < 2; ++k) dst[m][k] = *(const PG8_LAS bf16x8*)(lds + PG8_SA(b, h) + aoff + m * 2048 + k * 1024); } while (0)
; #define PG8_LDB(dst, b, h) do { _Pragma("unroll") for (int n = 0; n < 2; ++n) _Pragma("unroll") for (int k = 0; k < 2; ++k) dst[n][k] = *(const PG8_LAS bf16x8*)(lds + PG8_SB(b, h) + boff + n * 2048 + k * 1024); } while (0)
; #define PG8_MMA(ai, bj, At, Bt) do { __builtin_amdgcn_s_setprio(1); _Pragma("unroll") for (int m = 0; m < 4; ++m) _Pragma("unroll") for (int n = 0; n < 2; ++n) _Pragma("unroll") for (int k = 0; k < 2; ++k) \
;         acc[ai][bj][m][n] = __builtin_amdgcn_mfma_f32_16x16x32_bf16(Bt[n][k], At[m][k], acc[ai][bj][m][n], 0, 0, 0); __builtin_amdgcn_s_setprio(0); } while (0)
; #define PG8_WAIT_V(n) asm volatile("s_waitcnt vmcnt(" #n ")" ::: "memory")
; #define PG8_WAIT_L(n) asm volatile("s_waitcnt lgkmcnt(" #n ")" ::: "memory")
; #define PG8_BAR __builtin_amdgcn_s_barrier()
; #define PG8_SCHED __builtin_amdgcn_sched_barrier(0)
; template <class Epi, class Sched>
; __device__ __forceinline__ void gemm_phase(const int WID_, PG8_LAS unsigned char* lds, const Sched& S, const Epi& E) {
;     ...
;             PG8_WAIT_V(8); PG8_WAIT_L(0); PG8_BAR; PG8_MMA(1, 0, At, B0); PG8_MMA(1, 1, At, B1); PG8_BAR; PG8_SCHED;
;             PG8_LDB(B0, 1, 0); PG8_LDB(B1, 1, 1); PG8_SCHED; PG8_LDA(At, 1, 0); PG8_STAGE_A(PG8_SA(0, 1), a2 + hstepA, 1, last);
;             PG8_WAIT_V(8); PG8_WAIT_L(0); PG8_BAR; PG8_MMA(0, 0, At, B0); PG8_MMA(0, 1, At, B1); PG8_BAR; PG8_SCHED;
	s_nop 0
	s_setprio 1
	s_waitcnt lgkmcnt(0)
	v_mfma_f32_16x16x32_bf16 v[60:63], v[162:165], v[194:197], v[60:63]
	v_mfma_f32_16x16x32_bf16 v[52:55], v[170:173], v[194:197], v[52:55]
	v_mfma_f32_16x16x32_bf16 v[44:47], v[162:165], v[202:205], v[44:47]
	v_mfma_f32_16x16x32_bf16 v[36:39], v[170:173], v[202:205], v[36:39]
	v_mfma_f32_16x16x32_bf16 v[28:31], v[162:165], v[210:213], v[28:31]
	v_mfma_f32_16x16x32_bf16 v[20:23], v[170:173], v[210:213], v[20:23]
	v_mfma_f32_16x16x32_bf16 v[12:15], v[162:165], v[218:221], v[12:15]
	v_mfma_f32_16x16x32_bf16 v[4:7], v[170:173], v[218:221], v[4:7]
	v_mfma_f32_16x16x32_bf16 v[60:63], v[166:169], v[198:201], v[60:63]
	v_mfma_f32_16x16x32_bf16 v[52:55], v[174:177], v[198:201], v[52:55]
	v_mfma_f32_16x16x32_bf16 v[44:47], v[166:169], v[206:209], v[44:47]
	v_mfma_f32_16x16x32_bf16 v[36:39], v[174:177], v[206:209], v[36:39]
	v_mfma_f32_16x16x32_bf16 v[28:31], v[166:169], v[214:217], v[28:31]
	v_mfma_f32_16x16x32_bf16 v[20:23], v[174:177], v[214:217], v[20:23]
	v_mfma_f32_16x16x32_bf16 v[12:15], v[166:169], v[222:225], v[12:15]
	v_mfma_f32_16x16x32_bf16 v[4:7], v[174:177], v[222:225], v[4:7]
	s_setprio 0
	s_setprio 1
	v_mfma_f32_16x16x32_bf16 v[56:59], v[178:181], v[194:197], v[56:59]
	v_mfma_f32_16x16x32_bf16 v[48:51], v[186:189], v[194:197], v[48:51]
	v_mfma_f32_16x16x32_bf16 v[40:43], v[178:181], v[202:205], v[40:43]
	v_mfma_f32_16x16x32_bf16 v[32:35], v[186:189], v[202:205], v[32:35]
	v_mfma_f32_16x16x32_bf16 v[24:27], v[178:181], v[210:213], v[24:27]
	v_mfma_f32_16x16x32_bf16 v[16:19], v[186:189], v[210:213], v[16:19]
	v_mfma_f32_16x16x32_bf16 v[8:11], v[178:181], v[218:221], v[8:11]
	v_mfma_f32_16x16x32_bf16 v[0:3], v[186:189], v[218:221], v[0:3]
	v_mfma_f32_16x16x32_bf16 v[56:59], v[182:185], v[198:201], v[56:59]
	v_mfma_f32_16x16x32_bf16 v[48:51], v[190:193], v[198:201], v[48:51]
	v_mfma_f32_16x16x32_bf16 v[40:43], v[182:185], v[206:209], v[40:43]
	v_mfma_f32_16x16x32_bf16 v[32:35], v[190:193], v[206:209], v[32:35]
	v_mfma_f32_16x16x32_bf16 v[24:27], v[182:185], v[214:217], v[24:27]
	v_mfma_f32_16x16x32_bf16 v[16:19], v[190:193], v[214:217], v[16:19]
	v_mfma_f32_16x16x32_bf16 v[8:11], v[182:185], v[222:225], v[8:11]
	v_mfma_f32_16x16x32_bf16 v[0:3], v[190:193], v[222:225], v[0:3]
	s_setprio 0
	s_barrier
	ds_read_b128 v[162:165], v154
	ds_read_b128 v[166:169], v154 offset:1024
	ds_read_b128 v[170:173], v154 offset:2048
	ds_read_b128 v[174:177], v154 offset:3072
	ds_read_b128 v[178:181], v155
	ds_read_b128 v[182:185], v155 offset:1024
	ds_read_b128 v[186:189], v155 offset:2048
	ds_read_b128 v[190:193], v155 offset:3072
	s_mov_b32 m0, s46
	v_cndmask_b32_e32 v132, v138, v159, vcc
	ds_read_b128 v[194:197], v153 offset:32768
	ds_read_b128 v[198:201], v153 offset:33792
	ds_read_b128 v[202:205], v153 offset:34816
	ds_read_b128 v[206:209], v153 offset:35840
	ds_read_b128 v[210:213], v153 offset:36864
	ds_read_b128 v[214:217], v153 offset:37888
	ds_read_b128 v[218:221], v153 offset:38912
	ds_read_b128 v[222:225], v153 offset:39936
	global_load_lds_dwordx4 v132, s[8:9]
	v_cndmask_b32_e32 v132, v140, v160, vcc
	s_mov_b32 m0, s47
	s_nop 0
	global_load_lds_dwordx4 v132, s[8:9]
	s_waitcnt vmcnt(8)
	s_waitcnt lgkmcnt(0)
	s_barrier
	s_setprio 1
	s_waitcnt lgkmcnt(0)
	v_mfma_f32_16x16x32_bf16 v[124:127], v[162:165], v[194:197], v[124:127]
	v_mfma_f32_16x16x32_bf16 v[116:119], v[170:173], v[194:197], v[116:119]
	v_mfma_f32_16x16x32_bf16 v[108:111], v[162:165], v[202:205], v[108:111]
	v_mfma_f32_16x16x32_bf16 v[100:103], v[170:173], v[202:205], v[100:103]
	v_mfma_f32_16x16x32_bf16 v[92:95], v[162:165], v[210:213], v[92:95]
	v_mfma_f32_16x16x32_bf16 v[84:87], v[170:173], v[210:213], v[84:87]
	v_mfma_f32_16x16x32_bf16 v[76:79], v[162:165], v[218:221], v[76:79]
	v_mfma_f32_16x16x32_bf16 v[68:71], v[170:173], v[218:221], v[68:71]
	v_mfma_f32_16x16x32_bf16 v[124:127], v[166:169], v[198:201], v[124:127]
	v_mfma_f32_16x16x32_bf16 v[116:119], v[174:177], v[198:201], v[116:119]
	v_mfma_f32_16x16x32_bf16 v[108:111], v[166:169], v[206:209], v[108:111]
	v_mfma_f32_16x16x32_bf16 v[100:103], v[174:177], v[206:209], v[100:103]
	v_mfma_f32_16x16x32_bf16 v[92:95], v[166:169], v[214:217], v[92:95]
	v_mfma_f32_16x16x32_bf16 v[84:87], v[174:177], v[214:217], v[84:87]
	v_mfma_f32_16x16x32_bf16 v[76:79], v[166:169], v[222:225], v[76:79]
	v_mfma_f32_16x16x32_bf16 v[68:71], v[174:177], v[222:225], v[68:71]
	s_setprio 0
	s_setprio 1
	v_mfma_f32_16x16x32_bf16 v[120:123], v[178:181], v[194:197], v[120:123]
	v_mfma_f32_16x16x32_bf16 v[112:115], v[186:189], v[194:197], v[112:115]
	v_mfma_f32_16x16x32_bf16 v[104:107], v[178:181], v[202:205], v[104:107]
	v_mfma_f32_16x16x32_bf16 v[96:99], v[186:189], v[202:205], v[96:99]
	v_mfma_f32_16x16x32_bf16 v[88:91], v[178:181], v[210:213], v[88:91]
	v_mfma_f32_16x16x32_bf16 v[80:83], v[186:189], v[210:213], v[80:83]
	v_mfma_f32_16x16x32_bf16 v[72:75], v[178:181], v[218:221], v[72:75]
	v_mfma_f32_16x16x32_bf16 v[64:67], v[186:189], v[218:221], v[64:67]
	v_mfma_f32_16x16x32_bf16 v[120:123], v[182:185], v[198:201], v[120:123]
	v_mfma_f32_16x16x32_bf16 v[112:115], v[190:193], v[198:201], v[112:115]
	v_mfma_f32_16x16x32_bf16 v[104:107], v[182:185], v[206:209], v[104:107]
	v_mfma_f32_16x16x32_bf16 v[96:99], v[190:193], v[206:209], v[96:99]
	v_mfma_f32_16x16x32_bf16 v[88:91], v[182:185], v[214:217], v[88:91]
	v_mfma_f32_16x16x32_bf16 v[80:83], v[190:193], v[214:217], v[80:83]
	v_mfma_f32_16x16x32_bf16 v[72:75], v[182:185], v[222:225], v[72:75]
	v_mfma_f32_16x16x32_bf16 v[64:67], v[190:193], v[222:225], v[64:67]
	s_setprio 0
	s_barrier
; #define PG8_STAGE(bufoff, gbase, voff) do { _Pragma("unroll") for (int _i = 0; _i < 2; ++_i) \
;         __builtin_amdgcn_global_load_lds((const unsigned*)((const char*)(gbase) + (voff)[_i]), (PG8_LAS unsigned*)(lds + (bufoff) + ldsw + _i * 8192), 16, 0, 0); } while (0)
; #define PG8_STAGE_A(bufoff, gbase, h, nx) do { _Pragma("unroll") for (int _i = 0; _i < 2; ++_i) { \
;         const unsigned vo_ = GA ? ((nx) ? vgn[h][_i] : vgc[h][_i]) : voffA[_i]; \
;         __builtin_amdgcn_global_load_lds((const unsigned*)((const char*)(gbase) + vo_), (PG8_LAS unsigned*)(lds + (bufoff) + ldsw + _i * 8192), 16, 0, 0); } } while (0)
; #define PG8_LDA(dst, b, h) do { _Pragma("unroll") for (int m = 0; m < 4; ++m) _Pragma("unroll") for (int k = 0; k < 2; ++k) dst[m][k] = *(const PG8_LAS bf16x8*)(lds + PG8_SA(b, h) + aoff + m * 2048 + k * 1024); } while (0)
; #define PG8_MMA(ai, bj, At, Bt) do { __builtin_amdgcn_s_setprio(1); _Pragma("unroll") for (int m = 0; m < 4; ++m) _Pragma("unroll") for (int n = 0; n < 2; ++n) _Pragma("unroll") for (int k = 0; k < 2; ++k) \
;         acc[ai][bj][m][n] = __builtin_amdgcn_mfma_f32_16x16x32_bf16(Bt[n][k], At[m][k], acc[ai][bj][m][n], 0, 0, 0); __builtin_amdgcn_s_setprio(0); } while (0)
; #define PG8_WAIT_V(n) asm volatile("s_waitcnt vmcnt(" #n ")" ::: "memory")
; #define PG8_WAIT_L(n) asm volatile("s_waitcnt lgkmcnt(" #n ")" ::: "memory")
; #define PG8_BAR __builtin_amdgcn_s_barrier()
; #define PG8_SCHED __builtin_amdgcn_sched_barrier(0)
; template <class Epi, class Sched>
; __device__ __forceinline__ void gemm_phase(const int WID_, PG8_LAS unsigned char* lds, const Sched& S, const Epi& E) {
;     ...
;             PG8_LDA(At, 1, 1); PG8_STAGE(PG8_SB(1, 0), b3, voffB); PG8_STAGE(PG8_SB(1, 1), b3 + hstepB, voffB); PG8_STAGE_A(PG8_SA(1, 0), a3, 0, last);
;             PG8_WAIT_V(8); PG8_WAIT_L(0); PG8_BAR; PG8_MMA(1, 0, At, B0); PG8_MMA(1, 1, At, B1); PG8_BAR; PG8_SCHED;
;         }
;         if (wr == 0) PG8_BAR;
	s_mov_b32 m0, s60
	v_lshl_add_u64 v[226:227], v[226:227], 0, s[36:37]
	s_add_u32 s6, s6, 0x40080
	ds_read_b128 v[194:197], v153 offset:49152
	ds_read_b128 v[198:201], v153 offset:50176
	ds_read_b128 v[202:205], v153 offset:51200
	ds_read_b128 v[206:209], v153 offset:52224
	ds_read_b128 v[210:213], v153 offset:53248
	ds_read_b128 v[214:217], v153 offset:54272
	ds_read_b128 v[218:221], v153 offset:55296
	ds_read_b128 v[222:225], v153 offset:56320
	global_load_lds_dwordx4 v[226:227], off
	v_lshl_add_u64 v[226:227], v[228:229], 0, s[36:37]
	s_mov_b32 m0, s61
	s_addc_u32 s7, s7, 0
	global_load_lds_dwordx4 v[226:227], off
	v_lshl_add_u64 v[226:227], s[6:7], 0, v[128:129]
	s_mov_b32 m0, s62
	s_nop 0
	global_load_lds_dwordx4 v[226:227], off
	v_lshl_add_u64 v[226:227], s[6:7], 0, v[130:131]
	s_mov_b32 m0, s63
	s_nop 0
	global_load_lds_dwordx4 v[226:227], off
	v_lshl_add_u64 v[226:227], v[230:231], 0, s[36:37]
	s_mov_b32 m0, s49
	s_nop 0
	global_load_lds_dwordx4 v[226:227], off
	v_lshl_add_u64 v[226:227], v[232:233], 0, s[36:37]
	s_mov_b32 m0, s50
	s_nop 0
	global_load_lds_dwordx4 v[226:227], off
	s_waitcnt vmcnt(8)
	s_waitcnt lgkmcnt(0)
	s_barrier
	s_setprio 1
	s_waitcnt lgkmcnt(0)
	v_mfma_f32_16x16x32_bf16 v[60:63], v[162:165], v[194:197], v[60:63]
	v_mfma_f32_16x16x32_bf16 v[52:55], v[170:173], v[194:197], v[52:55]
	v_mfma_f32_16x16x32_bf16 v[44:47], v[162:165], v[202:205], v[44:47]
	v_mfma_f32_16x16x32_bf16 v[36:39], v[170:173], v[202:205], v[36:39]
	v_mfma_f32_16x16x32_bf16 v[28:31], v[162:165], v[210:213], v[28:31]
	v_mfma_f32_16x16x32_bf16 v[20:23], v[170:173], v[210:213], v[20:23]
	v_mfma_f32_16x16x32_bf16 v[12:15], v[162:165], v[218:221], v[12:15]
	v_mfma_f32_16x16x32_bf16 v[4:7], v[170:173], v[218:221], v[4:7]
	v_mfma_f32_16x16x32_bf16 v[60:63], v[166:169], v[198:201], v[60:63]
	v_mfma_f32_16x16x32_bf16 v[52:55], v[174:177], v[198:201], v[52:55]
	v_mfma_f32_16x16x32_bf16 v[44:47], v[166:169], v[206:209], v[44:47]
	v_mfma_f32_16x16x32_bf16 v[36:39], v[174:177], v[206:209], v[36:39]
	v_mfma_f32_16x16x32_bf16 v[28:31], v[166:169], v[214:217], v[28:31]
	v_mfma_f32_16x16x32_bf16 v[20:23], v[174:177], v[214:217], v[20:23]
	v_mfma_f32_16x16x32_bf16 v[12:15], v[166:169], v[222:225], v[12:15]
	v_mfma_f32_16x16x32_bf16 v[4:7], v[174:177], v[222:225], v[4:7]
	s_setprio 0
	s_setprio 1
	v_mfma_f32_16x16x32_bf16 v[56:59], v[178:181], v[194:197], v[56:59]
	v_mfma_f32_16x16x32_bf16 v[48:51], v[186:189], v[194:197], v[48:51]
	v_mfma_f32_16x16x32_bf16 v[40:43], v[178:181], v[202:205], v[40:43]
	v_mfma_f32_16x16x32_bf16 v[32:35], v[186:189], v[202:205], v[32:35]
	v_mfma_f32_16x16x32_bf16 v[24:27], v[178:181], v[210:213], v[24:27]
	v_mfma_f32_16x16x32_bf16 v[16:19], v[186:189], v[210:213], v[16:19]
	v_mfma_f32_16x16x32_bf16 v[8:11], v[178:181], v[218:221], v[8:11]
	v_mfma_f32_16x16x32_bf16 v[0:3], v[186:189], v[218:221], v[0:3]
	v_mfma_f32_16x16x32_bf16 v[56:59], v[182:185], v[198:201], v[56:59]
	v_mfma_f32_16x16x32_bf16 v[48:51], v[190:193], v[198:201], v[48:51]
	v_mfma_f32_16x16x32_bf16 v[40:43], v[182:185], v[206:209], v[40:43]
	v_mfma_f32_16x16x32_bf16 v[32:35], v[190:193], v[206:209], v[32:35]
	v_mfma_f32_16x16x32_bf16 v[24:27], v[182:185], v[214:217], v[24:27]
	v_mfma_f32_16x16x32_bf16 v[16:19], v[190:193], v[214:217], v[16:19]
	v_mfma_f32_16x16x32_bf16 v[8:11], v[182:185], v[222:225], v[8:11]
	v_mfma_f32_16x16x32_bf16 v[0:3], v[190:193], v[222:225], v[0:3]
	s_setprio 0
	s_barrier
	s_add_i32 s11, s11, 2
	s_add_u32 s4, s4, 0x100
	s_addc_u32 s5, s5, 0
	s_cmp_gt_u32 s11, 13
	s_cbranch_scc0 .LBB0_2294
	s_and_b64 vcc, exec, s[38:39]
	s_cbranch_vccz .LBB0_2297
	s_barrier

; #define PG8_STAGE(bufoff, gbase, voff) do { _Pragma("unroll") for (int _i = 0; _i < 2; ++_i) \
;         __builtin_amdgcn_global_load_lds((const unsigned*)((const char*)(gbase) + (voff)[_i]), (PG8_LAS unsigned*)(lds + (bufoff) + ldsw + _i * 8192), 16, 0, 0); } while (0)
; #define PG8_STAGE_A(bufoff, gbase, h, nx) do { _Pragma("unroll") for (int _i = 0; _i < 2; ++_i) { \
;         const unsigned vo_ = GA ? ((nx) ? vgn[h][_i] : vgc[h][_i]) : voffA[_i]; \
;         __builtin_amdgcn_global_load_lds((const unsigned*)((const char*)(gbase) + vo_), (PG8_LAS unsigned*)(lds + (bufoff) + ldsw + _i * 8192), 16, 0, 0); } } while (0)
; #define PG8_LDA(dst, b, h) do { _Pragma("unroll") for (int m = 0; m < 4; ++m) _Pragma("unroll") for (int k = 0; k < 2; ++k) dst[m][k] = *(const PG8_LAS bf16x8*)(lds + PG8_SA(b, h) + aoff + m * 2048 + k * 1024); } while (0)
; #define PG8_LDB(dst, b, h) do { _Pragma("unroll") for (int n = 0; n < 2; ++n) _Pragma("unroll") for (int k = 0; k < 2; ++k) dst[n][k] = *(const PG8_LAS bf16x8*)(lds + PG8_SB(b, h) + boff + n * 2048 + k * 1024); } while (0)
; #define PG8_WAIT_V(n) asm volatile("s_waitcnt vmcnt(" #n ")" ::: "memory")
; #define PG8_WAIT_L(n) asm volatile("s_waitcnt lgkmcnt(" #n ")" ::: "memory")
; #define PG8_BAR __builtin_amdgcn_s_barrier()
; #define PG8_SCHED __builtin_amdgcn_sched_barrier(0)
; template <class Epi, class Sched>
; __device__ __forceinline__ void gemm_phase(const int WID_, PG8_LAS unsigned char* lds, const Sched& S, const Epi& E) {
;     ...
;         for (int t = 0; t < nt; t += 2) {
;             const bool last = (t == nt - 2);
;             const char* a1 = cA + (size_t)(t + 1) * kstep;
;             const char* a2 = last ? nA : cA + (size_t)(t + 2) * kstep; const char* b2 = last ? nB : cB + (size_t)(t + 2) * kstep;
;             const char* a3 = a2 + kstep; const char* b3 = b2 + kstep;
;             PG8_LDB(B0, 0, 0); PG8_LDB(B1, 0, 1); PG8_SCHED; PG8_LDA(At, 0, 0); PG8_STAGE_A(PG8_SA(1, 1), a1 + hstepA, 1, false);
;             PG8_WAIT_V(8); PG8_WAIT_L(0); PG8_BAR; PG8_MMA(0, 0, At, B0); PG8_MMA(0, 1, At, B1); PG8_BAR; PG8_SCHED;
;             PG8_LDA(At, 0, 1); PG8_STAGE(PG8_SB(0, 0), b2, voffB); PG8_STAGE(PG8_SB(0, 1), b2 + hstepB, voffB); PG8_STAGE_A(PG8_SA(0, 0), a2, 0, last);
;             PG8_WAIT_V(8); PG8_WAIT_L(0); PG8_BAR; PG8_MMA(1, 0, At, B0); PG8_MMA(1, 1, At, B1); PG8_BAR; PG8_SCHED;
.Lg2_nofix:
	ds_read_b128 v[142:145], v148
	ds_read_b128 v[152:155], v148 offset:1024
	ds_read_b128 v[156:159], v148 offset:2048
	ds_read_b128 v[160:163], v148 offset:3072
	ds_read_b128 v[164:167], v149
	ds_read_b128 v[168:171], v149 offset:1024
	ds_read_b128 v[172:175], v149 offset:2048
	ds_read_b128 v[176:179], v149 offset:3072
	s_add_u32 s40, s38, 0xfffe0080
	s_addc_u32 s41, s39, -1
	s_cmp_eq_u32 s62, 4
	s_cselect_b32 s43, s31, s41
	s_cselect_b32 s42, s59, s40
	s_cselect_b32 s41, s29, s61
	s_cselect_b32 s40, s28, s60
	s_mov_b32 m0, s55
	v_lshl_add_u64 v[212:213], s[38:39], 0, v[138:139]
	ds_read_b128 v[180:183], v150
	ds_read_b128 v[184:187], v150 offset:1024
	ds_read_b128 v[188:191], v150 offset:2048
	ds_read_b128 v[192:195], v150 offset:3072
	ds_read_b128 v[196:199], v150 offset:4096
	ds_read_b128 v[200:203], v150 offset:5120
	ds_read_b128 v[204:207], v150 offset:6144
	ds_read_b128 v[208:211], v150 offset:7168
	global_load_lds_dwordx4 v[212:213], off
	v_lshl_add_u64 v[212:213], s[38:39], 0, v[140:141]
	s_mov_b32 m0, s56
	s_nop 0
	global_load_lds_dwordx4 v[212:213], off
	s_waitcnt vmcnt(8)
	s_waitcnt lgkmcnt(0)
	s_barrier
	s_setprio 1
	s_waitcnt lgkmcnt(0)
	v_mfma_f32_16x16x32_bf16 v[124:127], v[142:145], v[180:183], v[124:127]
	v_mfma_f32_16x16x32_bf16 v[120:123], v[156:159], v[180:183], v[120:123]
	v_mfma_f32_16x16x32_bf16 v[108:111], v[142:145], v[188:191], v[108:111]
	v_mfma_f32_16x16x32_bf16 v[104:107], v[156:159], v[188:191], v[104:107]
	v_mfma_f32_16x16x32_bf16 v[92:95], v[142:145], v[196:199], v[92:95]
	v_mfma_f32_16x16x32_bf16 v[88:91], v[156:159], v[196:199], v[88:91]
	v_mfma_f32_16x16x32_bf16 v[76:79], v[142:145], v[204:207], v[76:79]
	v_mfma_f32_16x16x32_bf16 v[72:75], v[156:159], v[204:207], v[72:75]
	v_mfma_f32_16x16x32_bf16 v[124:127], v[152:155], v[184:187], v[124:127]
	v_mfma_f32_16x16x32_bf16 v[120:123], v[160:163], v[184:187], v[120:123]
	v_mfma_f32_16x16x32_bf16 v[108:111], v[152:155], v[192:195], v[108:111]
	v_mfma_f32_16x16x32_bf16 v[104:107], v[160:163], v[192:195], v[104:107]
	v_mfma_f32_16x16x32_bf16 v[92:95], v[152:155], v[200:203], v[92:95]
	v_mfma_f32_16x16x32_bf16 v[88:91], v[160:163], v[200:203], v[88:91]
	v_mfma_f32_16x16x32_bf16 v[76:79], v[152:155], v[208:211], v[76:79]
	v_mfma_f32_16x16x32_bf16 v[72:75], v[160:163], v[208:211], v[72:75]
	s_setprio 0
	s_setprio 1
	v_mfma_f32_16x16x32_bf16 v[116:119], v[164:167], v[180:183], v[116:119]
	v_mfma_f32_16x16x32_bf16 v[112:115], v[172:175], v[180:183], v[112:115]
	v_mfma_f32_16x16x32_bf16 v[100:103], v[164:167], v[188:191], v[100:103]
	v_mfma_f32_16x16x32_bf16 v[96:99], v[172:175], v[188:191], v[96:99]
	v_mfma_f32_16x16x32_bf16 v[84:87], v[164:167], v[196:199], v[84:87]
	v_mfma_f32_16x16x32_bf16 v[80:83], v[172:175], v[196:199], v[80:83]
	v_mfma_f32_16x16x32_bf16 v[68:71], v[164:167], v[204:207], v[68:71]
	v_mfma_f32_16x16x32_bf16 v[64:67], v[172:175], v[204:207], v[64:67]
	v_mfma_f32_16x16x32_bf16 v[116:119], v[168:171], v[184:187], v[116:119]
	v_mfma_f32_16x16x32_bf16 v[112:115], v[176:179], v[184:187], v[112:115]
	v_mfma_f32_16x16x32_bf16 v[100:103], v[168:171], v[192:195], v[100:103]
	v_mfma_f32_16x16x32_bf16 v[96:99], v[176:179], v[192:195], v[96:99]
	v_mfma_f32_16x16x32_bf16 v[84:87], v[168:171], v[200:203], v[84:87]
	v_mfma_f32_16x16x32_bf16 v[80:83], v[176:179], v[200:203], v[80:83]
	v_mfma_f32_16x16x32_bf16 v[68:71], v[168:171], v[208:211], v[68:71]
	v_mfma_f32_16x16x32_bf16 v[64:67], v[176:179], v[208:211], v[64:67]
	s_setprio 0
	s_barrier
	s_mov_b32 m0, s57
	v_lshl_add_u64 v[212:213], s[40:41], 0, v[130:131]
	ds_read_b128 v[180:183], v150 offset:16384
	ds_read_b128 v[184:187], v150 offset:17408
	ds_read_b128 v[188:191], v150 offset:18432
	ds_read_b128 v[192:195], v150 offset:19456
	ds_read_b128 v[196:199], v150 offset:20480
	ds_read_b128 v[200:203], v150 offset:21504
	ds_read_b128 v[204:207], v150 offset:22528
	ds_read_b128 v[208:211], v150 offset:23552
	global_load_lds_dwordx4 v[212:213], off
	s_add_i32 m0, s57, 0x2000
	s_add_u32 s64, s40, 0x20000
	v_lshl_add_u64 v[214:215], s[40:41], 0, v[134:135]
	s_addc_u32 s65, s41, 0
	s_add_i32 s63, s50, s33
	global_load_lds_dwordx4 v[214:215], off
	v_lshl_add_u64 v[216:217], s[64:65], 0, v[130:131]
	s_mov_b32 m0, s63
	v_lshl_add_u64 v[218:219], s[42:43], 0, v[136:137]
	global_load_lds_dwordx4 v[216:217], off
	v_lshl_add_u64 v[216:217], s[64:65], 0, v[134:135]
	s_add_i32 m0, s63, 0x2000
	s_nop 0
	global_load_lds_dwordx4 v[216:217], off
	v_lshl_add_u64 v[216:217], s[42:43], 0, v[132:133]
	s_mov_b32 m0, s44
	s_nop 0
	global_load_lds_dwordx4 v[216:217], off
	s_mov_b32 m0, s21
	s_nop 0
	global_load_lds_dwordx4 v[218:219], off
	s_waitcnt vmcnt(8)
	s_waitcnt lgkmcnt(0)
	s_barrier
; #define PG8_STAGE_A(bufoff, gbase, h, nx) do { _Pragma("unroll") for (int _i = 0; _i < 2; ++_i) { \
;         const unsigned vo_ = GA ? ((nx) ? vgn[h][_i] : vgc[h][_i]) : voffA[_i]; \
;         __builtin_amdgcn_global_load_lds((const unsigned*)((const char*)(gbase) + vo_), (PG8_LAS unsigned*)(lds + (bufoff) + ldsw + _i * 8192), 16, 0, 0); } } while (0)
; #define PG8_LDA(dst, b, h) do { _Pragma("unroll") for (int m = 0; m < 4; ++m) _Pragma("unroll") for (int k = 0; k < 2; ++k) dst[m][k] = *(const PG8_LAS bf16x8*)(lds + PG8_SA(b, h) + aoff + m * 2048 + k * 1024); } while (0)
; #define PG8_LDB(dst, b, h) do { _Pragma("unroll") for (int n = 0; n < 2; ++n) _Pragma("unroll") for (int k = 0; k < 2; ++k) dst[n][k] = *(const PG8_LAS bf16x8*)(lds + PG8_SB(b, h) + boff + n * 2048 + k * 1024); } while (0)
; #define PG8_MMA(ai, bj, At, Bt) do { __builtin_amdgcn_s_setprio(1); _Pragma("unroll") for (int m = 0; m < 4; ++m) _Pragma("unroll") for (int n = 0; n < 2; ++n) _Pragma("unroll") for (int k = 0; k < 2; ++k) \
;         acc[ai][bj][m][n] = __builtin_amdgcn_mfma_f32_16x16x32_bf16(Bt[n][k], At[m][k], acc[ai][bj][m][n], 0, 0, 0); __builtin_amdgcn_s_setprio(0); } while (0)
; #define PG8_WAIT_V(n) asm volatile("s_waitcnt vmcnt(" #n ")" ::: "memory")
; #define PG8_WAIT_L(n) asm volatile("s_waitcnt lgkmcnt(" #n ")" ::: "memory")
; #define PG8_BAR __builtin_amdgcn_s_barrier()
; #define PG8_SCHED __builtin_amdgcn_sched_barrier(0)
; template <class Epi, class Sched>
; __device__ __forceinline__ void gemm_phase(const int WID_, PG8_LAS unsigned char* lds, const Sched& S, const Epi& E) {
;     ...
;             PG8_WAIT_V(8); PG8_WAIT_L(0); PG8_BAR; PG8_MMA(1, 0, At, B0); PG8_MMA(1, 1, At, B1); PG8_BAR; PG8_SCHED;
;             PG8_LDB(B0, 1, 0); PG8_LDB(B1, 1, 1); PG8_SCHED; PG8_LDA(At, 1, 0); PG8_STAGE_A(PG8_SA(0, 1), a2 + hstepA, 1, last);
;             PG8_WAIT_V(8); PG8_WAIT_L(0); PG8_BAR; PG8_MMA(0, 0, At, B0); PG8_MMA(0, 1, At, B1); PG8_BAR; PG8_SCHED;
	s_setprio 1
	s_waitcnt lgkmcnt(0)
	v_mfma_f32_16x16x32_bf16 v[60:63], v[142:145], v[180:183], v[60:63]
	v_mfma_f32_16x16x32_bf16 v[56:59], v[156:159], v[180:183], v[56:59]
	v_mfma_f32_16x16x32_bf16 v[44:47], v[142:145], v[188:191], v[44:47]
	v_mfma_f32_16x16x32_bf16 v[40:43], v[156:159], v[188:191], v[40:43]
	v_mfma_f32_16x16x32_bf16 v[28:31], v[142:145], v[196:199], v[28:31]
	v_mfma_f32_16x16x32_bf16 v[24:27], v[156:159], v[196:199], v[24:27]
	v_mfma_f32_16x16x32_bf16 v[12:15], v[142:145], v[204:207], v[12:15]
	v_mfma_f32_16x16x32_bf16 v[8:11], v[156:159], v[204:207], v[8:11]
	v_mfma_f32_16x16x32_bf16 v[60:63], v[152:155], v[184:187], v[60:63]
	v_mfma_f32_16x16x32_bf16 v[56:59], v[160:163], v[184:187], v[56:59]
	v_mfma_f32_16x16x32_bf16 v[44:47], v[152:155], v[192:195], v[44:47]
	v_mfma_f32_16x16x32_bf16 v[40:43], v[160:163], v[192:195], v[40:43]
	v_mfma_f32_16x16x32_bf16 v[28:31], v[152:155], v[200:203], v[28:31]
	v_mfma_f32_16x16x32_bf16 v[24:27], v[160:163], v[200:203], v[24:27]
	v_mfma_f32_16x16x32_bf16 v[12:15], v[152:155], v[208:211], v[12:15]
	v_mfma_f32_16x16x32_bf16 v[8:11], v[160:163], v[208:211], v[8:11]
	s_setprio 0
	s_setprio 1
	v_mfma_f32_16x16x32_bf16 v[52:55], v[164:167], v[180:183], v[52:55]
	v_mfma_f32_16x16x32_bf16 v[48:51], v[172:175], v[180:183], v[48:51]
	v_mfma_f32_16x16x32_bf16 v[36:39], v[164:167], v[188:191], v[36:39]
	v_mfma_f32_16x16x32_bf16 v[32:35], v[172:175], v[188:191], v[32:35]
	v_mfma_f32_16x16x32_bf16 v[20:23], v[164:167], v[196:199], v[20:23]
	v_mfma_f32_16x16x32_bf16 v[16:19], v[172:175], v[196:199], v[16:19]
	v_mfma_f32_16x16x32_bf16 v[4:7], v[164:167], v[204:207], v[4:7]
	v_mfma_f32_16x16x32_bf16 v[0:3], v[172:175], v[204:207], v[0:3]
	v_mfma_f32_16x16x32_bf16 v[52:55], v[168:171], v[184:187], v[52:55]
	v_mfma_f32_16x16x32_bf16 v[48:51], v[176:179], v[184:187], v[48:51]
	v_mfma_f32_16x16x32_bf16 v[36:39], v[168:171], v[192:195], v[36:39]
	v_mfma_f32_16x16x32_bf16 v[32:35], v[176:179], v[192:195], v[32:35]
	v_mfma_f32_16x16x32_bf16 v[20:23], v[168:171], v[200:203], v[20:23]
	v_mfma_f32_16x16x32_bf16 v[16:19], v[176:179], v[200:203], v[16:19]
	v_mfma_f32_16x16x32_bf16 v[4:7], v[168:171], v[208:211], v[4:7]
	v_mfma_f32_16x16x32_bf16 v[0:3], v[176:179], v[208:211], v[0:3]
	s_setprio 0
	s_barrier
	s_add_i32 s63, 0, 0x18000
	v_add_u32_e32 v128, s63, v147
	s_add_i32 s64, 0, 0x1c000
	ds_read_b128 v[142:145], v128
	ds_read_b128 v[152:155], v128 offset:1024
	ds_read_b128 v[156:159], v128 offset:2048
	ds_read_b128 v[160:163], v128 offset:3072
	v_add_u32_e32 v128, s64, v147
	ds_read_b128 v[164:167], v128
	ds_read_b128 v[168:171], v128 offset:1024
	ds_read_b128 v[172:175], v128 offset:2048
	ds_read_b128 v[176:179], v128 offset:3072
	s_add_u32 s42, s42, 0x20000
	s_addc_u32 s43, s43, 0
	s_mov_b32 m0, s45
	v_lshl_add_u64 v[220:221], s[42:43], 0, v[132:133]
	ds_read_b128 v[180:183], v150 offset:32768
	ds_read_b128 v[184:187], v150 offset:33792
	ds_read_b128 v[188:191], v150 offset:34816
	ds_read_b128 v[192:195], v150 offset:35840
	ds_read_b128 v[196:199], v150 offset:36864
	ds_read_b128 v[200:203], v150 offset:37888
	ds_read_b128 v[204:207], v150 offset:38912
	ds_read_b128 v[208:211], v150 offset:39936
	global_load_lds_dwordx4 v[220:221], off
	v_lshl_add_u64 v[220:221], s[42:43], 0, v[136:137]
	s_mov_b32 m0, s46
	s_nop 0
	global_load_lds_dwordx4 v[220:221], off
	s_waitcnt vmcnt(8)
	s_waitcnt lgkmcnt(0)
	s_barrier
	s_nop 0
	s_setprio 1
	s_waitcnt lgkmcnt(0)
	v_mfma_f32_16x16x32_bf16 v[124:127], v[142:145], v[180:183], v[124:127]
	v_mfma_f32_16x16x32_bf16 v[120:123], v[156:159], v[180:183], v[120:123]
	v_mfma_f32_16x16x32_bf16 v[108:111], v[142:145], v[188:191], v[108:111]
	v_mfma_f32_16x16x32_bf16 v[104:107], v[156:159], v[188:191], v[104:107]
	v_mfma_f32_16x16x32_bf16 v[92:95], v[142:145], v[196:199], v[92:95]
	v_mfma_f32_16x16x32_bf16 v[88:91], v[156:159], v[196:199], v[88:91]
	v_mfma_f32_16x16x32_bf16 v[76:79], v[142:145], v[204:207], v[76:79]
	v_mfma_f32_16x16x32_bf16 v[72:75], v[156:159], v[204:207], v[72:75]
	v_mfma_f32_16x16x32_bf16 v[124:127], v[152:155], v[184:187], v[124:127]
	v_mfma_f32_16x16x32_bf16 v[120:123], v[160:163], v[184:187], v[120:123]
	v_mfma_f32_16x16x32_bf16 v[108:111], v[152:155], v[192:195], v[108:111]
	v_mfma_f32_16x16x32_bf16 v[104:107], v[160:163], v[192:195], v[104:107]
	v_mfma_f32_16x16x32_bf16 v[92:95], v[152:155], v[200:203], v[92:95]
	v_mfma_f32_16x16x32_bf16 v[88:91], v[160:163], v[200:203], v[88:91]
	v_mfma_f32_16x16x32_bf16 v[76:79], v[152:155], v[208:211], v[76:79]
	v_mfma_f32_16x16x32_bf16 v[72:75], v[160:163], v[208:211], v[72:75]
	s_setprio 0
	s_setprio 1
	v_mfma_f32_16x16x32_bf16 v[116:119], v[164:167], v[180:183], v[116:119]
	v_mfma_f32_16x16x32_bf16 v[112:115], v[172:175], v[180:183], v[112:115]
	v_mfma_f32_16x16x32_bf16 v[100:103], v[164:167], v[188:191], v[100:103]
	v_mfma_f32_16x16x32_bf16 v[96:99], v[172:175], v[188:191], v[96:99]
	v_mfma_f32_16x16x32_bf16 v[84:87], v[164:167], v[196:199], v[84:87]
	v_mfma_f32_16x16x32_bf16 v[80:83], v[172:175], v[196:199], v[80:83]
	v_mfma_f32_16x16x32_bf16 v[68:71], v[164:167], v[204:207], v[68:71]
	v_mfma_f32_16x16x32_bf16 v[64:67], v[172:175], v[204:207], v[64:67]
	v_mfma_f32_16x16x32_bf16 v[116:119], v[168:171], v[184:187], v[116:119]
	v_mfma_f32_16x16x32_bf16 v[112:115], v[176:179], v[184:187], v[112:115]
	v_mfma_f32_16x16x32_bf16 v[100:103], v[168:171], v[192:195], v[100:103]
	v_mfma_f32_16x16x32_bf16 v[96:99], v[176:179], v[192:195], v[96:99]
	v_mfma_f32_16x16x32_bf16 v[84:87], v[168:171], v[200:203], v[84:87]
	v_mfma_f32_16x16x32_bf16 v[80:83], v[176:179], v[200:203], v[80:83]
	v_mfma_f32_16x16x32_bf16 v[68:71], v[168:171], v[208:211], v[68:71]
	v_mfma_f32_16x16x32_bf16 v[64:67], v[176:179], v[208:211], v[64:67]
	s_setprio 0
	s_barrier
; #define PG8_STAGE(bufoff, gbase, voff) do { _Pragma("unroll") for (int _i = 0; _i < 2; ++_i) \
;         __builtin_amdgcn_global_load_lds((const unsigned*)((const char*)(gbase) + (voff)[_i]), (PG8_LAS unsigned*)(lds + (bufoff) + ldsw + _i * 8192), 16, 0, 0); } while (0)
; #define PG8_STAGE_A(bufoff, gbase, h, nx) do { _Pragma("unroll") for (int _i = 0; _i < 2; ++_i) { \
;         const unsigned vo_ = GA ? ((nx) ? vgn[h][_i] : vgc[h][_i]) : voffA[_i]; \
;         __builtin_amdgcn_global_load_lds((const unsigned*)((const char*)(gbase) + vo_), (PG8_LAS unsigned*)(lds + (bufoff) + ldsw + _i * 8192), 16, 0, 0); } } while (0)
; #define PG8_LDA(dst, b, h) do { _Pragma("unroll") for (int m = 0; m < 4; ++m) _Pragma("unroll") for (int k = 0; k < 2; ++k) dst[m][k] = *(const PG8_LAS bf16x8*)(lds + PG8_SA(b, h) + aoff + m * 2048 + k * 1024); } while (0)
; #define PG8_MMA(ai, bj, At, Bt) do { __builtin_amdgcn_s_setprio(1); _Pragma("unroll") for (int m = 0; m < 4; ++m) _Pragma("unroll") for (int n = 0; n < 2; ++n) _Pragma("unroll") for (int k = 0; k < 2; ++k) \
;         acc[ai][bj][m][n] = __builtin_amdgcn_mfma_f32_16x16x32_bf16(Bt[n][k], At[m][k], acc[ai][bj][m][n], 0, 0, 0); __builtin_amdgcn_s_setprio(0); } while (0)
; #define PG8_WAIT_V(n) asm volatile("s_waitcnt vmcnt(" #n ")" ::: "memory")
; #define PG8_WAIT_L(n) asm volatile("s_waitcnt lgkmcnt(" #n ")" ::: "memory")
; #define PG8_BAR __builtin_amdgcn_s_barrier()
; #define PG8_SCHED __builtin_amdgcn_sched_barrier(0)
; template <class Epi, class Sched>
; __device__ __forceinline__ void gemm_phase(const int WID_, PG8_LAS unsigned char* lds, const Sched& S, const Epi& E) {
;     ...
;             PG8_LDA(At, 1, 1); PG8_STAGE(PG8_SB(1, 0), b3, voffB); PG8_STAGE(PG8_SB(1, 1), b3 + hstepB, voffB); PG8_STAGE_A(PG8_SA(1, 0), a3, 0, last);
;             PG8_WAIT_V(8); PG8_WAIT_L(0); PG8_BAR; PG8_MMA(1, 0, At, B0); PG8_MMA(1, 1, At, B1); PG8_BAR; PG8_SCHED;
;         }
;         if (wr == 0) PG8_BAR;
	s_add_i32 s42, s63, s33
	v_lshl_add_u64 v[212:213], v[212:213], 0, s[6:7]
	s_mov_b32 m0, s42
	ds_read_b128 v[180:183], v150 offset:49152
	ds_read_b128 v[184:187], v150 offset:50176
	ds_read_b128 v[188:191], v150 offset:51200
	ds_read_b128 v[192:195], v150 offset:52224
	ds_read_b128 v[196:199], v150 offset:53248
	ds_read_b128 v[200:203], v150 offset:54272
	ds_read_b128 v[204:207], v150 offset:55296
	ds_read_b128 v[208:211], v150 offset:56320
	global_load_lds_dwordx4 v[212:213], off
	s_add_i32 m0, s42, 0x2000
	s_add_u32 s40, s40, 0x20080
	v_lshl_add_u64 v[212:213], v[214:215], 0, s[6:7]
	s_addc_u32 s41, s41, 0
	s_add_i32 s42, s64, s33
	global_load_lds_dwordx4 v[212:213], off
	v_lshl_add_u64 v[212:213], s[40:41], 0, v[130:131]
	s_mov_b32 m0, s42
	s_nop 0
	global_load_lds_dwordx4 v[212:213], off
	v_lshl_add_u64 v[212:213], s[40:41], 0, v[134:135]
	s_add_i32 m0, s42, 0x2000
	s_nop 0
	global_load_lds_dwordx4 v[212:213], off
	v_lshl_add_u64 v[212:213], v[216:217], 0, s[6:7]
	s_mov_b32 m0, s48
	s_nop 0
	global_load_lds_dwordx4 v[212:213], off
	v_lshl_add_u64 v[212:213], v[218:219], 0, s[6:7]
	s_mov_b32 m0, s49
	s_nop 0
	global_load_lds_dwordx4 v[212:213], off
	s_waitcnt vmcnt(8)
	s_waitcnt lgkmcnt(0)
	s_barrier
	s_setprio 1
	s_waitcnt lgkmcnt(0)
	v_mfma_f32_16x16x32_bf16 v[60:63], v[142:145], v[180:183], v[60:63]
	v_mfma_f32_16x16x32_bf16 v[56:59], v[156:159], v[180:183], v[56:59]
	v_mfma_f32_16x16x32_bf16 v[44:47], v[142:145], v[188:191], v[44:47]
	v_mfma_f32_16x16x32_bf16 v[40:43], v[156:159], v[188:191], v[40:43]
	v_mfma_f32_16x16x32_bf16 v[28:31], v[142:145], v[196:199], v[28:31]
	v_mfma_f32_16x16x32_bf16 v[24:27], v[156:159], v[196:199], v[24:27]
	v_mfma_f32_16x16x32_bf16 v[12:15], v[142:145], v[204:207], v[12:15]
	v_mfma_f32_16x16x32_bf16 v[8:11], v[156:159], v[204:207], v[8:11]
	v_mfma_f32_16x16x32_bf16 v[60:63], v[152:155], v[184:187], v[60:63]
	v_mfma_f32_16x16x32_bf16 v[56:59], v[160:163], v[184:187], v[56:59]
	v_mfma_f32_16x16x32_bf16 v[44:47], v[152:155], v[192:195], v[44:47]
	v_mfma_f32_16x16x32_bf16 v[40:43], v[160:163], v[192:195], v[40:43]
	v_mfma_f32_16x16x32_bf16 v[28:31], v[152:155], v[200:203], v[28:31]
	v_mfma_f32_16x16x32_bf16 v[24:27], v[160:163], v[200:203], v[24:27]
	v_mfma_f32_16x16x32_bf16 v[12:15], v[152:155], v[208:211], v[12:15]
	v_mfma_f32_16x16x32_bf16 v[8:11], v[160:163], v[208:211], v[8:11]
	s_setprio 0
	s_setprio 1
	v_mfma_f32_16x16x32_bf16 v[52:55], v[164:167], v[180:183], v[52:55]
	v_mfma_f32_16x16x32_bf16 v[48:51], v[172:175], v[180:183], v[48:51]
	v_mfma_f32_16x16x32_bf16 v[36:39], v[164:167], v[188:191], v[36:39]
	v_mfma_f32_16x16x32_bf16 v[32:35], v[172:175], v[188:191], v[32:35]
	v_mfma_f32_16x16x32_bf16 v[20:23], v[164:167], v[196:199], v[20:23]
	v_mfma_f32_16x16x32_bf16 v[16:19], v[172:175], v[196:199], v[16:19]
	v_mfma_f32_16x16x32_bf16 v[4:7], v[164:167], v[204:207], v[4:7]
	v_mfma_f32_16x16x32_bf16 v[0:3], v[172:175], v[204:207], v[0:3]
	v_mfma_f32_16x16x32_bf16 v[52:55], v[168:171], v[184:187], v[52:55]
	v_mfma_f32_16x16x32_bf16 v[48:51], v[176:179], v[184:187], v[48:51]
	v_mfma_f32_16x16x32_bf16 v[36:39], v[168:171], v[192:195], v[36:39]
	v_mfma_f32_16x16x32_bf16 v[32:35], v[176:179], v[192:195], v[32:35]
	v_mfma_f32_16x16x32_bf16 v[20:23], v[168:171], v[200:203], v[20:23]
	v_mfma_f32_16x16x32_bf16 v[16:19], v[176:179], v[200:203], v[16:19]
	v_mfma_f32_16x16x32_bf16 v[4:7], v[168:171], v[208:211], v[4:7]
	v_mfma_f32_16x16x32_bf16 v[0:3], v[176:179], v[208:211], v[0:3]
	s_setprio 0
	s_barrier
	s_add_i32 s62, s62, 2
	s_add_u32 s38, s38, 0x100
	s_addc_u32 s39, s39, 0
	s_add_u32 s60, s60, 0x100
	s_addc_u32 s61, s61, 0
	s_cmp_gt_u32 s62, 5
	s_cbranch_scc0 .LBB0_2362
	s_and_b64 vcc, exec, s[8:9]
	s_cbranch_vccz .LBB0_2365
	s_barrier
